# whole layer-1 w_down transposition in the layer-1 in-projection idle slot (43 region steps per idle workgroup, loads three steps ahead)
# baseline (speedup 1.0000x reference)
; #define LDS_WAIT() asm volatile("s_waitcnt lgkmcnt(0)" ::: "memory")
;     const int pr = item >> 1, kb = 2 * (pr / nblk) + (item & 1), nb = pr % nblk, k0 = 64 * kb, n0 = 32 * nb;
;     const int nr = n0 + (lane & 31); const int sc = MAP == 1 ? src_col_in(nr) : nr;
;     float v[32];
; #pragma unroll
;     for (int i = 0; i < 32; ++i) v[i] = sc >= 0 ? W[(size_t)(k0 + 2 * i + (lane >> 5)) * Nsrc + sc] : 0.f;
; #pragma unroll
;     for (int i = 0; i < 32; ++i) { const int k = k0 + 2 * i + (lane >> 5); float x = v[i] * wscale; if (KS) x *= (k < ksplit ? ksA[k] : ksB[k - ksplit]); scr[(2 * i + (lane >> 5)) * 33 + (lane & 31)] = x; }
;     LDS_WAIT(); asm volatile("" ::: "memory");
; __global__ void __launch_bounds__(NWAVES * 64, 2) hybrid_fwd(Args args) {
;     ...
;             p0_transpose_item_f8<false>(args.in[16] + (size_t)l * FF * DM, FF, DM, DM / 32, (unsigned char*)(ws + WS_WDN + l * SZ_WDN), 128.f, args.in[16], args.in[16], 0, scr, r, lane);
.LBB0_575:
	s_waitcnt vmcnt(0)
	s_barrier
	s_cmpk_lt_u32 s77, 0xa0
	s_cbranch_scc1 .Llite_skip
	s_sub_i32 s16, s77, 160
	v_and_b32_e32 v17, 63, v0
	v_lshrrev_b32_e32 v18, 6, v0
	v_lshrrev_b32_e32 v14, 5, v17
	v_lshl_add_u32 v15, v18, 4, v14
	v_and_b32_e32 v16, 31, v17
	v_xor_b32_e32 v16, v16, v18
	v_lshlrev_b32_e32 v16, 4, v16
	v_lshl_add_u32 v4, v15, 9, v16
	v_add_u32_e32 v5, 0x10000, v4
	v_and_b32_e32 v16, 31, v17
	v_lshlrev_b32_e32 v16, 4, v16
	s_mov_b32 s21, 0x4000
	v_mad_u32_u24 v10, v15, s21, v16
	v_and_b32_e32 v14, 7, v17
	v_lshrrev_b32_e32 v15, 5, v17
	v_lshl_add_u32 v15, v18, 2, v15
	v_xor_b32_e32 v15, v15, v14
	v_lshlrev_b32_e32 v15, 4, v15
	v_lshl_add_u32 v15, v14, 13, v15
	v_bfe_u32 v16, v17, 3, 2
	v_lshl_add_u32 v6, v16, 2, v15
	v_add_u32_e32 v7, 0x10000, v6
	v_and_b32_e32 v14, 7, v17
	v_lshrrev_b32_e32 v15, 5, v17
	v_lshl_add_u32 v15, v18, 2, v15
	v_add_u32_e32 v15, 2, v15
	v_xor_b32_e32 v15, v15, v14
	v_lshlrev_b32_e32 v15, 4, v15
	v_lshl_add_u32 v15, v14, 13, v15
	v_bfe_u32 v16, v17, 3, 2
	v_lshl_add_u32 v8, v16, 2, v15
	v_add_u32_e32 v9, 0x10000, v8
	v_lshrrev_b32_e32 v14, 3, v17
	v_lshl_add_u32 v14, v18, 4, v14
	v_and_b32_e32 v15, 7, v17
	v_lshlrev_b32_e32 v15, 4, v15
	v_lshl_add_u32 v11, v14, 14, v15
	v_lshrrev_b32_e32 v14, 3, v17
	v_lshl_add_u32 v14, v18, 4, v14
	v_add_u32_e32 v14, 8, v14
	v_and_b32_e32 v15, 7, v17
	v_lshlrev_b32_e32 v15, 4, v15
	v_lshl_add_u32 v12, v14, 14, v15
	v_mov_b32_e32 v13, 0x43e00000
	s_mov_b32 s20, 0xc3e00000
	v_readlane_b32 s2, v253, 35
	v_readlane_b32 s3, v253, 36
	v_readlane_b32 s4, v253, 41
	v_readlane_b32 s5, v253, 42
	s_add_u32 s2, s2, 0x10000000
	s_addc_u32 s3, s3, 0
	s_add_u32 s4, s4, 0x27600000
	s_addc_u32 s5, s5, 0
	s_add_i32 s17, s16, 0
	s_min_u32 s17, s17, 0xfff
	s_lshr_b32 s18, s17, 5
	s_add_i32 s18, s18, 0
	s_and_b32 s19, s17, 31
	s_lshl_b32 s18, s18, 21
	s_lshl_b32 s19, s19, 9
	s_add_u32 s18, s18, s19
	s_add_u32 s12, s2, s18
	s_addc_u32 s13, s3, 0
	global_load_dwordx4 v[36:39], v10, s[12:13]
	s_add_u32 s12, s12, 0x8000
	s_addc_u32 s13, s13, 0
	global_load_dwordx4 v[40:43], v10, s[12:13]
	s_add_u32 s12, s12, 0x8000
	s_addc_u32 s13, s13, 0
	global_load_dwordx4 v[44:47], v10, s[12:13]
	s_add_u32 s12, s12, 0x8000
	s_addc_u32 s13, s13, 0
	global_load_dwordx4 v[48:51], v10, s[12:13]
	s_add_u32 s12, s12, 0x8000
	s_addc_u32 s13, s13, 0
	global_load_dwordx4 v[52:55], v10, s[12:13]
	s_add_u32 s12, s12, 0x8000
	s_addc_u32 s13, s13, 0
	global_load_dwordx4 v[56:59], v10, s[12:13]
	s_add_u32 s12, s12, 0x8000
	s_addc_u32 s13, s13, 0
	global_load_dwordx4 v[60:63], v10, s[12:13]
	s_add_u32 s12, s12, 0x8000
	s_addc_u32 s13, s13, 0
	global_load_dwordx4 v[64:67], v10, s[12:13]
	s_add_i32 s17, s16, 96
	s_min_u32 s17, s17, 0xfff
	s_lshr_b32 s18, s17, 5
	s_add_i32 s18, s18, 0
	s_and_b32 s19, s17, 31
	s_lshl_b32 s18, s18, 21
	s_lshl_b32 s19, s19, 9
	s_add_u32 s18, s18, s19
	s_add_u32 s12, s2, s18
	s_addc_u32 s13, s3, 0
	global_load_dwordx4 v[68:71], v10, s[12:13]
	s_add_u32 s12, s12, 0x8000
	s_addc_u32 s13, s13, 0
	global_load_dwordx4 v[72:75], v10, s[12:13]
	s_add_u32 s12, s12, 0x8000
	s_addc_u32 s13, s13, 0
	global_load_dwordx4 v[76:79], v10, s[12:13]
	s_add_u32 s12, s12, 0x8000
	s_addc_u32 s13, s13, 0
	global_load_dwordx4 v[80:83], v10, s[12:13]
	s_add_u32 s12, s12, 0x8000
	s_addc_u32 s13, s13, 0
	global_load_dwordx4 v[84:87], v10, s[12:13]
	s_add_u32 s12, s12, 0x8000
	s_addc_u32 s13, s13, 0
	global_load_dwordx4 v[88:91], v10, s[12:13]
	s_add_u32 s12, s12, 0x8000
	s_addc_u32 s13, s13, 0
	global_load_dwordx4 v[92:95], v10, s[12:13]
	s_add_u32 s12, s12, 0x8000
	s_addc_u32 s13, s13, 0
	global_load_dwordx4 v[96:99], v10, s[12:13]
	s_add_i32 s17, s16, 192
	s_min_u32 s17, s17, 0xfff
	s_lshr_b32 s18, s17, 5
	s_add_i32 s18, s18, 0
	s_and_b32 s19, s17, 31
	s_lshl_b32 s18, s18, 21
	s_lshl_b32 s19, s19, 9
	s_add_u32 s18, s18, s19
	s_add_u32 s12, s2, s18
	s_addc_u32 s13, s3, 0
	global_load_dwordx4 v[100:103], v10, s[12:13]
	s_add_u32 s12, s12, 0x8000
	s_addc_u32 s13, s13, 0
	global_load_dwordx4 v[104:107], v10, s[12:13]
	s_add_u32 s12, s12, 0x8000
	s_addc_u32 s13, s13, 0
	global_load_dwordx4 v[108:111], v10, s[12:13]
	s_add_u32 s12, s12, 0x8000
	s_addc_u32 s13, s13, 0
	global_load_dwordx4 v[112:115], v10, s[12:13]
	s_add_u32 s12, s12, 0x8000
	s_addc_u32 s13, s13, 0
	global_load_dwordx4 v[116:119], v10, s[12:13]
	s_add_u32 s12, s12, 0x8000
	s_addc_u32 s13, s13, 0
	global_load_dwordx4 v[120:123], v10, s[12:13]
	s_add_u32 s12, s12, 0x8000
	s_addc_u32 s13, s13, 0
	global_load_dwordx4 v[124:127], v10, s[12:13]
	s_add_u32 s12, s12, 0x8000
	s_addc_u32 s13, s13, 0
	global_load_dwordx4 v[128:131], v10, s[12:13]
	s_waitcnt vmcnt(16)
	v_mul_f32_e32 v36, 0x43000000, v36
	v_mul_f32_e32 v37, 0x43000000, v37
	v_mul_f32_e32 v38, 0x43000000, v38
	v_mul_f32_e32 v39, 0x43000000, v39
	ds_write_b128 v4, v[36:39]
	v_mul_f32_e32 v40, 0x43000000, v40
	v_mul_f32_e32 v41, 0x43000000, v41
	v_mul_f32_e32 v42, 0x43000000, v42
	v_mul_f32_e32 v43, 0x43000000, v43
	ds_write_b128 v4, v[40:43] offset:1024
	v_mul_f32_e32 v44, 0x43000000, v44
	v_mul_f32_e32 v45, 0x43000000, v45
	v_mul_f32_e32 v46, 0x43000000, v46
	v_mul_f32_e32 v47, 0x43000000, v47
	ds_write_b128 v4, v[44:47] offset:2048
	v_mul_f32_e32 v48, 0x43000000, v48
	v_mul_f32_e32 v49, 0x43000000, v49
	v_mul_f32_e32 v50, 0x43000000, v50
	v_mul_f32_e32 v51, 0x43000000, v51
	ds_write_b128 v4, v[48:51] offset:3072
	v_mul_f32_e32 v52, 0x43000000, v52
	v_mul_f32_e32 v53, 0x43000000, v53
	v_mul_f32_e32 v54, 0x43000000, v54
	v_mul_f32_e32 v55, 0x43000000, v55
	ds_write_b128 v4, v[52:55] offset:4096
	v_mul_f32_e32 v56, 0x43000000, v56
	v_mul_f32_e32 v57, 0x43000000, v57
	v_mul_f32_e32 v58, 0x43000000, v58
	v_mul_f32_e32 v59, 0x43000000, v59
	ds_write_b128 v4, v[56:59] offset:5120
	v_mul_f32_e32 v60, 0x43000000, v60
	v_mul_f32_e32 v61, 0x43000000, v61
	v_mul_f32_e32 v62, 0x43000000, v62
	v_mul_f32_e32 v63, 0x43000000, v63
	ds_write_b128 v4, v[60:63] offset:6144
	v_mul_f32_e32 v64, 0x43000000, v64
	v_mul_f32_e32 v65, 0x43000000, v65
	v_mul_f32_e32 v66, 0x43000000, v66
	v_mul_f32_e32 v67, 0x43000000, v67
	ds_write_b128 v4, v[64:67] offset:7168
	s_waitcnt lgkmcnt(0)
	s_barrier
; #define GAS __attribute__((address_space(1)))
; #define LAS __attribute__((address_space(3)))
; #define LDS_WAIT() asm volatile("s_waitcnt lgkmcnt(0)" ::: "memory")
; __device__ __forceinline__ unsigned pk4_fp8(float a, float b, float c, float d) {
;     a = fminf(fmaxf(a, -448.f), 448.f); b = fminf(fmaxf(b, -448.f), 448.f); c = fminf(fmaxf(c, -448.f), 448.f); d = fminf(fmaxf(d, -448.f), 448.f);
;     int w = __builtin_amdgcn_cvt_pk_fp8_f32(a, b, 0, false); w = __builtin_amdgcn_cvt_pk_fp8_f32(c, d, w, true); return (unsigned)w; }
;     const int pr = item >> 1, kb = 2 * (pr / nblk) + (item & 1), nb = pr % nblk, k0 = 64 * kb, n0 = 32 * nb;
;     const int nr = n0 + (lane & 31); const int sc = MAP == 1 ? src_col_in(nr) : nr;
;     float v[32];
; #pragma unroll
;     for (int i = 0; i < 32; ++i) v[i] = sc >= 0 ? W[(size_t)(k0 + 2 * i + (lane >> 5)) * Nsrc + sc] : 0.f;
; #pragma unroll
;     for (int i = 0; i < 32; ++i) { const int k = k0 + 2 * i + (lane >> 5); float x = v[i] * wscale; if (KS) x *= (k < ksplit ? ksA[k] : ksB[k - ksplit]); scr[(2 * i + (lane >> 5)) * 33 + (lane & 31)] = x; }
;     LDS_WAIT(); asm volatile("" ::: "memory");
;     const int c = lane & 7;
; #pragma unroll
;     for (int j = 0; j < 4; ++j) { const int n = (lane >> 3) + 8 * j; const LAS float* s = scr + (8 * c) * 33 + n;
;         const unsigned long long o = (unsigned long long)pg8::pk4_fp8(s[0 * 33], s[1 * 33], s[2 * 33], s[3 * 33]) | ((unsigned long long)pg8::pk4_fp8(s[4 * 33], s[5 * 33], s[6 * 33], s[7 * 33]) << 32);
;         *(GAS unsigned long long*)(WT + (size_t)(n0 + n) * K + k0 + 8 * c) = o; }
;     LDS_WAIT(); asm volatile("" ::: "memory");
	s_add_i32 s17, s16, 288
	s_min_u32 s17, s17, 0xfff
	s_lshr_b32 s18, s17, 5
	s_add_i32 s18, s18, 0
	s_and_b32 s19, s17, 31
	s_lshl_b32 s18, s18, 21
	s_lshl_b32 s19, s19, 9
	s_add_u32 s18, s18, s19
	s_add_u32 s12, s2, s18
	s_addc_u32 s13, s3, 0
	global_load_dwordx4 v[36:39], v10, s[12:13]
	s_add_u32 s12, s12, 0x8000
	s_addc_u32 s13, s13, 0
	global_load_dwordx4 v[40:43], v10, s[12:13]
	s_add_u32 s12, s12, 0x8000
	s_addc_u32 s13, s13, 0
	global_load_dwordx4 v[44:47], v10, s[12:13]
	s_add_u32 s12, s12, 0x8000
	s_addc_u32 s13, s13, 0
	global_load_dwordx4 v[48:51], v10, s[12:13]
	s_add_u32 s12, s12, 0x8000
	s_addc_u32 s13, s13, 0
	global_load_dwordx4 v[52:55], v10, s[12:13]
	s_add_u32 s12, s12, 0x8000
	s_addc_u32 s13, s13, 0
	global_load_dwordx4 v[56:59], v10, s[12:13]
	s_add_u32 s12, s12, 0x8000
	s_addc_u32 s13, s13, 0
	global_load_dwordx4 v[60:63], v10, s[12:13]
	s_add_u32 s12, s12, 0x8000
	s_addc_u32 s13, s13, 0
	global_load_dwordx4 v[64:67], v10, s[12:13]
	s_add_i32 s17, s16, 0
	s_min_u32 s17, s17, 0xfff
	s_lshr_b32 s18, s17, 5
	s_add_i32 s18, s18, 0
	s_and_b32 s19, s17, 31
	s_lshl_b32 s19, s19, 21
	s_lshl_b32 s18, s18, 7
	s_add_u32 s18, s18, s19
	s_add_u32 s14, s4, s18
	s_addc_u32 s15, s5, 0
	ds_read_b32 v132, v6
	ds_read_b32 v133, v6 offset:512
	ds_read_b32 v134, v6 offset:1024
	ds_read_b32 v135, v6 offset:1536
	ds_read_b32 v136, v6 offset:2048
	ds_read_b32 v137, v6 offset:2560
	ds_read_b32 v138, v6 offset:3072
	ds_read_b32 v139, v6 offset:3584
	ds_read_b32 v140, v6 offset:4096
	ds_read_b32 v141, v6 offset:4608
	ds_read_b32 v142, v6 offset:5120
	ds_read_b32 v143, v6 offset:5632
	ds_read_b32 v144, v6 offset:6144
	ds_read_b32 v145, v6 offset:6656
	ds_read_b32 v146, v6 offset:7168
	ds_read_b32 v147, v6 offset:7680
	s_waitcnt lgkmcnt(0)
	v_max_f32_e32 v132, v132, v132
	v_max_f32_e32 v133, v133, v133
	v_max_f32_e32 v134, v134, v134
	v_max_f32_e32 v135, v135, v135
	v_max_f32_e32 v136, v136, v136
	v_max_f32_e32 v137, v137, v137
	v_max_f32_e32 v138, v138, v138
	v_max_f32_e32 v139, v139, v139
	v_max_f32_e32 v140, v140, v140
	v_max_f32_e32 v141, v141, v141
	v_max_f32_e32 v142, v142, v142
	v_max_f32_e32 v143, v143, v143
	v_max_f32_e32 v144, v144, v144
	v_max_f32_e32 v145, v145, v145
	v_max_f32_e32 v146, v146, v146
	v_max_f32_e32 v147, v147, v147
	v_med3_f32 v132, v132, s20, v13
	v_med3_f32 v133, v133, s20, v13
	v_med3_f32 v134, v134, s20, v13
	v_med3_f32 v135, v135, s20, v13
	v_med3_f32 v136, v136, s20, v13
	v_med3_f32 v137, v137, s20, v13
	v_med3_f32 v138, v138, s20, v13
	v_med3_f32 v139, v139, s20, v13
	v_med3_f32 v140, v140, s20, v13
	v_med3_f32 v141, v141, s20, v13
	v_med3_f32 v142, v142, s20, v13
	v_med3_f32 v143, v143, s20, v13
	v_med3_f32 v144, v144, s20, v13
	v_med3_f32 v145, v145, s20, v13
	v_med3_f32 v146, v146, s20, v13
	v_med3_f32 v147, v147, s20, v13
	v_mov_b32_e32 v148, 0
	v_mov_b32_e32 v149, 0
	v_mov_b32_e32 v150, 0
	v_mov_b32_e32 v151, 0
	v_cvt_pk_fp8_f32 v148, v132, v133
	v_cvt_pk_fp8_f32 v149, v136, v137
	v_cvt_pk_fp8_f32 v150, v140, v141
	v_cvt_pk_fp8_f32 v151, v144, v145
	v_cvt_pk_fp8_f32 v148, v134, v135 op_sel:[0,0,1]
	v_cvt_pk_fp8_f32 v149, v138, v139 op_sel:[0,0,1]
	v_cvt_pk_fp8_f32 v150, v142, v143 op_sel:[0,0,1]
	v_cvt_pk_fp8_f32 v151, v146, v147 op_sel:[0,0,1]
	s_nop 0
	global_store_dwordx4 v11, v[148:151], s[14:15]
	ds_read_b32 v132, v8
	ds_read_b32 v133, v8 offset:512
	ds_read_b32 v134, v8 offset:1024
	ds_read_b32 v135, v8 offset:1536
	ds_read_b32 v136, v8 offset:2048
	ds_read_b32 v137, v8 offset:2560
	ds_read_b32 v138, v8 offset:3072
	ds_read_b32 v139, v8 offset:3584
	ds_read_b32 v140, v8 offset:4096
	ds_read_b32 v141, v8 offset:4608
	ds_read_b32 v142, v8 offset:5120
	ds_read_b32 v143, v8 offset:5632
	ds_read_b32 v144, v8 offset:6144
	ds_read_b32 v145, v8 offset:6656
	ds_read_b32 v146, v8 offset:7168
	ds_read_b32 v147, v8 offset:7680
	s_waitcnt lgkmcnt(0)
	v_max_f32_e32 v132, v132, v132
	v_max_f32_e32 v133, v133, v133
	v_max_f32_e32 v134, v134, v134
	v_max_f32_e32 v135, v135, v135
	v_max_f32_e32 v136, v136, v136
	v_max_f32_e32 v137, v137, v137
	v_max_f32_e32 v138, v138, v138
	v_max_f32_e32 v139, v139, v139
	v_max_f32_e32 v140, v140, v140
	v_max_f32_e32 v141, v141, v141
	v_max_f32_e32 v142, v142, v142
	v_max_f32_e32 v143, v143, v143
	v_max_f32_e32 v144, v144, v144
	v_max_f32_e32 v145, v145, v145
	v_max_f32_e32 v146, v146, v146
	v_max_f32_e32 v147, v147, v147
	v_med3_f32 v132, v132, s20, v13
	v_med3_f32 v133, v133, s20, v13
	v_med3_f32 v134, v134, s20, v13
	v_med3_f32 v135, v135, s20, v13
	v_med3_f32 v136, v136, s20, v13
	v_med3_f32 v137, v137, s20, v13
	v_med3_f32 v138, v138, s20, v13
	v_med3_f32 v139, v139, s20, v13
	v_med3_f32 v140, v140, s20, v13
	v_med3_f32 v141, v141, s20, v13
	v_med3_f32 v142, v142, s20, v13
	v_med3_f32 v143, v143, s20, v13
	v_med3_f32 v144, v144, s20, v13
	v_med3_f32 v145, v145, s20, v13
	v_med3_f32 v146, v146, s20, v13
	v_med3_f32 v147, v147, s20, v13
	v_mov_b32_e32 v148, 0
	v_mov_b32_e32 v149, 0
	v_mov_b32_e32 v150, 0
	v_mov_b32_e32 v151, 0
	v_cvt_pk_fp8_f32 v148, v132, v133
	v_cvt_pk_fp8_f32 v149, v136, v137
	v_cvt_pk_fp8_f32 v150, v140, v141
	v_cvt_pk_fp8_f32 v151, v144, v145
	v_cvt_pk_fp8_f32 v148, v134, v135 op_sel:[0,0,1]
	v_cvt_pk_fp8_f32 v149, v138, v139 op_sel:[0,0,1]
	v_cvt_pk_fp8_f32 v150, v142, v143 op_sel:[0,0,1]
	v_cvt_pk_fp8_f32 v151, v146, v147 op_sel:[0,0,1]
	s_nop 0
	global_store_dwordx4 v12, v[148:151], s[14:15]
	s_waitcnt vmcnt(18)
	v_mul_f32_e32 v68, 0x43000000, v68
	v_mul_f32_e32 v69, 0x43000000, v69
	v_mul_f32_e32 v70, 0x43000000, v70
	v_mul_f32_e32 v71, 0x43000000, v71
	ds_write_b128 v5, v[68:71]
	v_mul_f32_e32 v72, 0x43000000, v72
	v_mul_f32_e32 v73, 0x43000000, v73
	v_mul_f32_e32 v74, 0x43000000, v74
	v_mul_f32_e32 v75, 0x43000000, v75
	ds_write_b128 v5, v[72:75] offset:1024
	v_mul_f32_e32 v76, 0x43000000, v76
	v_mul_f32_e32 v77, 0x43000000, v77
	v_mul_f32_e32 v78, 0x43000000, v78
	v_mul_f32_e32 v79, 0x43000000, v79
	ds_write_b128 v5, v[76:79] offset:2048
	v_mul_f32_e32 v80, 0x43000000, v80
	v_mul_f32_e32 v81, 0x43000000, v81
	v_mul_f32_e32 v82, 0x43000000, v82
	v_mul_f32_e32 v83, 0x43000000, v83
	ds_write_b128 v5, v[80:83] offset:3072
	v_mul_f32_e32 v84, 0x43000000, v84
	v_mul_f32_e32 v85, 0x43000000, v85
	v_mul_f32_e32 v86, 0x43000000, v86
	v_mul_f32_e32 v87, 0x43000000, v87
	ds_write_b128 v5, v[84:87] offset:4096
	v_mul_f32_e32 v88, 0x43000000, v88
	v_mul_f32_e32 v89, 0x43000000, v89
	v_mul_f32_e32 v90, 0x43000000, v90
	v_mul_f32_e32 v91, 0x43000000, v91
	ds_write_b128 v5, v[88:91] offset:5120
	v_mul_f32_e32 v92, 0x43000000, v92
	v_mul_f32_e32 v93, 0x43000000, v93
	v_mul_f32_e32 v94, 0x43000000, v94
	v_mul_f32_e32 v95, 0x43000000, v95
	ds_write_b128 v5, v[92:95] offset:6144
	v_mul_f32_e32 v96, 0x43000000, v96
	v_mul_f32_e32 v97, 0x43000000, v97
	v_mul_f32_e32 v98, 0x43000000, v98
	v_mul_f32_e32 v99, 0x43000000, v99
	ds_write_b128 v5, v[96:99] offset:7168
	s_waitcnt lgkmcnt(0)
	s_barrier
; #define GAS __attribute__((address_space(1)))
; #define LAS __attribute__((address_space(3)))
; #define LDS_WAIT() asm volatile("s_waitcnt lgkmcnt(0)" ::: "memory")
; __device__ __forceinline__ unsigned pk4_fp8(float a, float b, float c, float d) {
;     a = fminf(fmaxf(a, -448.f), 448.f); b = fminf(fmaxf(b, -448.f), 448.f); c = fminf(fmaxf(c, -448.f), 448.f); d = fminf(fmaxf(d, -448.f), 448.f);
;     int w = __builtin_amdgcn_cvt_pk_fp8_f32(a, b, 0, false); w = __builtin_amdgcn_cvt_pk_fp8_f32(c, d, w, true); return (unsigned)w; }
;     const int pr = item >> 1, kb = 2 * (pr / nblk) + (item & 1), nb = pr % nblk, k0 = 64 * kb, n0 = 32 * nb;
;     const int nr = n0 + (lane & 31); const int sc = MAP == 1 ? src_col_in(nr) : nr;
;     float v[32];
; #pragma unroll
;     for (int i = 0; i < 32; ++i) v[i] = sc >= 0 ? W[(size_t)(k0 + 2 * i + (lane >> 5)) * Nsrc + sc] : 0.f;
; #pragma unroll
;     for (int i = 0; i < 32; ++i) { const int k = k0 + 2 * i + (lane >> 5); float x = v[i] * wscale; if (KS) x *= (k < ksplit ? ksA[k] : ksB[k - ksplit]); scr[(2 * i + (lane >> 5)) * 33 + (lane & 31)] = x; }
;     LDS_WAIT(); asm volatile("" ::: "memory");
;     const int c = lane & 7;
; #pragma unroll
;     for (int j = 0; j < 4; ++j) { const int n = (lane >> 3) + 8 * j; const LAS float* s = scr + (8 * c) * 33 + n;
;         const unsigned long long o = (unsigned long long)pg8::pk4_fp8(s[0 * 33], s[1 * 33], s[2 * 33], s[3 * 33]) | ((unsigned long long)pg8::pk4_fp8(s[4 * 33], s[5 * 33], s[6 * 33], s[7 * 33]) << 32);
;         *(GAS unsigned long long*)(WT + (size_t)(n0 + n) * K + k0 + 8 * c) = o; }
;     LDS_WAIT(); asm volatile("" ::: "memory");
	s_add_i32 s17, s16, 384
	s_min_u32 s17, s17, 0xfff
	s_lshr_b32 s18, s17, 5
	s_add_i32 s18, s18, 0
	s_and_b32 s19, s17, 31
	s_lshl_b32 s18, s18, 21
	s_lshl_b32 s19, s19, 9
	s_add_u32 s18, s18, s19
	s_add_u32 s12, s2, s18
	s_addc_u32 s13, s3, 0
	global_load_dwordx4 v[68:71], v10, s[12:13]
	s_add_u32 s12, s12, 0x8000
	s_addc_u32 s13, s13, 0
	global_load_dwordx4 v[72:75], v10, s[12:13]
	s_add_u32 s12, s12, 0x8000
	s_addc_u32 s13, s13, 0
	global_load_dwordx4 v[76:79], v10, s[12:13]
	s_add_u32 s12, s12, 0x8000
	s_addc_u32 s13, s13, 0
	global_load_dwordx4 v[80:83], v10, s[12:13]
	s_add_u32 s12, s12, 0x8000
	s_addc_u32 s13, s13, 0
	global_load_dwordx4 v[84:87], v10, s[12:13]
	s_add_u32 s12, s12, 0x8000
	s_addc_u32 s13, s13, 0
	global_load_dwordx4 v[88:91], v10, s[12:13]
	s_add_u32 s12, s12, 0x8000
	s_addc_u32 s13, s13, 0
	global_load_dwordx4 v[92:95], v10, s[12:13]
	s_add_u32 s12, s12, 0x8000
	s_addc_u32 s13, s13, 0
	global_load_dwordx4 v[96:99], v10, s[12:13]
	s_add_i32 s17, s16, 96
	s_min_u32 s17, s17, 0xfff
	s_lshr_b32 s18, s17, 5
	s_add_i32 s18, s18, 0
	s_and_b32 s19, s17, 31
	s_lshl_b32 s19, s19, 21
	s_lshl_b32 s18, s18, 7
	s_add_u32 s18, s18, s19
	s_add_u32 s14, s4, s18
	s_addc_u32 s15, s5, 0
	ds_read_b32 v132, v7
	ds_read_b32 v133, v7 offset:512
	ds_read_b32 v134, v7 offset:1024
	ds_read_b32 v135, v7 offset:1536
	ds_read_b32 v136, v7 offset:2048
	ds_read_b32 v137, v7 offset:2560
	ds_read_b32 v138, v7 offset:3072
	ds_read_b32 v139, v7 offset:3584
	ds_read_b32 v140, v7 offset:4096
	ds_read_b32 v141, v7 offset:4608
	ds_read_b32 v142, v7 offset:5120
	ds_read_b32 v143, v7 offset:5632
	ds_read_b32 v144, v7 offset:6144
	ds_read_b32 v145, v7 offset:6656
	ds_read_b32 v146, v7 offset:7168
	ds_read_b32 v147, v7 offset:7680
	s_waitcnt lgkmcnt(0)
	v_max_f32_e32 v132, v132, v132
	v_max_f32_e32 v133, v133, v133
	v_max_f32_e32 v134, v134, v134
	v_max_f32_e32 v135, v135, v135
	v_max_f32_e32 v136, v136, v136
	v_max_f32_e32 v137, v137, v137
	v_max_f32_e32 v138, v138, v138
	v_max_f32_e32 v139, v139, v139
	v_max_f32_e32 v140, v140, v140
	v_max_f32_e32 v141, v141, v141
	v_max_f32_e32 v142, v142, v142
	v_max_f32_e32 v143, v143, v143
	v_max_f32_e32 v144, v144, v144
	v_max_f32_e32 v145, v145, v145
	v_max_f32_e32 v146, v146, v146
	v_max_f32_e32 v147, v147, v147
	v_med3_f32 v132, v132, s20, v13
	v_med3_f32 v133, v133, s20, v13
	v_med3_f32 v134, v134, s20, v13
	v_med3_f32 v135, v135, s20, v13
	v_med3_f32 v136, v136, s20, v13
	v_med3_f32 v137, v137, s20, v13
	v_med3_f32 v138, v138, s20, v13
	v_med3_f32 v139, v139, s20, v13
	v_med3_f32 v140, v140, s20, v13
	v_med3_f32 v141, v141, s20, v13
	v_med3_f32 v142, v142, s20, v13
	v_med3_f32 v143, v143, s20, v13
	v_med3_f32 v144, v144, s20, v13
	v_med3_f32 v145, v145, s20, v13
	v_med3_f32 v146, v146, s20, v13
	v_med3_f32 v147, v147, s20, v13
	v_mov_b32_e32 v148, 0
	v_mov_b32_e32 v149, 0
	v_mov_b32_e32 v150, 0
	v_mov_b32_e32 v151, 0
	v_cvt_pk_fp8_f32 v148, v132, v133
	v_cvt_pk_fp8_f32 v149, v136, v137
	v_cvt_pk_fp8_f32 v150, v140, v141
	v_cvt_pk_fp8_f32 v151, v144, v145
	v_cvt_pk_fp8_f32 v148, v134, v135 op_sel:[0,0,1]
	v_cvt_pk_fp8_f32 v149, v138, v139 op_sel:[0,0,1]
	v_cvt_pk_fp8_f32 v150, v142, v143 op_sel:[0,0,1]
	v_cvt_pk_fp8_f32 v151, v146, v147 op_sel:[0,0,1]
	s_nop 0
	global_store_dwordx4 v11, v[148:151], s[14:15]
	ds_read_b32 v132, v9
	ds_read_b32 v133, v9 offset:512
	ds_read_b32 v134, v9 offset:1024
	ds_read_b32 v135, v9 offset:1536
	ds_read_b32 v136, v9 offset:2048
	ds_read_b32 v137, v9 offset:2560
	ds_read_b32 v138, v9 offset:3072
	ds_read_b32 v139, v9 offset:3584
	ds_read_b32 v140, v9 offset:4096
	ds_read_b32 v141, v9 offset:4608
	ds_read_b32 v142, v9 offset:5120
	ds_read_b32 v143, v9 offset:5632
	ds_read_b32 v144, v9 offset:6144
	ds_read_b32 v145, v9 offset:6656
	ds_read_b32 v146, v9 offset:7168
	ds_read_b32 v147, v9 offset:7680
	s_waitcnt lgkmcnt(0)
	v_max_f32_e32 v132, v132, v132
	v_max_f32_e32 v133, v133, v133
	v_max_f32_e32 v134, v134, v134
	v_max_f32_e32 v135, v135, v135
	v_max_f32_e32 v136, v136, v136
	v_max_f32_e32 v137, v137, v137
	v_max_f32_e32 v138, v138, v138
	v_max_f32_e32 v139, v139, v139
	v_max_f32_e32 v140, v140, v140
	v_max_f32_e32 v141, v141, v141
	v_max_f32_e32 v142, v142, v142
	v_max_f32_e32 v143, v143, v143
	v_max_f32_e32 v144, v144, v144
	v_max_f32_e32 v145, v145, v145
	v_max_f32_e32 v146, v146, v146
	v_max_f32_e32 v147, v147, v147
	v_med3_f32 v132, v132, s20, v13
	v_med3_f32 v133, v133, s20, v13
	v_med3_f32 v134, v134, s20, v13
	v_med3_f32 v135, v135, s20, v13
	v_med3_f32 v136, v136, s20, v13
	v_med3_f32 v137, v137, s20, v13
	v_med3_f32 v138, v138, s20, v13
	v_med3_f32 v139, v139, s20, v13
	v_med3_f32 v140, v140, s20, v13
	v_med3_f32 v141, v141, s20, v13
	v_med3_f32 v142, v142, s20, v13
	v_med3_f32 v143, v143, s20, v13
	v_med3_f32 v144, v144, s20, v13
	v_med3_f32 v145, v145, s20, v13
	v_med3_f32 v146, v146, s20, v13
	v_med3_f32 v147, v147, s20, v13
	v_mov_b32_e32 v148, 0
	v_mov_b32_e32 v149, 0
	v_mov_b32_e32 v150, 0
	v_mov_b32_e32 v151, 0
	v_cvt_pk_fp8_f32 v148, v132, v133
	v_cvt_pk_fp8_f32 v149, v136, v137
	v_cvt_pk_fp8_f32 v150, v140, v141
	v_cvt_pk_fp8_f32 v151, v144, v145
	v_cvt_pk_fp8_f32 v148, v134, v135 op_sel:[0,0,1]
	v_cvt_pk_fp8_f32 v149, v138, v139 op_sel:[0,0,1]
	v_cvt_pk_fp8_f32 v150, v142, v143 op_sel:[0,0,1]
	v_cvt_pk_fp8_f32 v151, v146, v147 op_sel:[0,0,1]
	s_nop 0
	global_store_dwordx4 v12, v[148:151], s[14:15]
	s_waitcnt vmcnt(20)
	v_mul_f32_e32 v100, 0x43000000, v100
	v_mul_f32_e32 v101, 0x43000000, v101
	v_mul_f32_e32 v102, 0x43000000, v102
	v_mul_f32_e32 v103, 0x43000000, v103
	ds_write_b128 v4, v[100:103]
	v_mul_f32_e32 v104, 0x43000000, v104
	v_mul_f32_e32 v105, 0x43000000, v105
	v_mul_f32_e32 v106, 0x43000000, v106
	v_mul_f32_e32 v107, 0x43000000, v107
	ds_write_b128 v4, v[104:107] offset:1024
	v_mul_f32_e32 v108, 0x43000000, v108
	v_mul_f32_e32 v109, 0x43000000, v109
	v_mul_f32_e32 v110, 0x43000000, v110
	v_mul_f32_e32 v111, 0x43000000, v111
	ds_write_b128 v4, v[108:111] offset:2048
	v_mul_f32_e32 v112, 0x43000000, v112
	v_mul_f32_e32 v113, 0x43000000, v113
	v_mul_f32_e32 v114, 0x43000000, v114
	v_mul_f32_e32 v115, 0x43000000, v115
	ds_write_b128 v4, v[112:115] offset:3072
	v_mul_f32_e32 v116, 0x43000000, v116
	v_mul_f32_e32 v117, 0x43000000, v117
	v_mul_f32_e32 v118, 0x43000000, v118
	v_mul_f32_e32 v119, 0x43000000, v119
	ds_write_b128 v4, v[116:119] offset:4096
	v_mul_f32_e32 v120, 0x43000000, v120
	v_mul_f32_e32 v121, 0x43000000, v121
	v_mul_f32_e32 v122, 0x43000000, v122
	v_mul_f32_e32 v123, 0x43000000, v123
	ds_write_b128 v4, v[120:123] offset:5120
	v_mul_f32_e32 v124, 0x43000000, v124
	v_mul_f32_e32 v125, 0x43000000, v125
	v_mul_f32_e32 v126, 0x43000000, v126
	v_mul_f32_e32 v127, 0x43000000, v127
	ds_write_b128 v4, v[124:127] offset:6144
	v_mul_f32_e32 v128, 0x43000000, v128
	v_mul_f32_e32 v129, 0x43000000, v129
	v_mul_f32_e32 v130, 0x43000000, v130
	v_mul_f32_e32 v131, 0x43000000, v131
	ds_write_b128 v4, v[128:131] offset:7168
	s_waitcnt lgkmcnt(0)
	s_barrier
; #define GAS __attribute__((address_space(1)))
; #define LAS __attribute__((address_space(3)))
; #define LDS_WAIT() asm volatile("s_waitcnt lgkmcnt(0)" ::: "memory")
; __device__ __forceinline__ unsigned pk4_fp8(float a, float b, float c, float d) {
;     a = fminf(fmaxf(a, -448.f), 448.f); b = fminf(fmaxf(b, -448.f), 448.f); c = fminf(fmaxf(c, -448.f), 448.f); d = fminf(fmaxf(d, -448.f), 448.f);
;     int w = __builtin_amdgcn_cvt_pk_fp8_f32(a, b, 0, false); w = __builtin_amdgcn_cvt_pk_fp8_f32(c, d, w, true); return (unsigned)w; }
;     const int pr = item >> 1, kb = 2 * (pr / nblk) + (item & 1), nb = pr % nblk, k0 = 64 * kb, n0 = 32 * nb;
;     const int nr = n0 + (lane & 31); const int sc = MAP == 1 ? src_col_in(nr) : nr;
;     float v[32];
; #pragma unroll
;     for (int i = 0; i < 32; ++i) v[i] = sc >= 0 ? W[(size_t)(k0 + 2 * i + (lane >> 5)) * Nsrc + sc] : 0.f;
; #pragma unroll
;     for (int i = 0; i < 32; ++i) { const int k = k0 + 2 * i + (lane >> 5); float x = v[i] * wscale; if (KS) x *= (k < ksplit ? ksA[k] : ksB[k - ksplit]); scr[(2 * i + (lane >> 5)) * 33 + (lane & 31)] = x; }
;     LDS_WAIT(); asm volatile("" ::: "memory");
;     const int c = lane & 7;
; #pragma unroll
;     for (int j = 0; j < 4; ++j) { const int n = (lane >> 3) + 8 * j; const LAS float* s = scr + (8 * c) * 33 + n;
;         const unsigned long long o = (unsigned long long)pg8::pk4_fp8(s[0 * 33], s[1 * 33], s[2 * 33], s[3 * 33]) | ((unsigned long long)pg8::pk4_fp8(s[4 * 33], s[5 * 33], s[6 * 33], s[7 * 33]) << 32);
;         *(GAS unsigned long long*)(WT + (size_t)(n0 + n) * K + k0 + 8 * c) = o; }
;     LDS_WAIT(); asm volatile("" ::: "memory");
	s_add_i32 s17, s16, 480
	s_min_u32 s17, s17, 0xfff
	s_lshr_b32 s18, s17, 5
	s_add_i32 s18, s18, 0
	s_and_b32 s19, s17, 31
	s_lshl_b32 s18, s18, 21
	s_lshl_b32 s19, s19, 9
	s_add_u32 s18, s18, s19
	s_add_u32 s12, s2, s18
	s_addc_u32 s13, s3, 0
	global_load_dwordx4 v[100:103], v10, s[12:13]
	s_add_u32 s12, s12, 0x8000
	s_addc_u32 s13, s13, 0
	global_load_dwordx4 v[104:107], v10, s[12:13]
	s_add_u32 s12, s12, 0x8000
	s_addc_u32 s13, s13, 0
	global_load_dwordx4 v[108:111], v10, s[12:13]
	s_add_u32 s12, s12, 0x8000
	s_addc_u32 s13, s13, 0
	global_load_dwordx4 v[112:115], v10, s[12:13]
	s_add_u32 s12, s12, 0x8000
	s_addc_u32 s13, s13, 0
	global_load_dwordx4 v[116:119], v10, s[12:13]
	s_add_u32 s12, s12, 0x8000
	s_addc_u32 s13, s13, 0
	global_load_dwordx4 v[120:123], v10, s[12:13]
	s_add_u32 s12, s12, 0x8000
	s_addc_u32 s13, s13, 0
	global_load_dwordx4 v[124:127], v10, s[12:13]
	s_add_u32 s12, s12, 0x8000
	s_addc_u32 s13, s13, 0
	global_load_dwordx4 v[128:131], v10, s[12:13]
	s_add_i32 s17, s16, 192
	s_min_u32 s17, s17, 0xfff
	s_lshr_b32 s18, s17, 5
	s_add_i32 s18, s18, 0
	s_and_b32 s19, s17, 31
	s_lshl_b32 s19, s19, 21
	s_lshl_b32 s18, s18, 7
	s_add_u32 s18, s18, s19
	s_add_u32 s14, s4, s18
	s_addc_u32 s15, s5, 0
	ds_read_b32 v132, v6
	ds_read_b32 v133, v6 offset:512
	ds_read_b32 v134, v6 offset:1024
	ds_read_b32 v135, v6 offset:1536
	ds_read_b32 v136, v6 offset:2048
	ds_read_b32 v137, v6 offset:2560
	ds_read_b32 v138, v6 offset:3072
	ds_read_b32 v139, v6 offset:3584
	ds_read_b32 v140, v6 offset:4096
	ds_read_b32 v141, v6 offset:4608
	ds_read_b32 v142, v6 offset:5120
	ds_read_b32 v143, v6 offset:5632
	ds_read_b32 v144, v6 offset:6144
	ds_read_b32 v145, v6 offset:6656
	ds_read_b32 v146, v6 offset:7168
	ds_read_b32 v147, v6 offset:7680
	s_waitcnt lgkmcnt(0)
	v_max_f32_e32 v132, v132, v132
	v_max_f32_e32 v133, v133, v133
	v_max_f32_e32 v134, v134, v134
	v_max_f32_e32 v135, v135, v135
	v_max_f32_e32 v136, v136, v136
	v_max_f32_e32 v137, v137, v137
	v_max_f32_e32 v138, v138, v138
	v_max_f32_e32 v139, v139, v139
	v_max_f32_e32 v140, v140, v140
	v_max_f32_e32 v141, v141, v141
	v_max_f32_e32 v142, v142, v142
	v_max_f32_e32 v143, v143, v143
	v_max_f32_e32 v144, v144, v144
	v_max_f32_e32 v145, v145, v145
	v_max_f32_e32 v146, v146, v146
	v_max_f32_e32 v147, v147, v147
	v_med3_f32 v132, v132, s20, v13
	v_med3_f32 v133, v133, s20, v13
	v_med3_f32 v134, v134, s20, v13
	v_med3_f32 v135, v135, s20, v13
	v_med3_f32 v136, v136, s20, v13
	v_med3_f32 v137, v137, s20, v13
	v_med3_f32 v138, v138, s20, v13
	v_med3_f32 v139, v139, s20, v13
	v_med3_f32 v140, v140, s20, v13
	v_med3_f32 v141, v141, s20, v13
	v_med3_f32 v142, v142, s20, v13
	v_med3_f32 v143, v143, s20, v13
	v_med3_f32 v144, v144, s20, v13
	v_med3_f32 v145, v145, s20, v13
	v_med3_f32 v146, v146, s20, v13
	v_med3_f32 v147, v147, s20, v13
	v_mov_b32_e32 v148, 0
	v_mov_b32_e32 v149, 0
	v_mov_b32_e32 v150, 0
	v_mov_b32_e32 v151, 0
	v_cvt_pk_fp8_f32 v148, v132, v133
	v_cvt_pk_fp8_f32 v149, v136, v137
	v_cvt_pk_fp8_f32 v150, v140, v141
	v_cvt_pk_fp8_f32 v151, v144, v145
	v_cvt_pk_fp8_f32 v148, v134, v135 op_sel:[0,0,1]
	v_cvt_pk_fp8_f32 v149, v138, v139 op_sel:[0,0,1]
	v_cvt_pk_fp8_f32 v150, v142, v143 op_sel:[0,0,1]
	v_cvt_pk_fp8_f32 v151, v146, v147 op_sel:[0,0,1]
	s_nop 0
	global_store_dwordx4 v11, v[148:151], s[14:15]
	ds_read_b32 v132, v8
	ds_read_b32 v133, v8 offset:512
	ds_read_b32 v134, v8 offset:1024
	ds_read_b32 v135, v8 offset:1536
	ds_read_b32 v136, v8 offset:2048
	ds_read_b32 v137, v8 offset:2560
	ds_read_b32 v138, v8 offset:3072
	ds_read_b32 v139, v8 offset:3584
	ds_read_b32 v140, v8 offset:4096
	ds_read_b32 v141, v8 offset:4608
	ds_read_b32 v142, v8 offset:5120
	ds_read_b32 v143, v8 offset:5632
	ds_read_b32 v144, v8 offset:6144
	ds_read_b32 v145, v8 offset:6656
	ds_read_b32 v146, v8 offset:7168
	ds_read_b32 v147, v8 offset:7680
	s_waitcnt lgkmcnt(0)
	v_max_f32_e32 v132, v132, v132
	v_max_f32_e32 v133, v133, v133
	v_max_f32_e32 v134, v134, v134
	v_max_f32_e32 v135, v135, v135
	v_max_f32_e32 v136, v136, v136
	v_max_f32_e32 v137, v137, v137
	v_max_f32_e32 v138, v138, v138
	v_max_f32_e32 v139, v139, v139
	v_max_f32_e32 v140, v140, v140
	v_max_f32_e32 v141, v141, v141
	v_max_f32_e32 v142, v142, v142
	v_max_f32_e32 v143, v143, v143
	v_max_f32_e32 v144, v144, v144
	v_max_f32_e32 v145, v145, v145
	v_max_f32_e32 v146, v146, v146
	v_max_f32_e32 v147, v147, v147
	v_med3_f32 v132, v132, s20, v13
	v_med3_f32 v133, v133, s20, v13
	v_med3_f32 v134, v134, s20, v13
	v_med3_f32 v135, v135, s20, v13
	v_med3_f32 v136, v136, s20, v13
	v_med3_f32 v137, v137, s20, v13
	v_med3_f32 v138, v138, s20, v13
	v_med3_f32 v139, v139, s20, v13
	v_med3_f32 v140, v140, s20, v13
	v_med3_f32 v141, v141, s20, v13
	v_med3_f32 v142, v142, s20, v13
	v_med3_f32 v143, v143, s20, v13
	v_med3_f32 v144, v144, s20, v13
	v_med3_f32 v145, v145, s20, v13
	v_med3_f32 v146, v146, s20, v13
	v_med3_f32 v147, v147, s20, v13
	v_mov_b32_e32 v148, 0
	v_mov_b32_e32 v149, 0
	v_mov_b32_e32 v150, 0
	v_mov_b32_e32 v151, 0
	v_cvt_pk_fp8_f32 v148, v132, v133
	v_cvt_pk_fp8_f32 v149, v136, v137
	v_cvt_pk_fp8_f32 v150, v140, v141
	v_cvt_pk_fp8_f32 v151, v144, v145
	v_cvt_pk_fp8_f32 v148, v134, v135 op_sel:[0,0,1]
	v_cvt_pk_fp8_f32 v149, v138, v139 op_sel:[0,0,1]
	v_cvt_pk_fp8_f32 v150, v142, v143 op_sel:[0,0,1]
	v_cvt_pk_fp8_f32 v151, v146, v147 op_sel:[0,0,1]
	s_nop 0
	global_store_dwordx4 v12, v[148:151], s[14:15]
	s_waitcnt vmcnt(22)
	v_mul_f32_e32 v36, 0x43000000, v36
	v_mul_f32_e32 v37, 0x43000000, v37
	v_mul_f32_e32 v38, 0x43000000, v38
	v_mul_f32_e32 v39, 0x43000000, v39
	ds_write_b128 v5, v[36:39]
	v_mul_f32_e32 v40, 0x43000000, v40
	v_mul_f32_e32 v41, 0x43000000, v41
	v_mul_f32_e32 v42, 0x43000000, v42
	v_mul_f32_e32 v43, 0x43000000, v43
	ds_write_b128 v5, v[40:43] offset:1024
	v_mul_f32_e32 v44, 0x43000000, v44
	v_mul_f32_e32 v45, 0x43000000, v45
	v_mul_f32_e32 v46, 0x43000000, v46
	v_mul_f32_e32 v47, 0x43000000, v47
	ds_write_b128 v5, v[44:47] offset:2048
	v_mul_f32_e32 v48, 0x43000000, v48
	v_mul_f32_e32 v49, 0x43000000, v49
	v_mul_f32_e32 v50, 0x43000000, v50
	v_mul_f32_e32 v51, 0x43000000, v51
	ds_write_b128 v5, v[48:51] offset:3072
	v_mul_f32_e32 v52, 0x43000000, v52
	v_mul_f32_e32 v53, 0x43000000, v53
	v_mul_f32_e32 v54, 0x43000000, v54
	v_mul_f32_e32 v55, 0x43000000, v55
	ds_write_b128 v5, v[52:55] offset:4096
	v_mul_f32_e32 v56, 0x43000000, v56
	v_mul_f32_e32 v57, 0x43000000, v57
	v_mul_f32_e32 v58, 0x43000000, v58
	v_mul_f32_e32 v59, 0x43000000, v59
	ds_write_b128 v5, v[56:59] offset:5120
	v_mul_f32_e32 v60, 0x43000000, v60
	v_mul_f32_e32 v61, 0x43000000, v61
	v_mul_f32_e32 v62, 0x43000000, v62
	v_mul_f32_e32 v63, 0x43000000, v63
	ds_write_b128 v5, v[60:63] offset:6144
	v_mul_f32_e32 v64, 0x43000000, v64
	v_mul_f32_e32 v65, 0x43000000, v65
	v_mul_f32_e32 v66, 0x43000000, v66
	v_mul_f32_e32 v67, 0x43000000, v67
	ds_write_b128 v5, v[64:67] offset:7168
	s_waitcnt lgkmcnt(0)
	s_barrier
; #define GAS __attribute__((address_space(1)))
; #define LAS __attribute__((address_space(3)))
; #define LDS_WAIT() asm volatile("s_waitcnt lgkmcnt(0)" ::: "memory")
; __device__ __forceinline__ unsigned pk4_fp8(float a, float b, float c, float d) {
;     a = fminf(fmaxf(a, -448.f), 448.f); b = fminf(fmaxf(b, -448.f), 448.f); c = fminf(fmaxf(c, -448.f), 448.f); d = fminf(fmaxf(d, -448.f), 448.f);
;     int w = __builtin_amdgcn_cvt_pk_fp8_f32(a, b, 0, false); w = __builtin_amdgcn_cvt_pk_fp8_f32(c, d, w, true); return (unsigned)w; }
;     const int pr = item >> 1, kb = 2 * (pr / nblk) + (item & 1), nb = pr % nblk, k0 = 64 * kb, n0 = 32 * nb;
;     const int nr = n0 + (lane & 31); const int sc = MAP == 1 ? src_col_in(nr) : nr;
;     float v[32];
; #pragma unroll
;     for (int i = 0; i < 32; ++i) v[i] = sc >= 0 ? W[(size_t)(k0 + 2 * i + (lane >> 5)) * Nsrc + sc] : 0.f;
; #pragma unroll
;     for (int i = 0; i < 32; ++i) { const int k = k0 + 2 * i + (lane >> 5); float x = v[i] * wscale; if (KS) x *= (k < ksplit ? ksA[k] : ksB[k - ksplit]); scr[(2 * i + (lane >> 5)) * 33 + (lane & 31)] = x; }
;     LDS_WAIT(); asm volatile("" ::: "memory");
;     const int c = lane & 7;
; #pragma unroll
;     for (int j = 0; j < 4; ++j) { const int n = (lane >> 3) + 8 * j; const LAS float* s = scr + (8 * c) * 33 + n;
;         const unsigned long long o = (unsigned long long)pg8::pk4_fp8(s[0 * 33], s[1 * 33], s[2 * 33], s[3 * 33]) | ((unsigned long long)pg8::pk4_fp8(s[4 * 33], s[5 * 33], s[6 * 33], s[7 * 33]) << 32);
;         *(GAS unsigned long long*)(WT + (size_t)(n0 + n) * K + k0 + 8 * c) = o; }
;     LDS_WAIT(); asm volatile("" ::: "memory");
	s_add_i32 s17, s16, 576
	s_min_u32 s17, s17, 0xfff
	s_lshr_b32 s18, s17, 5
	s_add_i32 s18, s18, 0
	s_and_b32 s19, s17, 31
	s_lshl_b32 s18, s18, 21
	s_lshl_b32 s19, s19, 9
	s_add_u32 s18, s18, s19
	s_add_u32 s12, s2, s18
	s_addc_u32 s13, s3, 0
	global_load_dwordx4 v[36:39], v10, s[12:13]
	s_add_u32 s12, s12, 0x8000
	s_addc_u32 s13, s13, 0
	global_load_dwordx4 v[40:43], v10, s[12:13]
	s_add_u32 s12, s12, 0x8000
	s_addc_u32 s13, s13, 0
	global_load_dwordx4 v[44:47], v10, s[12:13]
	s_add_u32 s12, s12, 0x8000
	s_addc_u32 s13, s13, 0
	global_load_dwordx4 v[48:51], v10, s[12:13]
	s_add_u32 s12, s12, 0x8000
	s_addc_u32 s13, s13, 0
	global_load_dwordx4 v[52:55], v10, s[12:13]
	s_add_u32 s12, s12, 0x8000
	s_addc_u32 s13, s13, 0
	global_load_dwordx4 v[56:59], v10, s[12:13]
	s_add_u32 s12, s12, 0x8000
	s_addc_u32 s13, s13, 0
	global_load_dwordx4 v[60:63], v10, s[12:13]
	s_add_u32 s12, s12, 0x8000
	s_addc_u32 s13, s13, 0
	global_load_dwordx4 v[64:67], v10, s[12:13]
	s_add_i32 s17, s16, 288
	s_min_u32 s17, s17, 0xfff
	s_lshr_b32 s18, s17, 5
	s_add_i32 s18, s18, 0
	s_and_b32 s19, s17, 31
	s_lshl_b32 s19, s19, 21
	s_lshl_b32 s18, s18, 7
	s_add_u32 s18, s18, s19
	s_add_u32 s14, s4, s18
	s_addc_u32 s15, s5, 0
	ds_read_b32 v132, v7
	ds_read_b32 v133, v7 offset:512
	ds_read_b32 v134, v7 offset:1024
	ds_read_b32 v135, v7 offset:1536
	ds_read_b32 v136, v7 offset:2048
	ds_read_b32 v137, v7 offset:2560
	ds_read_b32 v138, v7 offset:3072
	ds_read_b32 v139, v7 offset:3584
	ds_read_b32 v140, v7 offset:4096
	ds_read_b32 v141, v7 offset:4608
	ds_read_b32 v142, v7 offset:5120
	ds_read_b32 v143, v7 offset:5632
	ds_read_b32 v144, v7 offset:6144
	ds_read_b32 v145, v7 offset:6656
	ds_read_b32 v146, v7 offset:7168
	ds_read_b32 v147, v7 offset:7680
	s_waitcnt lgkmcnt(0)
	v_max_f32_e32 v132, v132, v132
	v_max_f32_e32 v133, v133, v133
	v_max_f32_e32 v134, v134, v134
	v_max_f32_e32 v135, v135, v135
	v_max_f32_e32 v136, v136, v136
	v_max_f32_e32 v137, v137, v137
	v_max_f32_e32 v138, v138, v138
	v_max_f32_e32 v139, v139, v139
	v_max_f32_e32 v140, v140, v140
	v_max_f32_e32 v141, v141, v141
	v_max_f32_e32 v142, v142, v142
	v_max_f32_e32 v143, v143, v143
	v_max_f32_e32 v144, v144, v144
	v_max_f32_e32 v145, v145, v145
	v_max_f32_e32 v146, v146, v146
	v_max_f32_e32 v147, v147, v147
	v_med3_f32 v132, v132, s20, v13
	v_med3_f32 v133, v133, s20, v13
	v_med3_f32 v134, v134, s20, v13
	v_med3_f32 v135, v135, s20, v13
	v_med3_f32 v136, v136, s20, v13
	v_med3_f32 v137, v137, s20, v13
	v_med3_f32 v138, v138, s20, v13
	v_med3_f32 v139, v139, s20, v13
	v_med3_f32 v140, v140, s20, v13
	v_med3_f32 v141, v141, s20, v13
	v_med3_f32 v142, v142, s20, v13
	v_med3_f32 v143, v143, s20, v13
	v_med3_f32 v144, v144, s20, v13
	v_med3_f32 v145, v145, s20, v13
	v_med3_f32 v146, v146, s20, v13
	v_med3_f32 v147, v147, s20, v13
	v_mov_b32_e32 v148, 0
	v_mov_b32_e32 v149, 0
	v_mov_b32_e32 v150, 0
	v_mov_b32_e32 v151, 0
	v_cvt_pk_fp8_f32 v148, v132, v133
	v_cvt_pk_fp8_f32 v149, v136, v137
	v_cvt_pk_fp8_f32 v150, v140, v141
	v_cvt_pk_fp8_f32 v151, v144, v145
	v_cvt_pk_fp8_f32 v148, v134, v135 op_sel:[0,0,1]
	v_cvt_pk_fp8_f32 v149, v138, v139 op_sel:[0,0,1]
	v_cvt_pk_fp8_f32 v150, v142, v143 op_sel:[0,0,1]
	v_cvt_pk_fp8_f32 v151, v146, v147 op_sel:[0,0,1]
	s_nop 0
	global_store_dwordx4 v11, v[148:151], s[14:15]
	ds_read_b32 v132, v9
	ds_read_b32 v133, v9 offset:512
	ds_read_b32 v134, v9 offset:1024
	ds_read_b32 v135, v9 offset:1536
	ds_read_b32 v136, v9 offset:2048
	ds_read_b32 v137, v9 offset:2560
	ds_read_b32 v138, v9 offset:3072
	ds_read_b32 v139, v9 offset:3584
	ds_read_b32 v140, v9 offset:4096
	ds_read_b32 v141, v9 offset:4608
	ds_read_b32 v142, v9 offset:5120
	ds_read_b32 v143, v9 offset:5632
	ds_read_b32 v144, v9 offset:6144
	ds_read_b32 v145, v9 offset:6656
	ds_read_b32 v146, v9 offset:7168
	ds_read_b32 v147, v9 offset:7680
	s_waitcnt lgkmcnt(0)
	v_max_f32_e32 v132, v132, v132
	v_max_f32_e32 v133, v133, v133
	v_max_f32_e32 v134, v134, v134
	v_max_f32_e32 v135, v135, v135
	v_max_f32_e32 v136, v136, v136
	v_max_f32_e32 v137, v137, v137
	v_max_f32_e32 v138, v138, v138
	v_max_f32_e32 v139, v139, v139
	v_max_f32_e32 v140, v140, v140
	v_max_f32_e32 v141, v141, v141
	v_max_f32_e32 v142, v142, v142
	v_max_f32_e32 v143, v143, v143
	v_max_f32_e32 v144, v144, v144
	v_max_f32_e32 v145, v145, v145
	v_max_f32_e32 v146, v146, v146
	v_max_f32_e32 v147, v147, v147
	v_med3_f32 v132, v132, s20, v13
	v_med3_f32 v133, v133, s20, v13
	v_med3_f32 v134, v134, s20, v13
	v_med3_f32 v135, v135, s20, v13
	v_med3_f32 v136, v136, s20, v13
	v_med3_f32 v137, v137, s20, v13
	v_med3_f32 v138, v138, s20, v13
	v_med3_f32 v139, v139, s20, v13
	v_med3_f32 v140, v140, s20, v13
	v_med3_f32 v141, v141, s20, v13
	v_med3_f32 v142, v142, s20, v13
	v_med3_f32 v143, v143, s20, v13
	v_med3_f32 v144, v144, s20, v13
	v_med3_f32 v145, v145, s20, v13
	v_med3_f32 v146, v146, s20, v13
	v_med3_f32 v147, v147, s20, v13
	v_mov_b32_e32 v148, 0
	v_mov_b32_e32 v149, 0
	v_mov_b32_e32 v150, 0
	v_mov_b32_e32 v151, 0
	v_cvt_pk_fp8_f32 v148, v132, v133
	v_cvt_pk_fp8_f32 v149, v136, v137
	v_cvt_pk_fp8_f32 v150, v140, v141
	v_cvt_pk_fp8_f32 v151, v144, v145
	v_cvt_pk_fp8_f32 v148, v134, v135 op_sel:[0,0,1]
	v_cvt_pk_fp8_f32 v149, v138, v139 op_sel:[0,0,1]
	v_cvt_pk_fp8_f32 v150, v142, v143 op_sel:[0,0,1]
	v_cvt_pk_fp8_f32 v151, v146, v147 op_sel:[0,0,1]
	s_nop 0
	global_store_dwordx4 v12, v[148:151], s[14:15]
	s_waitcnt vmcnt(22)
	v_mul_f32_e32 v68, 0x43000000, v68
	v_mul_f32_e32 v69, 0x43000000, v69
	v_mul_f32_e32 v70, 0x43000000, v70
	v_mul_f32_e32 v71, 0x43000000, v71
	ds_write_b128 v4, v[68:71]
	v_mul_f32_e32 v72, 0x43000000, v72
	v_mul_f32_e32 v73, 0x43000000, v73
	v_mul_f32_e32 v74, 0x43000000, v74
	v_mul_f32_e32 v75, 0x43000000, v75
	ds_write_b128 v4, v[72:75] offset:1024
	v_mul_f32_e32 v76, 0x43000000, v76
	v_mul_f32_e32 v77, 0x43000000, v77
	v_mul_f32_e32 v78, 0x43000000, v78
	v_mul_f32_e32 v79, 0x43000000, v79
	ds_write_b128 v4, v[76:79] offset:2048
	v_mul_f32_e32 v80, 0x43000000, v80
	v_mul_f32_e32 v81, 0x43000000, v81
	v_mul_f32_e32 v82, 0x43000000, v82
	v_mul_f32_e32 v83, 0x43000000, v83
	ds_write_b128 v4, v[80:83] offset:3072
	v_mul_f32_e32 v84, 0x43000000, v84
	v_mul_f32_e32 v85, 0x43000000, v85
	v_mul_f32_e32 v86, 0x43000000, v86
	v_mul_f32_e32 v87, 0x43000000, v87
	ds_write_b128 v4, v[84:87] offset:4096
	v_mul_f32_e32 v88, 0x43000000, v88
	v_mul_f32_e32 v89, 0x43000000, v89
	v_mul_f32_e32 v90, 0x43000000, v90
	v_mul_f32_e32 v91, 0x43000000, v91
	ds_write_b128 v4, v[88:91] offset:5120
	v_mul_f32_e32 v92, 0x43000000, v92
	v_mul_f32_e32 v93, 0x43000000, v93
	v_mul_f32_e32 v94, 0x43000000, v94
	v_mul_f32_e32 v95, 0x43000000, v95
	ds_write_b128 v4, v[92:95] offset:6144
	v_mul_f32_e32 v96, 0x43000000, v96
	v_mul_f32_e32 v97, 0x43000000, v97
	v_mul_f32_e32 v98, 0x43000000, v98
	v_mul_f32_e32 v99, 0x43000000, v99
	ds_write_b128 v4, v[96:99] offset:7168
	s_waitcnt lgkmcnt(0)
	s_barrier
; #define GAS __attribute__((address_space(1)))
; #define LAS __attribute__((address_space(3)))
; #define LDS_WAIT() asm volatile("s_waitcnt lgkmcnt(0)" ::: "memory")
; __device__ __forceinline__ unsigned pk4_fp8(float a, float b, float c, float d) {
;     a = fminf(fmaxf(a, -448.f), 448.f); b = fminf(fmaxf(b, -448.f), 448.f); c = fminf(fmaxf(c, -448.f), 448.f); d = fminf(fmaxf(d, -448.f), 448.f);
;     int w = __builtin_amdgcn_cvt_pk_fp8_f32(a, b, 0, false); w = __builtin_amdgcn_cvt_pk_fp8_f32(c, d, w, true); return (unsigned)w; }
;     const int pr = item >> 1, kb = 2 * (pr / nblk) + (item & 1), nb = pr % nblk, k0 = 64 * kb, n0 = 32 * nb;
;     const int nr = n0 + (lane & 31); const int sc = MAP == 1 ? src_col_in(nr) : nr;
;     float v[32];
; #pragma unroll
;     for (int i = 0; i < 32; ++i) v[i] = sc >= 0 ? W[(size_t)(k0 + 2 * i + (lane >> 5)) * Nsrc + sc] : 0.f;
; #pragma unroll
;     for (int i = 0; i < 32; ++i) { const int k = k0 + 2 * i + (lane >> 5); float x = v[i] * wscale; if (KS) x *= (k < ksplit ? ksA[k] : ksB[k - ksplit]); scr[(2 * i + (lane >> 5)) * 33 + (lane & 31)] = x; }
;     LDS_WAIT(); asm volatile("" ::: "memory");
;     const int c = lane & 7;
; #pragma unroll
;     for (int j = 0; j < 4; ++j) { const int n = (lane >> 3) + 8 * j; const LAS float* s = scr + (8 * c) * 33 + n;
;         const unsigned long long o = (unsigned long long)pg8::pk4_fp8(s[0 * 33], s[1 * 33], s[2 * 33], s[3 * 33]) | ((unsigned long long)pg8::pk4_fp8(s[4 * 33], s[5 * 33], s[6 * 33], s[7 * 33]) << 32);
;         *(GAS unsigned long long*)(WT + (size_t)(n0 + n) * K + k0 + 8 * c) = o; }
;     LDS_WAIT(); asm volatile("" ::: "memory");
	s_add_i32 s17, s16, 672
	s_min_u32 s17, s17, 0xfff
	s_lshr_b32 s18, s17, 5
	s_add_i32 s18, s18, 0
	s_and_b32 s19, s17, 31
	s_lshl_b32 s18, s18, 21
	s_lshl_b32 s19, s19, 9
	s_add_u32 s18, s18, s19
	s_add_u32 s12, s2, s18
	s_addc_u32 s13, s3, 0
	global_load_dwordx4 v[68:71], v10, s[12:13]
	s_add_u32 s12, s12, 0x8000
	s_addc_u32 s13, s13, 0
	global_load_dwordx4 v[72:75], v10, s[12:13]
	s_add_u32 s12, s12, 0x8000
	s_addc_u32 s13, s13, 0
	global_load_dwordx4 v[76:79], v10, s[12:13]
	s_add_u32 s12, s12, 0x8000
	s_addc_u32 s13, s13, 0
	global_load_dwordx4 v[80:83], v10, s[12:13]
	s_add_u32 s12, s12, 0x8000
	s_addc_u32 s13, s13, 0
	global_load_dwordx4 v[84:87], v10, s[12:13]
	s_add_u32 s12, s12, 0x8000
	s_addc_u32 s13, s13, 0
	global_load_dwordx4 v[88:91], v10, s[12:13]
	s_add_u32 s12, s12, 0x8000
	s_addc_u32 s13, s13, 0
	global_load_dwordx4 v[92:95], v10, s[12:13]
	s_add_u32 s12, s12, 0x8000
	s_addc_u32 s13, s13, 0
	global_load_dwordx4 v[96:99], v10, s[12:13]
	s_add_i32 s17, s16, 384
	s_min_u32 s17, s17, 0xfff
	s_lshr_b32 s18, s17, 5
	s_add_i32 s18, s18, 0
	s_and_b32 s19, s17, 31
	s_lshl_b32 s19, s19, 21
	s_lshl_b32 s18, s18, 7
	s_add_u32 s18, s18, s19
	s_add_u32 s14, s4, s18
	s_addc_u32 s15, s5, 0
	ds_read_b32 v132, v6
	ds_read_b32 v133, v6 offset:512
	ds_read_b32 v134, v6 offset:1024
	ds_read_b32 v135, v6 offset:1536
	ds_read_b32 v136, v6 offset:2048
	ds_read_b32 v137, v6 offset:2560
	ds_read_b32 v138, v6 offset:3072
	ds_read_b32 v139, v6 offset:3584
	ds_read_b32 v140, v6 offset:4096
	ds_read_b32 v141, v6 offset:4608
	ds_read_b32 v142, v6 offset:5120
	ds_read_b32 v143, v6 offset:5632
	ds_read_b32 v144, v6 offset:6144
	ds_read_b32 v145, v6 offset:6656
	ds_read_b32 v146, v6 offset:7168
	ds_read_b32 v147, v6 offset:7680
	s_waitcnt lgkmcnt(0)
	v_max_f32_e32 v132, v132, v132
	v_max_f32_e32 v133, v133, v133
	v_max_f32_e32 v134, v134, v134
	v_max_f32_e32 v135, v135, v135
	v_max_f32_e32 v136, v136, v136
	v_max_f32_e32 v137, v137, v137
	v_max_f32_e32 v138, v138, v138
	v_max_f32_e32 v139, v139, v139
	v_max_f32_e32 v140, v140, v140
	v_max_f32_e32 v141, v141, v141
	v_max_f32_e32 v142, v142, v142
	v_max_f32_e32 v143, v143, v143
	v_max_f32_e32 v144, v144, v144
	v_max_f32_e32 v145, v145, v145
	v_max_f32_e32 v146, v146, v146
	v_max_f32_e32 v147, v147, v147
	v_med3_f32 v132, v132, s20, v13
	v_med3_f32 v133, v133, s20, v13
	v_med3_f32 v134, v134, s20, v13
	v_med3_f32 v135, v135, s20, v13
	v_med3_f32 v136, v136, s20, v13
	v_med3_f32 v137, v137, s20, v13
	v_med3_f32 v138, v138, s20, v13
	v_med3_f32 v139, v139, s20, v13
	v_med3_f32 v140, v140, s20, v13
	v_med3_f32 v141, v141, s20, v13
	v_med3_f32 v142, v142, s20, v13
	v_med3_f32 v143, v143, s20, v13
	v_med3_f32 v144, v144, s20, v13
	v_med3_f32 v145, v145, s20, v13
	v_med3_f32 v146, v146, s20, v13
	v_med3_f32 v147, v147, s20, v13
	v_mov_b32_e32 v148, 0
	v_mov_b32_e32 v149, 0
	v_mov_b32_e32 v150, 0
	v_mov_b32_e32 v151, 0
	v_cvt_pk_fp8_f32 v148, v132, v133
	v_cvt_pk_fp8_f32 v149, v136, v137
	v_cvt_pk_fp8_f32 v150, v140, v141
	v_cvt_pk_fp8_f32 v151, v144, v145
	v_cvt_pk_fp8_f32 v148, v134, v135 op_sel:[0,0,1]
	v_cvt_pk_fp8_f32 v149, v138, v139 op_sel:[0,0,1]
	v_cvt_pk_fp8_f32 v150, v142, v143 op_sel:[0,0,1]
	v_cvt_pk_fp8_f32 v151, v146, v147 op_sel:[0,0,1]
	s_nop 0
	global_store_dwordx4 v11, v[148:151], s[14:15]
	ds_read_b32 v132, v8
	ds_read_b32 v133, v8 offset:512
	ds_read_b32 v134, v8 offset:1024
	ds_read_b32 v135, v8 offset:1536
	ds_read_b32 v136, v8 offset:2048
	ds_read_b32 v137, v8 offset:2560
	ds_read_b32 v138, v8 offset:3072
	ds_read_b32 v139, v8 offset:3584
	ds_read_b32 v140, v8 offset:4096
	ds_read_b32 v141, v8 offset:4608
	ds_read_b32 v142, v8 offset:5120
	ds_read_b32 v143, v8 offset:5632
	ds_read_b32 v144, v8 offset:6144
	ds_read_b32 v145, v8 offset:6656
	ds_read_b32 v146, v8 offset:7168
	ds_read_b32 v147, v8 offset:7680
	s_waitcnt lgkmcnt(0)
	v_max_f32_e32 v132, v132, v132
	v_max_f32_e32 v133, v133, v133
	v_max_f32_e32 v134, v134, v134
	v_max_f32_e32 v135, v135, v135
	v_max_f32_e32 v136, v136, v136
	v_max_f32_e32 v137, v137, v137
	v_max_f32_e32 v138, v138, v138
	v_max_f32_e32 v139, v139, v139
	v_max_f32_e32 v140, v140, v140
	v_max_f32_e32 v141, v141, v141
	v_max_f32_e32 v142, v142, v142
	v_max_f32_e32 v143, v143, v143
	v_max_f32_e32 v144, v144, v144
	v_max_f32_e32 v145, v145, v145
	v_max_f32_e32 v146, v146, v146
	v_max_f32_e32 v147, v147, v147
	v_med3_f32 v132, v132, s20, v13
	v_med3_f32 v133, v133, s20, v13
	v_med3_f32 v134, v134, s20, v13
	v_med3_f32 v135, v135, s20, v13
	v_med3_f32 v136, v136, s20, v13
	v_med3_f32 v137, v137, s20, v13
	v_med3_f32 v138, v138, s20, v13
	v_med3_f32 v139, v139, s20, v13
	v_med3_f32 v140, v140, s20, v13
	v_med3_f32 v141, v141, s20, v13
	v_med3_f32 v142, v142, s20, v13
	v_med3_f32 v143, v143, s20, v13
	v_med3_f32 v144, v144, s20, v13
	v_med3_f32 v145, v145, s20, v13
	v_med3_f32 v146, v146, s20, v13
	v_med3_f32 v147, v147, s20, v13
	v_mov_b32_e32 v148, 0
	v_mov_b32_e32 v149, 0
	v_mov_b32_e32 v150, 0
	v_mov_b32_e32 v151, 0
	v_cvt_pk_fp8_f32 v148, v132, v133
	v_cvt_pk_fp8_f32 v149, v136, v137
	v_cvt_pk_fp8_f32 v150, v140, v141
	v_cvt_pk_fp8_f32 v151, v144, v145
	v_cvt_pk_fp8_f32 v148, v134, v135 op_sel:[0,0,1]
	v_cvt_pk_fp8_f32 v149, v138, v139 op_sel:[0,0,1]
	v_cvt_pk_fp8_f32 v150, v142, v143 op_sel:[0,0,1]
	v_cvt_pk_fp8_f32 v151, v146, v147 op_sel:[0,0,1]
	s_nop 0
	global_store_dwordx4 v12, v[148:151], s[14:15]
	s_waitcnt vmcnt(22)
	v_mul_f32_e32 v100, 0x43000000, v100
	v_mul_f32_e32 v101, 0x43000000, v101
	v_mul_f32_e32 v102, 0x43000000, v102
	v_mul_f32_e32 v103, 0x43000000, v103
	ds_write_b128 v5, v[100:103]
	v_mul_f32_e32 v104, 0x43000000, v104
	v_mul_f32_e32 v105, 0x43000000, v105
	v_mul_f32_e32 v106, 0x43000000, v106
	v_mul_f32_e32 v107, 0x43000000, v107
	ds_write_b128 v5, v[104:107] offset:1024
	v_mul_f32_e32 v108, 0x43000000, v108
	v_mul_f32_e32 v109, 0x43000000, v109
	v_mul_f32_e32 v110, 0x43000000, v110
	v_mul_f32_e32 v111, 0x43000000, v111
	ds_write_b128 v5, v[108:111] offset:2048
	v_mul_f32_e32 v112, 0x43000000, v112
	v_mul_f32_e32 v113, 0x43000000, v113
	v_mul_f32_e32 v114, 0x43000000, v114
	v_mul_f32_e32 v115, 0x43000000, v115
	ds_write_b128 v5, v[112:115] offset:3072
	v_mul_f32_e32 v116, 0x43000000, v116
	v_mul_f32_e32 v117, 0x43000000, v117
	v_mul_f32_e32 v118, 0x43000000, v118
	v_mul_f32_e32 v119, 0x43000000, v119
	ds_write_b128 v5, v[116:119] offset:4096
	v_mul_f32_e32 v120, 0x43000000, v120
	v_mul_f32_e32 v121, 0x43000000, v121
	v_mul_f32_e32 v122, 0x43000000, v122
	v_mul_f32_e32 v123, 0x43000000, v123
	ds_write_b128 v5, v[120:123] offset:5120
	v_mul_f32_e32 v124, 0x43000000, v124
	v_mul_f32_e32 v125, 0x43000000, v125
	v_mul_f32_e32 v126, 0x43000000, v126
	v_mul_f32_e32 v127, 0x43000000, v127
	ds_write_b128 v5, v[124:127] offset:6144
	v_mul_f32_e32 v128, 0x43000000, v128
	v_mul_f32_e32 v129, 0x43000000, v129
	v_mul_f32_e32 v130, 0x43000000, v130
	v_mul_f32_e32 v131, 0x43000000, v131
	ds_write_b128 v5, v[128:131] offset:7168
	s_waitcnt lgkmcnt(0)
	s_barrier
; #define GAS __attribute__((address_space(1)))
; #define LAS __attribute__((address_space(3)))
; #define LDS_WAIT() asm volatile("s_waitcnt lgkmcnt(0)" ::: "memory")
; __device__ __forceinline__ unsigned pk4_fp8(float a, float b, float c, float d) {
;     a = fminf(fmaxf(a, -448.f), 448.f); b = fminf(fmaxf(b, -448.f), 448.f); c = fminf(fmaxf(c, -448.f), 448.f); d = fminf(fmaxf(d, -448.f), 448.f);
;     int w = __builtin_amdgcn_cvt_pk_fp8_f32(a, b, 0, false); w = __builtin_amdgcn_cvt_pk_fp8_f32(c, d, w, true); return (unsigned)w; }
;     const int pr = item >> 1, kb = 2 * (pr / nblk) + (item & 1), nb = pr % nblk, k0 = 64 * kb, n0 = 32 * nb;
;     const int nr = n0 + (lane & 31); const int sc = MAP == 1 ? src_col_in(nr) : nr;
;     float v[32];
; #pragma unroll
;     for (int i = 0; i < 32; ++i) v[i] = sc >= 0 ? W[(size_t)(k0 + 2 * i + (lane >> 5)) * Nsrc + sc] : 0.f;
; #pragma unroll
;     for (int i = 0; i < 32; ++i) { const int k = k0 + 2 * i + (lane >> 5); float x = v[i] * wscale; if (KS) x *= (k < ksplit ? ksA[k] : ksB[k - ksplit]); scr[(2 * i + (lane >> 5)) * 33 + (lane & 31)] = x; }
;     LDS_WAIT(); asm volatile("" ::: "memory");
;     const int c = lane & 7;
; #pragma unroll
;     for (int j = 0; j < 4; ++j) { const int n = (lane >> 3) + 8 * j; const LAS float* s = scr + (8 * c) * 33 + n;
;         const unsigned long long o = (unsigned long long)pg8::pk4_fp8(s[0 * 33], s[1 * 33], s[2 * 33], s[3 * 33]) | ((unsigned long long)pg8::pk4_fp8(s[4 * 33], s[5 * 33], s[6 * 33], s[7 * 33]) << 32);
;         *(GAS unsigned long long*)(WT + (size_t)(n0 + n) * K + k0 + 8 * c) = o; }
;     LDS_WAIT(); asm volatile("" ::: "memory");
	s_add_i32 s17, s16, 768
	s_min_u32 s17, s17, 0xfff
	s_lshr_b32 s18, s17, 5
	s_add_i32 s18, s18, 0
	s_and_b32 s19, s17, 31
	s_lshl_b32 s18, s18, 21
	s_lshl_b32 s19, s19, 9
	s_add_u32 s18, s18, s19
	s_add_u32 s12, s2, s18
	s_addc_u32 s13, s3, 0
	global_load_dwordx4 v[100:103], v10, s[12:13]
	s_add_u32 s12, s12, 0x8000
	s_addc_u32 s13, s13, 0
	global_load_dwordx4 v[104:107], v10, s[12:13]
	s_add_u32 s12, s12, 0x8000
	s_addc_u32 s13, s13, 0
	global_load_dwordx4 v[108:111], v10, s[12:13]
	s_add_u32 s12, s12, 0x8000
	s_addc_u32 s13, s13, 0
	global_load_dwordx4 v[112:115], v10, s[12:13]
	s_add_u32 s12, s12, 0x8000
	s_addc_u32 s13, s13, 0
	global_load_dwordx4 v[116:119], v10, s[12:13]
	s_add_u32 s12, s12, 0x8000
	s_addc_u32 s13, s13, 0
	global_load_dwordx4 v[120:123], v10, s[12:13]
	s_add_u32 s12, s12, 0x8000
	s_addc_u32 s13, s13, 0
	global_load_dwordx4 v[124:127], v10, s[12:13]
	s_add_u32 s12, s12, 0x8000
	s_addc_u32 s13, s13, 0
	global_load_dwordx4 v[128:131], v10, s[12:13]
	s_add_i32 s17, s16, 480
	s_min_u32 s17, s17, 0xfff
	s_lshr_b32 s18, s17, 5
	s_add_i32 s18, s18, 0
	s_and_b32 s19, s17, 31
	s_lshl_b32 s19, s19, 21
	s_lshl_b32 s18, s18, 7
	s_add_u32 s18, s18, s19
	s_add_u32 s14, s4, s18
	s_addc_u32 s15, s5, 0
	ds_read_b32 v132, v7
	ds_read_b32 v133, v7 offset:512
	ds_read_b32 v134, v7 offset:1024
	ds_read_b32 v135, v7 offset:1536
	ds_read_b32 v136, v7 offset:2048
	ds_read_b32 v137, v7 offset:2560
	ds_read_b32 v138, v7 offset:3072
	ds_read_b32 v139, v7 offset:3584
	ds_read_b32 v140, v7 offset:4096
	ds_read_b32 v141, v7 offset:4608
	ds_read_b32 v142, v7 offset:5120
	ds_read_b32 v143, v7 offset:5632
	ds_read_b32 v144, v7 offset:6144
	ds_read_b32 v145, v7 offset:6656
	ds_read_b32 v146, v7 offset:7168
	ds_read_b32 v147, v7 offset:7680
	s_waitcnt lgkmcnt(0)
	v_max_f32_e32 v132, v132, v132
	v_max_f32_e32 v133, v133, v133
	v_max_f32_e32 v134, v134, v134
	v_max_f32_e32 v135, v135, v135
	v_max_f32_e32 v136, v136, v136
	v_max_f32_e32 v137, v137, v137
	v_max_f32_e32 v138, v138, v138
	v_max_f32_e32 v139, v139, v139
	v_max_f32_e32 v140, v140, v140
	v_max_f32_e32 v141, v141, v141
	v_max_f32_e32 v142, v142, v142
	v_max_f32_e32 v143, v143, v143
	v_max_f32_e32 v144, v144, v144
	v_max_f32_e32 v145, v145, v145
	v_max_f32_e32 v146, v146, v146
	v_max_f32_e32 v147, v147, v147
	v_med3_f32 v132, v132, s20, v13
	v_med3_f32 v133, v133, s20, v13
	v_med3_f32 v134, v134, s20, v13
	v_med3_f32 v135, v135, s20, v13
	v_med3_f32 v136, v136, s20, v13
	v_med3_f32 v137, v137, s20, v13
	v_med3_f32 v138, v138, s20, v13
	v_med3_f32 v139, v139, s20, v13
	v_med3_f32 v140, v140, s20, v13
	v_med3_f32 v141, v141, s20, v13
	v_med3_f32 v142, v142, s20, v13
	v_med3_f32 v143, v143, s20, v13
	v_med3_f32 v144, v144, s20, v13
	v_med3_f32 v145, v145, s20, v13
	v_med3_f32 v146, v146, s20, v13
	v_med3_f32 v147, v147, s20, v13
	v_mov_b32_e32 v148, 0
	v_mov_b32_e32 v149, 0
	v_mov_b32_e32 v150, 0
	v_mov_b32_e32 v151, 0
	v_cvt_pk_fp8_f32 v148, v132, v133
	v_cvt_pk_fp8_f32 v149, v136, v137
	v_cvt_pk_fp8_f32 v150, v140, v141
	v_cvt_pk_fp8_f32 v151, v144, v145
	v_cvt_pk_fp8_f32 v148, v134, v135 op_sel:[0,0,1]
	v_cvt_pk_fp8_f32 v149, v138, v139 op_sel:[0,0,1]
	v_cvt_pk_fp8_f32 v150, v142, v143 op_sel:[0,0,1]
	v_cvt_pk_fp8_f32 v151, v146, v147 op_sel:[0,0,1]
	s_nop 0
	global_store_dwordx4 v11, v[148:151], s[14:15]
	ds_read_b32 v132, v9
	ds_read_b32 v133, v9 offset:512
	ds_read_b32 v134, v9 offset:1024
	ds_read_b32 v135, v9 offset:1536
	ds_read_b32 v136, v9 offset:2048
	ds_read_b32 v137, v9 offset:2560
	ds_read_b32 v138, v9 offset:3072
	ds_read_b32 v139, v9 offset:3584
	ds_read_b32 v140, v9 offset:4096
	ds_read_b32 v141, v9 offset:4608
	ds_read_b32 v142, v9 offset:5120
	ds_read_b32 v143, v9 offset:5632
	ds_read_b32 v144, v9 offset:6144
	ds_read_b32 v145, v9 offset:6656
	ds_read_b32 v146, v9 offset:7168
	ds_read_b32 v147, v9 offset:7680
	s_waitcnt lgkmcnt(0)
	v_max_f32_e32 v132, v132, v132
	v_max_f32_e32 v133, v133, v133
	v_max_f32_e32 v134, v134, v134
	v_max_f32_e32 v135, v135, v135
	v_max_f32_e32 v136, v136, v136
	v_max_f32_e32 v137, v137, v137
	v_max_f32_e32 v138, v138, v138
	v_max_f32_e32 v139, v139, v139
	v_max_f32_e32 v140, v140, v140
	v_max_f32_e32 v141, v141, v141
	v_max_f32_e32 v142, v142, v142
	v_max_f32_e32 v143, v143, v143
	v_max_f32_e32 v144, v144, v144
	v_max_f32_e32 v145, v145, v145
	v_max_f32_e32 v146, v146, v146
	v_max_f32_e32 v147, v147, v147
	v_med3_f32 v132, v132, s20, v13
	v_med3_f32 v133, v133, s20, v13
	v_med3_f32 v134, v134, s20, v13
	v_med3_f32 v135, v135, s20, v13
	v_med3_f32 v136, v136, s20, v13
	v_med3_f32 v137, v137, s20, v13
	v_med3_f32 v138, v138, s20, v13
	v_med3_f32 v139, v139, s20, v13
	v_med3_f32 v140, v140, s20, v13
	v_med3_f32 v141, v141, s20, v13
	v_med3_f32 v142, v142, s20, v13
	v_med3_f32 v143, v143, s20, v13
	v_med3_f32 v144, v144, s20, v13
	v_med3_f32 v145, v145, s20, v13
	v_med3_f32 v146, v146, s20, v13
	v_med3_f32 v147, v147, s20, v13
	v_mov_b32_e32 v148, 0
	v_mov_b32_e32 v149, 0
	v_mov_b32_e32 v150, 0
	v_mov_b32_e32 v151, 0
	v_cvt_pk_fp8_f32 v148, v132, v133
	v_cvt_pk_fp8_f32 v149, v136, v137
	v_cvt_pk_fp8_f32 v150, v140, v141
	v_cvt_pk_fp8_f32 v151, v144, v145
	v_cvt_pk_fp8_f32 v148, v134, v135 op_sel:[0,0,1]
	v_cvt_pk_fp8_f32 v149, v138, v139 op_sel:[0,0,1]
	v_cvt_pk_fp8_f32 v150, v142, v143 op_sel:[0,0,1]
	v_cvt_pk_fp8_f32 v151, v146, v147 op_sel:[0,0,1]
	s_nop 0
	global_store_dwordx4 v12, v[148:151], s[14:15]
	s_waitcnt vmcnt(22)
	v_mul_f32_e32 v36, 0x43000000, v36
	v_mul_f32_e32 v37, 0x43000000, v37
	v_mul_f32_e32 v38, 0x43000000, v38
	v_mul_f32_e32 v39, 0x43000000, v39
	ds_write_b128 v4, v[36:39]
	v_mul_f32_e32 v40, 0x43000000, v40
	v_mul_f32_e32 v41, 0x43000000, v41
	v_mul_f32_e32 v42, 0x43000000, v42
	v_mul_f32_e32 v43, 0x43000000, v43
	ds_write_b128 v4, v[40:43] offset:1024
	v_mul_f32_e32 v44, 0x43000000, v44
	v_mul_f32_e32 v45, 0x43000000, v45
	v_mul_f32_e32 v46, 0x43000000, v46
	v_mul_f32_e32 v47, 0x43000000, v47
	ds_write_b128 v4, v[44:47] offset:2048
	v_mul_f32_e32 v48, 0x43000000, v48
	v_mul_f32_e32 v49, 0x43000000, v49
	v_mul_f32_e32 v50, 0x43000000, v50
	v_mul_f32_e32 v51, 0x43000000, v51
	ds_write_b128 v4, v[48:51] offset:3072
	v_mul_f32_e32 v52, 0x43000000, v52
	v_mul_f32_e32 v53, 0x43000000, v53
	v_mul_f32_e32 v54, 0x43000000, v54
	v_mul_f32_e32 v55, 0x43000000, v55
	ds_write_b128 v4, v[52:55] offset:4096
	v_mul_f32_e32 v56, 0x43000000, v56
	v_mul_f32_e32 v57, 0x43000000, v57
	v_mul_f32_e32 v58, 0x43000000, v58
	v_mul_f32_e32 v59, 0x43000000, v59
	ds_write_b128 v4, v[56:59] offset:5120
	v_mul_f32_e32 v60, 0x43000000, v60
	v_mul_f32_e32 v61, 0x43000000, v61
	v_mul_f32_e32 v62, 0x43000000, v62
	v_mul_f32_e32 v63, 0x43000000, v63
	ds_write_b128 v4, v[60:63] offset:6144
	v_mul_f32_e32 v64, 0x43000000, v64
	v_mul_f32_e32 v65, 0x43000000, v65
	v_mul_f32_e32 v66, 0x43000000, v66
	v_mul_f32_e32 v67, 0x43000000, v67
	ds_write_b128 v4, v[64:67] offset:7168
	s_waitcnt lgkmcnt(0)
	s_barrier
; #define GAS __attribute__((address_space(1)))
; #define LAS __attribute__((address_space(3)))
; #define LDS_WAIT() asm volatile("s_waitcnt lgkmcnt(0)" ::: "memory")
; __device__ __forceinline__ unsigned pk4_fp8(float a, float b, float c, float d) {
;     a = fminf(fmaxf(a, -448.f), 448.f); b = fminf(fmaxf(b, -448.f), 448.f); c = fminf(fmaxf(c, -448.f), 448.f); d = fminf(fmaxf(d, -448.f), 448.f);
;     int w = __builtin_amdgcn_cvt_pk_fp8_f32(a, b, 0, false); w = __builtin_amdgcn_cvt_pk_fp8_f32(c, d, w, true); return (unsigned)w; }
;     const int pr = item >> 1, kb = 2 * (pr / nblk) + (item & 1), nb = pr % nblk, k0 = 64 * kb, n0 = 32 * nb;
;     const int nr = n0 + (lane & 31); const int sc = MAP == 1 ? src_col_in(nr) : nr;
;     float v[32];
; #pragma unroll
;     for (int i = 0; i < 32; ++i) v[i] = sc >= 0 ? W[(size_t)(k0 + 2 * i + (lane >> 5)) * Nsrc + sc] : 0.f;
; #pragma unroll
;     for (int i = 0; i < 32; ++i) { const int k = k0 + 2 * i + (lane >> 5); float x = v[i] * wscale; if (KS) x *= (k < ksplit ? ksA[k] : ksB[k - ksplit]); scr[(2 * i + (lane >> 5)) * 33 + (lane & 31)] = x; }
;     LDS_WAIT(); asm volatile("" ::: "memory");
;     const int c = lane & 7;
; #pragma unroll
;     for (int j = 0; j < 4; ++j) { const int n = (lane >> 3) + 8 * j; const LAS float* s = scr + (8 * c) * 33 + n;
;         const unsigned long long o = (unsigned long long)pg8::pk4_fp8(s[0 * 33], s[1 * 33], s[2 * 33], s[3 * 33]) | ((unsigned long long)pg8::pk4_fp8(s[4 * 33], s[5 * 33], s[6 * 33], s[7 * 33]) << 32);
;         *(GAS unsigned long long*)(WT + (size_t)(n0 + n) * K + k0 + 8 * c) = o; }
;     LDS_WAIT(); asm volatile("" ::: "memory");
	s_add_i32 s17, s16, 864
	s_min_u32 s17, s17, 0xfff
	s_lshr_b32 s18, s17, 5
	s_add_i32 s18, s18, 0
	s_and_b32 s19, s17, 31
	s_lshl_b32 s18, s18, 21
	s_lshl_b32 s19, s19, 9
	s_add_u32 s18, s18, s19
	s_add_u32 s12, s2, s18
	s_addc_u32 s13, s3, 0
	global_load_dwordx4 v[36:39], v10, s[12:13]
	s_add_u32 s12, s12, 0x8000
	s_addc_u32 s13, s13, 0
	global_load_dwordx4 v[40:43], v10, s[12:13]
	s_add_u32 s12, s12, 0x8000
	s_addc_u32 s13, s13, 0
	global_load_dwordx4 v[44:47], v10, s[12:13]
	s_add_u32 s12, s12, 0x8000
	s_addc_u32 s13, s13, 0
	global_load_dwordx4 v[48:51], v10, s[12:13]
	s_add_u32 s12, s12, 0x8000
	s_addc_u32 s13, s13, 0
	global_load_dwordx4 v[52:55], v10, s[12:13]
	s_add_u32 s12, s12, 0x8000
	s_addc_u32 s13, s13, 0
	global_load_dwordx4 v[56:59], v10, s[12:13]
	s_add_u32 s12, s12, 0x8000
	s_addc_u32 s13, s13, 0
	global_load_dwordx4 v[60:63], v10, s[12:13]
	s_add_u32 s12, s12, 0x8000
	s_addc_u32 s13, s13, 0
	global_load_dwordx4 v[64:67], v10, s[12:13]
	s_add_i32 s17, s16, 576
	s_min_u32 s17, s17, 0xfff
	s_lshr_b32 s18, s17, 5
	s_add_i32 s18, s18, 0
	s_and_b32 s19, s17, 31
	s_lshl_b32 s19, s19, 21
	s_lshl_b32 s18, s18, 7
	s_add_u32 s18, s18, s19
	s_add_u32 s14, s4, s18
	s_addc_u32 s15, s5, 0
	ds_read_b32 v132, v6
	ds_read_b32 v133, v6 offset:512
	ds_read_b32 v134, v6 offset:1024
	ds_read_b32 v135, v6 offset:1536
	ds_read_b32 v136, v6 offset:2048
	ds_read_b32 v137, v6 offset:2560
	ds_read_b32 v138, v6 offset:3072
	ds_read_b32 v139, v6 offset:3584
	ds_read_b32 v140, v6 offset:4096
	ds_read_b32 v141, v6 offset:4608
	ds_read_b32 v142, v6 offset:5120
	ds_read_b32 v143, v6 offset:5632
	ds_read_b32 v144, v6 offset:6144
	ds_read_b32 v145, v6 offset:6656
	ds_read_b32 v146, v6 offset:7168
	ds_read_b32 v147, v6 offset:7680
	s_waitcnt lgkmcnt(0)
	v_max_f32_e32 v132, v132, v132
	v_max_f32_e32 v133, v133, v133
	v_max_f32_e32 v134, v134, v134
	v_max_f32_e32 v135, v135, v135
	v_max_f32_e32 v136, v136, v136
	v_max_f32_e32 v137, v137, v137
	v_max_f32_e32 v138, v138, v138
	v_max_f32_e32 v139, v139, v139
	v_max_f32_e32 v140, v140, v140
	v_max_f32_e32 v141, v141, v141
	v_max_f32_e32 v142, v142, v142
	v_max_f32_e32 v143, v143, v143
	v_max_f32_e32 v144, v144, v144
	v_max_f32_e32 v145, v145, v145
	v_max_f32_e32 v146, v146, v146
	v_max_f32_e32 v147, v147, v147
	v_med3_f32 v132, v132, s20, v13
	v_med3_f32 v133, v133, s20, v13
	v_med3_f32 v134, v134, s20, v13
	v_med3_f32 v135, v135, s20, v13
	v_med3_f32 v136, v136, s20, v13
	v_med3_f32 v137, v137, s20, v13
	v_med3_f32 v138, v138, s20, v13
	v_med3_f32 v139, v139, s20, v13
	v_med3_f32 v140, v140, s20, v13
	v_med3_f32 v141, v141, s20, v13
	v_med3_f32 v142, v142, s20, v13
	v_med3_f32 v143, v143, s20, v13
	v_med3_f32 v144, v144, s20, v13
	v_med3_f32 v145, v145, s20, v13
	v_med3_f32 v146, v146, s20, v13
	v_med3_f32 v147, v147, s20, v13
	v_mov_b32_e32 v148, 0
	v_mov_b32_e32 v149, 0
	v_mov_b32_e32 v150, 0
	v_mov_b32_e32 v151, 0
	v_cvt_pk_fp8_f32 v148, v132, v133
	v_cvt_pk_fp8_f32 v149, v136, v137
	v_cvt_pk_fp8_f32 v150, v140, v141
	v_cvt_pk_fp8_f32 v151, v144, v145
	v_cvt_pk_fp8_f32 v148, v134, v135 op_sel:[0,0,1]
	v_cvt_pk_fp8_f32 v149, v138, v139 op_sel:[0,0,1]
	v_cvt_pk_fp8_f32 v150, v142, v143 op_sel:[0,0,1]
	v_cvt_pk_fp8_f32 v151, v146, v147 op_sel:[0,0,1]
	s_nop 0
	global_store_dwordx4 v11, v[148:151], s[14:15]
	ds_read_b32 v132, v8
	ds_read_b32 v133, v8 offset:512
	ds_read_b32 v134, v8 offset:1024
	ds_read_b32 v135, v8 offset:1536
	ds_read_b32 v136, v8 offset:2048
	ds_read_b32 v137, v8 offset:2560
	ds_read_b32 v138, v8 offset:3072
	ds_read_b32 v139, v8 offset:3584
	ds_read_b32 v140, v8 offset:4096
	ds_read_b32 v141, v8 offset:4608
	ds_read_b32 v142, v8 offset:5120
	ds_read_b32 v143, v8 offset:5632
	ds_read_b32 v144, v8 offset:6144
	ds_read_b32 v145, v8 offset:6656
	ds_read_b32 v146, v8 offset:7168
	ds_read_b32 v147, v8 offset:7680
	s_waitcnt lgkmcnt(0)
	v_max_f32_e32 v132, v132, v132
	v_max_f32_e32 v133, v133, v133
	v_max_f32_e32 v134, v134, v134
	v_max_f32_e32 v135, v135, v135
	v_max_f32_e32 v136, v136, v136
	v_max_f32_e32 v137, v137, v137
	v_max_f32_e32 v138, v138, v138
	v_max_f32_e32 v139, v139, v139
	v_max_f32_e32 v140, v140, v140
	v_max_f32_e32 v141, v141, v141
	v_max_f32_e32 v142, v142, v142
	v_max_f32_e32 v143, v143, v143
	v_max_f32_e32 v144, v144, v144
	v_max_f32_e32 v145, v145, v145
	v_max_f32_e32 v146, v146, v146
	v_max_f32_e32 v147, v147, v147
	v_med3_f32 v132, v132, s20, v13
	v_med3_f32 v133, v133, s20, v13
	v_med3_f32 v134, v134, s20, v13
	v_med3_f32 v135, v135, s20, v13
	v_med3_f32 v136, v136, s20, v13
	v_med3_f32 v137, v137, s20, v13
	v_med3_f32 v138, v138, s20, v13
	v_med3_f32 v139, v139, s20, v13
	v_med3_f32 v140, v140, s20, v13
	v_med3_f32 v141, v141, s20, v13
	v_med3_f32 v142, v142, s20, v13
	v_med3_f32 v143, v143, s20, v13
	v_med3_f32 v144, v144, s20, v13
	v_med3_f32 v145, v145, s20, v13
	v_med3_f32 v146, v146, s20, v13
	v_med3_f32 v147, v147, s20, v13
	v_mov_b32_e32 v148, 0
	v_mov_b32_e32 v149, 0
	v_mov_b32_e32 v150, 0
	v_mov_b32_e32 v151, 0
	v_cvt_pk_fp8_f32 v148, v132, v133
	v_cvt_pk_fp8_f32 v149, v136, v137
	v_cvt_pk_fp8_f32 v150, v140, v141
	v_cvt_pk_fp8_f32 v151, v144, v145
	v_cvt_pk_fp8_f32 v148, v134, v135 op_sel:[0,0,1]
	v_cvt_pk_fp8_f32 v149, v138, v139 op_sel:[0,0,1]
	v_cvt_pk_fp8_f32 v150, v142, v143 op_sel:[0,0,1]
	v_cvt_pk_fp8_f32 v151, v146, v147 op_sel:[0,0,1]
	s_nop 0
	global_store_dwordx4 v12, v[148:151], s[14:15]
	s_waitcnt vmcnt(22)
	v_mul_f32_e32 v68, 0x43000000, v68
	v_mul_f32_e32 v69, 0x43000000, v69
	v_mul_f32_e32 v70, 0x43000000, v70
	v_mul_f32_e32 v71, 0x43000000, v71
	ds_write_b128 v5, v[68:71]
	v_mul_f32_e32 v72, 0x43000000, v72
	v_mul_f32_e32 v73, 0x43000000, v73
	v_mul_f32_e32 v74, 0x43000000, v74
	v_mul_f32_e32 v75, 0x43000000, v75
	ds_write_b128 v5, v[72:75] offset:1024
	v_mul_f32_e32 v76, 0x43000000, v76
	v_mul_f32_e32 v77, 0x43000000, v77
	v_mul_f32_e32 v78, 0x43000000, v78
	v_mul_f32_e32 v79, 0x43000000, v79
	ds_write_b128 v5, v[76:79] offset:2048
	v_mul_f32_e32 v80, 0x43000000, v80
	v_mul_f32_e32 v81, 0x43000000, v81
	v_mul_f32_e32 v82, 0x43000000, v82
	v_mul_f32_e32 v83, 0x43000000, v83
	ds_write_b128 v5, v[80:83] offset:3072
	v_mul_f32_e32 v84, 0x43000000, v84
	v_mul_f32_e32 v85, 0x43000000, v85
	v_mul_f32_e32 v86, 0x43000000, v86
	v_mul_f32_e32 v87, 0x43000000, v87
	ds_write_b128 v5, v[84:87] offset:4096
	v_mul_f32_e32 v88, 0x43000000, v88
	v_mul_f32_e32 v89, 0x43000000, v89
	v_mul_f32_e32 v90, 0x43000000, v90
	v_mul_f32_e32 v91, 0x43000000, v91
	ds_write_b128 v5, v[88:91] offset:5120
	v_mul_f32_e32 v92, 0x43000000, v92
	v_mul_f32_e32 v93, 0x43000000, v93
	v_mul_f32_e32 v94, 0x43000000, v94
	v_mul_f32_e32 v95, 0x43000000, v95
	ds_write_b128 v5, v[92:95] offset:6144
	v_mul_f32_e32 v96, 0x43000000, v96
	v_mul_f32_e32 v97, 0x43000000, v97
	v_mul_f32_e32 v98, 0x43000000, v98
	v_mul_f32_e32 v99, 0x43000000, v99
	ds_write_b128 v5, v[96:99] offset:7168
	s_waitcnt lgkmcnt(0)
	s_barrier
; #define GAS __attribute__((address_space(1)))
; #define LAS __attribute__((address_space(3)))
; #define LDS_WAIT() asm volatile("s_waitcnt lgkmcnt(0)" ::: "memory")
; __device__ __forceinline__ unsigned pk4_fp8(float a, float b, float c, float d) {
;     a = fminf(fmaxf(a, -448.f), 448.f); b = fminf(fmaxf(b, -448.f), 448.f); c = fminf(fmaxf(c, -448.f), 448.f); d = fminf(fmaxf(d, -448.f), 448.f);
;     int w = __builtin_amdgcn_cvt_pk_fp8_f32(a, b, 0, false); w = __builtin_amdgcn_cvt_pk_fp8_f32(c, d, w, true); return (unsigned)w; }
;     const int pr = item >> 1, kb = 2 * (pr / nblk) + (item & 1), nb = pr % nblk, k0 = 64 * kb, n0 = 32 * nb;
;     const int nr = n0 + (lane & 31); const int sc = MAP == 1 ? src_col_in(nr) : nr;
;     float v[32];
; #pragma unroll
;     for (int i = 0; i < 32; ++i) v[i] = sc >= 0 ? W[(size_t)(k0 + 2 * i + (lane >> 5)) * Nsrc + sc] : 0.f;
; #pragma unroll
;     for (int i = 0; i < 32; ++i) { const int k = k0 + 2 * i + (lane >> 5); float x = v[i] * wscale; if (KS) x *= (k < ksplit ? ksA[k] : ksB[k - ksplit]); scr[(2 * i + (lane >> 5)) * 33 + (lane & 31)] = x; }
;     LDS_WAIT(); asm volatile("" ::: "memory");
;     const int c = lane & 7;
; #pragma unroll
;     for (int j = 0; j < 4; ++j) { const int n = (lane >> 3) + 8 * j; const LAS float* s = scr + (8 * c) * 33 + n;
;         const unsigned long long o = (unsigned long long)pg8::pk4_fp8(s[0 * 33], s[1 * 33], s[2 * 33], s[3 * 33]) | ((unsigned long long)pg8::pk4_fp8(s[4 * 33], s[5 * 33], s[6 * 33], s[7 * 33]) << 32);
;         *(GAS unsigned long long*)(WT + (size_t)(n0 + n) * K + k0 + 8 * c) = o; }
;     LDS_WAIT(); asm volatile("" ::: "memory");
	s_add_i32 s17, s16, 960
	s_min_u32 s17, s17, 0xfff
	s_lshr_b32 s18, s17, 5
	s_add_i32 s18, s18, 0
	s_and_b32 s19, s17, 31
	s_lshl_b32 s18, s18, 21
	s_lshl_b32 s19, s19, 9
	s_add_u32 s18, s18, s19
	s_add_u32 s12, s2, s18
	s_addc_u32 s13, s3, 0
	global_load_dwordx4 v[68:71], v10, s[12:13]
	s_add_u32 s12, s12, 0x8000
	s_addc_u32 s13, s13, 0
	global_load_dwordx4 v[72:75], v10, s[12:13]
	s_add_u32 s12, s12, 0x8000
	s_addc_u32 s13, s13, 0
	global_load_dwordx4 v[76:79], v10, s[12:13]
	s_add_u32 s12, s12, 0x8000
	s_addc_u32 s13, s13, 0
	global_load_dwordx4 v[80:83], v10, s[12:13]
	s_add_u32 s12, s12, 0x8000
	s_addc_u32 s13, s13, 0
	global_load_dwordx4 v[84:87], v10, s[12:13]
	s_add_u32 s12, s12, 0x8000
	s_addc_u32 s13, s13, 0
	global_load_dwordx4 v[88:91], v10, s[12:13]
	s_add_u32 s12, s12, 0x8000
	s_addc_u32 s13, s13, 0
	global_load_dwordx4 v[92:95], v10, s[12:13]
	s_add_u32 s12, s12, 0x8000
	s_addc_u32 s13, s13, 0
	global_load_dwordx4 v[96:99], v10, s[12:13]
	s_add_i32 s17, s16, 672
	s_min_u32 s17, s17, 0xfff
	s_lshr_b32 s18, s17, 5
	s_add_i32 s18, s18, 0
	s_and_b32 s19, s17, 31
	s_lshl_b32 s19, s19, 21
	s_lshl_b32 s18, s18, 7
	s_add_u32 s18, s18, s19
	s_add_u32 s14, s4, s18
	s_addc_u32 s15, s5, 0
	ds_read_b32 v132, v7
	ds_read_b32 v133, v7 offset:512
	ds_read_b32 v134, v7 offset:1024
	ds_read_b32 v135, v7 offset:1536
	ds_read_b32 v136, v7 offset:2048
	ds_read_b32 v137, v7 offset:2560
	ds_read_b32 v138, v7 offset:3072
	ds_read_b32 v139, v7 offset:3584
	ds_read_b32 v140, v7 offset:4096
	ds_read_b32 v141, v7 offset:4608
	ds_read_b32 v142, v7 offset:5120
	ds_read_b32 v143, v7 offset:5632
	ds_read_b32 v144, v7 offset:6144
	ds_read_b32 v145, v7 offset:6656
	ds_read_b32 v146, v7 offset:7168
	ds_read_b32 v147, v7 offset:7680
	s_waitcnt lgkmcnt(0)
	v_max_f32_e32 v132, v132, v132
	v_max_f32_e32 v133, v133, v133
	v_max_f32_e32 v134, v134, v134
	v_max_f32_e32 v135, v135, v135
	v_max_f32_e32 v136, v136, v136
	v_max_f32_e32 v137, v137, v137
	v_max_f32_e32 v138, v138, v138
	v_max_f32_e32 v139, v139, v139
	v_max_f32_e32 v140, v140, v140
	v_max_f32_e32 v141, v141, v141
	v_max_f32_e32 v142, v142, v142
	v_max_f32_e32 v143, v143, v143
	v_max_f32_e32 v144, v144, v144
	v_max_f32_e32 v145, v145, v145
	v_max_f32_e32 v146, v146, v146
	v_max_f32_e32 v147, v147, v147
	v_med3_f32 v132, v132, s20, v13
	v_med3_f32 v133, v133, s20, v13
	v_med3_f32 v134, v134, s20, v13
	v_med3_f32 v135, v135, s20, v13
	v_med3_f32 v136, v136, s20, v13
	v_med3_f32 v137, v137, s20, v13
	v_med3_f32 v138, v138, s20, v13
	v_med3_f32 v139, v139, s20, v13
	v_med3_f32 v140, v140, s20, v13
	v_med3_f32 v141, v141, s20, v13
	v_med3_f32 v142, v142, s20, v13
	v_med3_f32 v143, v143, s20, v13
	v_med3_f32 v144, v144, s20, v13
	v_med3_f32 v145, v145, s20, v13
	v_med3_f32 v146, v146, s20, v13
	v_med3_f32 v147, v147, s20, v13
	v_mov_b32_e32 v148, 0
	v_mov_b32_e32 v149, 0
	v_mov_b32_e32 v150, 0
	v_mov_b32_e32 v151, 0
	v_cvt_pk_fp8_f32 v148, v132, v133
	v_cvt_pk_fp8_f32 v149, v136, v137
	v_cvt_pk_fp8_f32 v150, v140, v141
	v_cvt_pk_fp8_f32 v151, v144, v145
	v_cvt_pk_fp8_f32 v148, v134, v135 op_sel:[0,0,1]
	v_cvt_pk_fp8_f32 v149, v138, v139 op_sel:[0,0,1]
	v_cvt_pk_fp8_f32 v150, v142, v143 op_sel:[0,0,1]
	v_cvt_pk_fp8_f32 v151, v146, v147 op_sel:[0,0,1]
	s_nop 0
	global_store_dwordx4 v11, v[148:151], s[14:15]
	ds_read_b32 v132, v9
	ds_read_b32 v133, v9 offset:512
	ds_read_b32 v134, v9 offset:1024
	ds_read_b32 v135, v9 offset:1536
	ds_read_b32 v136, v9 offset:2048
	ds_read_b32 v137, v9 offset:2560
	ds_read_b32 v138, v9 offset:3072
	ds_read_b32 v139, v9 offset:3584
	ds_read_b32 v140, v9 offset:4096
	ds_read_b32 v141, v9 offset:4608
	ds_read_b32 v142, v9 offset:5120
	ds_read_b32 v143, v9 offset:5632
	ds_read_b32 v144, v9 offset:6144
	ds_read_b32 v145, v9 offset:6656
	ds_read_b32 v146, v9 offset:7168
	ds_read_b32 v147, v9 offset:7680
	s_waitcnt lgkmcnt(0)
	v_max_f32_e32 v132, v132, v132
	v_max_f32_e32 v133, v133, v133
	v_max_f32_e32 v134, v134, v134
	v_max_f32_e32 v135, v135, v135
	v_max_f32_e32 v136, v136, v136
	v_max_f32_e32 v137, v137, v137
	v_max_f32_e32 v138, v138, v138
	v_max_f32_e32 v139, v139, v139
	v_max_f32_e32 v140, v140, v140
	v_max_f32_e32 v141, v141, v141
	v_max_f32_e32 v142, v142, v142
	v_max_f32_e32 v143, v143, v143
	v_max_f32_e32 v144, v144, v144
	v_max_f32_e32 v145, v145, v145
	v_max_f32_e32 v146, v146, v146
	v_max_f32_e32 v147, v147, v147
	v_med3_f32 v132, v132, s20, v13
	v_med3_f32 v133, v133, s20, v13
	v_med3_f32 v134, v134, s20, v13
	v_med3_f32 v135, v135, s20, v13
	v_med3_f32 v136, v136, s20, v13
	v_med3_f32 v137, v137, s20, v13
	v_med3_f32 v138, v138, s20, v13
	v_med3_f32 v139, v139, s20, v13
	v_med3_f32 v140, v140, s20, v13
	v_med3_f32 v141, v141, s20, v13
	v_med3_f32 v142, v142, s20, v13
	v_med3_f32 v143, v143, s20, v13
	v_med3_f32 v144, v144, s20, v13
	v_med3_f32 v145, v145, s20, v13
	v_med3_f32 v146, v146, s20, v13
	v_med3_f32 v147, v147, s20, v13
	v_mov_b32_e32 v148, 0
	v_mov_b32_e32 v149, 0
	v_mov_b32_e32 v150, 0
	v_mov_b32_e32 v151, 0
	v_cvt_pk_fp8_f32 v148, v132, v133
	v_cvt_pk_fp8_f32 v149, v136, v137
	v_cvt_pk_fp8_f32 v150, v140, v141
	v_cvt_pk_fp8_f32 v151, v144, v145
	v_cvt_pk_fp8_f32 v148, v134, v135 op_sel:[0,0,1]
	v_cvt_pk_fp8_f32 v149, v138, v139 op_sel:[0,0,1]
	v_cvt_pk_fp8_f32 v150, v142, v143 op_sel:[0,0,1]
	v_cvt_pk_fp8_f32 v151, v146, v147 op_sel:[0,0,1]
	s_nop 0
	global_store_dwordx4 v12, v[148:151], s[14:15]
	s_waitcnt vmcnt(22)
	v_mul_f32_e32 v100, 0x43000000, v100
	v_mul_f32_e32 v101, 0x43000000, v101
	v_mul_f32_e32 v102, 0x43000000, v102
	v_mul_f32_e32 v103, 0x43000000, v103
	ds_write_b128 v4, v[100:103]
	v_mul_f32_e32 v104, 0x43000000, v104
	v_mul_f32_e32 v105, 0x43000000, v105
	v_mul_f32_e32 v106, 0x43000000, v106
	v_mul_f32_e32 v107, 0x43000000, v107
	ds_write_b128 v4, v[104:107] offset:1024
	v_mul_f32_e32 v108, 0x43000000, v108
	v_mul_f32_e32 v109, 0x43000000, v109
	v_mul_f32_e32 v110, 0x43000000, v110
	v_mul_f32_e32 v111, 0x43000000, v111
	ds_write_b128 v4, v[108:111] offset:2048
	v_mul_f32_e32 v112, 0x43000000, v112
	v_mul_f32_e32 v113, 0x43000000, v113
	v_mul_f32_e32 v114, 0x43000000, v114
	v_mul_f32_e32 v115, 0x43000000, v115
	ds_write_b128 v4, v[112:115] offset:3072
	v_mul_f32_e32 v116, 0x43000000, v116
	v_mul_f32_e32 v117, 0x43000000, v117
	v_mul_f32_e32 v118, 0x43000000, v118
	v_mul_f32_e32 v119, 0x43000000, v119
	ds_write_b128 v4, v[116:119] offset:4096
	v_mul_f32_e32 v120, 0x43000000, v120
	v_mul_f32_e32 v121, 0x43000000, v121
	v_mul_f32_e32 v122, 0x43000000, v122
	v_mul_f32_e32 v123, 0x43000000, v123
	ds_write_b128 v4, v[120:123] offset:5120
	v_mul_f32_e32 v124, 0x43000000, v124
	v_mul_f32_e32 v125, 0x43000000, v125
	v_mul_f32_e32 v126, 0x43000000, v126
	v_mul_f32_e32 v127, 0x43000000, v127
	ds_write_b128 v4, v[124:127] offset:6144
	v_mul_f32_e32 v128, 0x43000000, v128
	v_mul_f32_e32 v129, 0x43000000, v129
	v_mul_f32_e32 v130, 0x43000000, v130
	v_mul_f32_e32 v131, 0x43000000, v131
	ds_write_b128 v4, v[128:131] offset:7168
	s_waitcnt lgkmcnt(0)
	s_barrier
; #define GAS __attribute__((address_space(1)))
; #define LAS __attribute__((address_space(3)))
; #define LDS_WAIT() asm volatile("s_waitcnt lgkmcnt(0)" ::: "memory")
; __device__ __forceinline__ unsigned pk4_fp8(float a, float b, float c, float d) {
;     a = fminf(fmaxf(a, -448.f), 448.f); b = fminf(fmaxf(b, -448.f), 448.f); c = fminf(fmaxf(c, -448.f), 448.f); d = fminf(fmaxf(d, -448.f), 448.f);
;     int w = __builtin_amdgcn_cvt_pk_fp8_f32(a, b, 0, false); w = __builtin_amdgcn_cvt_pk_fp8_f32(c, d, w, true); return (unsigned)w; }
;     const int pr = item >> 1, kb = 2 * (pr / nblk) + (item & 1), nb = pr % nblk, k0 = 64 * kb, n0 = 32 * nb;
;     const int nr = n0 + (lane & 31); const int sc = MAP == 1 ? src_col_in(nr) : nr;
;     float v[32];
; #pragma unroll
;     for (int i = 0; i < 32; ++i) v[i] = sc >= 0 ? W[(size_t)(k0 + 2 * i + (lane >> 5)) * Nsrc + sc] : 0.f;
; #pragma unroll
;     for (int i = 0; i < 32; ++i) { const int k = k0 + 2 * i + (lane >> 5); float x = v[i] * wscale; if (KS) x *= (k < ksplit ? ksA[k] : ksB[k - ksplit]); scr[(2 * i + (lane >> 5)) * 33 + (lane & 31)] = x; }
;     LDS_WAIT(); asm volatile("" ::: "memory");
;     const int c = lane & 7;
; #pragma unroll
;     for (int j = 0; j < 4; ++j) { const int n = (lane >> 3) + 8 * j; const LAS float* s = scr + (8 * c) * 33 + n;
;         const unsigned long long o = (unsigned long long)pg8::pk4_fp8(s[0 * 33], s[1 * 33], s[2 * 33], s[3 * 33]) | ((unsigned long long)pg8::pk4_fp8(s[4 * 33], s[5 * 33], s[6 * 33], s[7 * 33]) << 32);
;         *(GAS unsigned long long*)(WT + (size_t)(n0 + n) * K + k0 + 8 * c) = o; }
;     LDS_WAIT(); asm volatile("" ::: "memory");
	s_add_i32 s17, s16, 1056
	s_min_u32 s17, s17, 0xfff
	s_lshr_b32 s18, s17, 5
	s_add_i32 s18, s18, 0
	s_and_b32 s19, s17, 31
	s_lshl_b32 s18, s18, 21
	s_lshl_b32 s19, s19, 9
	s_add_u32 s18, s18, s19
	s_add_u32 s12, s2, s18
	s_addc_u32 s13, s3, 0
	global_load_dwordx4 v[100:103], v10, s[12:13]
	s_add_u32 s12, s12, 0x8000
	s_addc_u32 s13, s13, 0
	global_load_dwordx4 v[104:107], v10, s[12:13]
	s_add_u32 s12, s12, 0x8000
	s_addc_u32 s13, s13, 0
	global_load_dwordx4 v[108:111], v10, s[12:13]
	s_add_u32 s12, s12, 0x8000
	s_addc_u32 s13, s13, 0
	global_load_dwordx4 v[112:115], v10, s[12:13]
	s_add_u32 s12, s12, 0x8000
	s_addc_u32 s13, s13, 0
	global_load_dwordx4 v[116:119], v10, s[12:13]
	s_add_u32 s12, s12, 0x8000
	s_addc_u32 s13, s13, 0
	global_load_dwordx4 v[120:123], v10, s[12:13]
	s_add_u32 s12, s12, 0x8000
	s_addc_u32 s13, s13, 0
	global_load_dwordx4 v[124:127], v10, s[12:13]
	s_add_u32 s12, s12, 0x8000
	s_addc_u32 s13, s13, 0
	global_load_dwordx4 v[128:131], v10, s[12:13]
	s_add_i32 s17, s16, 768
	s_min_u32 s17, s17, 0xfff
	s_lshr_b32 s18, s17, 5
	s_add_i32 s18, s18, 0
	s_and_b32 s19, s17, 31
	s_lshl_b32 s19, s19, 21
	s_lshl_b32 s18, s18, 7
	s_add_u32 s18, s18, s19
	s_add_u32 s14, s4, s18
	s_addc_u32 s15, s5, 0
	ds_read_b32 v132, v6
	ds_read_b32 v133, v6 offset:512
	ds_read_b32 v134, v6 offset:1024
	ds_read_b32 v135, v6 offset:1536
	ds_read_b32 v136, v6 offset:2048
	ds_read_b32 v137, v6 offset:2560
	ds_read_b32 v138, v6 offset:3072
	ds_read_b32 v139, v6 offset:3584
	ds_read_b32 v140, v6 offset:4096
	ds_read_b32 v141, v6 offset:4608
	ds_read_b32 v142, v6 offset:5120
	ds_read_b32 v143, v6 offset:5632
	ds_read_b32 v144, v6 offset:6144
	ds_read_b32 v145, v6 offset:6656
	ds_read_b32 v146, v6 offset:7168
	ds_read_b32 v147, v6 offset:7680
	s_waitcnt lgkmcnt(0)
	v_max_f32_e32 v132, v132, v132
	v_max_f32_e32 v133, v133, v133
	v_max_f32_e32 v134, v134, v134
	v_max_f32_e32 v135, v135, v135
	v_max_f32_e32 v136, v136, v136
	v_max_f32_e32 v137, v137, v137
	v_max_f32_e32 v138, v138, v138
	v_max_f32_e32 v139, v139, v139
	v_max_f32_e32 v140, v140, v140
	v_max_f32_e32 v141, v141, v141
	v_max_f32_e32 v142, v142, v142
	v_max_f32_e32 v143, v143, v143
	v_max_f32_e32 v144, v144, v144
	v_max_f32_e32 v145, v145, v145
	v_max_f32_e32 v146, v146, v146
	v_max_f32_e32 v147, v147, v147
	v_med3_f32 v132, v132, s20, v13
	v_med3_f32 v133, v133, s20, v13
	v_med3_f32 v134, v134, s20, v13
	v_med3_f32 v135, v135, s20, v13
	v_med3_f32 v136, v136, s20, v13
	v_med3_f32 v137, v137, s20, v13
	v_med3_f32 v138, v138, s20, v13
	v_med3_f32 v139, v139, s20, v13
	v_med3_f32 v140, v140, s20, v13
	v_med3_f32 v141, v141, s20, v13
	v_med3_f32 v142, v142, s20, v13
	v_med3_f32 v143, v143, s20, v13
	v_med3_f32 v144, v144, s20, v13
	v_med3_f32 v145, v145, s20, v13
	v_med3_f32 v146, v146, s20, v13
	v_med3_f32 v147, v147, s20, v13
	v_mov_b32_e32 v148, 0
	v_mov_b32_e32 v149, 0
	v_mov_b32_e32 v150, 0
	v_mov_b32_e32 v151, 0
	v_cvt_pk_fp8_f32 v148, v132, v133
	v_cvt_pk_fp8_f32 v149, v136, v137
	v_cvt_pk_fp8_f32 v150, v140, v141
	v_cvt_pk_fp8_f32 v151, v144, v145
	v_cvt_pk_fp8_f32 v148, v134, v135 op_sel:[0,0,1]
	v_cvt_pk_fp8_f32 v149, v138, v139 op_sel:[0,0,1]
	v_cvt_pk_fp8_f32 v150, v142, v143 op_sel:[0,0,1]
	v_cvt_pk_fp8_f32 v151, v146, v147 op_sel:[0,0,1]
	s_nop 0
	global_store_dwordx4 v11, v[148:151], s[14:15]
	ds_read_b32 v132, v8
	ds_read_b32 v133, v8 offset:512
	ds_read_b32 v134, v8 offset:1024
	ds_read_b32 v135, v8 offset:1536
	ds_read_b32 v136, v8 offset:2048
	ds_read_b32 v137, v8 offset:2560
	ds_read_b32 v138, v8 offset:3072
	ds_read_b32 v139, v8 offset:3584
	ds_read_b32 v140, v8 offset:4096
	ds_read_b32 v141, v8 offset:4608
	ds_read_b32 v142, v8 offset:5120
	ds_read_b32 v143, v8 offset:5632
	ds_read_b32 v144, v8 offset:6144
	ds_read_b32 v145, v8 offset:6656
	ds_read_b32 v146, v8 offset:7168
	ds_read_b32 v147, v8 offset:7680
	s_waitcnt lgkmcnt(0)
	v_max_f32_e32 v132, v132, v132
	v_max_f32_e32 v133, v133, v133
	v_max_f32_e32 v134, v134, v134
	v_max_f32_e32 v135, v135, v135
	v_max_f32_e32 v136, v136, v136
	v_max_f32_e32 v137, v137, v137
	v_max_f32_e32 v138, v138, v138
	v_max_f32_e32 v139, v139, v139
	v_max_f32_e32 v140, v140, v140
	v_max_f32_e32 v141, v141, v141
	v_max_f32_e32 v142, v142, v142
	v_max_f32_e32 v143, v143, v143
	v_max_f32_e32 v144, v144, v144
	v_max_f32_e32 v145, v145, v145
	v_max_f32_e32 v146, v146, v146
	v_max_f32_e32 v147, v147, v147
	v_med3_f32 v132, v132, s20, v13
	v_med3_f32 v133, v133, s20, v13
	v_med3_f32 v134, v134, s20, v13
	v_med3_f32 v135, v135, s20, v13
	v_med3_f32 v136, v136, s20, v13
	v_med3_f32 v137, v137, s20, v13
	v_med3_f32 v138, v138, s20, v13
	v_med3_f32 v139, v139, s20, v13
	v_med3_f32 v140, v140, s20, v13
	v_med3_f32 v141, v141, s20, v13
	v_med3_f32 v142, v142, s20, v13
	v_med3_f32 v143, v143, s20, v13
	v_med3_f32 v144, v144, s20, v13
	v_med3_f32 v145, v145, s20, v13
	v_med3_f32 v146, v146, s20, v13
	v_med3_f32 v147, v147, s20, v13
	v_mov_b32_e32 v148, 0
	v_mov_b32_e32 v149, 0
	v_mov_b32_e32 v150, 0
	v_mov_b32_e32 v151, 0
	v_cvt_pk_fp8_f32 v148, v132, v133
	v_cvt_pk_fp8_f32 v149, v136, v137
	v_cvt_pk_fp8_f32 v150, v140, v141
	v_cvt_pk_fp8_f32 v151, v144, v145
	v_cvt_pk_fp8_f32 v148, v134, v135 op_sel:[0,0,1]
	v_cvt_pk_fp8_f32 v149, v138, v139 op_sel:[0,0,1]
	v_cvt_pk_fp8_f32 v150, v142, v143 op_sel:[0,0,1]
	v_cvt_pk_fp8_f32 v151, v146, v147 op_sel:[0,0,1]
	s_nop 0
	global_store_dwordx4 v12, v[148:151], s[14:15]
	s_waitcnt vmcnt(22)
	v_mul_f32_e32 v36, 0x43000000, v36
	v_mul_f32_e32 v37, 0x43000000, v37
	v_mul_f32_e32 v38, 0x43000000, v38
	v_mul_f32_e32 v39, 0x43000000, v39
	ds_write_b128 v5, v[36:39]
	v_mul_f32_e32 v40, 0x43000000, v40
	v_mul_f32_e32 v41, 0x43000000, v41
	v_mul_f32_e32 v42, 0x43000000, v42
	v_mul_f32_e32 v43, 0x43000000, v43
	ds_write_b128 v5, v[40:43] offset:1024
	v_mul_f32_e32 v44, 0x43000000, v44
	v_mul_f32_e32 v45, 0x43000000, v45
	v_mul_f32_e32 v46, 0x43000000, v46
	v_mul_f32_e32 v47, 0x43000000, v47
	ds_write_b128 v5, v[44:47] offset:2048
	v_mul_f32_e32 v48, 0x43000000, v48
	v_mul_f32_e32 v49, 0x43000000, v49
	v_mul_f32_e32 v50, 0x43000000, v50
	v_mul_f32_e32 v51, 0x43000000, v51
	ds_write_b128 v5, v[48:51] offset:3072
	v_mul_f32_e32 v52, 0x43000000, v52
	v_mul_f32_e32 v53, 0x43000000, v53
	v_mul_f32_e32 v54, 0x43000000, v54
	v_mul_f32_e32 v55, 0x43000000, v55
	ds_write_b128 v5, v[52:55] offset:4096
	v_mul_f32_e32 v56, 0x43000000, v56
	v_mul_f32_e32 v57, 0x43000000, v57
	v_mul_f32_e32 v58, 0x43000000, v58
	v_mul_f32_e32 v59, 0x43000000, v59
	ds_write_b128 v5, v[56:59] offset:5120
	v_mul_f32_e32 v60, 0x43000000, v60
	v_mul_f32_e32 v61, 0x43000000, v61
	v_mul_f32_e32 v62, 0x43000000, v62
	v_mul_f32_e32 v63, 0x43000000, v63
	ds_write_b128 v5, v[60:63] offset:6144
	v_mul_f32_e32 v64, 0x43000000, v64
	v_mul_f32_e32 v65, 0x43000000, v65
	v_mul_f32_e32 v66, 0x43000000, v66
	v_mul_f32_e32 v67, 0x43000000, v67
	ds_write_b128 v5, v[64:67] offset:7168
	s_waitcnt lgkmcnt(0)
	s_barrier
; #define GAS __attribute__((address_space(1)))
; #define LAS __attribute__((address_space(3)))
; #define LDS_WAIT() asm volatile("s_waitcnt lgkmcnt(0)" ::: "memory")
; __device__ __forceinline__ unsigned pk4_fp8(float a, float b, float c, float d) {
;     a = fminf(fmaxf(a, -448.f), 448.f); b = fminf(fmaxf(b, -448.f), 448.f); c = fminf(fmaxf(c, -448.f), 448.f); d = fminf(fmaxf(d, -448.f), 448.f);
;     int w = __builtin_amdgcn_cvt_pk_fp8_f32(a, b, 0, false); w = __builtin_amdgcn_cvt_pk_fp8_f32(c, d, w, true); return (unsigned)w; }
;     const int pr = item >> 1, kb = 2 * (pr / nblk) + (item & 1), nb = pr % nblk, k0 = 64 * kb, n0 = 32 * nb;
;     const int nr = n0 + (lane & 31); const int sc = MAP == 1 ? src_col_in(nr) : nr;
;     float v[32];
; #pragma unroll
;     for (int i = 0; i < 32; ++i) v[i] = sc >= 0 ? W[(size_t)(k0 + 2 * i + (lane >> 5)) * Nsrc + sc] : 0.f;
; #pragma unroll
;     for (int i = 0; i < 32; ++i) { const int k = k0 + 2 * i + (lane >> 5); float x = v[i] * wscale; if (KS) x *= (k < ksplit ? ksA[k] : ksB[k - ksplit]); scr[(2 * i + (lane >> 5)) * 33 + (lane & 31)] = x; }
;     LDS_WAIT(); asm volatile("" ::: "memory");
;     const int c = lane & 7;
; #pragma unroll
;     for (int j = 0; j < 4; ++j) { const int n = (lane >> 3) + 8 * j; const LAS float* s = scr + (8 * c) * 33 + n;
;         const unsigned long long o = (unsigned long long)pg8::pk4_fp8(s[0 * 33], s[1 * 33], s[2 * 33], s[3 * 33]) | ((unsigned long long)pg8::pk4_fp8(s[4 * 33], s[5 * 33], s[6 * 33], s[7 * 33]) << 32);
;         *(GAS unsigned long long*)(WT + (size_t)(n0 + n) * K + k0 + 8 * c) = o; }
;     LDS_WAIT(); asm volatile("" ::: "memory");
	s_add_i32 s17, s16, 1152
	s_min_u32 s17, s17, 0xfff
	s_lshr_b32 s18, s17, 5
	s_add_i32 s18, s18, 0
	s_and_b32 s19, s17, 31
	s_lshl_b32 s18, s18, 21
	s_lshl_b32 s19, s19, 9
	s_add_u32 s18, s18, s19
	s_add_u32 s12, s2, s18
	s_addc_u32 s13, s3, 0
	global_load_dwordx4 v[36:39], v10, s[12:13]
	s_add_u32 s12, s12, 0x8000
	s_addc_u32 s13, s13, 0
	global_load_dwordx4 v[40:43], v10, s[12:13]
	s_add_u32 s12, s12, 0x8000
	s_addc_u32 s13, s13, 0
	global_load_dwordx4 v[44:47], v10, s[12:13]
	s_add_u32 s12, s12, 0x8000
	s_addc_u32 s13, s13, 0
	global_load_dwordx4 v[48:51], v10, s[12:13]
	s_add_u32 s12, s12, 0x8000
	s_addc_u32 s13, s13, 0
	global_load_dwordx4 v[52:55], v10, s[12:13]
	s_add_u32 s12, s12, 0x8000
	s_addc_u32 s13, s13, 0
	global_load_dwordx4 v[56:59], v10, s[12:13]
	s_add_u32 s12, s12, 0x8000
	s_addc_u32 s13, s13, 0
	global_load_dwordx4 v[60:63], v10, s[12:13]
	s_add_u32 s12, s12, 0x8000
	s_addc_u32 s13, s13, 0
	global_load_dwordx4 v[64:67], v10, s[12:13]
	s_add_i32 s17, s16, 864
	s_min_u32 s17, s17, 0xfff
	s_lshr_b32 s18, s17, 5
	s_add_i32 s18, s18, 0
	s_and_b32 s19, s17, 31
	s_lshl_b32 s19, s19, 21
	s_lshl_b32 s18, s18, 7
	s_add_u32 s18, s18, s19
	s_add_u32 s14, s4, s18
	s_addc_u32 s15, s5, 0
	ds_read_b32 v132, v7
	ds_read_b32 v133, v7 offset:512
	ds_read_b32 v134, v7 offset:1024
	ds_read_b32 v135, v7 offset:1536
	ds_read_b32 v136, v7 offset:2048
	ds_read_b32 v137, v7 offset:2560
	ds_read_b32 v138, v7 offset:3072
	ds_read_b32 v139, v7 offset:3584
	ds_read_b32 v140, v7 offset:4096
	ds_read_b32 v141, v7 offset:4608
	ds_read_b32 v142, v7 offset:5120
	ds_read_b32 v143, v7 offset:5632
	ds_read_b32 v144, v7 offset:6144
	ds_read_b32 v145, v7 offset:6656
	ds_read_b32 v146, v7 offset:7168
	ds_read_b32 v147, v7 offset:7680
	s_waitcnt lgkmcnt(0)
	v_max_f32_e32 v132, v132, v132
	v_max_f32_e32 v133, v133, v133
	v_max_f32_e32 v134, v134, v134
	v_max_f32_e32 v135, v135, v135
	v_max_f32_e32 v136, v136, v136
	v_max_f32_e32 v137, v137, v137
	v_max_f32_e32 v138, v138, v138
	v_max_f32_e32 v139, v139, v139
	v_max_f32_e32 v140, v140, v140
	v_max_f32_e32 v141, v141, v141
	v_max_f32_e32 v142, v142, v142
	v_max_f32_e32 v143, v143, v143
	v_max_f32_e32 v144, v144, v144
	v_max_f32_e32 v145, v145, v145
	v_max_f32_e32 v146, v146, v146
	v_max_f32_e32 v147, v147, v147
	v_med3_f32 v132, v132, s20, v13
	v_med3_f32 v133, v133, s20, v13
	v_med3_f32 v134, v134, s20, v13
	v_med3_f32 v135, v135, s20, v13
	v_med3_f32 v136, v136, s20, v13
	v_med3_f32 v137, v137, s20, v13
	v_med3_f32 v138, v138, s20, v13
	v_med3_f32 v139, v139, s20, v13
	v_med3_f32 v140, v140, s20, v13
	v_med3_f32 v141, v141, s20, v13
	v_med3_f32 v142, v142, s20, v13
	v_med3_f32 v143, v143, s20, v13
	v_med3_f32 v144, v144, s20, v13
	v_med3_f32 v145, v145, s20, v13
	v_med3_f32 v146, v146, s20, v13
	v_med3_f32 v147, v147, s20, v13
	v_mov_b32_e32 v148, 0
	v_mov_b32_e32 v149, 0
	v_mov_b32_e32 v150, 0
	v_mov_b32_e32 v151, 0
	v_cvt_pk_fp8_f32 v148, v132, v133
	v_cvt_pk_fp8_f32 v149, v136, v137
	v_cvt_pk_fp8_f32 v150, v140, v141
	v_cvt_pk_fp8_f32 v151, v144, v145
	v_cvt_pk_fp8_f32 v148, v134, v135 op_sel:[0,0,1]
	v_cvt_pk_fp8_f32 v149, v138, v139 op_sel:[0,0,1]
	v_cvt_pk_fp8_f32 v150, v142, v143 op_sel:[0,0,1]
	v_cvt_pk_fp8_f32 v151, v146, v147 op_sel:[0,0,1]
	s_nop 0
	global_store_dwordx4 v11, v[148:151], s[14:15]
	ds_read_b32 v132, v9
	ds_read_b32 v133, v9 offset:512
	ds_read_b32 v134, v9 offset:1024
	ds_read_b32 v135, v9 offset:1536
	ds_read_b32 v136, v9 offset:2048
	ds_read_b32 v137, v9 offset:2560
	ds_read_b32 v138, v9 offset:3072
	ds_read_b32 v139, v9 offset:3584
	ds_read_b32 v140, v9 offset:4096
	ds_read_b32 v141, v9 offset:4608
	ds_read_b32 v142, v9 offset:5120
	ds_read_b32 v143, v9 offset:5632
	ds_read_b32 v144, v9 offset:6144
	ds_read_b32 v145, v9 offset:6656
	ds_read_b32 v146, v9 offset:7168
	ds_read_b32 v147, v9 offset:7680
	s_waitcnt lgkmcnt(0)
	v_max_f32_e32 v132, v132, v132
	v_max_f32_e32 v133, v133, v133
	v_max_f32_e32 v134, v134, v134
	v_max_f32_e32 v135, v135, v135
	v_max_f32_e32 v136, v136, v136
	v_max_f32_e32 v137, v137, v137
	v_max_f32_e32 v138, v138, v138
	v_max_f32_e32 v139, v139, v139
	v_max_f32_e32 v140, v140, v140
	v_max_f32_e32 v141, v141, v141
	v_max_f32_e32 v142, v142, v142
	v_max_f32_e32 v143, v143, v143
	v_max_f32_e32 v144, v144, v144
	v_max_f32_e32 v145, v145, v145
	v_max_f32_e32 v146, v146, v146
	v_max_f32_e32 v147, v147, v147
	v_med3_f32 v132, v132, s20, v13
	v_med3_f32 v133, v133, s20, v13
	v_med3_f32 v134, v134, s20, v13
	v_med3_f32 v135, v135, s20, v13
	v_med3_f32 v136, v136, s20, v13
	v_med3_f32 v137, v137, s20, v13
	v_med3_f32 v138, v138, s20, v13
	v_med3_f32 v139, v139, s20, v13
	v_med3_f32 v140, v140, s20, v13
	v_med3_f32 v141, v141, s20, v13
	v_med3_f32 v142, v142, s20, v13
	v_med3_f32 v143, v143, s20, v13
	v_med3_f32 v144, v144, s20, v13
	v_med3_f32 v145, v145, s20, v13
	v_med3_f32 v146, v146, s20, v13
	v_med3_f32 v147, v147, s20, v13
	v_mov_b32_e32 v148, 0
	v_mov_b32_e32 v149, 0
	v_mov_b32_e32 v150, 0
	v_mov_b32_e32 v151, 0
	v_cvt_pk_fp8_f32 v148, v132, v133
	v_cvt_pk_fp8_f32 v149, v136, v137
	v_cvt_pk_fp8_f32 v150, v140, v141
	v_cvt_pk_fp8_f32 v151, v144, v145
	v_cvt_pk_fp8_f32 v148, v134, v135 op_sel:[0,0,1]
	v_cvt_pk_fp8_f32 v149, v138, v139 op_sel:[0,0,1]
	v_cvt_pk_fp8_f32 v150, v142, v143 op_sel:[0,0,1]
	v_cvt_pk_fp8_f32 v151, v146, v147 op_sel:[0,0,1]
	s_nop 0
	global_store_dwordx4 v12, v[148:151], s[14:15]
	s_waitcnt vmcnt(22)
	v_mul_f32_e32 v68, 0x43000000, v68
	v_mul_f32_e32 v69, 0x43000000, v69
	v_mul_f32_e32 v70, 0x43000000, v70
	v_mul_f32_e32 v71, 0x43000000, v71
	ds_write_b128 v4, v[68:71]
	v_mul_f32_e32 v72, 0x43000000, v72
	v_mul_f32_e32 v73, 0x43000000, v73
	v_mul_f32_e32 v74, 0x43000000, v74
	v_mul_f32_e32 v75, 0x43000000, v75
	ds_write_b128 v4, v[72:75] offset:1024
	v_mul_f32_e32 v76, 0x43000000, v76
	v_mul_f32_e32 v77, 0x43000000, v77
	v_mul_f32_e32 v78, 0x43000000, v78
	v_mul_f32_e32 v79, 0x43000000, v79
	ds_write_b128 v4, v[76:79] offset:2048
	v_mul_f32_e32 v80, 0x43000000, v80
	v_mul_f32_e32 v81, 0x43000000, v81
	v_mul_f32_e32 v82, 0x43000000, v82
	v_mul_f32_e32 v83, 0x43000000, v83
	ds_write_b128 v4, v[80:83] offset:3072
	v_mul_f32_e32 v84, 0x43000000, v84
	v_mul_f32_e32 v85, 0x43000000, v85
	v_mul_f32_e32 v86, 0x43000000, v86
	v_mul_f32_e32 v87, 0x43000000, v87
	ds_write_b128 v4, v[84:87] offset:4096
	v_mul_f32_e32 v88, 0x43000000, v88
	v_mul_f32_e32 v89, 0x43000000, v89
	v_mul_f32_e32 v90, 0x43000000, v90
	v_mul_f32_e32 v91, 0x43000000, v91
	ds_write_b128 v4, v[88:91] offset:5120
	v_mul_f32_e32 v92, 0x43000000, v92
	v_mul_f32_e32 v93, 0x43000000, v93
	v_mul_f32_e32 v94, 0x43000000, v94
	v_mul_f32_e32 v95, 0x43000000, v95
	ds_write_b128 v4, v[92:95] offset:6144
	v_mul_f32_e32 v96, 0x43000000, v96
	v_mul_f32_e32 v97, 0x43000000, v97
	v_mul_f32_e32 v98, 0x43000000, v98
	v_mul_f32_e32 v99, 0x43000000, v99
	ds_write_b128 v4, v[96:99] offset:7168
	s_waitcnt lgkmcnt(0)
	s_barrier
; #define GAS __attribute__((address_space(1)))
; #define LAS __attribute__((address_space(3)))
; #define LDS_WAIT() asm volatile("s_waitcnt lgkmcnt(0)" ::: "memory")
;     const int pr = item >> 1, kb = 2 * (pr / nblk) + (item & 1), nb = pr % nblk, k0 = 64 * kb, n0 = 32 * nb;
;     const int nr = n0 + (lane & 31); const int sc = MAP == 1 ? src_col_in(nr) : nr;
;     float v[32];
; #pragma unroll
;     for (int i = 0; i < 32; ++i) v[i] = sc >= 0 ? W[(size_t)(k0 + 2 * i + (lane >> 5)) * Nsrc + sc] : 0.f;
; #pragma unroll
;     for (int i = 0; i < 32; ++i) { const int k = k0 + 2 * i + (lane >> 5); float x = v[i] * wscale; if (KS) x *= (k < ksplit ? ksA[k] : ksB[k - ksplit]); scr[(2 * i + (lane >> 5)) * 33 + (lane & 31)] = x; }
;     LDS_WAIT(); asm volatile("" ::: "memory");
;     const int c = lane & 7;
; #pragma unroll
;     for (int j = 0; j < 4; ++j) { const int n = (lane >> 3) + 8 * j; const LAS float* s = scr + (8 * c) * 33 + n;
;         const unsigned long long o = (unsigned long long)pg8::pk4_fp8(s[0 * 33], s[1 * 33], s[2 * 33], s[3 * 33]) | ((unsigned long long)pg8::pk4_fp8(s[4 * 33], s[5 * 33], s[6 * 33], s[7 * 33]) << 32);
;         *(GAS unsigned long long*)(WT + (size_t)(n0 + n) * K + k0 + 8 * c) = o; }
;     LDS_WAIT(); asm volatile("" ::: "memory");
; }
; __global__ void __launch_bounds__(NWAVES * 64, 2) hybrid_fwd(Args args) {
;     ...
;             p0_transpose_item_f8<false>(args.in[16] + (size_t)l * FF * DM, FF, DM, DM / 32, (unsigned char*)(ws + WS_WDN + l * SZ_WDN), 128.f, args.in[16], args.in[16], 0, scr, r, lane);
	s_add_i32 s17, s16, 1248
	s_min_u32 s17, s17, 0xfff
	s_lshr_b32 s18, s17, 5
	s_add_i32 s18, s18, 0
	s_and_b32 s19, s17, 31
	s_lshl_b32 s18, s18, 21
	s_lshl_b32 s19, s19, 9
	s_add_u32 s18, s18, s19
	s_add_u32 s12, s2, s18
	s_addc_u32 s13, s3, 0
	global_load_dwordx4 v[68:71], v10, s[12:13]
	s_add_u32 s12, s12, 0x8000
	s_addc_u32 s13, s13, 0
	global_load_dwordx4 v[72:75], v10, s[12:13]
	s_add_u32 s12, s12, 0x8000
	s_addc_u32 s13, s13, 0
	global_load_dwordx4 v[76:79], v10, s[12:13]
	s_add_u32 s12, s12, 0x8000
	s_addc_u32 s13, s13, 0
	global_load_dwordx4 v[80:83], v10, s[12:13]
	s_add_u32 s12, s12, 0x8000
	s_addc_u32 s13, s13, 0
	global_load_dwordx4 v[84:87], v10, s[12:13]
	s_add_u32 s12, s12, 0x8000
	s_addc_u32 s13, s13, 0
	global_load_dwordx4 v[88:91], v10, s[12:13]
	s_add_u32 s12, s12, 0x8000
	s_addc_u32 s13, s13, 0
	global_load_dwordx4 v[92:95], v10, s[12:13]
	s_add_u32 s12, s12, 0x8000
	s_addc_u32 s13, s13, 0
	global_load_dwordx4 v[96:99], v10, s[12:13]
	s_add_i32 s17, s16, 960
	s_min_u32 s17, s17, 0xfff
	s_lshr_b32 s18, s17, 5
	s_add_i32 s18, s18, 0
	s_and_b32 s19, s17, 31
	s_lshl_b32 s19, s19, 21
	s_lshl_b32 s18, s18, 7
	s_add_u32 s18, s18, s19
	s_add_u32 s14, s4, s18
	s_addc_u32 s15, s5, 0
	ds_read_b32 v132, v6
	ds_read_b32 v133, v6 offset:512
	ds_read_b32 v134, v6 offset:1024
	ds_read_b32 v135, v6 offset:1536
	ds_read_b32 v136, v6 offset:2048
	ds_read_b32 v137, v6 offset:2560
	ds_read_b32 v138, v6 offset:3072
	ds_read_b32 v139, v6 offset:3584
	ds_read_b32 v140, v6 offset:4096
	ds_read_b32 v141, v6 offset:4608
	ds_read_b32 v142, v6 offset:5120
	ds_read_b32 v143, v6 offset:5632
	ds_read_b32 v144, v6 offset:6144
	ds_read_b32 v145, v6 offset:6656
	ds_read_b32 v146, v6 offset:7168
	ds_read_b32 v147, v6 offset:7680
	s_waitcnt lgkmcnt(0)
	v_max_f32_e32 v132, v132, v132
	v_max_f32_e32 v133, v133, v133
	v_max_f32_e32 v134, v134, v134
	v_max_f32_e32 v135, v135, v135
	v_max_f32_e32 v136, v136, v136
	v_max_f32_e32 v137, v137, v137
	v_max_f32_e32 v138, v138, v138
	v_max_f32_e32 v139, v139, v139
	v_max_f32_e32 v140, v140, v140
	v_max_f32_e32 v141, v141, v141
	v_max_f32_e32 v142, v142, v142
	v_max_f32_e32 v143, v143, v143
	v_max_f32_e32 v144, v144, v144
	v_max_f32_e32 v145, v145, v145
	v_max_f32_e32 v146, v146, v146
	v_max_f32_e32 v147, v147, v147
	v_med3_f32 v132, v132, s20, v13
	v_med3_f32 v133, v133, s20, v13
	v_med3_f32 v134, v134, s20, v13
	v_med3_f32 v135, v135, s20, v13
	v_med3_f32 v136, v136, s20, v13
	v_med3_f32 v137, v137, s20, v13
	v_med3_f32 v138, v138, s20, v13
	v_med3_f32 v139, v139, s20, v13
	v_med3_f32 v140, v140, s20, v13
	v_med3_f32 v141, v141, s20, v13
	v_med3_f32 v142, v142, s20, v13
	v_med3_f32 v143, v143, s20, v13
	v_med3_f32 v144, v144, s20, v13
	v_med3_f32 v145, v145, s20, v13
	v_med3_f32 v146, v146, s20, v13
	v_med3_f32 v147, v147, s20, v13
	v_mov_b32_e32 v148, 0
	v_mov_b32_e32 v149, 0
	v_mov_b32_e32 v150, 0
	v_mov_b32_e32 v151, 0
	v_cvt_pk_fp8_f32 v148, v132, v133
	v_cvt_pk_fp8_f32 v149, v136, v137
	v_cvt_pk_fp8_f32 v150, v140, v141
	v_cvt_pk_fp8_f32 v151, v144, v145
	v_cvt_pk_fp8_f32 v148, v134, v135 op_sel:[0,0,1]
	v_cvt_pk_fp8_f32 v149, v138, v139 op_sel:[0,0,1]
	v_cvt_pk_fp8_f32 v150, v142, v143 op_sel:[0,0,1]
	v_cvt_pk_fp8_f32 v151, v146, v147 op_sel:[0,0,1]
	s_nop 0
	global_store_dwordx4 v11, v[148:151], s[14:15]
	ds_read_b32 v132, v8
	ds_read_b32 v133, v8 offset:512
	ds_read_b32 v134, v8 offset:1024
	ds_read_b32 v135, v8 offset:1536
	ds_read_b32 v136, v8 offset:2048
	ds_read_b32 v137, v8 offset:2560
	ds_read_b32 v138, v8 offset:3072
	ds_read_b32 v139, v8 offset:3584
	ds_read_b32 v140, v8 offset:4096
	ds_read_b32 v141, v8 offset:4608
	ds_read_b32 v142, v8 offset:5120
	ds_read_b32 v143, v8 offset:5632
	ds_read_b32 v144, v8 offset:6144
	ds_read_b32 v145, v8 offset:6656
	ds_read_b32 v146, v8 offset:7168
	ds_read_b32 v147, v8 offset:7680
	s_waitcnt lgkmcnt(0)
	v_max_f32_e32 v132, v132, v132
	v_max_f32_e32 v133, v133, v133
	v_max_f32_e32 v134, v134, v134
	v_max_f32_e32 v135, v135, v135
	v_max_f32_e32 v136, v136, v136
	v_max_f32_e32 v137, v137, v137
	v_max_f32_e32 v138, v138, v138
	v_max_f32_e32 v139, v139, v139
	v_max_f32_e32 v140, v140, v140
	v_max_f32_e32 v141, v141, v141
	v_max_f32_e32 v142, v142, v142
	v_max_f32_e32 v143, v143, v143
	v_max_f32_e32 v144, v144, v144
	v_max_f32_e32 v145, v145, v145
	v_max_f32_e32 v146, v146, v146
	v_max_f32_e32 v147, v147, v147
	v_med3_f32 v132, v132, s20, v13
	v_med3_f32 v133, v133, s20, v13
	v_med3_f32 v134, v134, s20, v13
	v_med3_f32 v135, v135, s20, v13
	v_med3_f32 v136, v136, s20, v13
	v_med3_f32 v137, v137, s20, v13
	v_med3_f32 v138, v138, s20, v13
	v_med3_f32 v139, v139, s20, v13
	v_med3_f32 v140, v140, s20, v13
	v_med3_f32 v141, v141, s20, v13
	v_med3_f32 v142, v142, s20, v13
	v_med3_f32 v143, v143, s20, v13
	v_med3_f32 v144, v144, s20, v13
	v_med3_f32 v145, v145, s20, v13
	v_med3_f32 v146, v146, s20, v13
	v_med3_f32 v147, v147, s20, v13
	v_mov_b32_e32 v148, 0
	v_mov_b32_e32 v149, 0
	v_mov_b32_e32 v150, 0
	v_mov_b32_e32 v151, 0
	v_cvt_pk_fp8_f32 v148, v132, v133
	v_cvt_pk_fp8_f32 v149, v136, v137
	v_cvt_pk_fp8_f32 v150, v140, v141
	v_cvt_pk_fp8_f32 v151, v144, v145
	v_cvt_pk_fp8_f32 v148, v134, v135 op_sel:[0,0,1]
	v_cvt_pk_fp8_f32 v149, v138, v139 op_sel:[0,0,1]
	v_cvt_pk_fp8_f32 v150, v142, v143 op_sel:[0,0,1]
	v_cvt_pk_fp8_f32 v151, v146, v147 op_sel:[0,0,1]
	s_nop 0
	global_store_dwordx4 v12, v[148:151], s[14:15]
	s_waitcnt vmcnt(22)
	v_mul_f32_e32 v100, 0x43000000, v100
	v_mul_f32_e32 v101, 0x43000000, v101
	v_mul_f32_e32 v102, 0x43000000, v102
	v_mul_f32_e32 v103, 0x43000000, v103
	ds_write_b128 v5, v[100:103]
	v_mul_f32_e32 v104, 0x43000000, v104
	v_mul_f32_e32 v105, 0x43000000, v105
	v_mul_f32_e32 v106, 0x43000000, v106
	v_mul_f32_e32 v107, 0x43000000, v107
	ds_write_b128 v5, v[104:107] offset:1024
	v_mul_f32_e32 v108, 0x43000000, v108
	v_mul_f32_e32 v109, 0x43000000, v109
	v_mul_f32_e32 v110, 0x43000000, v110
	v_mul_f32_e32 v111, 0x43000000, v111
	ds_write_b128 v5, v[108:111] offset:2048
	v_mul_f32_e32 v112, 0x43000000, v112
	v_mul_f32_e32 v113, 0x43000000, v113
	v_mul_f32_e32 v114, 0x43000000, v114
	v_mul_f32_e32 v115, 0x43000000, v115
	ds_write_b128 v5, v[112:115] offset:3072
	v_mul_f32_e32 v116, 0x43000000, v116
	v_mul_f32_e32 v117, 0x43000000, v117
	v_mul_f32_e32 v118, 0x43000000, v118
	v_mul_f32_e32 v119, 0x43000000, v119
	ds_write_b128 v5, v[116:119] offset:4096
	v_mul_f32_e32 v120, 0x43000000, v120
	v_mul_f32_e32 v121, 0x43000000, v121
	v_mul_f32_e32 v122, 0x43000000, v122
	v_mul_f32_e32 v123, 0x43000000, v123
	ds_write_b128 v5, v[120:123] offset:5120
	v_mul_f32_e32 v124, 0x43000000, v124
	v_mul_f32_e32 v125, 0x43000000, v125
	v_mul_f32_e32 v126, 0x43000000, v126
	v_mul_f32_e32 v127, 0x43000000, v127
	ds_write_b128 v5, v[124:127] offset:6144
	v_mul_f32_e32 v128, 0x43000000, v128
	v_mul_f32_e32 v129, 0x43000000, v129
	v_mul_f32_e32 v130, 0x43000000, v130
	v_mul_f32_e32 v131, 0x43000000, v131
	ds_write_b128 v5, v[128:131] offset:7168
	s_waitcnt lgkmcnt(0)
	s_barrier
; #define GAS __attribute__((address_space(1)))
; #define LAS __attribute__((address_space(3)))
; #define LDS_WAIT() asm volatile("s_waitcnt lgkmcnt(0)" ::: "memory")
;     const int pr = item >> 1, kb = 2 * (pr / nblk) + (item & 1), nb = pr % nblk, k0 = 64 * kb, n0 = 32 * nb;
;     const int nr = n0 + (lane & 31); const int sc = MAP == 1 ? src_col_in(nr) : nr;
;     float v[32];
; #pragma unroll
;     for (int i = 0; i < 32; ++i) v[i] = sc >= 0 ? W[(size_t)(k0 + 2 * i + (lane >> 5)) * Nsrc + sc] : 0.f;
; #pragma unroll
;     for (int i = 0; i < 32; ++i) { const int k = k0 + 2 * i + (lane >> 5); float x = v[i] * wscale; if (KS) x *= (k < ksplit ? ksA[k] : ksB[k - ksplit]); scr[(2 * i + (lane >> 5)) * 33 + (lane & 31)] = x; }
;     LDS_WAIT(); asm volatile("" ::: "memory");
;     const int c = lane & 7;
; #pragma unroll
;     for (int j = 0; j < 4; ++j) { const int n = (lane >> 3) + 8 * j; const LAS float* s = scr + (8 * c) * 33 + n;
;         const unsigned long long o = (unsigned long long)pg8::pk4_fp8(s[0 * 33], s[1 * 33], s[2 * 33], s[3 * 33]) | ((unsigned long long)pg8::pk4_fp8(s[4 * 33], s[5 * 33], s[6 * 33], s[7 * 33]) << 32);
;         *(GAS unsigned long long*)(WT + (size_t)(n0 + n) * K + k0 + 8 * c) = o; }
;     LDS_WAIT(); asm volatile("" ::: "memory");
; }
; __global__ void __launch_bounds__(NWAVES * 64, 2) hybrid_fwd(Args args) {
;     ...
;             p0_transpose_item_f8<false>(args.in[16] + (size_t)l * FF * DM, FF, DM, DM / 32, (unsigned char*)(ws + WS_WDN + l * SZ_WDN), 128.f, args.in[16], args.in[16], 0, scr, r, lane);
	s_add_i32 s17, s16, 1344
	s_min_u32 s17, s17, 0xfff
	s_lshr_b32 s18, s17, 5
	s_add_i32 s18, s18, 0
	s_and_b32 s19, s17, 31
	s_lshl_b32 s18, s18, 21
	s_lshl_b32 s19, s19, 9
	s_add_u32 s18, s18, s19
	s_add_u32 s12, s2, s18
	s_addc_u32 s13, s3, 0
	global_load_dwordx4 v[100:103], v10, s[12:13]
	s_add_u32 s12, s12, 0x8000
	s_addc_u32 s13, s13, 0
	global_load_dwordx4 v[104:107], v10, s[12:13]
	s_add_u32 s12, s12, 0x8000
	s_addc_u32 s13, s13, 0
	global_load_dwordx4 v[108:111], v10, s[12:13]
	s_add_u32 s12, s12, 0x8000
	s_addc_u32 s13, s13, 0
	global_load_dwordx4 v[112:115], v10, s[12:13]
	s_add_u32 s12, s12, 0x8000
	s_addc_u32 s13, s13, 0
	global_load_dwordx4 v[116:119], v10, s[12:13]
	s_add_u32 s12, s12, 0x8000
	s_addc_u32 s13, s13, 0
	global_load_dwordx4 v[120:123], v10, s[12:13]
	s_add_u32 s12, s12, 0x8000
	s_addc_u32 s13, s13, 0
	global_load_dwordx4 v[124:127], v10, s[12:13]
	s_add_u32 s12, s12, 0x8000
	s_addc_u32 s13, s13, 0
	global_load_dwordx4 v[128:131], v10, s[12:13]
	s_add_i32 s17, s16, 1056
	s_min_u32 s17, s17, 0xfff
	s_lshr_b32 s18, s17, 5
	s_add_i32 s18, s18, 0
	s_and_b32 s19, s17, 31
	s_lshl_b32 s19, s19, 21
	s_lshl_b32 s18, s18, 7
	s_add_u32 s18, s18, s19
	s_add_u32 s14, s4, s18
	s_addc_u32 s15, s5, 0
	ds_read_b32 v132, v7
	ds_read_b32 v133, v7 offset:512
	ds_read_b32 v134, v7 offset:1024
	ds_read_b32 v135, v7 offset:1536
	ds_read_b32 v136, v7 offset:2048
	ds_read_b32 v137, v7 offset:2560
	ds_read_b32 v138, v7 offset:3072
	ds_read_b32 v139, v7 offset:3584
	ds_read_b32 v140, v7 offset:4096
	ds_read_b32 v141, v7 offset:4608
	ds_read_b32 v142, v7 offset:5120
	ds_read_b32 v143, v7 offset:5632
	ds_read_b32 v144, v7 offset:6144
	ds_read_b32 v145, v7 offset:6656
	ds_read_b32 v146, v7 offset:7168
	ds_read_b32 v147, v7 offset:7680
	s_waitcnt lgkmcnt(0)
	v_max_f32_e32 v132, v132, v132
	v_max_f32_e32 v133, v133, v133
	v_max_f32_e32 v134, v134, v134
	v_max_f32_e32 v135, v135, v135
	v_max_f32_e32 v136, v136, v136
	v_max_f32_e32 v137, v137, v137
	v_max_f32_e32 v138, v138, v138
	v_max_f32_e32 v139, v139, v139
	v_max_f32_e32 v140, v140, v140
	v_max_f32_e32 v141, v141, v141
	v_max_f32_e32 v142, v142, v142
	v_max_f32_e32 v143, v143, v143
	v_max_f32_e32 v144, v144, v144
	v_max_f32_e32 v145, v145, v145
	v_max_f32_e32 v146, v146, v146
	v_max_f32_e32 v147, v147, v147
	v_med3_f32 v132, v132, s20, v13
	v_med3_f32 v133, v133, s20, v13
	v_med3_f32 v134, v134, s20, v13
	v_med3_f32 v135, v135, s20, v13
	v_med3_f32 v136, v136, s20, v13
	v_med3_f32 v137, v137, s20, v13
	v_med3_f32 v138, v138, s20, v13
	v_med3_f32 v139, v139, s20, v13
	v_med3_f32 v140, v140, s20, v13
	v_med3_f32 v141, v141, s20, v13
	v_med3_f32 v142, v142, s20, v13
	v_med3_f32 v143, v143, s20, v13
	v_med3_f32 v144, v144, s20, v13
	v_med3_f32 v145, v145, s20, v13
	v_med3_f32 v146, v146, s20, v13
	v_med3_f32 v147, v147, s20, v13
	v_mov_b32_e32 v148, 0
	v_mov_b32_e32 v149, 0
	v_mov_b32_e32 v150, 0
	v_mov_b32_e32 v151, 0
	v_cvt_pk_fp8_f32 v148, v132, v133
	v_cvt_pk_fp8_f32 v149, v136, v137
	v_cvt_pk_fp8_f32 v150, v140, v141
	v_cvt_pk_fp8_f32 v151, v144, v145
	v_cvt_pk_fp8_f32 v148, v134, v135 op_sel:[0,0,1]
	v_cvt_pk_fp8_f32 v149, v138, v139 op_sel:[0,0,1]
	v_cvt_pk_fp8_f32 v150, v142, v143 op_sel:[0,0,1]
	v_cvt_pk_fp8_f32 v151, v146, v147 op_sel:[0,0,1]
	s_nop 0
	global_store_dwordx4 v11, v[148:151], s[14:15]
	ds_read_b32 v132, v9
	ds_read_b32 v133, v9 offset:512
	ds_read_b32 v134, v9 offset:1024
	ds_read_b32 v135, v9 offset:1536
	ds_read_b32 v136, v9 offset:2048
	ds_read_b32 v137, v9 offset:2560
	ds_read_b32 v138, v9 offset:3072
	ds_read_b32 v139, v9 offset:3584
	ds_read_b32 v140, v9 offset:4096
	ds_read_b32 v141, v9 offset:4608
	ds_read_b32 v142, v9 offset:5120
	ds_read_b32 v143, v9 offset:5632
	ds_read_b32 v144, v9 offset:6144
	ds_read_b32 v145, v9 offset:6656
	ds_read_b32 v146, v9 offset:7168
	ds_read_b32 v147, v9 offset:7680
	s_waitcnt lgkmcnt(0)
	v_max_f32_e32 v132, v132, v132
	v_max_f32_e32 v133, v133, v133
	v_max_f32_e32 v134, v134, v134
	v_max_f32_e32 v135, v135, v135
	v_max_f32_e32 v136, v136, v136
	v_max_f32_e32 v137, v137, v137
	v_max_f32_e32 v138, v138, v138
	v_max_f32_e32 v139, v139, v139
	v_max_f32_e32 v140, v140, v140
	v_max_f32_e32 v141, v141, v141
	v_max_f32_e32 v142, v142, v142
	v_max_f32_e32 v143, v143, v143
	v_max_f32_e32 v144, v144, v144
	v_max_f32_e32 v145, v145, v145
	v_max_f32_e32 v146, v146, v146
	v_max_f32_e32 v147, v147, v147
	v_med3_f32 v132, v132, s20, v13
	v_med3_f32 v133, v133, s20, v13
	v_med3_f32 v134, v134, s20, v13
	v_med3_f32 v135, v135, s20, v13
	v_med3_f32 v136, v136, s20, v13
	v_med3_f32 v137, v137, s20, v13
	v_med3_f32 v138, v138, s20, v13
	v_med3_f32 v139, v139, s20, v13
	v_med3_f32 v140, v140, s20, v13
	v_med3_f32 v141, v141, s20, v13
	v_med3_f32 v142, v142, s20, v13
	v_med3_f32 v143, v143, s20, v13
	v_med3_f32 v144, v144, s20, v13
	v_med3_f32 v145, v145, s20, v13
	v_med3_f32 v146, v146, s20, v13
	v_med3_f32 v147, v147, s20, v13
	v_mov_b32_e32 v148, 0
	v_mov_b32_e32 v149, 0
	v_mov_b32_e32 v150, 0
	v_mov_b32_e32 v151, 0
	v_cvt_pk_fp8_f32 v148, v132, v133
	v_cvt_pk_fp8_f32 v149, v136, v137
	v_cvt_pk_fp8_f32 v150, v140, v141
	v_cvt_pk_fp8_f32 v151, v144, v145
	v_cvt_pk_fp8_f32 v148, v134, v135 op_sel:[0,0,1]
	v_cvt_pk_fp8_f32 v149, v138, v139 op_sel:[0,0,1]
	v_cvt_pk_fp8_f32 v150, v142, v143 op_sel:[0,0,1]
	v_cvt_pk_fp8_f32 v151, v146, v147 op_sel:[0,0,1]
	s_nop 0
	global_store_dwordx4 v12, v[148:151], s[14:15]
	s_waitcnt vmcnt(22)
	v_mul_f32_e32 v36, 0x43000000, v36
	v_mul_f32_e32 v37, 0x43000000, v37
	v_mul_f32_e32 v38, 0x43000000, v38
	v_mul_f32_e32 v39, 0x43000000, v39
	ds_write_b128 v4, v[36:39]
	v_mul_f32_e32 v40, 0x43000000, v40
	v_mul_f32_e32 v41, 0x43000000, v41
	v_mul_f32_e32 v42, 0x43000000, v42
	v_mul_f32_e32 v43, 0x43000000, v43
	ds_write_b128 v4, v[40:43] offset:1024
	v_mul_f32_e32 v44, 0x43000000, v44
	v_mul_f32_e32 v45, 0x43000000, v45
	v_mul_f32_e32 v46, 0x43000000, v46
	v_mul_f32_e32 v47, 0x43000000, v47
	ds_write_b128 v4, v[44:47] offset:2048
	v_mul_f32_e32 v48, 0x43000000, v48
	v_mul_f32_e32 v49, 0x43000000, v49
	v_mul_f32_e32 v50, 0x43000000, v50
	v_mul_f32_e32 v51, 0x43000000, v51
	ds_write_b128 v4, v[48:51] offset:3072
	v_mul_f32_e32 v52, 0x43000000, v52
	v_mul_f32_e32 v53, 0x43000000, v53
	v_mul_f32_e32 v54, 0x43000000, v54
	v_mul_f32_e32 v55, 0x43000000, v55
	ds_write_b128 v4, v[52:55] offset:4096
	v_mul_f32_e32 v56, 0x43000000, v56
	v_mul_f32_e32 v57, 0x43000000, v57
	v_mul_f32_e32 v58, 0x43000000, v58
	v_mul_f32_e32 v59, 0x43000000, v59
	ds_write_b128 v4, v[56:59] offset:5120
	v_mul_f32_e32 v60, 0x43000000, v60
	v_mul_f32_e32 v61, 0x43000000, v61
	v_mul_f32_e32 v62, 0x43000000, v62
	v_mul_f32_e32 v63, 0x43000000, v63
	ds_write_b128 v4, v[60:63] offset:6144
	v_mul_f32_e32 v64, 0x43000000, v64
	v_mul_f32_e32 v65, 0x43000000, v65
	v_mul_f32_e32 v66, 0x43000000, v66
	v_mul_f32_e32 v67, 0x43000000, v67
	ds_write_b128 v4, v[64:67] offset:7168
	s_waitcnt lgkmcnt(0)
	s_barrier
; #define GAS __attribute__((address_space(1)))
; #define LAS __attribute__((address_space(3)))
; #define LDS_WAIT() asm volatile("s_waitcnt lgkmcnt(0)" ::: "memory")
;     const int pr = item >> 1, kb = 2 * (pr / nblk) + (item & 1), nb = pr % nblk, k0 = 64 * kb, n0 = 32 * nb;
;     const int nr = n0 + (lane & 31); const int sc = MAP == 1 ? src_col_in(nr) : nr;
;     float v[32];
; #pragma unroll
;     for (int i = 0; i < 32; ++i) v[i] = sc >= 0 ? W[(size_t)(k0 + 2 * i + (lane >> 5)) * Nsrc + sc] : 0.f;
; #pragma unroll
;     for (int i = 0; i < 32; ++i) { const int k = k0 + 2 * i + (lane >> 5); float x = v[i] * wscale; if (KS) x *= (k < ksplit ? ksA[k] : ksB[k - ksplit]); scr[(2 * i + (lane >> 5)) * 33 + (lane & 31)] = x; }
;     LDS_WAIT(); asm volatile("" ::: "memory");
;     const int c = lane & 7;
; #pragma unroll
;     for (int j = 0; j < 4; ++j) { const int n = (lane >> 3) + 8 * j; const LAS float* s = scr + (8 * c) * 33 + n;
;         const unsigned long long o = (unsigned long long)pg8::pk4_fp8(s[0 * 33], s[1 * 33], s[2 * 33], s[3 * 33]) | ((unsigned long long)pg8::pk4_fp8(s[4 * 33], s[5 * 33], s[6 * 33], s[7 * 33]) << 32);
;         *(GAS unsigned long long*)(WT + (size_t)(n0 + n) * K + k0 + 8 * c) = o; }
;     LDS_WAIT(); asm volatile("" ::: "memory");
; }
; __global__ void __launch_bounds__(NWAVES * 64, 2) hybrid_fwd(Args args) {
;     ...
;             p0_transpose_item_f8<false>(args.in[16] + (size_t)l * FF * DM, FF, DM, DM / 32, (unsigned char*)(ws + WS_WDN + l * SZ_WDN), 128.f, args.in[16], args.in[16], 0, scr, r, lane);
	s_add_i32 s17, s16, 1440
	s_min_u32 s17, s17, 0xfff
	s_lshr_b32 s18, s17, 5
	s_add_i32 s18, s18, 0
	s_and_b32 s19, s17, 31
	s_lshl_b32 s18, s18, 21
	s_lshl_b32 s19, s19, 9
	s_add_u32 s18, s18, s19
	s_add_u32 s12, s2, s18
	s_addc_u32 s13, s3, 0
	global_load_dwordx4 v[36:39], v10, s[12:13]
	s_add_u32 s12, s12, 0x8000
	s_addc_u32 s13, s13, 0
	global_load_dwordx4 v[40:43], v10, s[12:13]
	s_add_u32 s12, s12, 0x8000
	s_addc_u32 s13, s13, 0
	global_load_dwordx4 v[44:47], v10, s[12:13]
	s_add_u32 s12, s12, 0x8000
	s_addc_u32 s13, s13, 0
	global_load_dwordx4 v[48:51], v10, s[12:13]
	s_add_u32 s12, s12, 0x8000
	s_addc_u32 s13, s13, 0
	global_load_dwordx4 v[52:55], v10, s[12:13]
	s_add_u32 s12, s12, 0x8000
	s_addc_u32 s13, s13, 0
	global_load_dwordx4 v[56:59], v10, s[12:13]
	s_add_u32 s12, s12, 0x8000
	s_addc_u32 s13, s13, 0
	global_load_dwordx4 v[60:63], v10, s[12:13]
	s_add_u32 s12, s12, 0x8000
	s_addc_u32 s13, s13, 0
	global_load_dwordx4 v[64:67], v10, s[12:13]
	s_add_i32 s17, s16, 1152
	s_min_u32 s17, s17, 0xfff
	s_lshr_b32 s18, s17, 5
	s_add_i32 s18, s18, 0
	s_and_b32 s19, s17, 31
	s_lshl_b32 s19, s19, 21
	s_lshl_b32 s18, s18, 7
	s_add_u32 s18, s18, s19
	s_add_u32 s14, s4, s18
	s_addc_u32 s15, s5, 0
	ds_read_b32 v132, v6
	ds_read_b32 v133, v6 offset:512
	ds_read_b32 v134, v6 offset:1024
	ds_read_b32 v135, v6 offset:1536
	ds_read_b32 v136, v6 offset:2048
	ds_read_b32 v137, v6 offset:2560
	ds_read_b32 v138, v6 offset:3072
	ds_read_b32 v139, v6 offset:3584
	ds_read_b32 v140, v6 offset:4096
	ds_read_b32 v141, v6 offset:4608
	ds_read_b32 v142, v6 offset:5120
	ds_read_b32 v143, v6 offset:5632
	ds_read_b32 v144, v6 offset:6144
	ds_read_b32 v145, v6 offset:6656
	ds_read_b32 v146, v6 offset:7168
	ds_read_b32 v147, v6 offset:7680
	s_waitcnt lgkmcnt(0)
	v_max_f32_e32 v132, v132, v132
	v_max_f32_e32 v133, v133, v133
	v_max_f32_e32 v134, v134, v134
	v_max_f32_e32 v135, v135, v135
	v_max_f32_e32 v136, v136, v136
	v_max_f32_e32 v137, v137, v137
	v_max_f32_e32 v138, v138, v138
	v_max_f32_e32 v139, v139, v139
	v_max_f32_e32 v140, v140, v140
	v_max_f32_e32 v141, v141, v141
	v_max_f32_e32 v142, v142, v142
	v_max_f32_e32 v143, v143, v143
	v_max_f32_e32 v144, v144, v144
	v_max_f32_e32 v145, v145, v145
	v_max_f32_e32 v146, v146, v146
	v_max_f32_e32 v147, v147, v147
	v_med3_f32 v132, v132, s20, v13
	v_med3_f32 v133, v133, s20, v13
	v_med3_f32 v134, v134, s20, v13
	v_med3_f32 v135, v135, s20, v13
	v_med3_f32 v136, v136, s20, v13
	v_med3_f32 v137, v137, s20, v13
	v_med3_f32 v138, v138, s20, v13
	v_med3_f32 v139, v139, s20, v13
	v_med3_f32 v140, v140, s20, v13
	v_med3_f32 v141, v141, s20, v13
	v_med3_f32 v142, v142, s20, v13
	v_med3_f32 v143, v143, s20, v13
	v_med3_f32 v144, v144, s20, v13
	v_med3_f32 v145, v145, s20, v13
	v_med3_f32 v146, v146, s20, v13
	v_med3_f32 v147, v147, s20, v13
	v_mov_b32_e32 v148, 0
	v_mov_b32_e32 v149, 0
	v_mov_b32_e32 v150, 0
	v_mov_b32_e32 v151, 0
	v_cvt_pk_fp8_f32 v148, v132, v133
	v_cvt_pk_fp8_f32 v149, v136, v137
	v_cvt_pk_fp8_f32 v150, v140, v141
	v_cvt_pk_fp8_f32 v151, v144, v145
	v_cvt_pk_fp8_f32 v148, v134, v135 op_sel:[0,0,1]
	v_cvt_pk_fp8_f32 v149, v138, v139 op_sel:[0,0,1]
	v_cvt_pk_fp8_f32 v150, v142, v143 op_sel:[0,0,1]
	v_cvt_pk_fp8_f32 v151, v146, v147 op_sel:[0,0,1]
	s_nop 0
	global_store_dwordx4 v11, v[148:151], s[14:15]
	ds_read_b32 v132, v8
	ds_read_b32 v133, v8 offset:512
	ds_read_b32 v134, v8 offset:1024
	ds_read_b32 v135, v8 offset:1536
	ds_read_b32 v136, v8 offset:2048
	ds_read_b32 v137, v8 offset:2560
	ds_read_b32 v138, v8 offset:3072
	ds_read_b32 v139, v8 offset:3584
	ds_read_b32 v140, v8 offset:4096
	ds_read_b32 v141, v8 offset:4608
	ds_read_b32 v142, v8 offset:5120
	ds_read_b32 v143, v8 offset:5632
	ds_read_b32 v144, v8 offset:6144
	ds_read_b32 v145, v8 offset:6656
	ds_read_b32 v146, v8 offset:7168
	ds_read_b32 v147, v8 offset:7680
	s_waitcnt lgkmcnt(0)
	v_max_f32_e32 v132, v132, v132
	v_max_f32_e32 v133, v133, v133
	v_max_f32_e32 v134, v134, v134
	v_max_f32_e32 v135, v135, v135
	v_max_f32_e32 v136, v136, v136
	v_max_f32_e32 v137, v137, v137
	v_max_f32_e32 v138, v138, v138
	v_max_f32_e32 v139, v139, v139
	v_max_f32_e32 v140, v140, v140
	v_max_f32_e32 v141, v141, v141
	v_max_f32_e32 v142, v142, v142
	v_max_f32_e32 v143, v143, v143
	v_max_f32_e32 v144, v144, v144
	v_max_f32_e32 v145, v145, v145
	v_max_f32_e32 v146, v146, v146
	v_max_f32_e32 v147, v147, v147
	v_med3_f32 v132, v132, s20, v13
	v_med3_f32 v133, v133, s20, v13
	v_med3_f32 v134, v134, s20, v13
	v_med3_f32 v135, v135, s20, v13
	v_med3_f32 v136, v136, s20, v13
	v_med3_f32 v137, v137, s20, v13
	v_med3_f32 v138, v138, s20, v13
	v_med3_f32 v139, v139, s20, v13
	v_med3_f32 v140, v140, s20, v13
	v_med3_f32 v141, v141, s20, v13
	v_med3_f32 v142, v142, s20, v13
	v_med3_f32 v143, v143, s20, v13
	v_med3_f32 v144, v144, s20, v13
	v_med3_f32 v145, v145, s20, v13
	v_med3_f32 v146, v146, s20, v13
	v_med3_f32 v147, v147, s20, v13
	v_mov_b32_e32 v148, 0
	v_mov_b32_e32 v149, 0
	v_mov_b32_e32 v150, 0
	v_mov_b32_e32 v151, 0
	v_cvt_pk_fp8_f32 v148, v132, v133
	v_cvt_pk_fp8_f32 v149, v136, v137
	v_cvt_pk_fp8_f32 v150, v140, v141
	v_cvt_pk_fp8_f32 v151, v144, v145
	v_cvt_pk_fp8_f32 v148, v134, v135 op_sel:[0,0,1]
	v_cvt_pk_fp8_f32 v149, v138, v139 op_sel:[0,0,1]
	v_cvt_pk_fp8_f32 v150, v142, v143 op_sel:[0,0,1]
	v_cvt_pk_fp8_f32 v151, v146, v147 op_sel:[0,0,1]
	s_nop 0
	global_store_dwordx4 v12, v[148:151], s[14:15]
	s_waitcnt vmcnt(22)
	v_mul_f32_e32 v68, 0x43000000, v68
	v_mul_f32_e32 v69, 0x43000000, v69
	v_mul_f32_e32 v70, 0x43000000, v70
	v_mul_f32_e32 v71, 0x43000000, v71
	ds_write_b128 v5, v[68:71]
	v_mul_f32_e32 v72, 0x43000000, v72
	v_mul_f32_e32 v73, 0x43000000, v73
	v_mul_f32_e32 v74, 0x43000000, v74
	v_mul_f32_e32 v75, 0x43000000, v75
	ds_write_b128 v5, v[72:75] offset:1024
	v_mul_f32_e32 v76, 0x43000000, v76
	v_mul_f32_e32 v77, 0x43000000, v77
	v_mul_f32_e32 v78, 0x43000000, v78
	v_mul_f32_e32 v79, 0x43000000, v79
	ds_write_b128 v5, v[76:79] offset:2048
	v_mul_f32_e32 v80, 0x43000000, v80
	v_mul_f32_e32 v81, 0x43000000, v81
	v_mul_f32_e32 v82, 0x43000000, v82
	v_mul_f32_e32 v83, 0x43000000, v83
	ds_write_b128 v5, v[80:83] offset:3072
	v_mul_f32_e32 v84, 0x43000000, v84
	v_mul_f32_e32 v85, 0x43000000, v85
	v_mul_f32_e32 v86, 0x43000000, v86
	v_mul_f32_e32 v87, 0x43000000, v87
	ds_write_b128 v5, v[84:87] offset:4096
	v_mul_f32_e32 v88, 0x43000000, v88
	v_mul_f32_e32 v89, 0x43000000, v89
	v_mul_f32_e32 v90, 0x43000000, v90
	v_mul_f32_e32 v91, 0x43000000, v91
	ds_write_b128 v5, v[88:91] offset:5120
	v_mul_f32_e32 v92, 0x43000000, v92
	v_mul_f32_e32 v93, 0x43000000, v93
	v_mul_f32_e32 v94, 0x43000000, v94
	v_mul_f32_e32 v95, 0x43000000, v95
	ds_write_b128 v5, v[92:95] offset:6144
	v_mul_f32_e32 v96, 0x43000000, v96
	v_mul_f32_e32 v97, 0x43000000, v97
	v_mul_f32_e32 v98, 0x43000000, v98
	v_mul_f32_e32 v99, 0x43000000, v99
	ds_write_b128 v5, v[96:99] offset:7168
	s_waitcnt lgkmcnt(0)
	s_barrier
; #define GAS __attribute__((address_space(1)))
; #define LAS __attribute__((address_space(3)))
; #define LDS_WAIT() asm volatile("s_waitcnt lgkmcnt(0)" ::: "memory")
;     const int pr = item >> 1, kb = 2 * (pr / nblk) + (item & 1), nb = pr % nblk, k0 = 64 * kb, n0 = 32 * nb;
;     const int nr = n0 + (lane & 31); const int sc = MAP == 1 ? src_col_in(nr) : nr;
;     float v[32];
; #pragma unroll
;     for (int i = 0; i < 32; ++i) v[i] = sc >= 0 ? W[(size_t)(k0 + 2 * i + (lane >> 5)) * Nsrc + sc] : 0.f;
; #pragma unroll
;     for (int i = 0; i < 32; ++i) { const int k = k0 + 2 * i + (lane >> 5); float x = v[i] * wscale; if (KS) x *= (k < ksplit ? ksA[k] : ksB[k - ksplit]); scr[(2 * i + (lane >> 5)) * 33 + (lane & 31)] = x; }
;     LDS_WAIT(); asm volatile("" ::: "memory");
;     const int c = lane & 7;
; #pragma unroll
;     for (int j = 0; j < 4; ++j) { const int n = (lane >> 3) + 8 * j; const LAS float* s = scr + (8 * c) * 33 + n;
;         const unsigned long long o = (unsigned long long)pg8::pk4_fp8(s[0 * 33], s[1 * 33], s[2 * 33], s[3 * 33]) | ((unsigned long long)pg8::pk4_fp8(s[4 * 33], s[5 * 33], s[6 * 33], s[7 * 33]) << 32);
;         *(GAS unsigned long long*)(WT + (size_t)(n0 + n) * K + k0 + 8 * c) = o; }
;     LDS_WAIT(); asm volatile("" ::: "memory");
; }
; __global__ void __launch_bounds__(NWAVES * 64, 2) hybrid_fwd(Args args) {
;     ...
;             p0_transpose_item_f8<false>(args.in[16] + (size_t)l * FF * DM, FF, DM, DM / 32, (unsigned char*)(ws + WS_WDN + l * SZ_WDN), 128.f, args.in[16], args.in[16], 0, scr, r, lane);
	s_add_i32 s17, s16, 1536
	s_min_u32 s17, s17, 0xfff
	s_lshr_b32 s18, s17, 5
	s_add_i32 s18, s18, 0
	s_and_b32 s19, s17, 31
	s_lshl_b32 s18, s18, 21
	s_lshl_b32 s19, s19, 9
	s_add_u32 s18, s18, s19
	s_add_u32 s12, s2, s18
	s_addc_u32 s13, s3, 0
	global_load_dwordx4 v[68:71], v10, s[12:13]
	s_add_u32 s12, s12, 0x8000
	s_addc_u32 s13, s13, 0
	global_load_dwordx4 v[72:75], v10, s[12:13]
	s_add_u32 s12, s12, 0x8000
	s_addc_u32 s13, s13, 0
	global_load_dwordx4 v[76:79], v10, s[12:13]
	s_add_u32 s12, s12, 0x8000
	s_addc_u32 s13, s13, 0
	global_load_dwordx4 v[80:83], v10, s[12:13]
	s_add_u32 s12, s12, 0x8000
	s_addc_u32 s13, s13, 0
	global_load_dwordx4 v[84:87], v10, s[12:13]
	s_add_u32 s12, s12, 0x8000
	s_addc_u32 s13, s13, 0
	global_load_dwordx4 v[88:91], v10, s[12:13]
	s_add_u32 s12, s12, 0x8000
	s_addc_u32 s13, s13, 0
	global_load_dwordx4 v[92:95], v10, s[12:13]
	s_add_u32 s12, s12, 0x8000
	s_addc_u32 s13, s13, 0
	global_load_dwordx4 v[96:99], v10, s[12:13]
	s_add_i32 s17, s16, 1248
	s_min_u32 s17, s17, 0xfff
	s_lshr_b32 s18, s17, 5
	s_add_i32 s18, s18, 0
	s_and_b32 s19, s17, 31
	s_lshl_b32 s19, s19, 21
	s_lshl_b32 s18, s18, 7
	s_add_u32 s18, s18, s19
	s_add_u32 s14, s4, s18
	s_addc_u32 s15, s5, 0
	ds_read_b32 v132, v7
	ds_read_b32 v133, v7 offset:512
	ds_read_b32 v134, v7 offset:1024
	ds_read_b32 v135, v7 offset:1536
	ds_read_b32 v136, v7 offset:2048
	ds_read_b32 v137, v7 offset:2560
	ds_read_b32 v138, v7 offset:3072
	ds_read_b32 v139, v7 offset:3584
	ds_read_b32 v140, v7 offset:4096
	ds_read_b32 v141, v7 offset:4608
	ds_read_b32 v142, v7 offset:5120
	ds_read_b32 v143, v7 offset:5632
	ds_read_b32 v144, v7 offset:6144
	ds_read_b32 v145, v7 offset:6656
	ds_read_b32 v146, v7 offset:7168
	ds_read_b32 v147, v7 offset:7680
	s_waitcnt lgkmcnt(0)
	v_max_f32_e32 v132, v132, v132
	v_max_f32_e32 v133, v133, v133
	v_max_f32_e32 v134, v134, v134
	v_max_f32_e32 v135, v135, v135
	v_max_f32_e32 v136, v136, v136
	v_max_f32_e32 v137, v137, v137
	v_max_f32_e32 v138, v138, v138
	v_max_f32_e32 v139, v139, v139
	v_max_f32_e32 v140, v140, v140
	v_max_f32_e32 v141, v141, v141
	v_max_f32_e32 v142, v142, v142
	v_max_f32_e32 v143, v143, v143
	v_max_f32_e32 v144, v144, v144
	v_max_f32_e32 v145, v145, v145
	v_max_f32_e32 v146, v146, v146
	v_max_f32_e32 v147, v147, v147
	v_med3_f32 v132, v132, s20, v13
	v_med3_f32 v133, v133, s20, v13
	v_med3_f32 v134, v134, s20, v13
	v_med3_f32 v135, v135, s20, v13
	v_med3_f32 v136, v136, s20, v13
	v_med3_f32 v137, v137, s20, v13
	v_med3_f32 v138, v138, s20, v13
	v_med3_f32 v139, v139, s20, v13
	v_med3_f32 v140, v140, s20, v13
	v_med3_f32 v141, v141, s20, v13
	v_med3_f32 v142, v142, s20, v13
	v_med3_f32 v143, v143, s20, v13
	v_med3_f32 v144, v144, s20, v13
	v_med3_f32 v145, v145, s20, v13
	v_med3_f32 v146, v146, s20, v13
	v_med3_f32 v147, v147, s20, v13
	v_mov_b32_e32 v148, 0
	v_mov_b32_e32 v149, 0
	v_mov_b32_e32 v150, 0
	v_mov_b32_e32 v151, 0
	v_cvt_pk_fp8_f32 v148, v132, v133
	v_cvt_pk_fp8_f32 v149, v136, v137
	v_cvt_pk_fp8_f32 v150, v140, v141
	v_cvt_pk_fp8_f32 v151, v144, v145
	v_cvt_pk_fp8_f32 v148, v134, v135 op_sel:[0,0,1]
	v_cvt_pk_fp8_f32 v149, v138, v139 op_sel:[0,0,1]
	v_cvt_pk_fp8_f32 v150, v142, v143 op_sel:[0,0,1]
	v_cvt_pk_fp8_f32 v151, v146, v147 op_sel:[0,0,1]
	s_nop 0
	global_store_dwordx4 v11, v[148:151], s[14:15]
	ds_read_b32 v132, v9
	ds_read_b32 v133, v9 offset:512
	ds_read_b32 v134, v9 offset:1024
	ds_read_b32 v135, v9 offset:1536
	ds_read_b32 v136, v9 offset:2048
	ds_read_b32 v137, v9 offset:2560
	ds_read_b32 v138, v9 offset:3072
	ds_read_b32 v139, v9 offset:3584
	ds_read_b32 v140, v9 offset:4096
	ds_read_b32 v141, v9 offset:4608
	ds_read_b32 v142, v9 offset:5120
	ds_read_b32 v143, v9 offset:5632
	ds_read_b32 v144, v9 offset:6144
	ds_read_b32 v145, v9 offset:6656
	ds_read_b32 v146, v9 offset:7168
	ds_read_b32 v147, v9 offset:7680
	s_waitcnt lgkmcnt(0)
	v_max_f32_e32 v132, v132, v132
	v_max_f32_e32 v133, v133, v133
	v_max_f32_e32 v134, v134, v134
	v_max_f32_e32 v135, v135, v135
	v_max_f32_e32 v136, v136, v136
	v_max_f32_e32 v137, v137, v137
	v_max_f32_e32 v138, v138, v138
	v_max_f32_e32 v139, v139, v139
	v_max_f32_e32 v140, v140, v140
	v_max_f32_e32 v141, v141, v141
	v_max_f32_e32 v142, v142, v142
	v_max_f32_e32 v143, v143, v143
	v_max_f32_e32 v144, v144, v144
	v_max_f32_e32 v145, v145, v145
	v_max_f32_e32 v146, v146, v146
	v_max_f32_e32 v147, v147, v147
	v_med3_f32 v132, v132, s20, v13
	v_med3_f32 v133, v133, s20, v13
	v_med3_f32 v134, v134, s20, v13
	v_med3_f32 v135, v135, s20, v13
	v_med3_f32 v136, v136, s20, v13
	v_med3_f32 v137, v137, s20, v13
	v_med3_f32 v138, v138, s20, v13
	v_med3_f32 v139, v139, s20, v13
	v_med3_f32 v140, v140, s20, v13
	v_med3_f32 v141, v141, s20, v13
	v_med3_f32 v142, v142, s20, v13
	v_med3_f32 v143, v143, s20, v13
	v_med3_f32 v144, v144, s20, v13
	v_med3_f32 v145, v145, s20, v13
	v_med3_f32 v146, v146, s20, v13
	v_med3_f32 v147, v147, s20, v13
	v_mov_b32_e32 v148, 0
	v_mov_b32_e32 v149, 0
	v_mov_b32_e32 v150, 0
	v_mov_b32_e32 v151, 0
	v_cvt_pk_fp8_f32 v148, v132, v133
	v_cvt_pk_fp8_f32 v149, v136, v137
	v_cvt_pk_fp8_f32 v150, v140, v141
	v_cvt_pk_fp8_f32 v151, v144, v145
	v_cvt_pk_fp8_f32 v148, v134, v135 op_sel:[0,0,1]
	v_cvt_pk_fp8_f32 v149, v138, v139 op_sel:[0,0,1]
	v_cvt_pk_fp8_f32 v150, v142, v143 op_sel:[0,0,1]
	v_cvt_pk_fp8_f32 v151, v146, v147 op_sel:[0,0,1]
	s_nop 0
	global_store_dwordx4 v12, v[148:151], s[14:15]
	s_waitcnt vmcnt(22)
	v_mul_f32_e32 v100, 0x43000000, v100
	v_mul_f32_e32 v101, 0x43000000, v101
	v_mul_f32_e32 v102, 0x43000000, v102
	v_mul_f32_e32 v103, 0x43000000, v103
	ds_write_b128 v4, v[100:103]
	v_mul_f32_e32 v104, 0x43000000, v104
	v_mul_f32_e32 v105, 0x43000000, v105
	v_mul_f32_e32 v106, 0x43000000, v106
	v_mul_f32_e32 v107, 0x43000000, v107
	ds_write_b128 v4, v[104:107] offset:1024
	v_mul_f32_e32 v108, 0x43000000, v108
	v_mul_f32_e32 v109, 0x43000000, v109
	v_mul_f32_e32 v110, 0x43000000, v110
	v_mul_f32_e32 v111, 0x43000000, v111
	ds_write_b128 v4, v[108:111] offset:2048
	v_mul_f32_e32 v112, 0x43000000, v112
	v_mul_f32_e32 v113, 0x43000000, v113
	v_mul_f32_e32 v114, 0x43000000, v114
	v_mul_f32_e32 v115, 0x43000000, v115
	ds_write_b128 v4, v[112:115] offset:3072
	v_mul_f32_e32 v116, 0x43000000, v116
	v_mul_f32_e32 v117, 0x43000000, v117
	v_mul_f32_e32 v118, 0x43000000, v118
	v_mul_f32_e32 v119, 0x43000000, v119
	ds_write_b128 v4, v[116:119] offset:4096
	v_mul_f32_e32 v120, 0x43000000, v120
	v_mul_f32_e32 v121, 0x43000000, v121
	v_mul_f32_e32 v122, 0x43000000, v122
	v_mul_f32_e32 v123, 0x43000000, v123
	ds_write_b128 v4, v[120:123] offset:5120
	v_mul_f32_e32 v124, 0x43000000, v124
	v_mul_f32_e32 v125, 0x43000000, v125
	v_mul_f32_e32 v126, 0x43000000, v126
	v_mul_f32_e32 v127, 0x43000000, v127
	ds_write_b128 v4, v[124:127] offset:6144
	v_mul_f32_e32 v128, 0x43000000, v128
	v_mul_f32_e32 v129, 0x43000000, v129
	v_mul_f32_e32 v130, 0x43000000, v130
	v_mul_f32_e32 v131, 0x43000000, v131
	ds_write_b128 v4, v[128:131] offset:7168
	s_waitcnt lgkmcnt(0)
	s_barrier
; #define GAS __attribute__((address_space(1)))
; #define LAS __attribute__((address_space(3)))
; #define LDS_WAIT() asm volatile("s_waitcnt lgkmcnt(0)" ::: "memory")
;     const int pr = item >> 1, kb = 2 * (pr / nblk) + (item & 1), nb = pr % nblk, k0 = 64 * kb, n0 = 32 * nb;
;     const int nr = n0 + (lane & 31); const int sc = MAP == 1 ? src_col_in(nr) : nr;
;     float v[32];
; #pragma unroll
;     for (int i = 0; i < 32; ++i) v[i] = sc >= 0 ? W[(size_t)(k0 + 2 * i + (lane >> 5)) * Nsrc + sc] : 0.f;
; #pragma unroll
;     for (int i = 0; i < 32; ++i) { const int k = k0 + 2 * i + (lane >> 5); float x = v[i] * wscale; if (KS) x *= (k < ksplit ? ksA[k] : ksB[k - ksplit]); scr[(2 * i + (lane >> 5)) * 33 + (lane & 31)] = x; }
;     LDS_WAIT(); asm volatile("" ::: "memory");
;     const int c = lane & 7;
; #pragma unroll
;     for (int j = 0; j < 4; ++j) { const int n = (lane >> 3) + 8 * j; const LAS float* s = scr + (8 * c) * 33 + n;
;         const unsigned long long o = (unsigned long long)pg8::pk4_fp8(s[0 * 33], s[1 * 33], s[2 * 33], s[3 * 33]) | ((unsigned long long)pg8::pk4_fp8(s[4 * 33], s[5 * 33], s[6 * 33], s[7 * 33]) << 32);
;         *(GAS unsigned long long*)(WT + (size_t)(n0 + n) * K + k0 + 8 * c) = o; }
;     LDS_WAIT(); asm volatile("" ::: "memory");
; }
; __global__ void __launch_bounds__(NWAVES * 64, 2) hybrid_fwd(Args args) {
;     ...
;             p0_transpose_item_f8<false>(args.in[16] + (size_t)l * FF * DM, FF, DM, DM / 32, (unsigned char*)(ws + WS_WDN + l * SZ_WDN), 128.f, args.in[16], args.in[16], 0, scr, r, lane);
	s_add_i32 s17, s16, 1632
	s_min_u32 s17, s17, 0xfff
	s_lshr_b32 s18, s17, 5
	s_add_i32 s18, s18, 0
	s_and_b32 s19, s17, 31
	s_lshl_b32 s18, s18, 21
	s_lshl_b32 s19, s19, 9
	s_add_u32 s18, s18, s19
	s_add_u32 s12, s2, s18
	s_addc_u32 s13, s3, 0
	global_load_dwordx4 v[100:103], v10, s[12:13]
	s_add_u32 s12, s12, 0x8000
	s_addc_u32 s13, s13, 0
	global_load_dwordx4 v[104:107], v10, s[12:13]
	s_add_u32 s12, s12, 0x8000
	s_addc_u32 s13, s13, 0
	global_load_dwordx4 v[108:111], v10, s[12:13]
	s_add_u32 s12, s12, 0x8000
	s_addc_u32 s13, s13, 0
	global_load_dwordx4 v[112:115], v10, s[12:13]
	s_add_u32 s12, s12, 0x8000
	s_addc_u32 s13, s13, 0
	global_load_dwordx4 v[116:119], v10, s[12:13]
	s_add_u32 s12, s12, 0x8000
	s_addc_u32 s13, s13, 0
	global_load_dwordx4 v[120:123], v10, s[12:13]
	s_add_u32 s12, s12, 0x8000
	s_addc_u32 s13, s13, 0
	global_load_dwordx4 v[124:127], v10, s[12:13]
	s_add_u32 s12, s12, 0x8000
	s_addc_u32 s13, s13, 0
	global_load_dwordx4 v[128:131], v10, s[12:13]
	s_add_i32 s17, s16, 1344
	s_min_u32 s17, s17, 0xfff
	s_lshr_b32 s18, s17, 5
	s_add_i32 s18, s18, 0
	s_and_b32 s19, s17, 31
	s_lshl_b32 s19, s19, 21
	s_lshl_b32 s18, s18, 7
	s_add_u32 s18, s18, s19
	s_add_u32 s14, s4, s18
	s_addc_u32 s15, s5, 0
	ds_read_b32 v132, v6
	ds_read_b32 v133, v6 offset:512
	ds_read_b32 v134, v6 offset:1024
	ds_read_b32 v135, v6 offset:1536
	ds_read_b32 v136, v6 offset:2048
	ds_read_b32 v137, v6 offset:2560
	ds_read_b32 v138, v6 offset:3072
	ds_read_b32 v139, v6 offset:3584
	ds_read_b32 v140, v6 offset:4096
	ds_read_b32 v141, v6 offset:4608
	ds_read_b32 v142, v6 offset:5120
	ds_read_b32 v143, v6 offset:5632
	ds_read_b32 v144, v6 offset:6144
	ds_read_b32 v145, v6 offset:6656
	ds_read_b32 v146, v6 offset:7168
	ds_read_b32 v147, v6 offset:7680
	s_waitcnt lgkmcnt(0)
	v_max_f32_e32 v132, v132, v132
	v_max_f32_e32 v133, v133, v133
	v_max_f32_e32 v134, v134, v134
	v_max_f32_e32 v135, v135, v135
	v_max_f32_e32 v136, v136, v136
	v_max_f32_e32 v137, v137, v137
	v_max_f32_e32 v138, v138, v138
	v_max_f32_e32 v139, v139, v139
	v_max_f32_e32 v140, v140, v140
	v_max_f32_e32 v141, v141, v141
	v_max_f32_e32 v142, v142, v142
	v_max_f32_e32 v143, v143, v143
	v_max_f32_e32 v144, v144, v144
	v_max_f32_e32 v145, v145, v145
	v_max_f32_e32 v146, v146, v146
	v_max_f32_e32 v147, v147, v147
	v_med3_f32 v132, v132, s20, v13
	v_med3_f32 v133, v133, s20, v13
	v_med3_f32 v134, v134, s20, v13
	v_med3_f32 v135, v135, s20, v13
	v_med3_f32 v136, v136, s20, v13
	v_med3_f32 v137, v137, s20, v13
	v_med3_f32 v138, v138, s20, v13
	v_med3_f32 v139, v139, s20, v13
	v_med3_f32 v140, v140, s20, v13
	v_med3_f32 v141, v141, s20, v13
	v_med3_f32 v142, v142, s20, v13
	v_med3_f32 v143, v143, s20, v13
	v_med3_f32 v144, v144, s20, v13
	v_med3_f32 v145, v145, s20, v13
	v_med3_f32 v146, v146, s20, v13
	v_med3_f32 v147, v147, s20, v13
	v_mov_b32_e32 v148, 0
	v_mov_b32_e32 v149, 0
	v_mov_b32_e32 v150, 0
	v_mov_b32_e32 v151, 0
	v_cvt_pk_fp8_f32 v148, v132, v133
	v_cvt_pk_fp8_f32 v149, v136, v137
	v_cvt_pk_fp8_f32 v150, v140, v141
	v_cvt_pk_fp8_f32 v151, v144, v145
	v_cvt_pk_fp8_f32 v148, v134, v135 op_sel:[0,0,1]
	v_cvt_pk_fp8_f32 v149, v138, v139 op_sel:[0,0,1]
	v_cvt_pk_fp8_f32 v150, v142, v143 op_sel:[0,0,1]
	v_cvt_pk_fp8_f32 v151, v146, v147 op_sel:[0,0,1]
	s_nop 0
	global_store_dwordx4 v11, v[148:151], s[14:15]
	ds_read_b32 v132, v8
	ds_read_b32 v133, v8 offset:512
	ds_read_b32 v134, v8 offset:1024
	ds_read_b32 v135, v8 offset:1536
	ds_read_b32 v136, v8 offset:2048
	ds_read_b32 v137, v8 offset:2560
	ds_read_b32 v138, v8 offset:3072
	ds_read_b32 v139, v8 offset:3584
	ds_read_b32 v140, v8 offset:4096
	ds_read_b32 v141, v8 offset:4608
	ds_read_b32 v142, v8 offset:5120
	ds_read_b32 v143, v8 offset:5632
	ds_read_b32 v144, v8 offset:6144
	ds_read_b32 v145, v8 offset:6656
	ds_read_b32 v146, v8 offset:7168
	ds_read_b32 v147, v8 offset:7680
	s_waitcnt lgkmcnt(0)
	v_max_f32_e32 v132, v132, v132
	v_max_f32_e32 v133, v133, v133
	v_max_f32_e32 v134, v134, v134
	v_max_f32_e32 v135, v135, v135
	v_max_f32_e32 v136, v136, v136
	v_max_f32_e32 v137, v137, v137
	v_max_f32_e32 v138, v138, v138
	v_max_f32_e32 v139, v139, v139
	v_max_f32_e32 v140, v140, v140
	v_max_f32_e32 v141, v141, v141
	v_max_f32_e32 v142, v142, v142
	v_max_f32_e32 v143, v143, v143
	v_max_f32_e32 v144, v144, v144
	v_max_f32_e32 v145, v145, v145
	v_max_f32_e32 v146, v146, v146
	v_max_f32_e32 v147, v147, v147
	v_med3_f32 v132, v132, s20, v13
	v_med3_f32 v133, v133, s20, v13
	v_med3_f32 v134, v134, s20, v13
	v_med3_f32 v135, v135, s20, v13
	v_med3_f32 v136, v136, s20, v13
	v_med3_f32 v137, v137, s20, v13
	v_med3_f32 v138, v138, s20, v13
	v_med3_f32 v139, v139, s20, v13
	v_med3_f32 v140, v140, s20, v13
	v_med3_f32 v141, v141, s20, v13
	v_med3_f32 v142, v142, s20, v13
	v_med3_f32 v143, v143, s20, v13
	v_med3_f32 v144, v144, s20, v13
	v_med3_f32 v145, v145, s20, v13
	v_med3_f32 v146, v146, s20, v13
	v_med3_f32 v147, v147, s20, v13
	v_mov_b32_e32 v148, 0
	v_mov_b32_e32 v149, 0
	v_mov_b32_e32 v150, 0
	v_mov_b32_e32 v151, 0
	v_cvt_pk_fp8_f32 v148, v132, v133
	v_cvt_pk_fp8_f32 v149, v136, v137
	v_cvt_pk_fp8_f32 v150, v140, v141
	v_cvt_pk_fp8_f32 v151, v144, v145
	v_cvt_pk_fp8_f32 v148, v134, v135 op_sel:[0,0,1]
	v_cvt_pk_fp8_f32 v149, v138, v139 op_sel:[0,0,1]
	v_cvt_pk_fp8_f32 v150, v142, v143 op_sel:[0,0,1]
	v_cvt_pk_fp8_f32 v151, v146, v147 op_sel:[0,0,1]
	s_nop 0
	global_store_dwordx4 v12, v[148:151], s[14:15]
	s_waitcnt vmcnt(22)
	v_mul_f32_e32 v36, 0x43000000, v36
	v_mul_f32_e32 v37, 0x43000000, v37
	v_mul_f32_e32 v38, 0x43000000, v38
	v_mul_f32_e32 v39, 0x43000000, v39
	ds_write_b128 v5, v[36:39]
	v_mul_f32_e32 v40, 0x43000000, v40
	v_mul_f32_e32 v41, 0x43000000, v41
	v_mul_f32_e32 v42, 0x43000000, v42
	v_mul_f32_e32 v43, 0x43000000, v43
	ds_write_b128 v5, v[40:43] offset:1024
	v_mul_f32_e32 v44, 0x43000000, v44
	v_mul_f32_e32 v45, 0x43000000, v45
	v_mul_f32_e32 v46, 0x43000000, v46
	v_mul_f32_e32 v47, 0x43000000, v47
	ds_write_b128 v5, v[44:47] offset:2048
	v_mul_f32_e32 v48, 0x43000000, v48
	v_mul_f32_e32 v49, 0x43000000, v49
	v_mul_f32_e32 v50, 0x43000000, v50
	v_mul_f32_e32 v51, 0x43000000, v51
	ds_write_b128 v5, v[48:51] offset:3072
	v_mul_f32_e32 v52, 0x43000000, v52
	v_mul_f32_e32 v53, 0x43000000, v53
	v_mul_f32_e32 v54, 0x43000000, v54
	v_mul_f32_e32 v55, 0x43000000, v55
	ds_write_b128 v5, v[52:55] offset:4096
	v_mul_f32_e32 v56, 0x43000000, v56
	v_mul_f32_e32 v57, 0x43000000, v57
	v_mul_f32_e32 v58, 0x43000000, v58
	v_mul_f32_e32 v59, 0x43000000, v59
	ds_write_b128 v5, v[56:59] offset:5120
	v_mul_f32_e32 v60, 0x43000000, v60
	v_mul_f32_e32 v61, 0x43000000, v61
	v_mul_f32_e32 v62, 0x43000000, v62
	v_mul_f32_e32 v63, 0x43000000, v63
	ds_write_b128 v5, v[60:63] offset:6144
	v_mul_f32_e32 v64, 0x43000000, v64
	v_mul_f32_e32 v65, 0x43000000, v65
	v_mul_f32_e32 v66, 0x43000000, v66
	v_mul_f32_e32 v67, 0x43000000, v67
	ds_write_b128 v5, v[64:67] offset:7168
	s_waitcnt lgkmcnt(0)
	s_barrier
; #define GAS __attribute__((address_space(1)))
; #define LAS __attribute__((address_space(3)))
; #define LDS_WAIT() asm volatile("s_waitcnt lgkmcnt(0)" ::: "memory")
;     const int pr = item >> 1, kb = 2 * (pr / nblk) + (item & 1), nb = pr % nblk, k0 = 64 * kb, n0 = 32 * nb;
;     const int nr = n0 + (lane & 31); const int sc = MAP == 1 ? src_col_in(nr) : nr;
;     float v[32];
; #pragma unroll
;     for (int i = 0; i < 32; ++i) v[i] = sc >= 0 ? W[(size_t)(k0 + 2 * i + (lane >> 5)) * Nsrc + sc] : 0.f;
; #pragma unroll
;     for (int i = 0; i < 32; ++i) { const int k = k0 + 2 * i + (lane >> 5); float x = v[i] * wscale; if (KS) x *= (k < ksplit ? ksA[k] : ksB[k - ksplit]); scr[(2 * i + (lane >> 5)) * 33 + (lane & 31)] = x; }
;     LDS_WAIT(); asm volatile("" ::: "memory");
;     const int c = lane & 7;
; #pragma unroll
;     for (int j = 0; j < 4; ++j) { const int n = (lane >> 3) + 8 * j; const LAS float* s = scr + (8 * c) * 33 + n;
;         const unsigned long long o = (unsigned long long)pg8::pk4_fp8(s[0 * 33], s[1 * 33], s[2 * 33], s[3 * 33]) | ((unsigned long long)pg8::pk4_fp8(s[4 * 33], s[5 * 33], s[6 * 33], s[7 * 33]) << 32);
;         *(GAS unsigned long long*)(WT + (size_t)(n0 + n) * K + k0 + 8 * c) = o; }
;     LDS_WAIT(); asm volatile("" ::: "memory");
; }
; __global__ void __launch_bounds__(NWAVES * 64, 2) hybrid_fwd(Args args) {
;     ...
;             p0_transpose_item_f8<false>(args.in[16] + (size_t)l * FF * DM, FF, DM, DM / 32, (unsigned char*)(ws + WS_WDN + l * SZ_WDN), 128.f, args.in[16], args.in[16], 0, scr, r, lane);
	s_add_i32 s17, s16, 1728
	s_min_u32 s17, s17, 0xfff
	s_lshr_b32 s18, s17, 5
	s_add_i32 s18, s18, 0
	s_and_b32 s19, s17, 31
	s_lshl_b32 s18, s18, 21
	s_lshl_b32 s19, s19, 9
	s_add_u32 s18, s18, s19
	s_add_u32 s12, s2, s18
	s_addc_u32 s13, s3, 0
	global_load_dwordx4 v[36:39], v10, s[12:13]
	s_add_u32 s12, s12, 0x8000
	s_addc_u32 s13, s13, 0
	global_load_dwordx4 v[40:43], v10, s[12:13]
	s_add_u32 s12, s12, 0x8000
	s_addc_u32 s13, s13, 0
	global_load_dwordx4 v[44:47], v10, s[12:13]
	s_add_u32 s12, s12, 0x8000
	s_addc_u32 s13, s13, 0
	global_load_dwordx4 v[48:51], v10, s[12:13]
	s_add_u32 s12, s12, 0x8000
	s_addc_u32 s13, s13, 0
	global_load_dwordx4 v[52:55], v10, s[12:13]
	s_add_u32 s12, s12, 0x8000
	s_addc_u32 s13, s13, 0
	global_load_dwordx4 v[56:59], v10, s[12:13]
	s_add_u32 s12, s12, 0x8000
	s_addc_u32 s13, s13, 0
	global_load_dwordx4 v[60:63], v10, s[12:13]
	s_add_u32 s12, s12, 0x8000
	s_addc_u32 s13, s13, 0
	global_load_dwordx4 v[64:67], v10, s[12:13]
	s_add_i32 s17, s16, 1440
	s_min_u32 s17, s17, 0xfff
	s_lshr_b32 s18, s17, 5
	s_add_i32 s18, s18, 0
	s_and_b32 s19, s17, 31
	s_lshl_b32 s19, s19, 21
	s_lshl_b32 s18, s18, 7
	s_add_u32 s18, s18, s19
	s_add_u32 s14, s4, s18
	s_addc_u32 s15, s5, 0
	ds_read_b32 v132, v7
	ds_read_b32 v133, v7 offset:512
	ds_read_b32 v134, v7 offset:1024
	ds_read_b32 v135, v7 offset:1536
	ds_read_b32 v136, v7 offset:2048
	ds_read_b32 v137, v7 offset:2560
	ds_read_b32 v138, v7 offset:3072
	ds_read_b32 v139, v7 offset:3584
	ds_read_b32 v140, v7 offset:4096
	ds_read_b32 v141, v7 offset:4608
	ds_read_b32 v142, v7 offset:5120
	ds_read_b32 v143, v7 offset:5632
	ds_read_b32 v144, v7 offset:6144
	ds_read_b32 v145, v7 offset:6656
	ds_read_b32 v146, v7 offset:7168
	ds_read_b32 v147, v7 offset:7680
	s_waitcnt lgkmcnt(0)
	v_max_f32_e32 v132, v132, v132
	v_max_f32_e32 v133, v133, v133
	v_max_f32_e32 v134, v134, v134
	v_max_f32_e32 v135, v135, v135
	v_max_f32_e32 v136, v136, v136
	v_max_f32_e32 v137, v137, v137
	v_max_f32_e32 v138, v138, v138
	v_max_f32_e32 v139, v139, v139
	v_max_f32_e32 v140, v140, v140
	v_max_f32_e32 v141, v141, v141
	v_max_f32_e32 v142, v142, v142
	v_max_f32_e32 v143, v143, v143
	v_max_f32_e32 v144, v144, v144
	v_max_f32_e32 v145, v145, v145
	v_max_f32_e32 v146, v146, v146
	v_max_f32_e32 v147, v147, v147
	v_med3_f32 v132, v132, s20, v13
	v_med3_f32 v133, v133, s20, v13
	v_med3_f32 v134, v134, s20, v13
	v_med3_f32 v135, v135, s20, v13
	v_med3_f32 v136, v136, s20, v13
	v_med3_f32 v137, v137, s20, v13
	v_med3_f32 v138, v138, s20, v13
	v_med3_f32 v139, v139, s20, v13
	v_med3_f32 v140, v140, s20, v13
	v_med3_f32 v141, v141, s20, v13
	v_med3_f32 v142, v142, s20, v13
	v_med3_f32 v143, v143, s20, v13
	v_med3_f32 v144, v144, s20, v13
	v_med3_f32 v145, v145, s20, v13
	v_med3_f32 v146, v146, s20, v13
	v_med3_f32 v147, v147, s20, v13
	v_mov_b32_e32 v148, 0
	v_mov_b32_e32 v149, 0
	v_mov_b32_e32 v150, 0
	v_mov_b32_e32 v151, 0
	v_cvt_pk_fp8_f32 v148, v132, v133
	v_cvt_pk_fp8_f32 v149, v136, v137
	v_cvt_pk_fp8_f32 v150, v140, v141
	v_cvt_pk_fp8_f32 v151, v144, v145
	v_cvt_pk_fp8_f32 v148, v134, v135 op_sel:[0,0,1]
	v_cvt_pk_fp8_f32 v149, v138, v139 op_sel:[0,0,1]
	v_cvt_pk_fp8_f32 v150, v142, v143 op_sel:[0,0,1]
	v_cvt_pk_fp8_f32 v151, v146, v147 op_sel:[0,0,1]
	s_nop 0
	global_store_dwordx4 v11, v[148:151], s[14:15]
	ds_read_b32 v132, v9
	ds_read_b32 v133, v9 offset:512
	ds_read_b32 v134, v9 offset:1024
	ds_read_b32 v135, v9 offset:1536
	ds_read_b32 v136, v9 offset:2048
	ds_read_b32 v137, v9 offset:2560
	ds_read_b32 v138, v9 offset:3072
	ds_read_b32 v139, v9 offset:3584
	ds_read_b32 v140, v9 offset:4096
	ds_read_b32 v141, v9 offset:4608
	ds_read_b32 v142, v9 offset:5120
	ds_read_b32 v143, v9 offset:5632
	ds_read_b32 v144, v9 offset:6144
	ds_read_b32 v145, v9 offset:6656
	ds_read_b32 v146, v9 offset:7168
	ds_read_b32 v147, v9 offset:7680
	s_waitcnt lgkmcnt(0)
	v_max_f32_e32 v132, v132, v132
	v_max_f32_e32 v133, v133, v133
	v_max_f32_e32 v134, v134, v134
	v_max_f32_e32 v135, v135, v135
	v_max_f32_e32 v136, v136, v136
	v_max_f32_e32 v137, v137, v137
	v_max_f32_e32 v138, v138, v138
	v_max_f32_e32 v139, v139, v139
	v_max_f32_e32 v140, v140, v140
	v_max_f32_e32 v141, v141, v141
	v_max_f32_e32 v142, v142, v142
	v_max_f32_e32 v143, v143, v143
	v_max_f32_e32 v144, v144, v144
	v_max_f32_e32 v145, v145, v145
	v_max_f32_e32 v146, v146, v146
	v_max_f32_e32 v147, v147, v147
	v_med3_f32 v132, v132, s20, v13
	v_med3_f32 v133, v133, s20, v13
	v_med3_f32 v134, v134, s20, v13
	v_med3_f32 v135, v135, s20, v13
	v_med3_f32 v136, v136, s20, v13
	v_med3_f32 v137, v137, s20, v13
	v_med3_f32 v138, v138, s20, v13
	v_med3_f32 v139, v139, s20, v13
	v_med3_f32 v140, v140, s20, v13
	v_med3_f32 v141, v141, s20, v13
	v_med3_f32 v142, v142, s20, v13
	v_med3_f32 v143, v143, s20, v13
	v_med3_f32 v144, v144, s20, v13
	v_med3_f32 v145, v145, s20, v13
	v_med3_f32 v146, v146, s20, v13
	v_med3_f32 v147, v147, s20, v13
	v_mov_b32_e32 v148, 0
	v_mov_b32_e32 v149, 0
	v_mov_b32_e32 v150, 0
	v_mov_b32_e32 v151, 0
	v_cvt_pk_fp8_f32 v148, v132, v133
	v_cvt_pk_fp8_f32 v149, v136, v137
	v_cvt_pk_fp8_f32 v150, v140, v141
	v_cvt_pk_fp8_f32 v151, v144, v145
	v_cvt_pk_fp8_f32 v148, v134, v135 op_sel:[0,0,1]
	v_cvt_pk_fp8_f32 v149, v138, v139 op_sel:[0,0,1]
	v_cvt_pk_fp8_f32 v150, v142, v143 op_sel:[0,0,1]
	v_cvt_pk_fp8_f32 v151, v146, v147 op_sel:[0,0,1]
	s_nop 0
	global_store_dwordx4 v12, v[148:151], s[14:15]
	s_waitcnt vmcnt(22)
	v_mul_f32_e32 v68, 0x43000000, v68
	v_mul_f32_e32 v69, 0x43000000, v69
	v_mul_f32_e32 v70, 0x43000000, v70
	v_mul_f32_e32 v71, 0x43000000, v71
	ds_write_b128 v4, v[68:71]
	v_mul_f32_e32 v72, 0x43000000, v72
	v_mul_f32_e32 v73, 0x43000000, v73
	v_mul_f32_e32 v74, 0x43000000, v74
	v_mul_f32_e32 v75, 0x43000000, v75
	ds_write_b128 v4, v[72:75] offset:1024
	v_mul_f32_e32 v76, 0x43000000, v76
	v_mul_f32_e32 v77, 0x43000000, v77
	v_mul_f32_e32 v78, 0x43000000, v78
	v_mul_f32_e32 v79, 0x43000000, v79
	ds_write_b128 v4, v[76:79] offset:2048
	v_mul_f32_e32 v80, 0x43000000, v80
	v_mul_f32_e32 v81, 0x43000000, v81
	v_mul_f32_e32 v82, 0x43000000, v82
	v_mul_f32_e32 v83, 0x43000000, v83
	ds_write_b128 v4, v[80:83] offset:3072
	v_mul_f32_e32 v84, 0x43000000, v84
	v_mul_f32_e32 v85, 0x43000000, v85
	v_mul_f32_e32 v86, 0x43000000, v86
	v_mul_f32_e32 v87, 0x43000000, v87
	ds_write_b128 v4, v[84:87] offset:4096
	v_mul_f32_e32 v88, 0x43000000, v88
	v_mul_f32_e32 v89, 0x43000000, v89
	v_mul_f32_e32 v90, 0x43000000, v90
	v_mul_f32_e32 v91, 0x43000000, v91
	ds_write_b128 v4, v[88:91] offset:5120
	v_mul_f32_e32 v92, 0x43000000, v92
	v_mul_f32_e32 v93, 0x43000000, v93
	v_mul_f32_e32 v94, 0x43000000, v94
	v_mul_f32_e32 v95, 0x43000000, v95
	ds_write_b128 v4, v[92:95] offset:6144
	v_mul_f32_e32 v96, 0x43000000, v96
	v_mul_f32_e32 v97, 0x43000000, v97
	v_mul_f32_e32 v98, 0x43000000, v98
	v_mul_f32_e32 v99, 0x43000000, v99
	ds_write_b128 v4, v[96:99] offset:7168
	s_waitcnt lgkmcnt(0)
	s_barrier
; #define GAS __attribute__((address_space(1)))
; #define LAS __attribute__((address_space(3)))
; #define LDS_WAIT() asm volatile("s_waitcnt lgkmcnt(0)" ::: "memory")
;     const int pr = item >> 1, kb = 2 * (pr / nblk) + (item & 1), nb = pr % nblk, k0 = 64 * kb, n0 = 32 * nb;
;     const int nr = n0 + (lane & 31); const int sc = MAP == 1 ? src_col_in(nr) : nr;
;     float v[32];
; #pragma unroll
;     for (int i = 0; i < 32; ++i) v[i] = sc >= 0 ? W[(size_t)(k0 + 2 * i + (lane >> 5)) * Nsrc + sc] : 0.f;
; #pragma unroll
;     for (int i = 0; i < 32; ++i) { const int k = k0 + 2 * i + (lane >> 5); float x = v[i] * wscale; if (KS) x *= (k < ksplit ? ksA[k] : ksB[k - ksplit]); scr[(2 * i + (lane >> 5)) * 33 + (lane & 31)] = x; }
;     LDS_WAIT(); asm volatile("" ::: "memory");
;     const int c = lane & 7;
; #pragma unroll
;     for (int j = 0; j < 4; ++j) { const int n = (lane >> 3) + 8 * j; const LAS float* s = scr + (8 * c) * 33 + n;
;         const unsigned long long o = (unsigned long long)pg8::pk4_fp8(s[0 * 33], s[1 * 33], s[2 * 33], s[3 * 33]) | ((unsigned long long)pg8::pk4_fp8(s[4 * 33], s[5 * 33], s[6 * 33], s[7 * 33]) << 32);
;         *(GAS unsigned long long*)(WT + (size_t)(n0 + n) * K + k0 + 8 * c) = o; }
;     LDS_WAIT(); asm volatile("" ::: "memory");
; }
; __global__ void __launch_bounds__(NWAVES * 64, 2) hybrid_fwd(Args args) {
;     ...
;             p0_transpose_item_f8<false>(args.in[16] + (size_t)l * FF * DM, FF, DM, DM / 32, (unsigned char*)(ws + WS_WDN + l * SZ_WDN), 128.f, args.in[16], args.in[16], 0, scr, r, lane);
	s_add_i32 s17, s16, 1824
	s_min_u32 s17, s17, 0xfff
	s_lshr_b32 s18, s17, 5
	s_add_i32 s18, s18, 0
	s_and_b32 s19, s17, 31
	s_lshl_b32 s18, s18, 21
	s_lshl_b32 s19, s19, 9
	s_add_u32 s18, s18, s19
	s_add_u32 s12, s2, s18
	s_addc_u32 s13, s3, 0
	global_load_dwordx4 v[68:71], v10, s[12:13]
	s_add_u32 s12, s12, 0x8000
	s_addc_u32 s13, s13, 0
	global_load_dwordx4 v[72:75], v10, s[12:13]
	s_add_u32 s12, s12, 0x8000
	s_addc_u32 s13, s13, 0
	global_load_dwordx4 v[76:79], v10, s[12:13]
	s_add_u32 s12, s12, 0x8000
	s_addc_u32 s13, s13, 0
	global_load_dwordx4 v[80:83], v10, s[12:13]
	s_add_u32 s12, s12, 0x8000
	s_addc_u32 s13, s13, 0
	global_load_dwordx4 v[84:87], v10, s[12:13]
	s_add_u32 s12, s12, 0x8000
	s_addc_u32 s13, s13, 0
	global_load_dwordx4 v[88:91], v10, s[12:13]
	s_add_u32 s12, s12, 0x8000
	s_addc_u32 s13, s13, 0
	global_load_dwordx4 v[92:95], v10, s[12:13]
	s_add_u32 s12, s12, 0x8000
	s_addc_u32 s13, s13, 0
	global_load_dwordx4 v[96:99], v10, s[12:13]
	s_add_i32 s17, s16, 1536
	s_min_u32 s17, s17, 0xfff
	s_lshr_b32 s18, s17, 5
	s_add_i32 s18, s18, 0
	s_and_b32 s19, s17, 31
	s_lshl_b32 s19, s19, 21
	s_lshl_b32 s18, s18, 7
	s_add_u32 s18, s18, s19
	s_add_u32 s14, s4, s18
	s_addc_u32 s15, s5, 0
	ds_read_b32 v132, v6
	ds_read_b32 v133, v6 offset:512
	ds_read_b32 v134, v6 offset:1024
	ds_read_b32 v135, v6 offset:1536
	ds_read_b32 v136, v6 offset:2048
	ds_read_b32 v137, v6 offset:2560
	ds_read_b32 v138, v6 offset:3072
	ds_read_b32 v139, v6 offset:3584
	ds_read_b32 v140, v6 offset:4096
	ds_read_b32 v141, v6 offset:4608
	ds_read_b32 v142, v6 offset:5120
	ds_read_b32 v143, v6 offset:5632
	ds_read_b32 v144, v6 offset:6144
	ds_read_b32 v145, v6 offset:6656
	ds_read_b32 v146, v6 offset:7168
	ds_read_b32 v147, v6 offset:7680
	s_waitcnt lgkmcnt(0)
	v_max_f32_e32 v132, v132, v132
	v_max_f32_e32 v133, v133, v133
	v_max_f32_e32 v134, v134, v134
	v_max_f32_e32 v135, v135, v135
	v_max_f32_e32 v136, v136, v136
	v_max_f32_e32 v137, v137, v137
	v_max_f32_e32 v138, v138, v138
	v_max_f32_e32 v139, v139, v139
	v_max_f32_e32 v140, v140, v140
	v_max_f32_e32 v141, v141, v141
	v_max_f32_e32 v142, v142, v142
	v_max_f32_e32 v143, v143, v143
	v_max_f32_e32 v144, v144, v144
	v_max_f32_e32 v145, v145, v145
	v_max_f32_e32 v146, v146, v146
	v_max_f32_e32 v147, v147, v147
	v_med3_f32 v132, v132, s20, v13
	v_med3_f32 v133, v133, s20, v13
	v_med3_f32 v134, v134, s20, v13
	v_med3_f32 v135, v135, s20, v13
	v_med3_f32 v136, v136, s20, v13
	v_med3_f32 v137, v137, s20, v13
	v_med3_f32 v138, v138, s20, v13
	v_med3_f32 v139, v139, s20, v13
	v_med3_f32 v140, v140, s20, v13
	v_med3_f32 v141, v141, s20, v13
	v_med3_f32 v142, v142, s20, v13
	v_med3_f32 v143, v143, s20, v13
	v_med3_f32 v144, v144, s20, v13
	v_med3_f32 v145, v145, s20, v13
	v_med3_f32 v146, v146, s20, v13
	v_med3_f32 v147, v147, s20, v13
	v_mov_b32_e32 v148, 0
	v_mov_b32_e32 v149, 0
	v_mov_b32_e32 v150, 0
	v_mov_b32_e32 v151, 0
	v_cvt_pk_fp8_f32 v148, v132, v133
	v_cvt_pk_fp8_f32 v149, v136, v137
	v_cvt_pk_fp8_f32 v150, v140, v141
	v_cvt_pk_fp8_f32 v151, v144, v145
	v_cvt_pk_fp8_f32 v148, v134, v135 op_sel:[0,0,1]
	v_cvt_pk_fp8_f32 v149, v138, v139 op_sel:[0,0,1]
	v_cvt_pk_fp8_f32 v150, v142, v143 op_sel:[0,0,1]
	v_cvt_pk_fp8_f32 v151, v146, v147 op_sel:[0,0,1]
	s_nop 0
	global_store_dwordx4 v11, v[148:151], s[14:15]
	ds_read_b32 v132, v8
	ds_read_b32 v133, v8 offset:512
	ds_read_b32 v134, v8 offset:1024
	ds_read_b32 v135, v8 offset:1536
	ds_read_b32 v136, v8 offset:2048
	ds_read_b32 v137, v8 offset:2560
	ds_read_b32 v138, v8 offset:3072
	ds_read_b32 v139, v8 offset:3584
	ds_read_b32 v140, v8 offset:4096
	ds_read_b32 v141, v8 offset:4608
	ds_read_b32 v142, v8 offset:5120
	ds_read_b32 v143, v8 offset:5632
	ds_read_b32 v144, v8 offset:6144
	ds_read_b32 v145, v8 offset:6656
	ds_read_b32 v146, v8 offset:7168
	ds_read_b32 v147, v8 offset:7680
	s_waitcnt lgkmcnt(0)
	v_max_f32_e32 v132, v132, v132
	v_max_f32_e32 v133, v133, v133
	v_max_f32_e32 v134, v134, v134
	v_max_f32_e32 v135, v135, v135
	v_max_f32_e32 v136, v136, v136
	v_max_f32_e32 v137, v137, v137
	v_max_f32_e32 v138, v138, v138
	v_max_f32_e32 v139, v139, v139
	v_max_f32_e32 v140, v140, v140
	v_max_f32_e32 v141, v141, v141
	v_max_f32_e32 v142, v142, v142
	v_max_f32_e32 v143, v143, v143
	v_max_f32_e32 v144, v144, v144
	v_max_f32_e32 v145, v145, v145
	v_max_f32_e32 v146, v146, v146
	v_max_f32_e32 v147, v147, v147
	v_med3_f32 v132, v132, s20, v13
	v_med3_f32 v133, v133, s20, v13
	v_med3_f32 v134, v134, s20, v13
	v_med3_f32 v135, v135, s20, v13
	v_med3_f32 v136, v136, s20, v13
	v_med3_f32 v137, v137, s20, v13
	v_med3_f32 v138, v138, s20, v13
	v_med3_f32 v139, v139, s20, v13
	v_med3_f32 v140, v140, s20, v13
	v_med3_f32 v141, v141, s20, v13
	v_med3_f32 v142, v142, s20, v13
	v_med3_f32 v143, v143, s20, v13
	v_med3_f32 v144, v144, s20, v13
	v_med3_f32 v145, v145, s20, v13
	v_med3_f32 v146, v146, s20, v13
	v_med3_f32 v147, v147, s20, v13
	v_mov_b32_e32 v148, 0
	v_mov_b32_e32 v149, 0
	v_mov_b32_e32 v150, 0
	v_mov_b32_e32 v151, 0
	v_cvt_pk_fp8_f32 v148, v132, v133
	v_cvt_pk_fp8_f32 v149, v136, v137
	v_cvt_pk_fp8_f32 v150, v140, v141
	v_cvt_pk_fp8_f32 v151, v144, v145
	v_cvt_pk_fp8_f32 v148, v134, v135 op_sel:[0,0,1]
	v_cvt_pk_fp8_f32 v149, v138, v139 op_sel:[0,0,1]
	v_cvt_pk_fp8_f32 v150, v142, v143 op_sel:[0,0,1]
	v_cvt_pk_fp8_f32 v151, v146, v147 op_sel:[0,0,1]
	s_nop 0
	global_store_dwordx4 v12, v[148:151], s[14:15]
	s_waitcnt vmcnt(22)
	v_mul_f32_e32 v100, 0x43000000, v100
	v_mul_f32_e32 v101, 0x43000000, v101
	v_mul_f32_e32 v102, 0x43000000, v102
	v_mul_f32_e32 v103, 0x43000000, v103
	ds_write_b128 v5, v[100:103]
	v_mul_f32_e32 v104, 0x43000000, v104
	v_mul_f32_e32 v105, 0x43000000, v105
	v_mul_f32_e32 v106, 0x43000000, v106
	v_mul_f32_e32 v107, 0x43000000, v107
	ds_write_b128 v5, v[104:107] offset:1024
	v_mul_f32_e32 v108, 0x43000000, v108
	v_mul_f32_e32 v109, 0x43000000, v109
	v_mul_f32_e32 v110, 0x43000000, v110
	v_mul_f32_e32 v111, 0x43000000, v111
	ds_write_b128 v5, v[108:111] offset:2048
	v_mul_f32_e32 v112, 0x43000000, v112
	v_mul_f32_e32 v113, 0x43000000, v113
	v_mul_f32_e32 v114, 0x43000000, v114
	v_mul_f32_e32 v115, 0x43000000, v115
	ds_write_b128 v5, v[112:115] offset:3072
	v_mul_f32_e32 v116, 0x43000000, v116
	v_mul_f32_e32 v117, 0x43000000, v117
	v_mul_f32_e32 v118, 0x43000000, v118
	v_mul_f32_e32 v119, 0x43000000, v119
	ds_write_b128 v5, v[116:119] offset:4096
	v_mul_f32_e32 v120, 0x43000000, v120
	v_mul_f32_e32 v121, 0x43000000, v121
	v_mul_f32_e32 v122, 0x43000000, v122
	v_mul_f32_e32 v123, 0x43000000, v123
	ds_write_b128 v5, v[120:123] offset:5120
	v_mul_f32_e32 v124, 0x43000000, v124
	v_mul_f32_e32 v125, 0x43000000, v125
	v_mul_f32_e32 v126, 0x43000000, v126
	v_mul_f32_e32 v127, 0x43000000, v127
	ds_write_b128 v5, v[124:127] offset:6144
	v_mul_f32_e32 v128, 0x43000000, v128
	v_mul_f32_e32 v129, 0x43000000, v129
	v_mul_f32_e32 v130, 0x43000000, v130
	v_mul_f32_e32 v131, 0x43000000, v131
	ds_write_b128 v5, v[128:131] offset:7168
	s_waitcnt lgkmcnt(0)
	s_barrier
; #define GAS __attribute__((address_space(1)))
; #define LAS __attribute__((address_space(3)))
; #define LDS_WAIT() asm volatile("s_waitcnt lgkmcnt(0)" ::: "memory")
;     const int pr = item >> 1, kb = 2 * (pr / nblk) + (item & 1), nb = pr % nblk, k0 = 64 * kb, n0 = 32 * nb;
;     const int nr = n0 + (lane & 31); const int sc = MAP == 1 ? src_col_in(nr) : nr;
;     float v[32];
; #pragma unroll
;     for (int i = 0; i < 32; ++i) v[i] = sc >= 0 ? W[(size_t)(k0 + 2 * i + (lane >> 5)) * Nsrc + sc] : 0.f;
; #pragma unroll
;     for (int i = 0; i < 32; ++i) { const int k = k0 + 2 * i + (lane >> 5); float x = v[i] * wscale; if (KS) x *= (k < ksplit ? ksA[k] : ksB[k - ksplit]); scr[(2 * i + (lane >> 5)) * 33 + (lane & 31)] = x; }
;     LDS_WAIT(); asm volatile("" ::: "memory");
;     const int c = lane & 7;
; #pragma unroll
;     for (int j = 0; j < 4; ++j) { const int n = (lane >> 3) + 8 * j; const LAS float* s = scr + (8 * c) * 33 + n;
;         const unsigned long long o = (unsigned long long)pg8::pk4_fp8(s[0 * 33], s[1 * 33], s[2 * 33], s[3 * 33]) | ((unsigned long long)pg8::pk4_fp8(s[4 * 33], s[5 * 33], s[6 * 33], s[7 * 33]) << 32);
;         *(GAS unsigned long long*)(WT + (size_t)(n0 + n) * K + k0 + 8 * c) = o; }
;     LDS_WAIT(); asm volatile("" ::: "memory");
; }
; __global__ void __launch_bounds__(NWAVES * 64, 2) hybrid_fwd(Args args) {
;     ...
;             p0_transpose_item_f8<false>(args.in[16] + (size_t)l * FF * DM, FF, DM, DM / 32, (unsigned char*)(ws + WS_WDN + l * SZ_WDN), 128.f, args.in[16], args.in[16], 0, scr, r, lane);
	s_add_i32 s17, s16, 1920
	s_min_u32 s17, s17, 0xfff
	s_lshr_b32 s18, s17, 5
	s_add_i32 s18, s18, 0
	s_and_b32 s19, s17, 31
	s_lshl_b32 s18, s18, 21
	s_lshl_b32 s19, s19, 9
	s_add_u32 s18, s18, s19
	s_add_u32 s12, s2, s18
	s_addc_u32 s13, s3, 0
	global_load_dwordx4 v[100:103], v10, s[12:13]
	s_add_u32 s12, s12, 0x8000
	s_addc_u32 s13, s13, 0
	global_load_dwordx4 v[104:107], v10, s[12:13]
	s_add_u32 s12, s12, 0x8000
	s_addc_u32 s13, s13, 0
	global_load_dwordx4 v[108:111], v10, s[12:13]
	s_add_u32 s12, s12, 0x8000
	s_addc_u32 s13, s13, 0
	global_load_dwordx4 v[112:115], v10, s[12:13]
	s_add_u32 s12, s12, 0x8000
	s_addc_u32 s13, s13, 0
	global_load_dwordx4 v[116:119], v10, s[12:13]
	s_add_u32 s12, s12, 0x8000
	s_addc_u32 s13, s13, 0
	global_load_dwordx4 v[120:123], v10, s[12:13]
	s_add_u32 s12, s12, 0x8000
	s_addc_u32 s13, s13, 0
	global_load_dwordx4 v[124:127], v10, s[12:13]
	s_add_u32 s12, s12, 0x8000
	s_addc_u32 s13, s13, 0
	global_load_dwordx4 v[128:131], v10, s[12:13]
	s_add_i32 s17, s16, 1632
	s_min_u32 s17, s17, 0xfff
	s_lshr_b32 s18, s17, 5
	s_add_i32 s18, s18, 0
	s_and_b32 s19, s17, 31
	s_lshl_b32 s19, s19, 21
	s_lshl_b32 s18, s18, 7
	s_add_u32 s18, s18, s19
	s_add_u32 s14, s4, s18
	s_addc_u32 s15, s5, 0
	ds_read_b32 v132, v7
	ds_read_b32 v133, v7 offset:512
	ds_read_b32 v134, v7 offset:1024
	ds_read_b32 v135, v7 offset:1536
	ds_read_b32 v136, v7 offset:2048
	ds_read_b32 v137, v7 offset:2560
	ds_read_b32 v138, v7 offset:3072
	ds_read_b32 v139, v7 offset:3584
	ds_read_b32 v140, v7 offset:4096
	ds_read_b32 v141, v7 offset:4608
	ds_read_b32 v142, v7 offset:5120
	ds_read_b32 v143, v7 offset:5632
	ds_read_b32 v144, v7 offset:6144
	ds_read_b32 v145, v7 offset:6656
	ds_read_b32 v146, v7 offset:7168
	ds_read_b32 v147, v7 offset:7680
	s_waitcnt lgkmcnt(0)
	v_max_f32_e32 v132, v132, v132
	v_max_f32_e32 v133, v133, v133
	v_max_f32_e32 v134, v134, v134
	v_max_f32_e32 v135, v135, v135
	v_max_f32_e32 v136, v136, v136
	v_max_f32_e32 v137, v137, v137
	v_max_f32_e32 v138, v138, v138
	v_max_f32_e32 v139, v139, v139
	v_max_f32_e32 v140, v140, v140
	v_max_f32_e32 v141, v141, v141
	v_max_f32_e32 v142, v142, v142
	v_max_f32_e32 v143, v143, v143
	v_max_f32_e32 v144, v144, v144
	v_max_f32_e32 v145, v145, v145
	v_max_f32_e32 v146, v146, v146
	v_max_f32_e32 v147, v147, v147
	v_med3_f32 v132, v132, s20, v13
	v_med3_f32 v133, v133, s20, v13
	v_med3_f32 v134, v134, s20, v13
	v_med3_f32 v135, v135, s20, v13
	v_med3_f32 v136, v136, s20, v13
	v_med3_f32 v137, v137, s20, v13
	v_med3_f32 v138, v138, s20, v13
	v_med3_f32 v139, v139, s20, v13
	v_med3_f32 v140, v140, s20, v13
	v_med3_f32 v141, v141, s20, v13
	v_med3_f32 v142, v142, s20, v13
	v_med3_f32 v143, v143, s20, v13
	v_med3_f32 v144, v144, s20, v13
	v_med3_f32 v145, v145, s20, v13
	v_med3_f32 v146, v146, s20, v13
	v_med3_f32 v147, v147, s20, v13
	v_mov_b32_e32 v148, 0
	v_mov_b32_e32 v149, 0
	v_mov_b32_e32 v150, 0
	v_mov_b32_e32 v151, 0
	v_cvt_pk_fp8_f32 v148, v132, v133
	v_cvt_pk_fp8_f32 v149, v136, v137
	v_cvt_pk_fp8_f32 v150, v140, v141
	v_cvt_pk_fp8_f32 v151, v144, v145
	v_cvt_pk_fp8_f32 v148, v134, v135 op_sel:[0,0,1]
	v_cvt_pk_fp8_f32 v149, v138, v139 op_sel:[0,0,1]
	v_cvt_pk_fp8_f32 v150, v142, v143 op_sel:[0,0,1]
	v_cvt_pk_fp8_f32 v151, v146, v147 op_sel:[0,0,1]
	s_nop 0
	global_store_dwordx4 v11, v[148:151], s[14:15]
	ds_read_b32 v132, v9
	ds_read_b32 v133, v9 offset:512
	ds_read_b32 v134, v9 offset:1024
	ds_read_b32 v135, v9 offset:1536
	ds_read_b32 v136, v9 offset:2048
	ds_read_b32 v137, v9 offset:2560
	ds_read_b32 v138, v9 offset:3072
	ds_read_b32 v139, v9 offset:3584
	ds_read_b32 v140, v9 offset:4096
	ds_read_b32 v141, v9 offset:4608
	ds_read_b32 v142, v9 offset:5120
	ds_read_b32 v143, v9 offset:5632
	ds_read_b32 v144, v9 offset:6144
	ds_read_b32 v145, v9 offset:6656
	ds_read_b32 v146, v9 offset:7168
	ds_read_b32 v147, v9 offset:7680
	s_waitcnt lgkmcnt(0)
	v_max_f32_e32 v132, v132, v132
	v_max_f32_e32 v133, v133, v133
	v_max_f32_e32 v134, v134, v134
	v_max_f32_e32 v135, v135, v135
	v_max_f32_e32 v136, v136, v136
	v_max_f32_e32 v137, v137, v137
	v_max_f32_e32 v138, v138, v138
	v_max_f32_e32 v139, v139, v139
	v_max_f32_e32 v140, v140, v140
	v_max_f32_e32 v141, v141, v141
	v_max_f32_e32 v142, v142, v142
	v_max_f32_e32 v143, v143, v143
	v_max_f32_e32 v144, v144, v144
	v_max_f32_e32 v145, v145, v145
	v_max_f32_e32 v146, v146, v146
	v_max_f32_e32 v147, v147, v147
	v_med3_f32 v132, v132, s20, v13
	v_med3_f32 v133, v133, s20, v13
	v_med3_f32 v134, v134, s20, v13
	v_med3_f32 v135, v135, s20, v13
	v_med3_f32 v136, v136, s20, v13
	v_med3_f32 v137, v137, s20, v13
	v_med3_f32 v138, v138, s20, v13
	v_med3_f32 v139, v139, s20, v13
	v_med3_f32 v140, v140, s20, v13
	v_med3_f32 v141, v141, s20, v13
	v_med3_f32 v142, v142, s20, v13
	v_med3_f32 v143, v143, s20, v13
	v_med3_f32 v144, v144, s20, v13
	v_med3_f32 v145, v145, s20, v13
	v_med3_f32 v146, v146, s20, v13
	v_med3_f32 v147, v147, s20, v13
	v_mov_b32_e32 v148, 0
	v_mov_b32_e32 v149, 0
	v_mov_b32_e32 v150, 0
	v_mov_b32_e32 v151, 0
	v_cvt_pk_fp8_f32 v148, v132, v133
	v_cvt_pk_fp8_f32 v149, v136, v137
	v_cvt_pk_fp8_f32 v150, v140, v141
	v_cvt_pk_fp8_f32 v151, v144, v145
	v_cvt_pk_fp8_f32 v148, v134, v135 op_sel:[0,0,1]
	v_cvt_pk_fp8_f32 v149, v138, v139 op_sel:[0,0,1]
	v_cvt_pk_fp8_f32 v150, v142, v143 op_sel:[0,0,1]
	v_cvt_pk_fp8_f32 v151, v146, v147 op_sel:[0,0,1]
	s_nop 0
	global_store_dwordx4 v12, v[148:151], s[14:15]
	s_waitcnt vmcnt(22)
	v_mul_f32_e32 v36, 0x43000000, v36
	v_mul_f32_e32 v37, 0x43000000, v37
	v_mul_f32_e32 v38, 0x43000000, v38
	v_mul_f32_e32 v39, 0x43000000, v39
	ds_write_b128 v4, v[36:39]
	v_mul_f32_e32 v40, 0x43000000, v40
	v_mul_f32_e32 v41, 0x43000000, v41
	v_mul_f32_e32 v42, 0x43000000, v42
	v_mul_f32_e32 v43, 0x43000000, v43
	ds_write_b128 v4, v[40:43] offset:1024
	v_mul_f32_e32 v44, 0x43000000, v44
	v_mul_f32_e32 v45, 0x43000000, v45
	v_mul_f32_e32 v46, 0x43000000, v46
	v_mul_f32_e32 v47, 0x43000000, v47
	ds_write_b128 v4, v[44:47] offset:2048
	v_mul_f32_e32 v48, 0x43000000, v48
	v_mul_f32_e32 v49, 0x43000000, v49
	v_mul_f32_e32 v50, 0x43000000, v50
	v_mul_f32_e32 v51, 0x43000000, v51
	ds_write_b128 v4, v[48:51] offset:3072
	v_mul_f32_e32 v52, 0x43000000, v52
	v_mul_f32_e32 v53, 0x43000000, v53
	v_mul_f32_e32 v54, 0x43000000, v54
	v_mul_f32_e32 v55, 0x43000000, v55
	ds_write_b128 v4, v[52:55] offset:4096
	v_mul_f32_e32 v56, 0x43000000, v56
	v_mul_f32_e32 v57, 0x43000000, v57
	v_mul_f32_e32 v58, 0x43000000, v58
	v_mul_f32_e32 v59, 0x43000000, v59
	ds_write_b128 v4, v[56:59] offset:5120
	v_mul_f32_e32 v60, 0x43000000, v60
	v_mul_f32_e32 v61, 0x43000000, v61
	v_mul_f32_e32 v62, 0x43000000, v62
	v_mul_f32_e32 v63, 0x43000000, v63
	ds_write_b128 v4, v[60:63] offset:6144
	v_mul_f32_e32 v64, 0x43000000, v64
	v_mul_f32_e32 v65, 0x43000000, v65
	v_mul_f32_e32 v66, 0x43000000, v66
	v_mul_f32_e32 v67, 0x43000000, v67
	ds_write_b128 v4, v[64:67] offset:7168
	s_waitcnt lgkmcnt(0)
	s_barrier
; #define GAS __attribute__((address_space(1)))
; #define LAS __attribute__((address_space(3)))
; #define LDS_WAIT() asm volatile("s_waitcnt lgkmcnt(0)" ::: "memory")
;     const int pr = item >> 1, kb = 2 * (pr / nblk) + (item & 1), nb = pr % nblk, k0 = 64 * kb, n0 = 32 * nb;
;     const int nr = n0 + (lane & 31); const int sc = MAP == 1 ? src_col_in(nr) : nr;
;     float v[32];
; #pragma unroll
;     for (int i = 0; i < 32; ++i) v[i] = sc >= 0 ? W[(size_t)(k0 + 2 * i + (lane >> 5)) * Nsrc + sc] : 0.f;
; #pragma unroll
;     for (int i = 0; i < 32; ++i) { const int k = k0 + 2 * i + (lane >> 5); float x = v[i] * wscale; if (KS) x *= (k < ksplit ? ksA[k] : ksB[k - ksplit]); scr[(2 * i + (lane >> 5)) * 33 + (lane & 31)] = x; }
;     LDS_WAIT(); asm volatile("" ::: "memory");
;     const int c = lane & 7;
; #pragma unroll
;     for (int j = 0; j < 4; ++j) { const int n = (lane >> 3) + 8 * j; const LAS float* s = scr + (8 * c) * 33 + n;
;         const unsigned long long o = (unsigned long long)pg8::pk4_fp8(s[0 * 33], s[1 * 33], s[2 * 33], s[3 * 33]) | ((unsigned long long)pg8::pk4_fp8(s[4 * 33], s[5 * 33], s[6 * 33], s[7 * 33]) << 32);
;         *(GAS unsigned long long*)(WT + (size_t)(n0 + n) * K + k0 + 8 * c) = o; }
;     LDS_WAIT(); asm volatile("" ::: "memory");
; }
; __global__ void __launch_bounds__(NWAVES * 64, 2) hybrid_fwd(Args args) {
;     ...
;             p0_transpose_item_f8<false>(args.in[16] + (size_t)l * FF * DM, FF, DM, DM / 32, (unsigned char*)(ws + WS_WDN + l * SZ_WDN), 128.f, args.in[16], args.in[16], 0, scr, r, lane);
	s_add_i32 s17, s16, 2016
	s_min_u32 s17, s17, 0xfff
	s_lshr_b32 s18, s17, 5
	s_add_i32 s18, s18, 0
	s_and_b32 s19, s17, 31
	s_lshl_b32 s18, s18, 21
	s_lshl_b32 s19, s19, 9
	s_add_u32 s18, s18, s19
	s_add_u32 s12, s2, s18
	s_addc_u32 s13, s3, 0
	global_load_dwordx4 v[36:39], v10, s[12:13]
	s_add_u32 s12, s12, 0x8000
	s_addc_u32 s13, s13, 0
	global_load_dwordx4 v[40:43], v10, s[12:13]
	s_add_u32 s12, s12, 0x8000
	s_addc_u32 s13, s13, 0
	global_load_dwordx4 v[44:47], v10, s[12:13]
	s_add_u32 s12, s12, 0x8000
	s_addc_u32 s13, s13, 0
	global_load_dwordx4 v[48:51], v10, s[12:13]
	s_add_u32 s12, s12, 0x8000
	s_addc_u32 s13, s13, 0
	global_load_dwordx4 v[52:55], v10, s[12:13]
	s_add_u32 s12, s12, 0x8000
	s_addc_u32 s13, s13, 0
	global_load_dwordx4 v[56:59], v10, s[12:13]
	s_add_u32 s12, s12, 0x8000
	s_addc_u32 s13, s13, 0
	global_load_dwordx4 v[60:63], v10, s[12:13]
	s_add_u32 s12, s12, 0x8000
	s_addc_u32 s13, s13, 0
	global_load_dwordx4 v[64:67], v10, s[12:13]
	s_add_i32 s17, s16, 1728
	s_min_u32 s17, s17, 0xfff
	s_lshr_b32 s18, s17, 5
	s_add_i32 s18, s18, 0
	s_and_b32 s19, s17, 31
	s_lshl_b32 s19, s19, 21
	s_lshl_b32 s18, s18, 7
	s_add_u32 s18, s18, s19
	s_add_u32 s14, s4, s18
	s_addc_u32 s15, s5, 0
	ds_read_b32 v132, v6
	ds_read_b32 v133, v6 offset:512
	ds_read_b32 v134, v6 offset:1024
	ds_read_b32 v135, v6 offset:1536
	ds_read_b32 v136, v6 offset:2048
	ds_read_b32 v137, v6 offset:2560
	ds_read_b32 v138, v6 offset:3072
	ds_read_b32 v139, v6 offset:3584
	ds_read_b32 v140, v6 offset:4096
	ds_read_b32 v141, v6 offset:4608
	ds_read_b32 v142, v6 offset:5120
	ds_read_b32 v143, v6 offset:5632
	ds_read_b32 v144, v6 offset:6144
	ds_read_b32 v145, v6 offset:6656
	ds_read_b32 v146, v6 offset:7168
	ds_read_b32 v147, v6 offset:7680
	s_waitcnt lgkmcnt(0)
	v_max_f32_e32 v132, v132, v132
	v_max_f32_e32 v133, v133, v133
	v_max_f32_e32 v134, v134, v134
	v_max_f32_e32 v135, v135, v135
	v_max_f32_e32 v136, v136, v136
	v_max_f32_e32 v137, v137, v137
	v_max_f32_e32 v138, v138, v138
	v_max_f32_e32 v139, v139, v139
	v_max_f32_e32 v140, v140, v140
	v_max_f32_e32 v141, v141, v141
	v_max_f32_e32 v142, v142, v142
	v_max_f32_e32 v143, v143, v143
	v_max_f32_e32 v144, v144, v144
	v_max_f32_e32 v145, v145, v145
	v_max_f32_e32 v146, v146, v146
	v_max_f32_e32 v147, v147, v147
	v_med3_f32 v132, v132, s20, v13
	v_med3_f32 v133, v133, s20, v13
	v_med3_f32 v134, v134, s20, v13
	v_med3_f32 v135, v135, s20, v13
	v_med3_f32 v136, v136, s20, v13
	v_med3_f32 v137, v137, s20, v13
	v_med3_f32 v138, v138, s20, v13
	v_med3_f32 v139, v139, s20, v13
	v_med3_f32 v140, v140, s20, v13
	v_med3_f32 v141, v141, s20, v13
	v_med3_f32 v142, v142, s20, v13
	v_med3_f32 v143, v143, s20, v13
	v_med3_f32 v144, v144, s20, v13
	v_med3_f32 v145, v145, s20, v13
	v_med3_f32 v146, v146, s20, v13
	v_med3_f32 v147, v147, s20, v13
	v_mov_b32_e32 v148, 0
	v_mov_b32_e32 v149, 0
	v_mov_b32_e32 v150, 0
	v_mov_b32_e32 v151, 0
	v_cvt_pk_fp8_f32 v148, v132, v133
	v_cvt_pk_fp8_f32 v149, v136, v137
	v_cvt_pk_fp8_f32 v150, v140, v141
	v_cvt_pk_fp8_f32 v151, v144, v145
	v_cvt_pk_fp8_f32 v148, v134, v135 op_sel:[0,0,1]
	v_cvt_pk_fp8_f32 v149, v138, v139 op_sel:[0,0,1]
	v_cvt_pk_fp8_f32 v150, v142, v143 op_sel:[0,0,1]
	v_cvt_pk_fp8_f32 v151, v146, v147 op_sel:[0,0,1]
	s_nop 0
	global_store_dwordx4 v11, v[148:151], s[14:15]
	ds_read_b32 v132, v8
	ds_read_b32 v133, v8 offset:512
	ds_read_b32 v134, v8 offset:1024
	ds_read_b32 v135, v8 offset:1536
	ds_read_b32 v136, v8 offset:2048
	ds_read_b32 v137, v8 offset:2560
	ds_read_b32 v138, v8 offset:3072
	ds_read_b32 v139, v8 offset:3584
	ds_read_b32 v140, v8 offset:4096
	ds_read_b32 v141, v8 offset:4608
	ds_read_b32 v142, v8 offset:5120
	ds_read_b32 v143, v8 offset:5632
	ds_read_b32 v144, v8 offset:6144
	ds_read_b32 v145, v8 offset:6656
	ds_read_b32 v146, v8 offset:7168
	ds_read_b32 v147, v8 offset:7680
	s_waitcnt lgkmcnt(0)
	v_max_f32_e32 v132, v132, v132
	v_max_f32_e32 v133, v133, v133
	v_max_f32_e32 v134, v134, v134
	v_max_f32_e32 v135, v135, v135
	v_max_f32_e32 v136, v136, v136
	v_max_f32_e32 v137, v137, v137
	v_max_f32_e32 v138, v138, v138
	v_max_f32_e32 v139, v139, v139
	v_max_f32_e32 v140, v140, v140
	v_max_f32_e32 v141, v141, v141
	v_max_f32_e32 v142, v142, v142
	v_max_f32_e32 v143, v143, v143
	v_max_f32_e32 v144, v144, v144
	v_max_f32_e32 v145, v145, v145
	v_max_f32_e32 v146, v146, v146
	v_max_f32_e32 v147, v147, v147
	v_med3_f32 v132, v132, s20, v13
	v_med3_f32 v133, v133, s20, v13
	v_med3_f32 v134, v134, s20, v13
	v_med3_f32 v135, v135, s20, v13
	v_med3_f32 v136, v136, s20, v13
	v_med3_f32 v137, v137, s20, v13
	v_med3_f32 v138, v138, s20, v13
	v_med3_f32 v139, v139, s20, v13
	v_med3_f32 v140, v140, s20, v13
	v_med3_f32 v141, v141, s20, v13
	v_med3_f32 v142, v142, s20, v13
	v_med3_f32 v143, v143, s20, v13
	v_med3_f32 v144, v144, s20, v13
	v_med3_f32 v145, v145, s20, v13
	v_med3_f32 v146, v146, s20, v13
	v_med3_f32 v147, v147, s20, v13
	v_mov_b32_e32 v148, 0
	v_mov_b32_e32 v149, 0
	v_mov_b32_e32 v150, 0
	v_mov_b32_e32 v151, 0
	v_cvt_pk_fp8_f32 v148, v132, v133
	v_cvt_pk_fp8_f32 v149, v136, v137
	v_cvt_pk_fp8_f32 v150, v140, v141
	v_cvt_pk_fp8_f32 v151, v144, v145
	v_cvt_pk_fp8_f32 v148, v134, v135 op_sel:[0,0,1]
	v_cvt_pk_fp8_f32 v149, v138, v139 op_sel:[0,0,1]
	v_cvt_pk_fp8_f32 v150, v142, v143 op_sel:[0,0,1]
	v_cvt_pk_fp8_f32 v151, v146, v147 op_sel:[0,0,1]
	s_nop 0
	global_store_dwordx4 v12, v[148:151], s[14:15]
	s_waitcnt vmcnt(22)
	v_mul_f32_e32 v68, 0x43000000, v68
	v_mul_f32_e32 v69, 0x43000000, v69
	v_mul_f32_e32 v70, 0x43000000, v70
	v_mul_f32_e32 v71, 0x43000000, v71
	ds_write_b128 v5, v[68:71]
	v_mul_f32_e32 v72, 0x43000000, v72
	v_mul_f32_e32 v73, 0x43000000, v73
	v_mul_f32_e32 v74, 0x43000000, v74
	v_mul_f32_e32 v75, 0x43000000, v75
	ds_write_b128 v5, v[72:75] offset:1024
	v_mul_f32_e32 v76, 0x43000000, v76
	v_mul_f32_e32 v77, 0x43000000, v77
	v_mul_f32_e32 v78, 0x43000000, v78
	v_mul_f32_e32 v79, 0x43000000, v79
	ds_write_b128 v5, v[76:79] offset:2048
	v_mul_f32_e32 v80, 0x43000000, v80
	v_mul_f32_e32 v81, 0x43000000, v81
	v_mul_f32_e32 v82, 0x43000000, v82
	v_mul_f32_e32 v83, 0x43000000, v83
	ds_write_b128 v5, v[80:83] offset:3072
	v_mul_f32_e32 v84, 0x43000000, v84
	v_mul_f32_e32 v85, 0x43000000, v85
	v_mul_f32_e32 v86, 0x43000000, v86
	v_mul_f32_e32 v87, 0x43000000, v87
	ds_write_b128 v5, v[84:87] offset:4096
	v_mul_f32_e32 v88, 0x43000000, v88
	v_mul_f32_e32 v89, 0x43000000, v89
	v_mul_f32_e32 v90, 0x43000000, v90
	v_mul_f32_e32 v91, 0x43000000, v91
	ds_write_b128 v5, v[88:91] offset:5120
	v_mul_f32_e32 v92, 0x43000000, v92
	v_mul_f32_e32 v93, 0x43000000, v93
	v_mul_f32_e32 v94, 0x43000000, v94
	v_mul_f32_e32 v95, 0x43000000, v95
	ds_write_b128 v5, v[92:95] offset:6144
	v_mul_f32_e32 v96, 0x43000000, v96
	v_mul_f32_e32 v97, 0x43000000, v97
	v_mul_f32_e32 v98, 0x43000000, v98
	v_mul_f32_e32 v99, 0x43000000, v99
	ds_write_b128 v5, v[96:99] offset:7168
	s_waitcnt lgkmcnt(0)
	s_barrier
; #define GAS __attribute__((address_space(1)))
; #define LAS __attribute__((address_space(3)))
; #define LDS_WAIT() asm volatile("s_waitcnt lgkmcnt(0)" ::: "memory")
;     const int pr = item >> 1, kb = 2 * (pr / nblk) + (item & 1), nb = pr % nblk, k0 = 64 * kb, n0 = 32 * nb;
;     const int nr = n0 + (lane & 31); const int sc = MAP == 1 ? src_col_in(nr) : nr;
;     float v[32];
; #pragma unroll
;     for (int i = 0; i < 32; ++i) v[i] = sc >= 0 ? W[(size_t)(k0 + 2 * i + (lane >> 5)) * Nsrc + sc] : 0.f;
; #pragma unroll
;     for (int i = 0; i < 32; ++i) { const int k = k0 + 2 * i + (lane >> 5); float x = v[i] * wscale; if (KS) x *= (k < ksplit ? ksA[k] : ksB[k - ksplit]); scr[(2 * i + (lane >> 5)) * 33 + (lane & 31)] = x; }
;     LDS_WAIT(); asm volatile("" ::: "memory");
;     const int c = lane & 7;
; #pragma unroll
;     for (int j = 0; j < 4; ++j) { const int n = (lane >> 3) + 8 * j; const LAS float* s = scr + (8 * c) * 33 + n;
;         const unsigned long long o = (unsigned long long)pg8::pk4_fp8(s[0 * 33], s[1 * 33], s[2 * 33], s[3 * 33]) | ((unsigned long long)pg8::pk4_fp8(s[4 * 33], s[5 * 33], s[6 * 33], s[7 * 33]) << 32);
;         *(GAS unsigned long long*)(WT + (size_t)(n0 + n) * K + k0 + 8 * c) = o; }
;     LDS_WAIT(); asm volatile("" ::: "memory");
; }
; __global__ void __launch_bounds__(NWAVES * 64, 2) hybrid_fwd(Args args) {
;     ...
;             p0_transpose_item_f8<false>(args.in[16] + (size_t)l * FF * DM, FF, DM, DM / 32, (unsigned char*)(ws + WS_WDN + l * SZ_WDN), 128.f, args.in[16], args.in[16], 0, scr, r, lane);
	s_add_i32 s17, s16, 2112
	s_min_u32 s17, s17, 0xfff
	s_lshr_b32 s18, s17, 5
	s_add_i32 s18, s18, 0
	s_and_b32 s19, s17, 31
	s_lshl_b32 s18, s18, 21
	s_lshl_b32 s19, s19, 9
	s_add_u32 s18, s18, s19
	s_add_u32 s12, s2, s18
	s_addc_u32 s13, s3, 0
	global_load_dwordx4 v[68:71], v10, s[12:13]
	s_add_u32 s12, s12, 0x8000
	s_addc_u32 s13, s13, 0
	global_load_dwordx4 v[72:75], v10, s[12:13]
	s_add_u32 s12, s12, 0x8000
	s_addc_u32 s13, s13, 0
	global_load_dwordx4 v[76:79], v10, s[12:13]
	s_add_u32 s12, s12, 0x8000
	s_addc_u32 s13, s13, 0
	global_load_dwordx4 v[80:83], v10, s[12:13]
	s_add_u32 s12, s12, 0x8000
	s_addc_u32 s13, s13, 0
	global_load_dwordx4 v[84:87], v10, s[12:13]
	s_add_u32 s12, s12, 0x8000
	s_addc_u32 s13, s13, 0
	global_load_dwordx4 v[88:91], v10, s[12:13]
	s_add_u32 s12, s12, 0x8000
	s_addc_u32 s13, s13, 0
	global_load_dwordx4 v[92:95], v10, s[12:13]
	s_add_u32 s12, s12, 0x8000
	s_addc_u32 s13, s13, 0
	global_load_dwordx4 v[96:99], v10, s[12:13]
	s_add_i32 s17, s16, 1824
	s_min_u32 s17, s17, 0xfff
	s_lshr_b32 s18, s17, 5
	s_add_i32 s18, s18, 0
	s_and_b32 s19, s17, 31
	s_lshl_b32 s19, s19, 21
	s_lshl_b32 s18, s18, 7
	s_add_u32 s18, s18, s19
	s_add_u32 s14, s4, s18
	s_addc_u32 s15, s5, 0
	ds_read_b32 v132, v7
	ds_read_b32 v133, v7 offset:512
	ds_read_b32 v134, v7 offset:1024
	ds_read_b32 v135, v7 offset:1536
	ds_read_b32 v136, v7 offset:2048
	ds_read_b32 v137, v7 offset:2560
	ds_read_b32 v138, v7 offset:3072
	ds_read_b32 v139, v7 offset:3584
	ds_read_b32 v140, v7 offset:4096
	ds_read_b32 v141, v7 offset:4608
	ds_read_b32 v142, v7 offset:5120
	ds_read_b32 v143, v7 offset:5632
	ds_read_b32 v144, v7 offset:6144
	ds_read_b32 v145, v7 offset:6656
	ds_read_b32 v146, v7 offset:7168
	ds_read_b32 v147, v7 offset:7680
	s_waitcnt lgkmcnt(0)
	v_max_f32_e32 v132, v132, v132
	v_max_f32_e32 v133, v133, v133
	v_max_f32_e32 v134, v134, v134
	v_max_f32_e32 v135, v135, v135
	v_max_f32_e32 v136, v136, v136
	v_max_f32_e32 v137, v137, v137
	v_max_f32_e32 v138, v138, v138
	v_max_f32_e32 v139, v139, v139
	v_max_f32_e32 v140, v140, v140
	v_max_f32_e32 v141, v141, v141
	v_max_f32_e32 v142, v142, v142
	v_max_f32_e32 v143, v143, v143
	v_max_f32_e32 v144, v144, v144
	v_max_f32_e32 v145, v145, v145
	v_max_f32_e32 v146, v146, v146
	v_max_f32_e32 v147, v147, v147
	v_med3_f32 v132, v132, s20, v13
	v_med3_f32 v133, v133, s20, v13
	v_med3_f32 v134, v134, s20, v13
	v_med3_f32 v135, v135, s20, v13
	v_med3_f32 v136, v136, s20, v13
	v_med3_f32 v137, v137, s20, v13
	v_med3_f32 v138, v138, s20, v13
	v_med3_f32 v139, v139, s20, v13
	v_med3_f32 v140, v140, s20, v13
	v_med3_f32 v141, v141, s20, v13
	v_med3_f32 v142, v142, s20, v13
	v_med3_f32 v143, v143, s20, v13
	v_med3_f32 v144, v144, s20, v13
	v_med3_f32 v145, v145, s20, v13
	v_med3_f32 v146, v146, s20, v13
	v_med3_f32 v147, v147, s20, v13
	v_mov_b32_e32 v148, 0
	v_mov_b32_e32 v149, 0
	v_mov_b32_e32 v150, 0
	v_mov_b32_e32 v151, 0
	v_cvt_pk_fp8_f32 v148, v132, v133
	v_cvt_pk_fp8_f32 v149, v136, v137
	v_cvt_pk_fp8_f32 v150, v140, v141
	v_cvt_pk_fp8_f32 v151, v144, v145
	v_cvt_pk_fp8_f32 v148, v134, v135 op_sel:[0,0,1]
	v_cvt_pk_fp8_f32 v149, v138, v139 op_sel:[0,0,1]
	v_cvt_pk_fp8_f32 v150, v142, v143 op_sel:[0,0,1]
	v_cvt_pk_fp8_f32 v151, v146, v147 op_sel:[0,0,1]
	s_nop 0
	global_store_dwordx4 v11, v[148:151], s[14:15]
	ds_read_b32 v132, v9
	ds_read_b32 v133, v9 offset:512
	ds_read_b32 v134, v9 offset:1024
	ds_read_b32 v135, v9 offset:1536
	ds_read_b32 v136, v9 offset:2048
	ds_read_b32 v137, v9 offset:2560
	ds_read_b32 v138, v9 offset:3072
	ds_read_b32 v139, v9 offset:3584
	ds_read_b32 v140, v9 offset:4096
	ds_read_b32 v141, v9 offset:4608
	ds_read_b32 v142, v9 offset:5120
	ds_read_b32 v143, v9 offset:5632
	ds_read_b32 v144, v9 offset:6144
	ds_read_b32 v145, v9 offset:6656
	ds_read_b32 v146, v9 offset:7168
	ds_read_b32 v147, v9 offset:7680
	s_waitcnt lgkmcnt(0)
	v_max_f32_e32 v132, v132, v132
	v_max_f32_e32 v133, v133, v133
	v_max_f32_e32 v134, v134, v134
	v_max_f32_e32 v135, v135, v135
	v_max_f32_e32 v136, v136, v136
	v_max_f32_e32 v137, v137, v137
	v_max_f32_e32 v138, v138, v138
	v_max_f32_e32 v139, v139, v139
	v_max_f32_e32 v140, v140, v140
	v_max_f32_e32 v141, v141, v141
	v_max_f32_e32 v142, v142, v142
	v_max_f32_e32 v143, v143, v143
	v_max_f32_e32 v144, v144, v144
	v_max_f32_e32 v145, v145, v145
	v_max_f32_e32 v146, v146, v146
	v_max_f32_e32 v147, v147, v147
	v_med3_f32 v132, v132, s20, v13
	v_med3_f32 v133, v133, s20, v13
	v_med3_f32 v134, v134, s20, v13
	v_med3_f32 v135, v135, s20, v13
	v_med3_f32 v136, v136, s20, v13
	v_med3_f32 v137, v137, s20, v13
	v_med3_f32 v138, v138, s20, v13
	v_med3_f32 v139, v139, s20, v13
	v_med3_f32 v140, v140, s20, v13
	v_med3_f32 v141, v141, s20, v13
	v_med3_f32 v142, v142, s20, v13
	v_med3_f32 v143, v143, s20, v13
	v_med3_f32 v144, v144, s20, v13
	v_med3_f32 v145, v145, s20, v13
	v_med3_f32 v146, v146, s20, v13
	v_med3_f32 v147, v147, s20, v13
	v_mov_b32_e32 v148, 0
	v_mov_b32_e32 v149, 0
	v_mov_b32_e32 v150, 0
	v_mov_b32_e32 v151, 0
	v_cvt_pk_fp8_f32 v148, v132, v133
	v_cvt_pk_fp8_f32 v149, v136, v137
	v_cvt_pk_fp8_f32 v150, v140, v141
	v_cvt_pk_fp8_f32 v151, v144, v145
	v_cvt_pk_fp8_f32 v148, v134, v135 op_sel:[0,0,1]
	v_cvt_pk_fp8_f32 v149, v138, v139 op_sel:[0,0,1]
	v_cvt_pk_fp8_f32 v150, v142, v143 op_sel:[0,0,1]
	v_cvt_pk_fp8_f32 v151, v146, v147 op_sel:[0,0,1]
	s_nop 0
	global_store_dwordx4 v12, v[148:151], s[14:15]
	s_waitcnt vmcnt(22)
	v_mul_f32_e32 v100, 0x43000000, v100
	v_mul_f32_e32 v101, 0x43000000, v101
	v_mul_f32_e32 v102, 0x43000000, v102
	v_mul_f32_e32 v103, 0x43000000, v103
	ds_write_b128 v4, v[100:103]
	v_mul_f32_e32 v104, 0x43000000, v104
	v_mul_f32_e32 v105, 0x43000000, v105
	v_mul_f32_e32 v106, 0x43000000, v106
	v_mul_f32_e32 v107, 0x43000000, v107
	ds_write_b128 v4, v[104:107] offset:1024
	v_mul_f32_e32 v108, 0x43000000, v108
	v_mul_f32_e32 v109, 0x43000000, v109
	v_mul_f32_e32 v110, 0x43000000, v110
	v_mul_f32_e32 v111, 0x43000000, v111
	ds_write_b128 v4, v[108:111] offset:2048
	v_mul_f32_e32 v112, 0x43000000, v112
	v_mul_f32_e32 v113, 0x43000000, v113
	v_mul_f32_e32 v114, 0x43000000, v114
	v_mul_f32_e32 v115, 0x43000000, v115
	ds_write_b128 v4, v[112:115] offset:3072
	v_mul_f32_e32 v116, 0x43000000, v116
	v_mul_f32_e32 v117, 0x43000000, v117
	v_mul_f32_e32 v118, 0x43000000, v118
	v_mul_f32_e32 v119, 0x43000000, v119
	ds_write_b128 v4, v[116:119] offset:4096
	v_mul_f32_e32 v120, 0x43000000, v120
	v_mul_f32_e32 v121, 0x43000000, v121
	v_mul_f32_e32 v122, 0x43000000, v122
	v_mul_f32_e32 v123, 0x43000000, v123
	ds_write_b128 v4, v[120:123] offset:5120
	v_mul_f32_e32 v124, 0x43000000, v124
	v_mul_f32_e32 v125, 0x43000000, v125
	v_mul_f32_e32 v126, 0x43000000, v126
	v_mul_f32_e32 v127, 0x43000000, v127
	ds_write_b128 v4, v[124:127] offset:6144
	v_mul_f32_e32 v128, 0x43000000, v128
	v_mul_f32_e32 v129, 0x43000000, v129
	v_mul_f32_e32 v130, 0x43000000, v130
	v_mul_f32_e32 v131, 0x43000000, v131
	ds_write_b128 v4, v[128:131] offset:7168
	s_waitcnt lgkmcnt(0)
	s_barrier
; #define GAS __attribute__((address_space(1)))
; #define LAS __attribute__((address_space(3)))
; #define LDS_WAIT() asm volatile("s_waitcnt lgkmcnt(0)" ::: "memory")
;     const int pr = item >> 1, kb = 2 * (pr / nblk) + (item & 1), nb = pr % nblk, k0 = 64 * kb, n0 = 32 * nb;
;     const int nr = n0 + (lane & 31); const int sc = MAP == 1 ? src_col_in(nr) : nr;
;     float v[32];
; #pragma unroll
;     for (int i = 0; i < 32; ++i) v[i] = sc >= 0 ? W[(size_t)(k0 + 2 * i + (lane >> 5)) * Nsrc + sc] : 0.f;
; #pragma unroll
;     for (int i = 0; i < 32; ++i) { const int k = k0 + 2 * i + (lane >> 5); float x = v[i] * wscale; if (KS) x *= (k < ksplit ? ksA[k] : ksB[k - ksplit]); scr[(2 * i + (lane >> 5)) * 33 + (lane & 31)] = x; }
;     LDS_WAIT(); asm volatile("" ::: "memory");
;     const int c = lane & 7;
; #pragma unroll
;     for (int j = 0; j < 4; ++j) { const int n = (lane >> 3) + 8 * j; const LAS float* s = scr + (8 * c) * 33 + n;
;         const unsigned long long o = (unsigned long long)pg8::pk4_fp8(s[0 * 33], s[1 * 33], s[2 * 33], s[3 * 33]) | ((unsigned long long)pg8::pk4_fp8(s[4 * 33], s[5 * 33], s[6 * 33], s[7 * 33]) << 32);
;         *(GAS unsigned long long*)(WT + (size_t)(n0 + n) * K + k0 + 8 * c) = o; }
;     LDS_WAIT(); asm volatile("" ::: "memory");
; }
; __global__ void __launch_bounds__(NWAVES * 64, 2) hybrid_fwd(Args args) {
;     ...
;             p0_transpose_item_f8<false>(args.in[16] + (size_t)l * FF * DM, FF, DM, DM / 32, (unsigned char*)(ws + WS_WDN + l * SZ_WDN), 128.f, args.in[16], args.in[16], 0, scr, r, lane);
	s_add_i32 s17, s16, 2208
	s_min_u32 s17, s17, 0xfff
	s_lshr_b32 s18, s17, 5
	s_add_i32 s18, s18, 0
	s_and_b32 s19, s17, 31
	s_lshl_b32 s18, s18, 21
	s_lshl_b32 s19, s19, 9
	s_add_u32 s18, s18, s19
	s_add_u32 s12, s2, s18
	s_addc_u32 s13, s3, 0
	global_load_dwordx4 v[100:103], v10, s[12:13]
	s_add_u32 s12, s12, 0x8000
	s_addc_u32 s13, s13, 0
	global_load_dwordx4 v[104:107], v10, s[12:13]
	s_add_u32 s12, s12, 0x8000
	s_addc_u32 s13, s13, 0
	global_load_dwordx4 v[108:111], v10, s[12:13]
	s_add_u32 s12, s12, 0x8000
	s_addc_u32 s13, s13, 0
	global_load_dwordx4 v[112:115], v10, s[12:13]
	s_add_u32 s12, s12, 0x8000
	s_addc_u32 s13, s13, 0
	global_load_dwordx4 v[116:119], v10, s[12:13]
	s_add_u32 s12, s12, 0x8000
	s_addc_u32 s13, s13, 0
	global_load_dwordx4 v[120:123], v10, s[12:13]
	s_add_u32 s12, s12, 0x8000
	s_addc_u32 s13, s13, 0
	global_load_dwordx4 v[124:127], v10, s[12:13]
	s_add_u32 s12, s12, 0x8000
	s_addc_u32 s13, s13, 0
	global_load_dwordx4 v[128:131], v10, s[12:13]
	s_add_i32 s17, s16, 1920
	s_min_u32 s17, s17, 0xfff
	s_lshr_b32 s18, s17, 5
	s_add_i32 s18, s18, 0
	s_and_b32 s19, s17, 31
	s_lshl_b32 s19, s19, 21
	s_lshl_b32 s18, s18, 7
	s_add_u32 s18, s18, s19
	s_add_u32 s14, s4, s18
	s_addc_u32 s15, s5, 0
	ds_read_b32 v132, v6
	ds_read_b32 v133, v6 offset:512
	ds_read_b32 v134, v6 offset:1024
	ds_read_b32 v135, v6 offset:1536
	ds_read_b32 v136, v6 offset:2048
	ds_read_b32 v137, v6 offset:2560
	ds_read_b32 v138, v6 offset:3072
	ds_read_b32 v139, v6 offset:3584
	ds_read_b32 v140, v6 offset:4096
	ds_read_b32 v141, v6 offset:4608
	ds_read_b32 v142, v6 offset:5120
	ds_read_b32 v143, v6 offset:5632
	ds_read_b32 v144, v6 offset:6144
	ds_read_b32 v145, v6 offset:6656
	ds_read_b32 v146, v6 offset:7168
	ds_read_b32 v147, v6 offset:7680
	s_waitcnt lgkmcnt(0)
	v_max_f32_e32 v132, v132, v132
	v_max_f32_e32 v133, v133, v133
	v_max_f32_e32 v134, v134, v134
	v_max_f32_e32 v135, v135, v135
	v_max_f32_e32 v136, v136, v136
	v_max_f32_e32 v137, v137, v137
	v_max_f32_e32 v138, v138, v138
	v_max_f32_e32 v139, v139, v139
	v_max_f32_e32 v140, v140, v140
	v_max_f32_e32 v141, v141, v141
	v_max_f32_e32 v142, v142, v142
	v_max_f32_e32 v143, v143, v143
	v_max_f32_e32 v144, v144, v144
	v_max_f32_e32 v145, v145, v145
	v_max_f32_e32 v146, v146, v146
	v_max_f32_e32 v147, v147, v147
	v_med3_f32 v132, v132, s20, v13
	v_med3_f32 v133, v133, s20, v13
	v_med3_f32 v134, v134, s20, v13
	v_med3_f32 v135, v135, s20, v13
	v_med3_f32 v136, v136, s20, v13
	v_med3_f32 v137, v137, s20, v13
	v_med3_f32 v138, v138, s20, v13
	v_med3_f32 v139, v139, s20, v13
	v_med3_f32 v140, v140, s20, v13
	v_med3_f32 v141, v141, s20, v13
	v_med3_f32 v142, v142, s20, v13
	v_med3_f32 v143, v143, s20, v13
	v_med3_f32 v144, v144, s20, v13
	v_med3_f32 v145, v145, s20, v13
	v_med3_f32 v146, v146, s20, v13
	v_med3_f32 v147, v147, s20, v13
	v_mov_b32_e32 v148, 0
	v_mov_b32_e32 v149, 0
	v_mov_b32_e32 v150, 0
	v_mov_b32_e32 v151, 0
	v_cvt_pk_fp8_f32 v148, v132, v133
	v_cvt_pk_fp8_f32 v149, v136, v137
	v_cvt_pk_fp8_f32 v150, v140, v141
	v_cvt_pk_fp8_f32 v151, v144, v145
	v_cvt_pk_fp8_f32 v148, v134, v135 op_sel:[0,0,1]
	v_cvt_pk_fp8_f32 v149, v138, v139 op_sel:[0,0,1]
	v_cvt_pk_fp8_f32 v150, v142, v143 op_sel:[0,0,1]
	v_cvt_pk_fp8_f32 v151, v146, v147 op_sel:[0,0,1]
	s_nop 0
	global_store_dwordx4 v11, v[148:151], s[14:15]
	ds_read_b32 v132, v8
	ds_read_b32 v133, v8 offset:512
	ds_read_b32 v134, v8 offset:1024
	ds_read_b32 v135, v8 offset:1536
	ds_read_b32 v136, v8 offset:2048
	ds_read_b32 v137, v8 offset:2560
	ds_read_b32 v138, v8 offset:3072
	ds_read_b32 v139, v8 offset:3584
	ds_read_b32 v140, v8 offset:4096
	ds_read_b32 v141, v8 offset:4608
	ds_read_b32 v142, v8 offset:5120
	ds_read_b32 v143, v8 offset:5632
	ds_read_b32 v144, v8 offset:6144
	ds_read_b32 v145, v8 offset:6656
	ds_read_b32 v146, v8 offset:7168
	ds_read_b32 v147, v8 offset:7680
	s_waitcnt lgkmcnt(0)
	v_max_f32_e32 v132, v132, v132
	v_max_f32_e32 v133, v133, v133
	v_max_f32_e32 v134, v134, v134
	v_max_f32_e32 v135, v135, v135
	v_max_f32_e32 v136, v136, v136
	v_max_f32_e32 v137, v137, v137
	v_max_f32_e32 v138, v138, v138
	v_max_f32_e32 v139, v139, v139
	v_max_f32_e32 v140, v140, v140
	v_max_f32_e32 v141, v141, v141
	v_max_f32_e32 v142, v142, v142
	v_max_f32_e32 v143, v143, v143
	v_max_f32_e32 v144, v144, v144
	v_max_f32_e32 v145, v145, v145
	v_max_f32_e32 v146, v146, v146
	v_max_f32_e32 v147, v147, v147
	v_med3_f32 v132, v132, s20, v13
	v_med3_f32 v133, v133, s20, v13
	v_med3_f32 v134, v134, s20, v13
	v_med3_f32 v135, v135, s20, v13
	v_med3_f32 v136, v136, s20, v13
	v_med3_f32 v137, v137, s20, v13
	v_med3_f32 v138, v138, s20, v13
	v_med3_f32 v139, v139, s20, v13
	v_med3_f32 v140, v140, s20, v13
	v_med3_f32 v141, v141, s20, v13
	v_med3_f32 v142, v142, s20, v13
	v_med3_f32 v143, v143, s20, v13
	v_med3_f32 v144, v144, s20, v13
	v_med3_f32 v145, v145, s20, v13
	v_med3_f32 v146, v146, s20, v13
	v_med3_f32 v147, v147, s20, v13
	v_mov_b32_e32 v148, 0
	v_mov_b32_e32 v149, 0
	v_mov_b32_e32 v150, 0
	v_mov_b32_e32 v151, 0
	v_cvt_pk_fp8_f32 v148, v132, v133
	v_cvt_pk_fp8_f32 v149, v136, v137
	v_cvt_pk_fp8_f32 v150, v140, v141
	v_cvt_pk_fp8_f32 v151, v144, v145
	v_cvt_pk_fp8_f32 v148, v134, v135 op_sel:[0,0,1]
	v_cvt_pk_fp8_f32 v149, v138, v139 op_sel:[0,0,1]
	v_cvt_pk_fp8_f32 v150, v142, v143 op_sel:[0,0,1]
	v_cvt_pk_fp8_f32 v151, v146, v147 op_sel:[0,0,1]
	s_nop 0
	global_store_dwordx4 v12, v[148:151], s[14:15]
	s_waitcnt vmcnt(22)
	v_mul_f32_e32 v36, 0x43000000, v36
	v_mul_f32_e32 v37, 0x43000000, v37
	v_mul_f32_e32 v38, 0x43000000, v38
	v_mul_f32_e32 v39, 0x43000000, v39
	ds_write_b128 v5, v[36:39]
	v_mul_f32_e32 v40, 0x43000000, v40
	v_mul_f32_e32 v41, 0x43000000, v41
	v_mul_f32_e32 v42, 0x43000000, v42
	v_mul_f32_e32 v43, 0x43000000, v43
	ds_write_b128 v5, v[40:43] offset:1024
	v_mul_f32_e32 v44, 0x43000000, v44
	v_mul_f32_e32 v45, 0x43000000, v45
	v_mul_f32_e32 v46, 0x43000000, v46
	v_mul_f32_e32 v47, 0x43000000, v47
	ds_write_b128 v5, v[44:47] offset:2048
	v_mul_f32_e32 v48, 0x43000000, v48
	v_mul_f32_e32 v49, 0x43000000, v49
	v_mul_f32_e32 v50, 0x43000000, v50
	v_mul_f32_e32 v51, 0x43000000, v51
	ds_write_b128 v5, v[48:51] offset:3072
	v_mul_f32_e32 v52, 0x43000000, v52
	v_mul_f32_e32 v53, 0x43000000, v53
	v_mul_f32_e32 v54, 0x43000000, v54
	v_mul_f32_e32 v55, 0x43000000, v55
	ds_write_b128 v5, v[52:55] offset:4096
	v_mul_f32_e32 v56, 0x43000000, v56
	v_mul_f32_e32 v57, 0x43000000, v57
	v_mul_f32_e32 v58, 0x43000000, v58
	v_mul_f32_e32 v59, 0x43000000, v59
	ds_write_b128 v5, v[56:59] offset:5120
	v_mul_f32_e32 v60, 0x43000000, v60
	v_mul_f32_e32 v61, 0x43000000, v61
	v_mul_f32_e32 v62, 0x43000000, v62
	v_mul_f32_e32 v63, 0x43000000, v63
	ds_write_b128 v5, v[60:63] offset:6144
	v_mul_f32_e32 v64, 0x43000000, v64
	v_mul_f32_e32 v65, 0x43000000, v65
	v_mul_f32_e32 v66, 0x43000000, v66
	v_mul_f32_e32 v67, 0x43000000, v67
	ds_write_b128 v5, v[64:67] offset:7168
	s_waitcnt lgkmcnt(0)
	s_barrier
; #define GAS __attribute__((address_space(1)))
; #define LAS __attribute__((address_space(3)))
; #define LDS_WAIT() asm volatile("s_waitcnt lgkmcnt(0)" ::: "memory")
;     const int pr = item >> 1, kb = 2 * (pr / nblk) + (item & 1), nb = pr % nblk, k0 = 64 * kb, n0 = 32 * nb;
;     const int nr = n0 + (lane & 31); const int sc = MAP == 1 ? src_col_in(nr) : nr;
;     float v[32];
; #pragma unroll
;     for (int i = 0; i < 32; ++i) v[i] = sc >= 0 ? W[(size_t)(k0 + 2 * i + (lane >> 5)) * Nsrc + sc] : 0.f;
; #pragma unroll
;     for (int i = 0; i < 32; ++i) { const int k = k0 + 2 * i + (lane >> 5); float x = v[i] * wscale; if (KS) x *= (k < ksplit ? ksA[k] : ksB[k - ksplit]); scr[(2 * i + (lane >> 5)) * 33 + (lane & 31)] = x; }
;     LDS_WAIT(); asm volatile("" ::: "memory");
;     const int c = lane & 7;
; #pragma unroll
;     for (int j = 0; j < 4; ++j) { const int n = (lane >> 3) + 8 * j; const LAS float* s = scr + (8 * c) * 33 + n;
;         const unsigned long long o = (unsigned long long)pg8::pk4_fp8(s[0 * 33], s[1 * 33], s[2 * 33], s[3 * 33]) | ((unsigned long long)pg8::pk4_fp8(s[4 * 33], s[5 * 33], s[6 * 33], s[7 * 33]) << 32);
;         *(GAS unsigned long long*)(WT + (size_t)(n0 + n) * K + k0 + 8 * c) = o; }
;     LDS_WAIT(); asm volatile("" ::: "memory");
; }
; __global__ void __launch_bounds__(NWAVES * 64, 2) hybrid_fwd(Args args) {
;     ...
;             p0_transpose_item_f8<false>(args.in[16] + (size_t)l * FF * DM, FF, DM, DM / 32, (unsigned char*)(ws + WS_WDN + l * SZ_WDN), 128.f, args.in[16], args.in[16], 0, scr, r, lane);
	s_add_i32 s17, s16, 2304
	s_min_u32 s17, s17, 0xfff
	s_lshr_b32 s18, s17, 5
	s_add_i32 s18, s18, 0
	s_and_b32 s19, s17, 31
	s_lshl_b32 s18, s18, 21
	s_lshl_b32 s19, s19, 9
	s_add_u32 s18, s18, s19
	s_add_u32 s12, s2, s18
	s_addc_u32 s13, s3, 0
	global_load_dwordx4 v[36:39], v10, s[12:13]
	s_add_u32 s12, s12, 0x8000
	s_addc_u32 s13, s13, 0
	global_load_dwordx4 v[40:43], v10, s[12:13]
	s_add_u32 s12, s12, 0x8000
	s_addc_u32 s13, s13, 0
	global_load_dwordx4 v[44:47], v10, s[12:13]
	s_add_u32 s12, s12, 0x8000
	s_addc_u32 s13, s13, 0
	global_load_dwordx4 v[48:51], v10, s[12:13]
	s_add_u32 s12, s12, 0x8000
	s_addc_u32 s13, s13, 0
	global_load_dwordx4 v[52:55], v10, s[12:13]
	s_add_u32 s12, s12, 0x8000
	s_addc_u32 s13, s13, 0
	global_load_dwordx4 v[56:59], v10, s[12:13]
	s_add_u32 s12, s12, 0x8000
	s_addc_u32 s13, s13, 0
	global_load_dwordx4 v[60:63], v10, s[12:13]
	s_add_u32 s12, s12, 0x8000
	s_addc_u32 s13, s13, 0
	global_load_dwordx4 v[64:67], v10, s[12:13]
	s_add_i32 s17, s16, 2016
	s_min_u32 s17, s17, 0xfff
	s_lshr_b32 s18, s17, 5
	s_add_i32 s18, s18, 0
	s_and_b32 s19, s17, 31
	s_lshl_b32 s19, s19, 21
	s_lshl_b32 s18, s18, 7
	s_add_u32 s18, s18, s19
	s_add_u32 s14, s4, s18
	s_addc_u32 s15, s5, 0
	ds_read_b32 v132, v7
	ds_read_b32 v133, v7 offset:512
	ds_read_b32 v134, v7 offset:1024
	ds_read_b32 v135, v7 offset:1536
	ds_read_b32 v136, v7 offset:2048
	ds_read_b32 v137, v7 offset:2560
	ds_read_b32 v138, v7 offset:3072
	ds_read_b32 v139, v7 offset:3584
	ds_read_b32 v140, v7 offset:4096
	ds_read_b32 v141, v7 offset:4608
	ds_read_b32 v142, v7 offset:5120
	ds_read_b32 v143, v7 offset:5632
	ds_read_b32 v144, v7 offset:6144
	ds_read_b32 v145, v7 offset:6656
	ds_read_b32 v146, v7 offset:7168
	ds_read_b32 v147, v7 offset:7680
	s_waitcnt lgkmcnt(0)
	v_max_f32_e32 v132, v132, v132
	v_max_f32_e32 v133, v133, v133
	v_max_f32_e32 v134, v134, v134
	v_max_f32_e32 v135, v135, v135
	v_max_f32_e32 v136, v136, v136
	v_max_f32_e32 v137, v137, v137
	v_max_f32_e32 v138, v138, v138
	v_max_f32_e32 v139, v139, v139
	v_max_f32_e32 v140, v140, v140
	v_max_f32_e32 v141, v141, v141
	v_max_f32_e32 v142, v142, v142
	v_max_f32_e32 v143, v143, v143
	v_max_f32_e32 v144, v144, v144
	v_max_f32_e32 v145, v145, v145
	v_max_f32_e32 v146, v146, v146
	v_max_f32_e32 v147, v147, v147
	v_med3_f32 v132, v132, s20, v13
	v_med3_f32 v133, v133, s20, v13
	v_med3_f32 v134, v134, s20, v13
	v_med3_f32 v135, v135, s20, v13
	v_med3_f32 v136, v136, s20, v13
	v_med3_f32 v137, v137, s20, v13
	v_med3_f32 v138, v138, s20, v13
	v_med3_f32 v139, v139, s20, v13
	v_med3_f32 v140, v140, s20, v13
	v_med3_f32 v141, v141, s20, v13
	v_med3_f32 v142, v142, s20, v13
	v_med3_f32 v143, v143, s20, v13
	v_med3_f32 v144, v144, s20, v13
	v_med3_f32 v145, v145, s20, v13
	v_med3_f32 v146, v146, s20, v13
	v_med3_f32 v147, v147, s20, v13
	v_mov_b32_e32 v148, 0
	v_mov_b32_e32 v149, 0
	v_mov_b32_e32 v150, 0
	v_mov_b32_e32 v151, 0
	v_cvt_pk_fp8_f32 v148, v132, v133
	v_cvt_pk_fp8_f32 v149, v136, v137
	v_cvt_pk_fp8_f32 v150, v140, v141
	v_cvt_pk_fp8_f32 v151, v144, v145
	v_cvt_pk_fp8_f32 v148, v134, v135 op_sel:[0,0,1]
	v_cvt_pk_fp8_f32 v149, v138, v139 op_sel:[0,0,1]
	v_cvt_pk_fp8_f32 v150, v142, v143 op_sel:[0,0,1]
	v_cvt_pk_fp8_f32 v151, v146, v147 op_sel:[0,0,1]
	s_nop 0
	global_store_dwordx4 v11, v[148:151], s[14:15]
	ds_read_b32 v132, v9
	ds_read_b32 v133, v9 offset:512
	ds_read_b32 v134, v9 offset:1024
	ds_read_b32 v135, v9 offset:1536
	ds_read_b32 v136, v9 offset:2048
	ds_read_b32 v137, v9 offset:2560
	ds_read_b32 v138, v9 offset:3072
	ds_read_b32 v139, v9 offset:3584
	ds_read_b32 v140, v9 offset:4096
	ds_read_b32 v141, v9 offset:4608
	ds_read_b32 v142, v9 offset:5120
	ds_read_b32 v143, v9 offset:5632
	ds_read_b32 v144, v9 offset:6144
	ds_read_b32 v145, v9 offset:6656
	ds_read_b32 v146, v9 offset:7168
	ds_read_b32 v147, v9 offset:7680
	s_waitcnt lgkmcnt(0)
	v_max_f32_e32 v132, v132, v132
	v_max_f32_e32 v133, v133, v133
	v_max_f32_e32 v134, v134, v134
	v_max_f32_e32 v135, v135, v135
	v_max_f32_e32 v136, v136, v136
	v_max_f32_e32 v137, v137, v137
	v_max_f32_e32 v138, v138, v138
	v_max_f32_e32 v139, v139, v139
	v_max_f32_e32 v140, v140, v140
	v_max_f32_e32 v141, v141, v141
	v_max_f32_e32 v142, v142, v142
	v_max_f32_e32 v143, v143, v143
	v_max_f32_e32 v144, v144, v144
	v_max_f32_e32 v145, v145, v145
	v_max_f32_e32 v146, v146, v146
	v_max_f32_e32 v147, v147, v147
	v_med3_f32 v132, v132, s20, v13
	v_med3_f32 v133, v133, s20, v13
	v_med3_f32 v134, v134, s20, v13
	v_med3_f32 v135, v135, s20, v13
	v_med3_f32 v136, v136, s20, v13
	v_med3_f32 v137, v137, s20, v13
	v_med3_f32 v138, v138, s20, v13
	v_med3_f32 v139, v139, s20, v13
	v_med3_f32 v140, v140, s20, v13
	v_med3_f32 v141, v141, s20, v13
	v_med3_f32 v142, v142, s20, v13
	v_med3_f32 v143, v143, s20, v13
	v_med3_f32 v144, v144, s20, v13
	v_med3_f32 v145, v145, s20, v13
	v_med3_f32 v146, v146, s20, v13
	v_med3_f32 v147, v147, s20, v13
	v_mov_b32_e32 v148, 0
	v_mov_b32_e32 v149, 0
	v_mov_b32_e32 v150, 0
	v_mov_b32_e32 v151, 0
	v_cvt_pk_fp8_f32 v148, v132, v133
	v_cvt_pk_fp8_f32 v149, v136, v137
	v_cvt_pk_fp8_f32 v150, v140, v141
	v_cvt_pk_fp8_f32 v151, v144, v145
	v_cvt_pk_fp8_f32 v148, v134, v135 op_sel:[0,0,1]
	v_cvt_pk_fp8_f32 v149, v138, v139 op_sel:[0,0,1]
	v_cvt_pk_fp8_f32 v150, v142, v143 op_sel:[0,0,1]
	v_cvt_pk_fp8_f32 v151, v146, v147 op_sel:[0,0,1]
	s_nop 0
	global_store_dwordx4 v12, v[148:151], s[14:15]
	s_waitcnt vmcnt(22)
	v_mul_f32_e32 v68, 0x43000000, v68
	v_mul_f32_e32 v69, 0x43000000, v69
	v_mul_f32_e32 v70, 0x43000000, v70
	v_mul_f32_e32 v71, 0x43000000, v71
	ds_write_b128 v4, v[68:71]
	v_mul_f32_e32 v72, 0x43000000, v72
	v_mul_f32_e32 v73, 0x43000000, v73
	v_mul_f32_e32 v74, 0x43000000, v74
	v_mul_f32_e32 v75, 0x43000000, v75
	ds_write_b128 v4, v[72:75] offset:1024
	v_mul_f32_e32 v76, 0x43000000, v76
	v_mul_f32_e32 v77, 0x43000000, v77
	v_mul_f32_e32 v78, 0x43000000, v78
	v_mul_f32_e32 v79, 0x43000000, v79
	ds_write_b128 v4, v[76:79] offset:2048
	v_mul_f32_e32 v80, 0x43000000, v80
	v_mul_f32_e32 v81, 0x43000000, v81
	v_mul_f32_e32 v82, 0x43000000, v82
	v_mul_f32_e32 v83, 0x43000000, v83
	ds_write_b128 v4, v[80:83] offset:3072
	v_mul_f32_e32 v84, 0x43000000, v84
	v_mul_f32_e32 v85, 0x43000000, v85
	v_mul_f32_e32 v86, 0x43000000, v86
	v_mul_f32_e32 v87, 0x43000000, v87
	ds_write_b128 v4, v[84:87] offset:4096
	v_mul_f32_e32 v88, 0x43000000, v88
	v_mul_f32_e32 v89, 0x43000000, v89
	v_mul_f32_e32 v90, 0x43000000, v90
	v_mul_f32_e32 v91, 0x43000000, v91
	ds_write_b128 v4, v[88:91] offset:5120
	v_mul_f32_e32 v92, 0x43000000, v92
	v_mul_f32_e32 v93, 0x43000000, v93
	v_mul_f32_e32 v94, 0x43000000, v94
	v_mul_f32_e32 v95, 0x43000000, v95
	ds_write_b128 v4, v[92:95] offset:6144
	v_mul_f32_e32 v96, 0x43000000, v96
	v_mul_f32_e32 v97, 0x43000000, v97
	v_mul_f32_e32 v98, 0x43000000, v98
	v_mul_f32_e32 v99, 0x43000000, v99
	ds_write_b128 v4, v[96:99] offset:7168
	s_waitcnt lgkmcnt(0)
	s_barrier
; #define GAS __attribute__((address_space(1)))
; #define LAS __attribute__((address_space(3)))
; #define LDS_WAIT() asm volatile("s_waitcnt lgkmcnt(0)" ::: "memory")
;     const int pr = item >> 1, kb = 2 * (pr / nblk) + (item & 1), nb = pr % nblk, k0 = 64 * kb, n0 = 32 * nb;
;     const int nr = n0 + (lane & 31); const int sc = MAP == 1 ? src_col_in(nr) : nr;
;     float v[32];
; #pragma unroll
;     for (int i = 0; i < 32; ++i) v[i] = sc >= 0 ? W[(size_t)(k0 + 2 * i + (lane >> 5)) * Nsrc + sc] : 0.f;
; #pragma unroll
;     for (int i = 0; i < 32; ++i) { const int k = k0 + 2 * i + (lane >> 5); float x = v[i] * wscale; if (KS) x *= (k < ksplit ? ksA[k] : ksB[k - ksplit]); scr[(2 * i + (lane >> 5)) * 33 + (lane & 31)] = x; }
;     LDS_WAIT(); asm volatile("" ::: "memory");
;     const int c = lane & 7;
; #pragma unroll
;     for (int j = 0; j < 4; ++j) { const int n = (lane >> 3) + 8 * j; const LAS float* s = scr + (8 * c) * 33 + n;
;         const unsigned long long o = (unsigned long long)pg8::pk4_fp8(s[0 * 33], s[1 * 33], s[2 * 33], s[3 * 33]) | ((unsigned long long)pg8::pk4_fp8(s[4 * 33], s[5 * 33], s[6 * 33], s[7 * 33]) << 32);
;         *(GAS unsigned long long*)(WT + (size_t)(n0 + n) * K + k0 + 8 * c) = o; }
;     LDS_WAIT(); asm volatile("" ::: "memory");
; }
; __global__ void __launch_bounds__(NWAVES * 64, 2) hybrid_fwd(Args args) {
;     ...
;             p0_transpose_item_f8<false>(args.in[16] + (size_t)l * FF * DM, FF, DM, DM / 32, (unsigned char*)(ws + WS_WDN + l * SZ_WDN), 128.f, args.in[16], args.in[16], 0, scr, r, lane);
	s_add_i32 s17, s16, 2400
	s_min_u32 s17, s17, 0xfff
	s_lshr_b32 s18, s17, 5
	s_add_i32 s18, s18, 0
	s_and_b32 s19, s17, 31
	s_lshl_b32 s18, s18, 21
	s_lshl_b32 s19, s19, 9
	s_add_u32 s18, s18, s19
	s_add_u32 s12, s2, s18
	s_addc_u32 s13, s3, 0
	global_load_dwordx4 v[68:71], v10, s[12:13]
	s_add_u32 s12, s12, 0x8000
	s_addc_u32 s13, s13, 0
	global_load_dwordx4 v[72:75], v10, s[12:13]
	s_add_u32 s12, s12, 0x8000
	s_addc_u32 s13, s13, 0
	global_load_dwordx4 v[76:79], v10, s[12:13]
	s_add_u32 s12, s12, 0x8000
	s_addc_u32 s13, s13, 0
	global_load_dwordx4 v[80:83], v10, s[12:13]
	s_add_u32 s12, s12, 0x8000
	s_addc_u32 s13, s13, 0
	global_load_dwordx4 v[84:87], v10, s[12:13]
	s_add_u32 s12, s12, 0x8000
	s_addc_u32 s13, s13, 0
	global_load_dwordx4 v[88:91], v10, s[12:13]
	s_add_u32 s12, s12, 0x8000
	s_addc_u32 s13, s13, 0
	global_load_dwordx4 v[92:95], v10, s[12:13]
	s_add_u32 s12, s12, 0x8000
	s_addc_u32 s13, s13, 0
	global_load_dwordx4 v[96:99], v10, s[12:13]
	s_add_i32 s17, s16, 2112
	s_min_u32 s17, s17, 0xfff
	s_lshr_b32 s18, s17, 5
	s_add_i32 s18, s18, 0
	s_and_b32 s19, s17, 31
	s_lshl_b32 s19, s19, 21
	s_lshl_b32 s18, s18, 7
	s_add_u32 s18, s18, s19
	s_add_u32 s14, s4, s18
	s_addc_u32 s15, s5, 0
	ds_read_b32 v132, v6
	ds_read_b32 v133, v6 offset:512
	ds_read_b32 v134, v6 offset:1024
	ds_read_b32 v135, v6 offset:1536
	ds_read_b32 v136, v6 offset:2048
	ds_read_b32 v137, v6 offset:2560
	ds_read_b32 v138, v6 offset:3072
	ds_read_b32 v139, v6 offset:3584
	ds_read_b32 v140, v6 offset:4096
	ds_read_b32 v141, v6 offset:4608
	ds_read_b32 v142, v6 offset:5120
	ds_read_b32 v143, v6 offset:5632
	ds_read_b32 v144, v6 offset:6144
	ds_read_b32 v145, v6 offset:6656
	ds_read_b32 v146, v6 offset:7168
	ds_read_b32 v147, v6 offset:7680
	s_waitcnt lgkmcnt(0)
	v_max_f32_e32 v132, v132, v132
	v_max_f32_e32 v133, v133, v133
	v_max_f32_e32 v134, v134, v134
	v_max_f32_e32 v135, v135, v135
	v_max_f32_e32 v136, v136, v136
	v_max_f32_e32 v137, v137, v137
	v_max_f32_e32 v138, v138, v138
	v_max_f32_e32 v139, v139, v139
	v_max_f32_e32 v140, v140, v140
	v_max_f32_e32 v141, v141, v141
	v_max_f32_e32 v142, v142, v142
	v_max_f32_e32 v143, v143, v143
	v_max_f32_e32 v144, v144, v144
	v_max_f32_e32 v145, v145, v145
	v_max_f32_e32 v146, v146, v146
	v_max_f32_e32 v147, v147, v147
	v_med3_f32 v132, v132, s20, v13
	v_med3_f32 v133, v133, s20, v13
	v_med3_f32 v134, v134, s20, v13
	v_med3_f32 v135, v135, s20, v13
	v_med3_f32 v136, v136, s20, v13
	v_med3_f32 v137, v137, s20, v13
	v_med3_f32 v138, v138, s20, v13
	v_med3_f32 v139, v139, s20, v13
	v_med3_f32 v140, v140, s20, v13
	v_med3_f32 v141, v141, s20, v13
	v_med3_f32 v142, v142, s20, v13
	v_med3_f32 v143, v143, s20, v13
	v_med3_f32 v144, v144, s20, v13
	v_med3_f32 v145, v145, s20, v13
	v_med3_f32 v146, v146, s20, v13
	v_med3_f32 v147, v147, s20, v13
	v_mov_b32_e32 v148, 0
	v_mov_b32_e32 v149, 0
	v_mov_b32_e32 v150, 0
	v_mov_b32_e32 v151, 0
	v_cvt_pk_fp8_f32 v148, v132, v133
	v_cvt_pk_fp8_f32 v149, v136, v137
	v_cvt_pk_fp8_f32 v150, v140, v141
	v_cvt_pk_fp8_f32 v151, v144, v145
	v_cvt_pk_fp8_f32 v148, v134, v135 op_sel:[0,0,1]
	v_cvt_pk_fp8_f32 v149, v138, v139 op_sel:[0,0,1]
	v_cvt_pk_fp8_f32 v150, v142, v143 op_sel:[0,0,1]
	v_cvt_pk_fp8_f32 v151, v146, v147 op_sel:[0,0,1]
	s_nop 0
	global_store_dwordx4 v11, v[148:151], s[14:15]
	ds_read_b32 v132, v8
	ds_read_b32 v133, v8 offset:512
	ds_read_b32 v134, v8 offset:1024
	ds_read_b32 v135, v8 offset:1536
	ds_read_b32 v136, v8 offset:2048
	ds_read_b32 v137, v8 offset:2560
	ds_read_b32 v138, v8 offset:3072
	ds_read_b32 v139, v8 offset:3584
	ds_read_b32 v140, v8 offset:4096
	ds_read_b32 v141, v8 offset:4608
	ds_read_b32 v142, v8 offset:5120
	ds_read_b32 v143, v8 offset:5632
	ds_read_b32 v144, v8 offset:6144
	ds_read_b32 v145, v8 offset:6656
	ds_read_b32 v146, v8 offset:7168
	ds_read_b32 v147, v8 offset:7680
	s_waitcnt lgkmcnt(0)
	v_max_f32_e32 v132, v132, v132
	v_max_f32_e32 v133, v133, v133
	v_max_f32_e32 v134, v134, v134
	v_max_f32_e32 v135, v135, v135
	v_max_f32_e32 v136, v136, v136
	v_max_f32_e32 v137, v137, v137
	v_max_f32_e32 v138, v138, v138
	v_max_f32_e32 v139, v139, v139
	v_max_f32_e32 v140, v140, v140
	v_max_f32_e32 v141, v141, v141
	v_max_f32_e32 v142, v142, v142
	v_max_f32_e32 v143, v143, v143
	v_max_f32_e32 v144, v144, v144
	v_max_f32_e32 v145, v145, v145
	v_max_f32_e32 v146, v146, v146
	v_max_f32_e32 v147, v147, v147
	v_med3_f32 v132, v132, s20, v13
	v_med3_f32 v133, v133, s20, v13
	v_med3_f32 v134, v134, s20, v13
	v_med3_f32 v135, v135, s20, v13
	v_med3_f32 v136, v136, s20, v13
	v_med3_f32 v137, v137, s20, v13
	v_med3_f32 v138, v138, s20, v13
	v_med3_f32 v139, v139, s20, v13
	v_med3_f32 v140, v140, s20, v13
	v_med3_f32 v141, v141, s20, v13
	v_med3_f32 v142, v142, s20, v13
	v_med3_f32 v143, v143, s20, v13
	v_med3_f32 v144, v144, s20, v13
	v_med3_f32 v145, v145, s20, v13
	v_med3_f32 v146, v146, s20, v13
	v_med3_f32 v147, v147, s20, v13
	v_mov_b32_e32 v148, 0
	v_mov_b32_e32 v149, 0
	v_mov_b32_e32 v150, 0
	v_mov_b32_e32 v151, 0
	v_cvt_pk_fp8_f32 v148, v132, v133
	v_cvt_pk_fp8_f32 v149, v136, v137
	v_cvt_pk_fp8_f32 v150, v140, v141
	v_cvt_pk_fp8_f32 v151, v144, v145
	v_cvt_pk_fp8_f32 v148, v134, v135 op_sel:[0,0,1]
	v_cvt_pk_fp8_f32 v149, v138, v139 op_sel:[0,0,1]
	v_cvt_pk_fp8_f32 v150, v142, v143 op_sel:[0,0,1]
	v_cvt_pk_fp8_f32 v151, v146, v147 op_sel:[0,0,1]
	s_nop 0
	global_store_dwordx4 v12, v[148:151], s[14:15]
	s_waitcnt vmcnt(22)
	v_mul_f32_e32 v100, 0x43000000, v100
	v_mul_f32_e32 v101, 0x43000000, v101
	v_mul_f32_e32 v102, 0x43000000, v102
	v_mul_f32_e32 v103, 0x43000000, v103
	ds_write_b128 v5, v[100:103]
	v_mul_f32_e32 v104, 0x43000000, v104
	v_mul_f32_e32 v105, 0x43000000, v105
	v_mul_f32_e32 v106, 0x43000000, v106
	v_mul_f32_e32 v107, 0x43000000, v107
	ds_write_b128 v5, v[104:107] offset:1024
	v_mul_f32_e32 v108, 0x43000000, v108
	v_mul_f32_e32 v109, 0x43000000, v109
	v_mul_f32_e32 v110, 0x43000000, v110
	v_mul_f32_e32 v111, 0x43000000, v111
	ds_write_b128 v5, v[108:111] offset:2048
	v_mul_f32_e32 v112, 0x43000000, v112
	v_mul_f32_e32 v113, 0x43000000, v113
	v_mul_f32_e32 v114, 0x43000000, v114
	v_mul_f32_e32 v115, 0x43000000, v115
	ds_write_b128 v5, v[112:115] offset:3072
	v_mul_f32_e32 v116, 0x43000000, v116
	v_mul_f32_e32 v117, 0x43000000, v117
	v_mul_f32_e32 v118, 0x43000000, v118
	v_mul_f32_e32 v119, 0x43000000, v119
	ds_write_b128 v5, v[116:119] offset:4096
	v_mul_f32_e32 v120, 0x43000000, v120
	v_mul_f32_e32 v121, 0x43000000, v121
	v_mul_f32_e32 v122, 0x43000000, v122
	v_mul_f32_e32 v123, 0x43000000, v123
	ds_write_b128 v5, v[120:123] offset:5120
	v_mul_f32_e32 v124, 0x43000000, v124
	v_mul_f32_e32 v125, 0x43000000, v125
	v_mul_f32_e32 v126, 0x43000000, v126
	v_mul_f32_e32 v127, 0x43000000, v127
	ds_write_b128 v5, v[124:127] offset:6144
	v_mul_f32_e32 v128, 0x43000000, v128
	v_mul_f32_e32 v129, 0x43000000, v129
	v_mul_f32_e32 v130, 0x43000000, v130
	v_mul_f32_e32 v131, 0x43000000, v131
	ds_write_b128 v5, v[128:131] offset:7168
	s_waitcnt lgkmcnt(0)
	s_barrier
; #define GAS __attribute__((address_space(1)))
; #define LAS __attribute__((address_space(3)))
; #define LDS_WAIT() asm volatile("s_waitcnt lgkmcnt(0)" ::: "memory")
;     const int pr = item >> 1, kb = 2 * (pr / nblk) + (item & 1), nb = pr % nblk, k0 = 64 * kb, n0 = 32 * nb;
;     const int nr = n0 + (lane & 31); const int sc = MAP == 1 ? src_col_in(nr) : nr;
;     float v[32];
; #pragma unroll
;     for (int i = 0; i < 32; ++i) v[i] = sc >= 0 ? W[(size_t)(k0 + 2 * i + (lane >> 5)) * Nsrc + sc] : 0.f;
; #pragma unroll
;     for (int i = 0; i < 32; ++i) { const int k = k0 + 2 * i + (lane >> 5); float x = v[i] * wscale; if (KS) x *= (k < ksplit ? ksA[k] : ksB[k - ksplit]); scr[(2 * i + (lane >> 5)) * 33 + (lane & 31)] = x; }
;     LDS_WAIT(); asm volatile("" ::: "memory");
;     const int c = lane & 7;
; #pragma unroll
;     for (int j = 0; j < 4; ++j) { const int n = (lane >> 3) + 8 * j; const LAS float* s = scr + (8 * c) * 33 + n;
;         const unsigned long long o = (unsigned long long)pg8::pk4_fp8(s[0 * 33], s[1 * 33], s[2 * 33], s[3 * 33]) | ((unsigned long long)pg8::pk4_fp8(s[4 * 33], s[5 * 33], s[6 * 33], s[7 * 33]) << 32);
;         *(GAS unsigned long long*)(WT + (size_t)(n0 + n) * K + k0 + 8 * c) = o; }
;     LDS_WAIT(); asm volatile("" ::: "memory");
; }
; __global__ void __launch_bounds__(NWAVES * 64, 2) hybrid_fwd(Args args) {
;     ...
;             p0_transpose_item_f8<false>(args.in[16] + (size_t)l * FF * DM, FF, DM, DM / 32, (unsigned char*)(ws + WS_WDN + l * SZ_WDN), 128.f, args.in[16], args.in[16], 0, scr, r, lane);
	s_add_i32 s17, s16, 2496
	s_min_u32 s17, s17, 0xfff
	s_lshr_b32 s18, s17, 5
	s_add_i32 s18, s18, 0
	s_and_b32 s19, s17, 31
	s_lshl_b32 s18, s18, 21
	s_lshl_b32 s19, s19, 9
	s_add_u32 s18, s18, s19
	s_add_u32 s12, s2, s18
	s_addc_u32 s13, s3, 0
	global_load_dwordx4 v[100:103], v10, s[12:13]
	s_add_u32 s12, s12, 0x8000
	s_addc_u32 s13, s13, 0
	global_load_dwordx4 v[104:107], v10, s[12:13]
	s_add_u32 s12, s12, 0x8000
	s_addc_u32 s13, s13, 0
	global_load_dwordx4 v[108:111], v10, s[12:13]
	s_add_u32 s12, s12, 0x8000
	s_addc_u32 s13, s13, 0
	global_load_dwordx4 v[112:115], v10, s[12:13]
	s_add_u32 s12, s12, 0x8000
	s_addc_u32 s13, s13, 0
	global_load_dwordx4 v[116:119], v10, s[12:13]
	s_add_u32 s12, s12, 0x8000
	s_addc_u32 s13, s13, 0
	global_load_dwordx4 v[120:123], v10, s[12:13]
	s_add_u32 s12, s12, 0x8000
	s_addc_u32 s13, s13, 0
	global_load_dwordx4 v[124:127], v10, s[12:13]
	s_add_u32 s12, s12, 0x8000
	s_addc_u32 s13, s13, 0
	global_load_dwordx4 v[128:131], v10, s[12:13]
	s_add_i32 s17, s16, 2208
	s_min_u32 s17, s17, 0xfff
	s_lshr_b32 s18, s17, 5
	s_add_i32 s18, s18, 0
	s_and_b32 s19, s17, 31
	s_lshl_b32 s19, s19, 21
	s_lshl_b32 s18, s18, 7
	s_add_u32 s18, s18, s19
	s_add_u32 s14, s4, s18
	s_addc_u32 s15, s5, 0
	ds_read_b32 v132, v7
	ds_read_b32 v133, v7 offset:512
	ds_read_b32 v134, v7 offset:1024
	ds_read_b32 v135, v7 offset:1536
	ds_read_b32 v136, v7 offset:2048
	ds_read_b32 v137, v7 offset:2560
	ds_read_b32 v138, v7 offset:3072
	ds_read_b32 v139, v7 offset:3584
	ds_read_b32 v140, v7 offset:4096
	ds_read_b32 v141, v7 offset:4608
	ds_read_b32 v142, v7 offset:5120
	ds_read_b32 v143, v7 offset:5632
	ds_read_b32 v144, v7 offset:6144
	ds_read_b32 v145, v7 offset:6656
	ds_read_b32 v146, v7 offset:7168
	ds_read_b32 v147, v7 offset:7680
	s_waitcnt lgkmcnt(0)
	v_max_f32_e32 v132, v132, v132
	v_max_f32_e32 v133, v133, v133
	v_max_f32_e32 v134, v134, v134
	v_max_f32_e32 v135, v135, v135
	v_max_f32_e32 v136, v136, v136
	v_max_f32_e32 v137, v137, v137
	v_max_f32_e32 v138, v138, v138
	v_max_f32_e32 v139, v139, v139
	v_max_f32_e32 v140, v140, v140
	v_max_f32_e32 v141, v141, v141
	v_max_f32_e32 v142, v142, v142
	v_max_f32_e32 v143, v143, v143
	v_max_f32_e32 v144, v144, v144
	v_max_f32_e32 v145, v145, v145
	v_max_f32_e32 v146, v146, v146
	v_max_f32_e32 v147, v147, v147
	v_med3_f32 v132, v132, s20, v13
	v_med3_f32 v133, v133, s20, v13
	v_med3_f32 v134, v134, s20, v13
	v_med3_f32 v135, v135, s20, v13
	v_med3_f32 v136, v136, s20, v13
	v_med3_f32 v137, v137, s20, v13
	v_med3_f32 v138, v138, s20, v13
	v_med3_f32 v139, v139, s20, v13
	v_med3_f32 v140, v140, s20, v13
	v_med3_f32 v141, v141, s20, v13
	v_med3_f32 v142, v142, s20, v13
	v_med3_f32 v143, v143, s20, v13
	v_med3_f32 v144, v144, s20, v13
	v_med3_f32 v145, v145, s20, v13
	v_med3_f32 v146, v146, s20, v13
	v_med3_f32 v147, v147, s20, v13
	v_mov_b32_e32 v148, 0
	v_mov_b32_e32 v149, 0
	v_mov_b32_e32 v150, 0
	v_mov_b32_e32 v151, 0
	v_cvt_pk_fp8_f32 v148, v132, v133
	v_cvt_pk_fp8_f32 v149, v136, v137
	v_cvt_pk_fp8_f32 v150, v140, v141
	v_cvt_pk_fp8_f32 v151, v144, v145
	v_cvt_pk_fp8_f32 v148, v134, v135 op_sel:[0,0,1]
	v_cvt_pk_fp8_f32 v149, v138, v139 op_sel:[0,0,1]
	v_cvt_pk_fp8_f32 v150, v142, v143 op_sel:[0,0,1]
	v_cvt_pk_fp8_f32 v151, v146, v147 op_sel:[0,0,1]
	s_nop 0
	global_store_dwordx4 v11, v[148:151], s[14:15]
	ds_read_b32 v132, v9
	ds_read_b32 v133, v9 offset:512
	ds_read_b32 v134, v9 offset:1024
	ds_read_b32 v135, v9 offset:1536
	ds_read_b32 v136, v9 offset:2048
	ds_read_b32 v137, v9 offset:2560
	ds_read_b32 v138, v9 offset:3072
	ds_read_b32 v139, v9 offset:3584
	ds_read_b32 v140, v9 offset:4096
	ds_read_b32 v141, v9 offset:4608
	ds_read_b32 v142, v9 offset:5120
	ds_read_b32 v143, v9 offset:5632
	ds_read_b32 v144, v9 offset:6144
	ds_read_b32 v145, v9 offset:6656
	ds_read_b32 v146, v9 offset:7168
	ds_read_b32 v147, v9 offset:7680
	s_waitcnt lgkmcnt(0)
	v_max_f32_e32 v132, v132, v132
	v_max_f32_e32 v133, v133, v133
	v_max_f32_e32 v134, v134, v134
	v_max_f32_e32 v135, v135, v135
	v_max_f32_e32 v136, v136, v136
	v_max_f32_e32 v137, v137, v137
	v_max_f32_e32 v138, v138, v138
	v_max_f32_e32 v139, v139, v139
	v_max_f32_e32 v140, v140, v140
	v_max_f32_e32 v141, v141, v141
	v_max_f32_e32 v142, v142, v142
	v_max_f32_e32 v143, v143, v143
	v_max_f32_e32 v144, v144, v144
	v_max_f32_e32 v145, v145, v145
	v_max_f32_e32 v146, v146, v146
	v_max_f32_e32 v147, v147, v147
	v_med3_f32 v132, v132, s20, v13
	v_med3_f32 v133, v133, s20, v13
	v_med3_f32 v134, v134, s20, v13
	v_med3_f32 v135, v135, s20, v13
	v_med3_f32 v136, v136, s20, v13
	v_med3_f32 v137, v137, s20, v13
	v_med3_f32 v138, v138, s20, v13
	v_med3_f32 v139, v139, s20, v13
	v_med3_f32 v140, v140, s20, v13
	v_med3_f32 v141, v141, s20, v13
	v_med3_f32 v142, v142, s20, v13
	v_med3_f32 v143, v143, s20, v13
	v_med3_f32 v144, v144, s20, v13
	v_med3_f32 v145, v145, s20, v13
	v_med3_f32 v146, v146, s20, v13
	v_med3_f32 v147, v147, s20, v13
	v_mov_b32_e32 v148, 0
	v_mov_b32_e32 v149, 0
	v_mov_b32_e32 v150, 0
	v_mov_b32_e32 v151, 0
	v_cvt_pk_fp8_f32 v148, v132, v133
	v_cvt_pk_fp8_f32 v149, v136, v137
	v_cvt_pk_fp8_f32 v150, v140, v141
	v_cvt_pk_fp8_f32 v151, v144, v145
	v_cvt_pk_fp8_f32 v148, v134, v135 op_sel:[0,0,1]
	v_cvt_pk_fp8_f32 v149, v138, v139 op_sel:[0,0,1]
	v_cvt_pk_fp8_f32 v150, v142, v143 op_sel:[0,0,1]
	v_cvt_pk_fp8_f32 v151, v146, v147 op_sel:[0,0,1]
	s_nop 0
	global_store_dwordx4 v12, v[148:151], s[14:15]
	s_waitcnt vmcnt(22)
	v_mul_f32_e32 v36, 0x43000000, v36
	v_mul_f32_e32 v37, 0x43000000, v37
	v_mul_f32_e32 v38, 0x43000000, v38
	v_mul_f32_e32 v39, 0x43000000, v39
	ds_write_b128 v4, v[36:39]
	v_mul_f32_e32 v40, 0x43000000, v40
	v_mul_f32_e32 v41, 0x43000000, v41
	v_mul_f32_e32 v42, 0x43000000, v42
	v_mul_f32_e32 v43, 0x43000000, v43
	ds_write_b128 v4, v[40:43] offset:1024
	v_mul_f32_e32 v44, 0x43000000, v44
	v_mul_f32_e32 v45, 0x43000000, v45
	v_mul_f32_e32 v46, 0x43000000, v46
	v_mul_f32_e32 v47, 0x43000000, v47
	ds_write_b128 v4, v[44:47] offset:2048
	v_mul_f32_e32 v48, 0x43000000, v48
	v_mul_f32_e32 v49, 0x43000000, v49
	v_mul_f32_e32 v50, 0x43000000, v50
	v_mul_f32_e32 v51, 0x43000000, v51
	ds_write_b128 v4, v[48:51] offset:3072
	v_mul_f32_e32 v52, 0x43000000, v52
	v_mul_f32_e32 v53, 0x43000000, v53
	v_mul_f32_e32 v54, 0x43000000, v54
	v_mul_f32_e32 v55, 0x43000000, v55
	ds_write_b128 v4, v[52:55] offset:4096
	v_mul_f32_e32 v56, 0x43000000, v56
	v_mul_f32_e32 v57, 0x43000000, v57
	v_mul_f32_e32 v58, 0x43000000, v58
	v_mul_f32_e32 v59, 0x43000000, v59
	ds_write_b128 v4, v[56:59] offset:5120
	v_mul_f32_e32 v60, 0x43000000, v60
	v_mul_f32_e32 v61, 0x43000000, v61
	v_mul_f32_e32 v62, 0x43000000, v62
	v_mul_f32_e32 v63, 0x43000000, v63
	ds_write_b128 v4, v[60:63] offset:6144
	v_mul_f32_e32 v64, 0x43000000, v64
	v_mul_f32_e32 v65, 0x43000000, v65
	v_mul_f32_e32 v66, 0x43000000, v66
	v_mul_f32_e32 v67, 0x43000000, v67
	ds_write_b128 v4, v[64:67] offset:7168
	s_waitcnt lgkmcnt(0)
	s_barrier
; #define GAS __attribute__((address_space(1)))
; #define LAS __attribute__((address_space(3)))
; #define LDS_WAIT() asm volatile("s_waitcnt lgkmcnt(0)" ::: "memory")
;     const int pr = item >> 1, kb = 2 * (pr / nblk) + (item & 1), nb = pr % nblk, k0 = 64 * kb, n0 = 32 * nb;
;     const int nr = n0 + (lane & 31); const int sc = MAP == 1 ? src_col_in(nr) : nr;
;     float v[32];
; #pragma unroll
;     for (int i = 0; i < 32; ++i) v[i] = sc >= 0 ? W[(size_t)(k0 + 2 * i + (lane >> 5)) * Nsrc + sc] : 0.f;
; #pragma unroll
;     for (int i = 0; i < 32; ++i) { const int k = k0 + 2 * i + (lane >> 5); float x = v[i] * wscale; if (KS) x *= (k < ksplit ? ksA[k] : ksB[k - ksplit]); scr[(2 * i + (lane >> 5)) * 33 + (lane & 31)] = x; }
;     LDS_WAIT(); asm volatile("" ::: "memory");
;     const int c = lane & 7;
; #pragma unroll
;     for (int j = 0; j < 4; ++j) { const int n = (lane >> 3) + 8 * j; const LAS float* s = scr + (8 * c) * 33 + n;
;         const unsigned long long o = (unsigned long long)pg8::pk4_fp8(s[0 * 33], s[1 * 33], s[2 * 33], s[3 * 33]) | ((unsigned long long)pg8::pk4_fp8(s[4 * 33], s[5 * 33], s[6 * 33], s[7 * 33]) << 32);
;         *(GAS unsigned long long*)(WT + (size_t)(n0 + n) * K + k0 + 8 * c) = o; }
;     LDS_WAIT(); asm volatile("" ::: "memory");
; }
; __global__ void __launch_bounds__(NWAVES * 64, 2) hybrid_fwd(Args args) {
;     ...
;             p0_transpose_item_f8<false>(args.in[16] + (size_t)l * FF * DM, FF, DM, DM / 32, (unsigned char*)(ws + WS_WDN + l * SZ_WDN), 128.f, args.in[16], args.in[16], 0, scr, r, lane);
	s_add_i32 s17, s16, 2592
	s_min_u32 s17, s17, 0xfff
	s_lshr_b32 s18, s17, 5
	s_add_i32 s18, s18, 0
	s_and_b32 s19, s17, 31
	s_lshl_b32 s18, s18, 21
	s_lshl_b32 s19, s19, 9
	s_add_u32 s18, s18, s19
	s_add_u32 s12, s2, s18
	s_addc_u32 s13, s3, 0
	global_load_dwordx4 v[36:39], v10, s[12:13]
	s_add_u32 s12, s12, 0x8000
	s_addc_u32 s13, s13, 0
	global_load_dwordx4 v[40:43], v10, s[12:13]
	s_add_u32 s12, s12, 0x8000
	s_addc_u32 s13, s13, 0
	global_load_dwordx4 v[44:47], v10, s[12:13]
	s_add_u32 s12, s12, 0x8000
	s_addc_u32 s13, s13, 0
	global_load_dwordx4 v[48:51], v10, s[12:13]
	s_add_u32 s12, s12, 0x8000
	s_addc_u32 s13, s13, 0
	global_load_dwordx4 v[52:55], v10, s[12:13]
	s_add_u32 s12, s12, 0x8000
	s_addc_u32 s13, s13, 0
	global_load_dwordx4 v[56:59], v10, s[12:13]
	s_add_u32 s12, s12, 0x8000
	s_addc_u32 s13, s13, 0
	global_load_dwordx4 v[60:63], v10, s[12:13]
	s_add_u32 s12, s12, 0x8000
	s_addc_u32 s13, s13, 0
	global_load_dwordx4 v[64:67], v10, s[12:13]
	s_add_i32 s17, s16, 2304
	s_min_u32 s17, s17, 0xfff
	s_lshr_b32 s18, s17, 5
	s_add_i32 s18, s18, 0
	s_and_b32 s19, s17, 31
	s_lshl_b32 s19, s19, 21
	s_lshl_b32 s18, s18, 7
	s_add_u32 s18, s18, s19
	s_add_u32 s14, s4, s18
	s_addc_u32 s15, s5, 0
	ds_read_b32 v132, v6
	ds_read_b32 v133, v6 offset:512
	ds_read_b32 v134, v6 offset:1024
	ds_read_b32 v135, v6 offset:1536
	ds_read_b32 v136, v6 offset:2048
	ds_read_b32 v137, v6 offset:2560
	ds_read_b32 v138, v6 offset:3072
	ds_read_b32 v139, v6 offset:3584
	ds_read_b32 v140, v6 offset:4096
	ds_read_b32 v141, v6 offset:4608
	ds_read_b32 v142, v6 offset:5120
	ds_read_b32 v143, v6 offset:5632
	ds_read_b32 v144, v6 offset:6144
	ds_read_b32 v145, v6 offset:6656
	ds_read_b32 v146, v6 offset:7168
	ds_read_b32 v147, v6 offset:7680
	s_waitcnt lgkmcnt(0)
	v_max_f32_e32 v132, v132, v132
	v_max_f32_e32 v133, v133, v133
	v_max_f32_e32 v134, v134, v134
	v_max_f32_e32 v135, v135, v135
	v_max_f32_e32 v136, v136, v136
	v_max_f32_e32 v137, v137, v137
	v_max_f32_e32 v138, v138, v138
	v_max_f32_e32 v139, v139, v139
	v_max_f32_e32 v140, v140, v140
	v_max_f32_e32 v141, v141, v141
	v_max_f32_e32 v142, v142, v142
	v_max_f32_e32 v143, v143, v143
	v_max_f32_e32 v144, v144, v144
	v_max_f32_e32 v145, v145, v145
	v_max_f32_e32 v146, v146, v146
	v_max_f32_e32 v147, v147, v147
	v_med3_f32 v132, v132, s20, v13
	v_med3_f32 v133, v133, s20, v13
	v_med3_f32 v134, v134, s20, v13
	v_med3_f32 v135, v135, s20, v13
	v_med3_f32 v136, v136, s20, v13
	v_med3_f32 v137, v137, s20, v13
	v_med3_f32 v138, v138, s20, v13
	v_med3_f32 v139, v139, s20, v13
	v_med3_f32 v140, v140, s20, v13
	v_med3_f32 v141, v141, s20, v13
	v_med3_f32 v142, v142, s20, v13
	v_med3_f32 v143, v143, s20, v13
	v_med3_f32 v144, v144, s20, v13
	v_med3_f32 v145, v145, s20, v13
	v_med3_f32 v146, v146, s20, v13
	v_med3_f32 v147, v147, s20, v13
	v_mov_b32_e32 v148, 0
	v_mov_b32_e32 v149, 0
	v_mov_b32_e32 v150, 0
	v_mov_b32_e32 v151, 0
	v_cvt_pk_fp8_f32 v148, v132, v133
	v_cvt_pk_fp8_f32 v149, v136, v137
	v_cvt_pk_fp8_f32 v150, v140, v141
	v_cvt_pk_fp8_f32 v151, v144, v145
	v_cvt_pk_fp8_f32 v148, v134, v135 op_sel:[0,0,1]
	v_cvt_pk_fp8_f32 v149, v138, v139 op_sel:[0,0,1]
	v_cvt_pk_fp8_f32 v150, v142, v143 op_sel:[0,0,1]
	v_cvt_pk_fp8_f32 v151, v146, v147 op_sel:[0,0,1]
	s_nop 0
	global_store_dwordx4 v11, v[148:151], s[14:15]
	ds_read_b32 v132, v8
	ds_read_b32 v133, v8 offset:512
	ds_read_b32 v134, v8 offset:1024
	ds_read_b32 v135, v8 offset:1536
	ds_read_b32 v136, v8 offset:2048
	ds_read_b32 v137, v8 offset:2560
	ds_read_b32 v138, v8 offset:3072
	ds_read_b32 v139, v8 offset:3584
	ds_read_b32 v140, v8 offset:4096
	ds_read_b32 v141, v8 offset:4608
	ds_read_b32 v142, v8 offset:5120
	ds_read_b32 v143, v8 offset:5632
	ds_read_b32 v144, v8 offset:6144
	ds_read_b32 v145, v8 offset:6656
	ds_read_b32 v146, v8 offset:7168
	ds_read_b32 v147, v8 offset:7680
	s_waitcnt lgkmcnt(0)
	v_max_f32_e32 v132, v132, v132
	v_max_f32_e32 v133, v133, v133
	v_max_f32_e32 v134, v134, v134
	v_max_f32_e32 v135, v135, v135
	v_max_f32_e32 v136, v136, v136
	v_max_f32_e32 v137, v137, v137
	v_max_f32_e32 v138, v138, v138
	v_max_f32_e32 v139, v139, v139
	v_max_f32_e32 v140, v140, v140
	v_max_f32_e32 v141, v141, v141
	v_max_f32_e32 v142, v142, v142
	v_max_f32_e32 v143, v143, v143
	v_max_f32_e32 v144, v144, v144
	v_max_f32_e32 v145, v145, v145
	v_max_f32_e32 v146, v146, v146
	v_max_f32_e32 v147, v147, v147
	v_med3_f32 v132, v132, s20, v13
	v_med3_f32 v133, v133, s20, v13
	v_med3_f32 v134, v134, s20, v13
	v_med3_f32 v135, v135, s20, v13
	v_med3_f32 v136, v136, s20, v13
	v_med3_f32 v137, v137, s20, v13
	v_med3_f32 v138, v138, s20, v13
	v_med3_f32 v139, v139, s20, v13
	v_med3_f32 v140, v140, s20, v13
	v_med3_f32 v141, v141, s20, v13
	v_med3_f32 v142, v142, s20, v13
	v_med3_f32 v143, v143, s20, v13
	v_med3_f32 v144, v144, s20, v13
	v_med3_f32 v145, v145, s20, v13
	v_med3_f32 v146, v146, s20, v13
	v_med3_f32 v147, v147, s20, v13
	v_mov_b32_e32 v148, 0
	v_mov_b32_e32 v149, 0
	v_mov_b32_e32 v150, 0
	v_mov_b32_e32 v151, 0
	v_cvt_pk_fp8_f32 v148, v132, v133
	v_cvt_pk_fp8_f32 v149, v136, v137
	v_cvt_pk_fp8_f32 v150, v140, v141
	v_cvt_pk_fp8_f32 v151, v144, v145
	v_cvt_pk_fp8_f32 v148, v134, v135 op_sel:[0,0,1]
	v_cvt_pk_fp8_f32 v149, v138, v139 op_sel:[0,0,1]
	v_cvt_pk_fp8_f32 v150, v142, v143 op_sel:[0,0,1]
	v_cvt_pk_fp8_f32 v151, v146, v147 op_sel:[0,0,1]
	s_nop 0
	global_store_dwordx4 v12, v[148:151], s[14:15]
	s_waitcnt vmcnt(22)
	v_mul_f32_e32 v68, 0x43000000, v68
	v_mul_f32_e32 v69, 0x43000000, v69
	v_mul_f32_e32 v70, 0x43000000, v70
	v_mul_f32_e32 v71, 0x43000000, v71
	ds_write_b128 v5, v[68:71]
	v_mul_f32_e32 v72, 0x43000000, v72
	v_mul_f32_e32 v73, 0x43000000, v73
	v_mul_f32_e32 v74, 0x43000000, v74
	v_mul_f32_e32 v75, 0x43000000, v75
	ds_write_b128 v5, v[72:75] offset:1024
	v_mul_f32_e32 v76, 0x43000000, v76
	v_mul_f32_e32 v77, 0x43000000, v77
	v_mul_f32_e32 v78, 0x43000000, v78
	v_mul_f32_e32 v79, 0x43000000, v79
	ds_write_b128 v5, v[76:79] offset:2048
	v_mul_f32_e32 v80, 0x43000000, v80
	v_mul_f32_e32 v81, 0x43000000, v81
	v_mul_f32_e32 v82, 0x43000000, v82
	v_mul_f32_e32 v83, 0x43000000, v83
	ds_write_b128 v5, v[80:83] offset:3072
	v_mul_f32_e32 v84, 0x43000000, v84
	v_mul_f32_e32 v85, 0x43000000, v85
	v_mul_f32_e32 v86, 0x43000000, v86
	v_mul_f32_e32 v87, 0x43000000, v87
	ds_write_b128 v5, v[84:87] offset:4096
	v_mul_f32_e32 v88, 0x43000000, v88
	v_mul_f32_e32 v89, 0x43000000, v89
	v_mul_f32_e32 v90, 0x43000000, v90
	v_mul_f32_e32 v91, 0x43000000, v91
	ds_write_b128 v5, v[88:91] offset:5120
	v_mul_f32_e32 v92, 0x43000000, v92
	v_mul_f32_e32 v93, 0x43000000, v93
	v_mul_f32_e32 v94, 0x43000000, v94
	v_mul_f32_e32 v95, 0x43000000, v95
	ds_write_b128 v5, v[92:95] offset:6144
	v_mul_f32_e32 v96, 0x43000000, v96
	v_mul_f32_e32 v97, 0x43000000, v97
	v_mul_f32_e32 v98, 0x43000000, v98
	v_mul_f32_e32 v99, 0x43000000, v99
	ds_write_b128 v5, v[96:99] offset:7168
	s_waitcnt lgkmcnt(0)
	s_barrier
; #define GAS __attribute__((address_space(1)))
; #define LAS __attribute__((address_space(3)))
; #define LDS_WAIT() asm volatile("s_waitcnt lgkmcnt(0)" ::: "memory")
;     const int pr = item >> 1, kb = 2 * (pr / nblk) + (item & 1), nb = pr % nblk, k0 = 64 * kb, n0 = 32 * nb;
;     const int nr = n0 + (lane & 31); const int sc = MAP == 1 ? src_col_in(nr) : nr;
;     float v[32];
; #pragma unroll
;     for (int i = 0; i < 32; ++i) v[i] = sc >= 0 ? W[(size_t)(k0 + 2 * i + (lane >> 5)) * Nsrc + sc] : 0.f;
; #pragma unroll
;     for (int i = 0; i < 32; ++i) { const int k = k0 + 2 * i + (lane >> 5); float x = v[i] * wscale; if (KS) x *= (k < ksplit ? ksA[k] : ksB[k - ksplit]); scr[(2 * i + (lane >> 5)) * 33 + (lane & 31)] = x; }
;     LDS_WAIT(); asm volatile("" ::: "memory");
;     const int c = lane & 7;
; #pragma unroll
;     for (int j = 0; j < 4; ++j) { const int n = (lane >> 3) + 8 * j; const LAS float* s = scr + (8 * c) * 33 + n;
;         const unsigned long long o = (unsigned long long)pg8::pk4_fp8(s[0 * 33], s[1 * 33], s[2 * 33], s[3 * 33]) | ((unsigned long long)pg8::pk4_fp8(s[4 * 33], s[5 * 33], s[6 * 33], s[7 * 33]) << 32);
;         *(GAS unsigned long long*)(WT + (size_t)(n0 + n) * K + k0 + 8 * c) = o; }
;     LDS_WAIT(); asm volatile("" ::: "memory");
; }
; __global__ void __launch_bounds__(NWAVES * 64, 2) hybrid_fwd(Args args) {
;     ...
;             p0_transpose_item_f8<false>(args.in[16] + (size_t)l * FF * DM, FF, DM, DM / 32, (unsigned char*)(ws + WS_WDN + l * SZ_WDN), 128.f, args.in[16], args.in[16], 0, scr, r, lane);
	s_add_i32 s17, s16, 2688
	s_min_u32 s17, s17, 0xfff
	s_lshr_b32 s18, s17, 5
	s_add_i32 s18, s18, 0
	s_and_b32 s19, s17, 31
	s_lshl_b32 s18, s18, 21
	s_lshl_b32 s19, s19, 9
	s_add_u32 s18, s18, s19
	s_add_u32 s12, s2, s18
	s_addc_u32 s13, s3, 0
	global_load_dwordx4 v[68:71], v10, s[12:13]
	s_add_u32 s12, s12, 0x8000
	s_addc_u32 s13, s13, 0
	global_load_dwordx4 v[72:75], v10, s[12:13]
	s_add_u32 s12, s12, 0x8000
	s_addc_u32 s13, s13, 0
	global_load_dwordx4 v[76:79], v10, s[12:13]
	s_add_u32 s12, s12, 0x8000
	s_addc_u32 s13, s13, 0
	global_load_dwordx4 v[80:83], v10, s[12:13]
	s_add_u32 s12, s12, 0x8000
	s_addc_u32 s13, s13, 0
	global_load_dwordx4 v[84:87], v10, s[12:13]
	s_add_u32 s12, s12, 0x8000
	s_addc_u32 s13, s13, 0
	global_load_dwordx4 v[88:91], v10, s[12:13]
	s_add_u32 s12, s12, 0x8000
	s_addc_u32 s13, s13, 0
	global_load_dwordx4 v[92:95], v10, s[12:13]
	s_add_u32 s12, s12, 0x8000
	s_addc_u32 s13, s13, 0
	global_load_dwordx4 v[96:99], v10, s[12:13]
	s_add_i32 s17, s16, 2400
	s_min_u32 s17, s17, 0xfff
	s_lshr_b32 s18, s17, 5
	s_add_i32 s18, s18, 0
	s_and_b32 s19, s17, 31
	s_lshl_b32 s19, s19, 21
	s_lshl_b32 s18, s18, 7
	s_add_u32 s18, s18, s19
	s_add_u32 s14, s4, s18
	s_addc_u32 s15, s5, 0
	ds_read_b32 v132, v7
	ds_read_b32 v133, v7 offset:512
	ds_read_b32 v134, v7 offset:1024
	ds_read_b32 v135, v7 offset:1536
	ds_read_b32 v136, v7 offset:2048
	ds_read_b32 v137, v7 offset:2560
	ds_read_b32 v138, v7 offset:3072
	ds_read_b32 v139, v7 offset:3584
	ds_read_b32 v140, v7 offset:4096
	ds_read_b32 v141, v7 offset:4608
	ds_read_b32 v142, v7 offset:5120
	ds_read_b32 v143, v7 offset:5632
	ds_read_b32 v144, v7 offset:6144
	ds_read_b32 v145, v7 offset:6656
	ds_read_b32 v146, v7 offset:7168
	ds_read_b32 v147, v7 offset:7680
	s_waitcnt lgkmcnt(0)
	v_max_f32_e32 v132, v132, v132
	v_max_f32_e32 v133, v133, v133
	v_max_f32_e32 v134, v134, v134
	v_max_f32_e32 v135, v135, v135
	v_max_f32_e32 v136, v136, v136
	v_max_f32_e32 v137, v137, v137
	v_max_f32_e32 v138, v138, v138
	v_max_f32_e32 v139, v139, v139
	v_max_f32_e32 v140, v140, v140
	v_max_f32_e32 v141, v141, v141
	v_max_f32_e32 v142, v142, v142
	v_max_f32_e32 v143, v143, v143
	v_max_f32_e32 v144, v144, v144
	v_max_f32_e32 v145, v145, v145
	v_max_f32_e32 v146, v146, v146
	v_max_f32_e32 v147, v147, v147
	v_med3_f32 v132, v132, s20, v13
	v_med3_f32 v133, v133, s20, v13
	v_med3_f32 v134, v134, s20, v13
	v_med3_f32 v135, v135, s20, v13
	v_med3_f32 v136, v136, s20, v13
	v_med3_f32 v137, v137, s20, v13
	v_med3_f32 v138, v138, s20, v13
	v_med3_f32 v139, v139, s20, v13
	v_med3_f32 v140, v140, s20, v13
	v_med3_f32 v141, v141, s20, v13
	v_med3_f32 v142, v142, s20, v13
	v_med3_f32 v143, v143, s20, v13
	v_med3_f32 v144, v144, s20, v13
	v_med3_f32 v145, v145, s20, v13
	v_med3_f32 v146, v146, s20, v13
	v_med3_f32 v147, v147, s20, v13
	v_mov_b32_e32 v148, 0
	v_mov_b32_e32 v149, 0
	v_mov_b32_e32 v150, 0
	v_mov_b32_e32 v151, 0
	v_cvt_pk_fp8_f32 v148, v132, v133
	v_cvt_pk_fp8_f32 v149, v136, v137
	v_cvt_pk_fp8_f32 v150, v140, v141
	v_cvt_pk_fp8_f32 v151, v144, v145
	v_cvt_pk_fp8_f32 v148, v134, v135 op_sel:[0,0,1]
	v_cvt_pk_fp8_f32 v149, v138, v139 op_sel:[0,0,1]
	v_cvt_pk_fp8_f32 v150, v142, v143 op_sel:[0,0,1]
	v_cvt_pk_fp8_f32 v151, v146, v147 op_sel:[0,0,1]
	s_nop 0
	global_store_dwordx4 v11, v[148:151], s[14:15]
	ds_read_b32 v132, v9
	ds_read_b32 v133, v9 offset:512
	ds_read_b32 v134, v9 offset:1024
	ds_read_b32 v135, v9 offset:1536
	ds_read_b32 v136, v9 offset:2048
	ds_read_b32 v137, v9 offset:2560
	ds_read_b32 v138, v9 offset:3072
	ds_read_b32 v139, v9 offset:3584
	ds_read_b32 v140, v9 offset:4096
	ds_read_b32 v141, v9 offset:4608
	ds_read_b32 v142, v9 offset:5120
	ds_read_b32 v143, v9 offset:5632
	ds_read_b32 v144, v9 offset:6144
	ds_read_b32 v145, v9 offset:6656
	ds_read_b32 v146, v9 offset:7168
	ds_read_b32 v147, v9 offset:7680
	s_waitcnt lgkmcnt(0)
	v_max_f32_e32 v132, v132, v132
	v_max_f32_e32 v133, v133, v133
	v_max_f32_e32 v134, v134, v134
	v_max_f32_e32 v135, v135, v135
	v_max_f32_e32 v136, v136, v136
	v_max_f32_e32 v137, v137, v137
	v_max_f32_e32 v138, v138, v138
	v_max_f32_e32 v139, v139, v139
	v_max_f32_e32 v140, v140, v140
	v_max_f32_e32 v141, v141, v141
	v_max_f32_e32 v142, v142, v142
	v_max_f32_e32 v143, v143, v143
	v_max_f32_e32 v144, v144, v144
	v_max_f32_e32 v145, v145, v145
	v_max_f32_e32 v146, v146, v146
	v_max_f32_e32 v147, v147, v147
	v_med3_f32 v132, v132, s20, v13
	v_med3_f32 v133, v133, s20, v13
	v_med3_f32 v134, v134, s20, v13
	v_med3_f32 v135, v135, s20, v13
	v_med3_f32 v136, v136, s20, v13
	v_med3_f32 v137, v137, s20, v13
	v_med3_f32 v138, v138, s20, v13
	v_med3_f32 v139, v139, s20, v13
	v_med3_f32 v140, v140, s20, v13
	v_med3_f32 v141, v141, s20, v13
	v_med3_f32 v142, v142, s20, v13
	v_med3_f32 v143, v143, s20, v13
	v_med3_f32 v144, v144, s20, v13
	v_med3_f32 v145, v145, s20, v13
	v_med3_f32 v146, v146, s20, v13
	v_med3_f32 v147, v147, s20, v13
	v_mov_b32_e32 v148, 0
	v_mov_b32_e32 v149, 0
	v_mov_b32_e32 v150, 0
	v_mov_b32_e32 v151, 0
	v_cvt_pk_fp8_f32 v148, v132, v133
	v_cvt_pk_fp8_f32 v149, v136, v137
	v_cvt_pk_fp8_f32 v150, v140, v141
	v_cvt_pk_fp8_f32 v151, v144, v145
	v_cvt_pk_fp8_f32 v148, v134, v135 op_sel:[0,0,1]
	v_cvt_pk_fp8_f32 v149, v138, v139 op_sel:[0,0,1]
	v_cvt_pk_fp8_f32 v150, v142, v143 op_sel:[0,0,1]
	v_cvt_pk_fp8_f32 v151, v146, v147 op_sel:[0,0,1]
	s_nop 0
	global_store_dwordx4 v12, v[148:151], s[14:15]
	s_waitcnt vmcnt(22)
	v_mul_f32_e32 v100, 0x43000000, v100
	v_mul_f32_e32 v101, 0x43000000, v101
	v_mul_f32_e32 v102, 0x43000000, v102
	v_mul_f32_e32 v103, 0x43000000, v103
	ds_write_b128 v4, v[100:103]
	v_mul_f32_e32 v104, 0x43000000, v104
	v_mul_f32_e32 v105, 0x43000000, v105
	v_mul_f32_e32 v106, 0x43000000, v106
	v_mul_f32_e32 v107, 0x43000000, v107
	ds_write_b128 v4, v[104:107] offset:1024
	v_mul_f32_e32 v108, 0x43000000, v108
	v_mul_f32_e32 v109, 0x43000000, v109
	v_mul_f32_e32 v110, 0x43000000, v110
	v_mul_f32_e32 v111, 0x43000000, v111
	ds_write_b128 v4, v[108:111] offset:2048
	v_mul_f32_e32 v112, 0x43000000, v112
	v_mul_f32_e32 v113, 0x43000000, v113
	v_mul_f32_e32 v114, 0x43000000, v114
	v_mul_f32_e32 v115, 0x43000000, v115
	ds_write_b128 v4, v[112:115] offset:3072
	v_mul_f32_e32 v116, 0x43000000, v116
	v_mul_f32_e32 v117, 0x43000000, v117
	v_mul_f32_e32 v118, 0x43000000, v118
	v_mul_f32_e32 v119, 0x43000000, v119
	ds_write_b128 v4, v[116:119] offset:4096
	v_mul_f32_e32 v120, 0x43000000, v120
	v_mul_f32_e32 v121, 0x43000000, v121
	v_mul_f32_e32 v122, 0x43000000, v122
	v_mul_f32_e32 v123, 0x43000000, v123
	ds_write_b128 v4, v[120:123] offset:5120
	v_mul_f32_e32 v124, 0x43000000, v124
	v_mul_f32_e32 v125, 0x43000000, v125
	v_mul_f32_e32 v126, 0x43000000, v126
	v_mul_f32_e32 v127, 0x43000000, v127
	ds_write_b128 v4, v[124:127] offset:6144
	v_mul_f32_e32 v128, 0x43000000, v128
	v_mul_f32_e32 v129, 0x43000000, v129
	v_mul_f32_e32 v130, 0x43000000, v130
	v_mul_f32_e32 v131, 0x43000000, v131
	ds_write_b128 v4, v[128:131] offset:7168
	s_waitcnt lgkmcnt(0)
	s_barrier
; #define GAS __attribute__((address_space(1)))
; #define LAS __attribute__((address_space(3)))
; #define LDS_WAIT() asm volatile("s_waitcnt lgkmcnt(0)" ::: "memory")
;     const int pr = item >> 1, kb = 2 * (pr / nblk) + (item & 1), nb = pr % nblk, k0 = 64 * kb, n0 = 32 * nb;
;     const int nr = n0 + (lane & 31); const int sc = MAP == 1 ? src_col_in(nr) : nr;
;     float v[32];
; #pragma unroll
;     for (int i = 0; i < 32; ++i) v[i] = sc >= 0 ? W[(size_t)(k0 + 2 * i + (lane >> 5)) * Nsrc + sc] : 0.f;
; #pragma unroll
;     for (int i = 0; i < 32; ++i) { const int k = k0 + 2 * i + (lane >> 5); float x = v[i] * wscale; if (KS) x *= (k < ksplit ? ksA[k] : ksB[k - ksplit]); scr[(2 * i + (lane >> 5)) * 33 + (lane & 31)] = x; }
;     LDS_WAIT(); asm volatile("" ::: "memory");
;     const int c = lane & 7;
; #pragma unroll
;     for (int j = 0; j < 4; ++j) { const int n = (lane >> 3) + 8 * j; const LAS float* s = scr + (8 * c) * 33 + n;
;         const unsigned long long o = (unsigned long long)pg8::pk4_fp8(s[0 * 33], s[1 * 33], s[2 * 33], s[3 * 33]) | ((unsigned long long)pg8::pk4_fp8(s[4 * 33], s[5 * 33], s[6 * 33], s[7 * 33]) << 32);
;         *(GAS unsigned long long*)(WT + (size_t)(n0 + n) * K + k0 + 8 * c) = o; }
;     LDS_WAIT(); asm volatile("" ::: "memory");
; }
; __global__ void __launch_bounds__(NWAVES * 64, 2) hybrid_fwd(Args args) {
;     ...
;             p0_transpose_item_f8<false>(args.in[16] + (size_t)l * FF * DM, FF, DM, DM / 32, (unsigned char*)(ws + WS_WDN + l * SZ_WDN), 128.f, args.in[16], args.in[16], 0, scr, r, lane);
	s_add_i32 s17, s16, 2784
	s_min_u32 s17, s17, 0xfff
	s_lshr_b32 s18, s17, 5
	s_add_i32 s18, s18, 0
	s_and_b32 s19, s17, 31
	s_lshl_b32 s18, s18, 21
	s_lshl_b32 s19, s19, 9
	s_add_u32 s18, s18, s19
	s_add_u32 s12, s2, s18
	s_addc_u32 s13, s3, 0
	global_load_dwordx4 v[100:103], v10, s[12:13]
	s_add_u32 s12, s12, 0x8000
	s_addc_u32 s13, s13, 0
	global_load_dwordx4 v[104:107], v10, s[12:13]
	s_add_u32 s12, s12, 0x8000
	s_addc_u32 s13, s13, 0
	global_load_dwordx4 v[108:111], v10, s[12:13]
	s_add_u32 s12, s12, 0x8000
	s_addc_u32 s13, s13, 0
	global_load_dwordx4 v[112:115], v10, s[12:13]
	s_add_u32 s12, s12, 0x8000
	s_addc_u32 s13, s13, 0
	global_load_dwordx4 v[116:119], v10, s[12:13]
	s_add_u32 s12, s12, 0x8000
	s_addc_u32 s13, s13, 0
	global_load_dwordx4 v[120:123], v10, s[12:13]
	s_add_u32 s12, s12, 0x8000
	s_addc_u32 s13, s13, 0
	global_load_dwordx4 v[124:127], v10, s[12:13]
	s_add_u32 s12, s12, 0x8000
	s_addc_u32 s13, s13, 0
	global_load_dwordx4 v[128:131], v10, s[12:13]
	s_add_i32 s17, s16, 2496
	s_min_u32 s17, s17, 0xfff
	s_lshr_b32 s18, s17, 5
	s_add_i32 s18, s18, 0
	s_and_b32 s19, s17, 31
	s_lshl_b32 s19, s19, 21
	s_lshl_b32 s18, s18, 7
	s_add_u32 s18, s18, s19
	s_add_u32 s14, s4, s18
	s_addc_u32 s15, s5, 0
	ds_read_b32 v132, v6
	ds_read_b32 v133, v6 offset:512
	ds_read_b32 v134, v6 offset:1024
	ds_read_b32 v135, v6 offset:1536
	ds_read_b32 v136, v6 offset:2048
	ds_read_b32 v137, v6 offset:2560
	ds_read_b32 v138, v6 offset:3072
	ds_read_b32 v139, v6 offset:3584
	ds_read_b32 v140, v6 offset:4096
	ds_read_b32 v141, v6 offset:4608
	ds_read_b32 v142, v6 offset:5120
	ds_read_b32 v143, v6 offset:5632
	ds_read_b32 v144, v6 offset:6144
	ds_read_b32 v145, v6 offset:6656
	ds_read_b32 v146, v6 offset:7168
	ds_read_b32 v147, v6 offset:7680
	s_waitcnt lgkmcnt(0)
	v_max_f32_e32 v132, v132, v132
	v_max_f32_e32 v133, v133, v133
	v_max_f32_e32 v134, v134, v134
	v_max_f32_e32 v135, v135, v135
	v_max_f32_e32 v136, v136, v136
	v_max_f32_e32 v137, v137, v137
	v_max_f32_e32 v138, v138, v138
	v_max_f32_e32 v139, v139, v139
	v_max_f32_e32 v140, v140, v140
	v_max_f32_e32 v141, v141, v141
	v_max_f32_e32 v142, v142, v142
	v_max_f32_e32 v143, v143, v143
	v_max_f32_e32 v144, v144, v144
	v_max_f32_e32 v145, v145, v145
	v_max_f32_e32 v146, v146, v146
	v_max_f32_e32 v147, v147, v147
	v_med3_f32 v132, v132, s20, v13
	v_med3_f32 v133, v133, s20, v13
	v_med3_f32 v134, v134, s20, v13
	v_med3_f32 v135, v135, s20, v13
	v_med3_f32 v136, v136, s20, v13
	v_med3_f32 v137, v137, s20, v13
	v_med3_f32 v138, v138, s20, v13
	v_med3_f32 v139, v139, s20, v13
	v_med3_f32 v140, v140, s20, v13
	v_med3_f32 v141, v141, s20, v13
	v_med3_f32 v142, v142, s20, v13
	v_med3_f32 v143, v143, s20, v13
	v_med3_f32 v144, v144, s20, v13
	v_med3_f32 v145, v145, s20, v13
	v_med3_f32 v146, v146, s20, v13
	v_med3_f32 v147, v147, s20, v13
	v_mov_b32_e32 v148, 0
	v_mov_b32_e32 v149, 0
	v_mov_b32_e32 v150, 0
	v_mov_b32_e32 v151, 0
	v_cvt_pk_fp8_f32 v148, v132, v133
	v_cvt_pk_fp8_f32 v149, v136, v137
	v_cvt_pk_fp8_f32 v150, v140, v141
	v_cvt_pk_fp8_f32 v151, v144, v145
	v_cvt_pk_fp8_f32 v148, v134, v135 op_sel:[0,0,1]
	v_cvt_pk_fp8_f32 v149, v138, v139 op_sel:[0,0,1]
	v_cvt_pk_fp8_f32 v150, v142, v143 op_sel:[0,0,1]
	v_cvt_pk_fp8_f32 v151, v146, v147 op_sel:[0,0,1]
	s_nop 0
	global_store_dwordx4 v11, v[148:151], s[14:15]
	ds_read_b32 v132, v8
	ds_read_b32 v133, v8 offset:512
	ds_read_b32 v134, v8 offset:1024
	ds_read_b32 v135, v8 offset:1536
	ds_read_b32 v136, v8 offset:2048
	ds_read_b32 v137, v8 offset:2560
	ds_read_b32 v138, v8 offset:3072
	ds_read_b32 v139, v8 offset:3584
	ds_read_b32 v140, v8 offset:4096
	ds_read_b32 v141, v8 offset:4608
	ds_read_b32 v142, v8 offset:5120
	ds_read_b32 v143, v8 offset:5632
	ds_read_b32 v144, v8 offset:6144
	ds_read_b32 v145, v8 offset:6656
	ds_read_b32 v146, v8 offset:7168
	ds_read_b32 v147, v8 offset:7680
	s_waitcnt lgkmcnt(0)
	v_max_f32_e32 v132, v132, v132
	v_max_f32_e32 v133, v133, v133
	v_max_f32_e32 v134, v134, v134
	v_max_f32_e32 v135, v135, v135
	v_max_f32_e32 v136, v136, v136
	v_max_f32_e32 v137, v137, v137
	v_max_f32_e32 v138, v138, v138
	v_max_f32_e32 v139, v139, v139
	v_max_f32_e32 v140, v140, v140
	v_max_f32_e32 v141, v141, v141
	v_max_f32_e32 v142, v142, v142
	v_max_f32_e32 v143, v143, v143
	v_max_f32_e32 v144, v144, v144
	v_max_f32_e32 v145, v145, v145
	v_max_f32_e32 v146, v146, v146
	v_max_f32_e32 v147, v147, v147
	v_med3_f32 v132, v132, s20, v13
	v_med3_f32 v133, v133, s20, v13
	v_med3_f32 v134, v134, s20, v13
	v_med3_f32 v135, v135, s20, v13
	v_med3_f32 v136, v136, s20, v13
	v_med3_f32 v137, v137, s20, v13
	v_med3_f32 v138, v138, s20, v13
	v_med3_f32 v139, v139, s20, v13
	v_med3_f32 v140, v140, s20, v13
	v_med3_f32 v141, v141, s20, v13
	v_med3_f32 v142, v142, s20, v13
	v_med3_f32 v143, v143, s20, v13
	v_med3_f32 v144, v144, s20, v13
	v_med3_f32 v145, v145, s20, v13
	v_med3_f32 v146, v146, s20, v13
	v_med3_f32 v147, v147, s20, v13
	v_mov_b32_e32 v148, 0
	v_mov_b32_e32 v149, 0
	v_mov_b32_e32 v150, 0
	v_mov_b32_e32 v151, 0
	v_cvt_pk_fp8_f32 v148, v132, v133
	v_cvt_pk_fp8_f32 v149, v136, v137
	v_cvt_pk_fp8_f32 v150, v140, v141
	v_cvt_pk_fp8_f32 v151, v144, v145
	v_cvt_pk_fp8_f32 v148, v134, v135 op_sel:[0,0,1]
	v_cvt_pk_fp8_f32 v149, v138, v139 op_sel:[0,0,1]
	v_cvt_pk_fp8_f32 v150, v142, v143 op_sel:[0,0,1]
	v_cvt_pk_fp8_f32 v151, v146, v147 op_sel:[0,0,1]
	s_nop 0
	global_store_dwordx4 v12, v[148:151], s[14:15]
	s_waitcnt vmcnt(22)
	v_mul_f32_e32 v36, 0x43000000, v36
	v_mul_f32_e32 v37, 0x43000000, v37
	v_mul_f32_e32 v38, 0x43000000, v38
	v_mul_f32_e32 v39, 0x43000000, v39
	ds_write_b128 v5, v[36:39]
	v_mul_f32_e32 v40, 0x43000000, v40
	v_mul_f32_e32 v41, 0x43000000, v41
	v_mul_f32_e32 v42, 0x43000000, v42
	v_mul_f32_e32 v43, 0x43000000, v43
	ds_write_b128 v5, v[40:43] offset:1024
	v_mul_f32_e32 v44, 0x43000000, v44
	v_mul_f32_e32 v45, 0x43000000, v45
	v_mul_f32_e32 v46, 0x43000000, v46
	v_mul_f32_e32 v47, 0x43000000, v47
	ds_write_b128 v5, v[44:47] offset:2048
	v_mul_f32_e32 v48, 0x43000000, v48
	v_mul_f32_e32 v49, 0x43000000, v49
	v_mul_f32_e32 v50, 0x43000000, v50
	v_mul_f32_e32 v51, 0x43000000, v51
	ds_write_b128 v5, v[48:51] offset:3072
	v_mul_f32_e32 v52, 0x43000000, v52
	v_mul_f32_e32 v53, 0x43000000, v53
	v_mul_f32_e32 v54, 0x43000000, v54
	v_mul_f32_e32 v55, 0x43000000, v55
	ds_write_b128 v5, v[52:55] offset:4096
	v_mul_f32_e32 v56, 0x43000000, v56
	v_mul_f32_e32 v57, 0x43000000, v57
	v_mul_f32_e32 v58, 0x43000000, v58
	v_mul_f32_e32 v59, 0x43000000, v59
	ds_write_b128 v5, v[56:59] offset:5120
	v_mul_f32_e32 v60, 0x43000000, v60
	v_mul_f32_e32 v61, 0x43000000, v61
	v_mul_f32_e32 v62, 0x43000000, v62
	v_mul_f32_e32 v63, 0x43000000, v63
	ds_write_b128 v5, v[60:63] offset:6144
	v_mul_f32_e32 v64, 0x43000000, v64
	v_mul_f32_e32 v65, 0x43000000, v65
	v_mul_f32_e32 v66, 0x43000000, v66
	v_mul_f32_e32 v67, 0x43000000, v67
	ds_write_b128 v5, v[64:67] offset:7168
	s_waitcnt lgkmcnt(0)
	s_barrier
; #define GAS __attribute__((address_space(1)))
; #define LAS __attribute__((address_space(3)))
; #define LDS_WAIT() asm volatile("s_waitcnt lgkmcnt(0)" ::: "memory")
; __device__ __forceinline__ unsigned pk4_fp8(float a, float b, float c, float d) {
;     a = fminf(fmaxf(a, -448.f), 448.f); b = fminf(fmaxf(b, -448.f), 448.f); c = fminf(fmaxf(c, -448.f), 448.f); d = fminf(fmaxf(d, -448.f), 448.f);
;     int w = __builtin_amdgcn_cvt_pk_fp8_f32(a, b, 0, false); w = __builtin_amdgcn_cvt_pk_fp8_f32(c, d, w, true); return (unsigned)w; }
;     const int pr = item >> 1, kb = 2 * (pr / nblk) + (item & 1), nb = pr % nblk, k0 = 64 * kb, n0 = 32 * nb;
;     const int nr = n0 + (lane & 31); const int sc = MAP == 1 ? src_col_in(nr) : nr;
;     float v[32];
; #pragma unroll
;     for (int i = 0; i < 32; ++i) v[i] = sc >= 0 ? W[(size_t)(k0 + 2 * i + (lane >> 5)) * Nsrc + sc] : 0.f;
; #pragma unroll
;     for (int i = 0; i < 32; ++i) { const int k = k0 + 2 * i + (lane >> 5); float x = v[i] * wscale; if (KS) x *= (k < ksplit ? ksA[k] : ksB[k - ksplit]); scr[(2 * i + (lane >> 5)) * 33 + (lane & 31)] = x; }
;     LDS_WAIT(); asm volatile("" ::: "memory");
;     const int c = lane & 7;
; #pragma unroll
;     for (int j = 0; j < 4; ++j) { const int n = (lane >> 3) + 8 * j; const LAS float* s = scr + (8 * c) * 33 + n;
;         const unsigned long long o = (unsigned long long)pg8::pk4_fp8(s[0 * 33], s[1 * 33], s[2 * 33], s[3 * 33]) | ((unsigned long long)pg8::pk4_fp8(s[4 * 33], s[5 * 33], s[6 * 33], s[7 * 33]) << 32);
;         *(GAS unsigned long long*)(WT + (size_t)(n0 + n) * K + k0 + 8 * c) = o; }
;     LDS_WAIT(); asm volatile("" ::: "memory");
	s_add_i32 s17, s16, 2880
	s_min_u32 s17, s17, 0xfff
	s_lshr_b32 s18, s17, 5
	s_add_i32 s18, s18, 0
	s_and_b32 s19, s17, 31
	s_lshl_b32 s18, s18, 21
	s_lshl_b32 s19, s19, 9
	s_add_u32 s18, s18, s19
	s_add_u32 s12, s2, s18
	s_addc_u32 s13, s3, 0
	global_load_dwordx4 v[36:39], v10, s[12:13]
	s_add_u32 s12, s12, 0x8000
	s_addc_u32 s13, s13, 0
	global_load_dwordx4 v[40:43], v10, s[12:13]
	s_add_u32 s12, s12, 0x8000
	s_addc_u32 s13, s13, 0
	global_load_dwordx4 v[44:47], v10, s[12:13]
	s_add_u32 s12, s12, 0x8000
	s_addc_u32 s13, s13, 0
	global_load_dwordx4 v[48:51], v10, s[12:13]
	s_add_u32 s12, s12, 0x8000
	s_addc_u32 s13, s13, 0
	global_load_dwordx4 v[52:55], v10, s[12:13]
	s_add_u32 s12, s12, 0x8000
	s_addc_u32 s13, s13, 0
	global_load_dwordx4 v[56:59], v10, s[12:13]
	s_add_u32 s12, s12, 0x8000
	s_addc_u32 s13, s13, 0
	global_load_dwordx4 v[60:63], v10, s[12:13]
	s_add_u32 s12, s12, 0x8000
	s_addc_u32 s13, s13, 0
	global_load_dwordx4 v[64:67], v10, s[12:13]
	s_add_i32 s17, s16, 2592
	s_min_u32 s17, s17, 0xfff
	s_lshr_b32 s18, s17, 5
	s_add_i32 s18, s18, 0
	s_and_b32 s19, s17, 31
	s_lshl_b32 s19, s19, 21
	s_lshl_b32 s18, s18, 7
	s_add_u32 s18, s18, s19
	s_add_u32 s14, s4, s18
	s_addc_u32 s15, s5, 0
	ds_read_b32 v132, v7
	ds_read_b32 v133, v7 offset:512
	ds_read_b32 v134, v7 offset:1024
	ds_read_b32 v135, v7 offset:1536
	ds_read_b32 v136, v7 offset:2048
	ds_read_b32 v137, v7 offset:2560
	ds_read_b32 v138, v7 offset:3072
	ds_read_b32 v139, v7 offset:3584
	ds_read_b32 v140, v7 offset:4096
	ds_read_b32 v141, v7 offset:4608
	ds_read_b32 v142, v7 offset:5120
	ds_read_b32 v143, v7 offset:5632
	ds_read_b32 v144, v7 offset:6144
	ds_read_b32 v145, v7 offset:6656
	ds_read_b32 v146, v7 offset:7168
	ds_read_b32 v147, v7 offset:7680
	s_waitcnt lgkmcnt(0)
	v_max_f32_e32 v132, v132, v132
	v_max_f32_e32 v133, v133, v133
	v_max_f32_e32 v134, v134, v134
	v_max_f32_e32 v135, v135, v135
	v_max_f32_e32 v136, v136, v136
	v_max_f32_e32 v137, v137, v137
	v_max_f32_e32 v138, v138, v138
	v_max_f32_e32 v139, v139, v139
	v_max_f32_e32 v140, v140, v140
	v_max_f32_e32 v141, v141, v141
	v_max_f32_e32 v142, v142, v142
	v_max_f32_e32 v143, v143, v143
	v_max_f32_e32 v144, v144, v144
	v_max_f32_e32 v145, v145, v145
	v_max_f32_e32 v146, v146, v146
	v_max_f32_e32 v147, v147, v147
	v_med3_f32 v132, v132, s20, v13
	v_med3_f32 v133, v133, s20, v13
	v_med3_f32 v134, v134, s20, v13
	v_med3_f32 v135, v135, s20, v13
	v_med3_f32 v136, v136, s20, v13
	v_med3_f32 v137, v137, s20, v13
	v_med3_f32 v138, v138, s20, v13
	v_med3_f32 v139, v139, s20, v13
	v_med3_f32 v140, v140, s20, v13
	v_med3_f32 v141, v141, s20, v13
	v_med3_f32 v142, v142, s20, v13
	v_med3_f32 v143, v143, s20, v13
	v_med3_f32 v144, v144, s20, v13
	v_med3_f32 v145, v145, s20, v13
	v_med3_f32 v146, v146, s20, v13
	v_med3_f32 v147, v147, s20, v13
	v_mov_b32_e32 v148, 0
	v_mov_b32_e32 v149, 0
	v_mov_b32_e32 v150, 0
	v_mov_b32_e32 v151, 0
	v_cvt_pk_fp8_f32 v148, v132, v133
	v_cvt_pk_fp8_f32 v149, v136, v137
	v_cvt_pk_fp8_f32 v150, v140, v141
	v_cvt_pk_fp8_f32 v151, v144, v145
	v_cvt_pk_fp8_f32 v148, v134, v135 op_sel:[0,0,1]
	v_cvt_pk_fp8_f32 v149, v138, v139 op_sel:[0,0,1]
	v_cvt_pk_fp8_f32 v150, v142, v143 op_sel:[0,0,1]
	v_cvt_pk_fp8_f32 v151, v146, v147 op_sel:[0,0,1]
	s_nop 0
	global_store_dwordx4 v11, v[148:151], s[14:15]
	ds_read_b32 v132, v9
	ds_read_b32 v133, v9 offset:512
	ds_read_b32 v134, v9 offset:1024
	ds_read_b32 v135, v9 offset:1536
	ds_read_b32 v136, v9 offset:2048
	ds_read_b32 v137, v9 offset:2560
	ds_read_b32 v138, v9 offset:3072
	ds_read_b32 v139, v9 offset:3584
	ds_read_b32 v140, v9 offset:4096
	ds_read_b32 v141, v9 offset:4608
	ds_read_b32 v142, v9 offset:5120
	ds_read_b32 v143, v9 offset:5632
	ds_read_b32 v144, v9 offset:6144
	ds_read_b32 v145, v9 offset:6656
	ds_read_b32 v146, v9 offset:7168
	ds_read_b32 v147, v9 offset:7680
	s_waitcnt lgkmcnt(0)
	v_max_f32_e32 v132, v132, v132
	v_max_f32_e32 v133, v133, v133
	v_max_f32_e32 v134, v134, v134
	v_max_f32_e32 v135, v135, v135
	v_max_f32_e32 v136, v136, v136
	v_max_f32_e32 v137, v137, v137
	v_max_f32_e32 v138, v138, v138
	v_max_f32_e32 v139, v139, v139
	v_max_f32_e32 v140, v140, v140
	v_max_f32_e32 v141, v141, v141
	v_max_f32_e32 v142, v142, v142
	v_max_f32_e32 v143, v143, v143
	v_max_f32_e32 v144, v144, v144
	v_max_f32_e32 v145, v145, v145
	v_max_f32_e32 v146, v146, v146
	v_max_f32_e32 v147, v147, v147
	v_med3_f32 v132, v132, s20, v13
	v_med3_f32 v133, v133, s20, v13
	v_med3_f32 v134, v134, s20, v13
	v_med3_f32 v135, v135, s20, v13
	v_med3_f32 v136, v136, s20, v13
	v_med3_f32 v137, v137, s20, v13
	v_med3_f32 v138, v138, s20, v13
	v_med3_f32 v139, v139, s20, v13
	v_med3_f32 v140, v140, s20, v13
	v_med3_f32 v141, v141, s20, v13
	v_med3_f32 v142, v142, s20, v13
	v_med3_f32 v143, v143, s20, v13
	v_med3_f32 v144, v144, s20, v13
	v_med3_f32 v145, v145, s20, v13
	v_med3_f32 v146, v146, s20, v13
	v_med3_f32 v147, v147, s20, v13
	v_mov_b32_e32 v148, 0
	v_mov_b32_e32 v149, 0
	v_mov_b32_e32 v150, 0
	v_mov_b32_e32 v151, 0
	v_cvt_pk_fp8_f32 v148, v132, v133
	v_cvt_pk_fp8_f32 v149, v136, v137
	v_cvt_pk_fp8_f32 v150, v140, v141
	v_cvt_pk_fp8_f32 v151, v144, v145
	v_cvt_pk_fp8_f32 v148, v134, v135 op_sel:[0,0,1]
	v_cvt_pk_fp8_f32 v149, v138, v139 op_sel:[0,0,1]
	v_cvt_pk_fp8_f32 v150, v142, v143 op_sel:[0,0,1]
	v_cvt_pk_fp8_f32 v151, v146, v147 op_sel:[0,0,1]
	s_nop 0
	global_store_dwordx4 v12, v[148:151], s[14:15]
	s_waitcnt vmcnt(22)
	v_mul_f32_e32 v68, 0x43000000, v68
	v_mul_f32_e32 v69, 0x43000000, v69
	v_mul_f32_e32 v70, 0x43000000, v70
	v_mul_f32_e32 v71, 0x43000000, v71
	ds_write_b128 v4, v[68:71]
	v_mul_f32_e32 v72, 0x43000000, v72
	v_mul_f32_e32 v73, 0x43000000, v73
	v_mul_f32_e32 v74, 0x43000000, v74
	v_mul_f32_e32 v75, 0x43000000, v75
	ds_write_b128 v4, v[72:75] offset:1024
	v_mul_f32_e32 v76, 0x43000000, v76
	v_mul_f32_e32 v77, 0x43000000, v77
	v_mul_f32_e32 v78, 0x43000000, v78
	v_mul_f32_e32 v79, 0x43000000, v79
	ds_write_b128 v4, v[76:79] offset:2048
	v_mul_f32_e32 v80, 0x43000000, v80
	v_mul_f32_e32 v81, 0x43000000, v81
	v_mul_f32_e32 v82, 0x43000000, v82
	v_mul_f32_e32 v83, 0x43000000, v83
	ds_write_b128 v4, v[80:83] offset:3072
	v_mul_f32_e32 v84, 0x43000000, v84
	v_mul_f32_e32 v85, 0x43000000, v85
	v_mul_f32_e32 v86, 0x43000000, v86
	v_mul_f32_e32 v87, 0x43000000, v87
	ds_write_b128 v4, v[84:87] offset:4096
	v_mul_f32_e32 v88, 0x43000000, v88
	v_mul_f32_e32 v89, 0x43000000, v89
	v_mul_f32_e32 v90, 0x43000000, v90
	v_mul_f32_e32 v91, 0x43000000, v91
	ds_write_b128 v4, v[88:91] offset:5120
	v_mul_f32_e32 v92, 0x43000000, v92
	v_mul_f32_e32 v93, 0x43000000, v93
	v_mul_f32_e32 v94, 0x43000000, v94
	v_mul_f32_e32 v95, 0x43000000, v95
	ds_write_b128 v4, v[92:95] offset:6144
	v_mul_f32_e32 v96, 0x43000000, v96
	v_mul_f32_e32 v97, 0x43000000, v97
	v_mul_f32_e32 v98, 0x43000000, v98
	v_mul_f32_e32 v99, 0x43000000, v99
	ds_write_b128 v4, v[96:99] offset:7168
	s_waitcnt lgkmcnt(0)
	s_barrier
; #define GAS __attribute__((address_space(1)))
; #define LAS __attribute__((address_space(3)))
; #define LDS_WAIT() asm volatile("s_waitcnt lgkmcnt(0)" ::: "memory")
; __device__ __forceinline__ unsigned pk4_fp8(float a, float b, float c, float d) {
;     a = fminf(fmaxf(a, -448.f), 448.f); b = fminf(fmaxf(b, -448.f), 448.f); c = fminf(fmaxf(c, -448.f), 448.f); d = fminf(fmaxf(d, -448.f), 448.f);
;     int w = __builtin_amdgcn_cvt_pk_fp8_f32(a, b, 0, false); w = __builtin_amdgcn_cvt_pk_fp8_f32(c, d, w, true); return (unsigned)w; }
;     const int pr = item >> 1, kb = 2 * (pr / nblk) + (item & 1), nb = pr % nblk, k0 = 64 * kb, n0 = 32 * nb;
;     const int nr = n0 + (lane & 31); const int sc = MAP == 1 ? src_col_in(nr) : nr;
;     float v[32];
; #pragma unroll
;     for (int i = 0; i < 32; ++i) v[i] = sc >= 0 ? W[(size_t)(k0 + 2 * i + (lane >> 5)) * Nsrc + sc] : 0.f;
; #pragma unroll
;     for (int i = 0; i < 32; ++i) { const int k = k0 + 2 * i + (lane >> 5); float x = v[i] * wscale; if (KS) x *= (k < ksplit ? ksA[k] : ksB[k - ksplit]); scr[(2 * i + (lane >> 5)) * 33 + (lane & 31)] = x; }
;     LDS_WAIT(); asm volatile("" ::: "memory");
;     const int c = lane & 7;
; #pragma unroll
;     for (int j = 0; j < 4; ++j) { const int n = (lane >> 3) + 8 * j; const LAS float* s = scr + (8 * c) * 33 + n;
;         const unsigned long long o = (unsigned long long)pg8::pk4_fp8(s[0 * 33], s[1 * 33], s[2 * 33], s[3 * 33]) | ((unsigned long long)pg8::pk4_fp8(s[4 * 33], s[5 * 33], s[6 * 33], s[7 * 33]) << 32);
;         *(GAS unsigned long long*)(WT + (size_t)(n0 + n) * K + k0 + 8 * c) = o; }
;     LDS_WAIT(); asm volatile("" ::: "memory");
	s_add_i32 s17, s16, 2976
	s_min_u32 s17, s17, 0xfff
	s_lshr_b32 s18, s17, 5
	s_add_i32 s18, s18, 0
	s_and_b32 s19, s17, 31
	s_lshl_b32 s18, s18, 21
	s_lshl_b32 s19, s19, 9
	s_add_u32 s18, s18, s19
	s_add_u32 s12, s2, s18
	s_addc_u32 s13, s3, 0
	global_load_dwordx4 v[68:71], v10, s[12:13]
	s_add_u32 s12, s12, 0x8000
	s_addc_u32 s13, s13, 0
	global_load_dwordx4 v[72:75], v10, s[12:13]
	s_add_u32 s12, s12, 0x8000
	s_addc_u32 s13, s13, 0
	global_load_dwordx4 v[76:79], v10, s[12:13]
	s_add_u32 s12, s12, 0x8000
	s_addc_u32 s13, s13, 0
	global_load_dwordx4 v[80:83], v10, s[12:13]
	s_add_u32 s12, s12, 0x8000
	s_addc_u32 s13, s13, 0
	global_load_dwordx4 v[84:87], v10, s[12:13]
	s_add_u32 s12, s12, 0x8000
	s_addc_u32 s13, s13, 0
	global_load_dwordx4 v[88:91], v10, s[12:13]
	s_add_u32 s12, s12, 0x8000
	s_addc_u32 s13, s13, 0
	global_load_dwordx4 v[92:95], v10, s[12:13]
	s_add_u32 s12, s12, 0x8000
	s_addc_u32 s13, s13, 0
	global_load_dwordx4 v[96:99], v10, s[12:13]
	s_add_i32 s17, s16, 2688
	s_min_u32 s17, s17, 0xfff
	s_lshr_b32 s18, s17, 5
	s_add_i32 s18, s18, 0
	s_and_b32 s19, s17, 31
	s_lshl_b32 s19, s19, 21
	s_lshl_b32 s18, s18, 7
	s_add_u32 s18, s18, s19
	s_add_u32 s14, s4, s18
	s_addc_u32 s15, s5, 0
	ds_read_b32 v132, v6
	ds_read_b32 v133, v6 offset:512
	ds_read_b32 v134, v6 offset:1024
	ds_read_b32 v135, v6 offset:1536
	ds_read_b32 v136, v6 offset:2048
	ds_read_b32 v137, v6 offset:2560
	ds_read_b32 v138, v6 offset:3072
	ds_read_b32 v139, v6 offset:3584
	ds_read_b32 v140, v6 offset:4096
	ds_read_b32 v141, v6 offset:4608
	ds_read_b32 v142, v6 offset:5120
	ds_read_b32 v143, v6 offset:5632
	ds_read_b32 v144, v6 offset:6144
	ds_read_b32 v145, v6 offset:6656
	ds_read_b32 v146, v6 offset:7168
	ds_read_b32 v147, v6 offset:7680
	s_waitcnt lgkmcnt(0)
	v_max_f32_e32 v132, v132, v132
	v_max_f32_e32 v133, v133, v133
	v_max_f32_e32 v134, v134, v134
	v_max_f32_e32 v135, v135, v135
	v_max_f32_e32 v136, v136, v136
	v_max_f32_e32 v137, v137, v137
	v_max_f32_e32 v138, v138, v138
	v_max_f32_e32 v139, v139, v139
	v_max_f32_e32 v140, v140, v140
	v_max_f32_e32 v141, v141, v141
	v_max_f32_e32 v142, v142, v142
	v_max_f32_e32 v143, v143, v143
	v_max_f32_e32 v144, v144, v144
	v_max_f32_e32 v145, v145, v145
	v_max_f32_e32 v146, v146, v146
	v_max_f32_e32 v147, v147, v147
	v_med3_f32 v132, v132, s20, v13
	v_med3_f32 v133, v133, s20, v13
	v_med3_f32 v134, v134, s20, v13
	v_med3_f32 v135, v135, s20, v13
	v_med3_f32 v136, v136, s20, v13
	v_med3_f32 v137, v137, s20, v13
	v_med3_f32 v138, v138, s20, v13
	v_med3_f32 v139, v139, s20, v13
	v_med3_f32 v140, v140, s20, v13
	v_med3_f32 v141, v141, s20, v13
	v_med3_f32 v142, v142, s20, v13
	v_med3_f32 v143, v143, s20, v13
	v_med3_f32 v144, v144, s20, v13
	v_med3_f32 v145, v145, s20, v13
	v_med3_f32 v146, v146, s20, v13
	v_med3_f32 v147, v147, s20, v13
	v_mov_b32_e32 v148, 0
	v_mov_b32_e32 v149, 0
	v_mov_b32_e32 v150, 0
	v_mov_b32_e32 v151, 0
	v_cvt_pk_fp8_f32 v148, v132, v133
	v_cvt_pk_fp8_f32 v149, v136, v137
	v_cvt_pk_fp8_f32 v150, v140, v141
	v_cvt_pk_fp8_f32 v151, v144, v145
	v_cvt_pk_fp8_f32 v148, v134, v135 op_sel:[0,0,1]
	v_cvt_pk_fp8_f32 v149, v138, v139 op_sel:[0,0,1]
	v_cvt_pk_fp8_f32 v150, v142, v143 op_sel:[0,0,1]
	v_cvt_pk_fp8_f32 v151, v146, v147 op_sel:[0,0,1]
	s_nop 0
	global_store_dwordx4 v11, v[148:151], s[14:15]
	ds_read_b32 v132, v8
	ds_read_b32 v133, v8 offset:512
	ds_read_b32 v134, v8 offset:1024
	ds_read_b32 v135, v8 offset:1536
	ds_read_b32 v136, v8 offset:2048
	ds_read_b32 v137, v8 offset:2560
	ds_read_b32 v138, v8 offset:3072
	ds_read_b32 v139, v8 offset:3584
	ds_read_b32 v140, v8 offset:4096
	ds_read_b32 v141, v8 offset:4608
	ds_read_b32 v142, v8 offset:5120
	ds_read_b32 v143, v8 offset:5632
	ds_read_b32 v144, v8 offset:6144
	ds_read_b32 v145, v8 offset:6656
	ds_read_b32 v146, v8 offset:7168
	ds_read_b32 v147, v8 offset:7680
	s_waitcnt lgkmcnt(0)
	v_max_f32_e32 v132, v132, v132
	v_max_f32_e32 v133, v133, v133
	v_max_f32_e32 v134, v134, v134
	v_max_f32_e32 v135, v135, v135
	v_max_f32_e32 v136, v136, v136
	v_max_f32_e32 v137, v137, v137
	v_max_f32_e32 v138, v138, v138
	v_max_f32_e32 v139, v139, v139
	v_max_f32_e32 v140, v140, v140
	v_max_f32_e32 v141, v141, v141
	v_max_f32_e32 v142, v142, v142
	v_max_f32_e32 v143, v143, v143
	v_max_f32_e32 v144, v144, v144
	v_max_f32_e32 v145, v145, v145
	v_max_f32_e32 v146, v146, v146
	v_max_f32_e32 v147, v147, v147
	v_med3_f32 v132, v132, s20, v13
	v_med3_f32 v133, v133, s20, v13
	v_med3_f32 v134, v134, s20, v13
	v_med3_f32 v135, v135, s20, v13
	v_med3_f32 v136, v136, s20, v13
	v_med3_f32 v137, v137, s20, v13
	v_med3_f32 v138, v138, s20, v13
	v_med3_f32 v139, v139, s20, v13
	v_med3_f32 v140, v140, s20, v13
	v_med3_f32 v141, v141, s20, v13
	v_med3_f32 v142, v142, s20, v13
	v_med3_f32 v143, v143, s20, v13
	v_med3_f32 v144, v144, s20, v13
	v_med3_f32 v145, v145, s20, v13
	v_med3_f32 v146, v146, s20, v13
	v_med3_f32 v147, v147, s20, v13
	v_mov_b32_e32 v148, 0
	v_mov_b32_e32 v149, 0
	v_mov_b32_e32 v150, 0
	v_mov_b32_e32 v151, 0
	v_cvt_pk_fp8_f32 v148, v132, v133
	v_cvt_pk_fp8_f32 v149, v136, v137
	v_cvt_pk_fp8_f32 v150, v140, v141
	v_cvt_pk_fp8_f32 v151, v144, v145
	v_cvt_pk_fp8_f32 v148, v134, v135 op_sel:[0,0,1]
	v_cvt_pk_fp8_f32 v149, v138, v139 op_sel:[0,0,1]
	v_cvt_pk_fp8_f32 v150, v142, v143 op_sel:[0,0,1]
	v_cvt_pk_fp8_f32 v151, v146, v147 op_sel:[0,0,1]
	s_nop 0
	global_store_dwordx4 v12, v[148:151], s[14:15]
	s_waitcnt vmcnt(22)
	v_mul_f32_e32 v100, 0x43000000, v100
	v_mul_f32_e32 v101, 0x43000000, v101
	v_mul_f32_e32 v102, 0x43000000, v102
	v_mul_f32_e32 v103, 0x43000000, v103
	ds_write_b128 v5, v[100:103]
	v_mul_f32_e32 v104, 0x43000000, v104
	v_mul_f32_e32 v105, 0x43000000, v105
	v_mul_f32_e32 v106, 0x43000000, v106
	v_mul_f32_e32 v107, 0x43000000, v107
	ds_write_b128 v5, v[104:107] offset:1024
	v_mul_f32_e32 v108, 0x43000000, v108
	v_mul_f32_e32 v109, 0x43000000, v109
	v_mul_f32_e32 v110, 0x43000000, v110
	v_mul_f32_e32 v111, 0x43000000, v111
	ds_write_b128 v5, v[108:111] offset:2048
	v_mul_f32_e32 v112, 0x43000000, v112
	v_mul_f32_e32 v113, 0x43000000, v113
	v_mul_f32_e32 v114, 0x43000000, v114
	v_mul_f32_e32 v115, 0x43000000, v115
	ds_write_b128 v5, v[112:115] offset:3072
	v_mul_f32_e32 v116, 0x43000000, v116
	v_mul_f32_e32 v117, 0x43000000, v117
	v_mul_f32_e32 v118, 0x43000000, v118
	v_mul_f32_e32 v119, 0x43000000, v119
	ds_write_b128 v5, v[116:119] offset:4096
	v_mul_f32_e32 v120, 0x43000000, v120
	v_mul_f32_e32 v121, 0x43000000, v121
	v_mul_f32_e32 v122, 0x43000000, v122
	v_mul_f32_e32 v123, 0x43000000, v123
	ds_write_b128 v5, v[120:123] offset:5120
	v_mul_f32_e32 v124, 0x43000000, v124
	v_mul_f32_e32 v125, 0x43000000, v125
	v_mul_f32_e32 v126, 0x43000000, v126
	v_mul_f32_e32 v127, 0x43000000, v127
	ds_write_b128 v5, v[124:127] offset:6144
	v_mul_f32_e32 v128, 0x43000000, v128
	v_mul_f32_e32 v129, 0x43000000, v129
	v_mul_f32_e32 v130, 0x43000000, v130
	v_mul_f32_e32 v131, 0x43000000, v131
	ds_write_b128 v5, v[128:131] offset:7168
	s_waitcnt lgkmcnt(0)
	s_barrier
; #define GAS __attribute__((address_space(1)))
; #define LAS __attribute__((address_space(3)))
; #define LDS_WAIT() asm volatile("s_waitcnt lgkmcnt(0)" ::: "memory")
; __device__ __forceinline__ unsigned pk4_fp8(float a, float b, float c, float d) {
;     a = fminf(fmaxf(a, -448.f), 448.f); b = fminf(fmaxf(b, -448.f), 448.f); c = fminf(fmaxf(c, -448.f), 448.f); d = fminf(fmaxf(d, -448.f), 448.f);
;     int w = __builtin_amdgcn_cvt_pk_fp8_f32(a, b, 0, false); w = __builtin_amdgcn_cvt_pk_fp8_f32(c, d, w, true); return (unsigned)w; }
;     const int pr = item >> 1, kb = 2 * (pr / nblk) + (item & 1), nb = pr % nblk, k0 = 64 * kb, n0 = 32 * nb;
;     const int nr = n0 + (lane & 31); const int sc = MAP == 1 ? src_col_in(nr) : nr;
;     float v[32];
; #pragma unroll
;     for (int i = 0; i < 32; ++i) v[i] = sc >= 0 ? W[(size_t)(k0 + 2 * i + (lane >> 5)) * Nsrc + sc] : 0.f;
; #pragma unroll
;     for (int i = 0; i < 32; ++i) { const int k = k0 + 2 * i + (lane >> 5); float x = v[i] * wscale; if (KS) x *= (k < ksplit ? ksA[k] : ksB[k - ksplit]); scr[(2 * i + (lane >> 5)) * 33 + (lane & 31)] = x; }
;     LDS_WAIT(); asm volatile("" ::: "memory");
;     const int c = lane & 7;
; #pragma unroll
;     for (int j = 0; j < 4; ++j) { const int n = (lane >> 3) + 8 * j; const LAS float* s = scr + (8 * c) * 33 + n;
;         const unsigned long long o = (unsigned long long)pg8::pk4_fp8(s[0 * 33], s[1 * 33], s[2 * 33], s[3 * 33]) | ((unsigned long long)pg8::pk4_fp8(s[4 * 33], s[5 * 33], s[6 * 33], s[7 * 33]) << 32);
;         *(GAS unsigned long long*)(WT + (size_t)(n0 + n) * K + k0 + 8 * c) = o; }
;     LDS_WAIT(); asm volatile("" ::: "memory");
	s_add_i32 s17, s16, 3072
	s_min_u32 s17, s17, 0xfff
	s_lshr_b32 s18, s17, 5
	s_add_i32 s18, s18, 0
	s_and_b32 s19, s17, 31
	s_lshl_b32 s18, s18, 21
	s_lshl_b32 s19, s19, 9
	s_add_u32 s18, s18, s19
	s_add_u32 s12, s2, s18
	s_addc_u32 s13, s3, 0
	global_load_dwordx4 v[100:103], v10, s[12:13]
	s_add_u32 s12, s12, 0x8000
	s_addc_u32 s13, s13, 0
	global_load_dwordx4 v[104:107], v10, s[12:13]
	s_add_u32 s12, s12, 0x8000
	s_addc_u32 s13, s13, 0
	global_load_dwordx4 v[108:111], v10, s[12:13]
	s_add_u32 s12, s12, 0x8000
	s_addc_u32 s13, s13, 0
	global_load_dwordx4 v[112:115], v10, s[12:13]
	s_add_u32 s12, s12, 0x8000
	s_addc_u32 s13, s13, 0
	global_load_dwordx4 v[116:119], v10, s[12:13]
	s_add_u32 s12, s12, 0x8000
	s_addc_u32 s13, s13, 0
	global_load_dwordx4 v[120:123], v10, s[12:13]
	s_add_u32 s12, s12, 0x8000
	s_addc_u32 s13, s13, 0
	global_load_dwordx4 v[124:127], v10, s[12:13]
	s_add_u32 s12, s12, 0x8000
	s_addc_u32 s13, s13, 0
	global_load_dwordx4 v[128:131], v10, s[12:13]
	s_add_i32 s17, s16, 2784
	s_min_u32 s17, s17, 0xfff
	s_lshr_b32 s18, s17, 5
	s_add_i32 s18, s18, 0
	s_and_b32 s19, s17, 31
	s_lshl_b32 s19, s19, 21
	s_lshl_b32 s18, s18, 7
	s_add_u32 s18, s18, s19
	s_add_u32 s14, s4, s18
	s_addc_u32 s15, s5, 0
	ds_read_b32 v132, v7
	ds_read_b32 v133, v7 offset:512
	ds_read_b32 v134, v7 offset:1024
	ds_read_b32 v135, v7 offset:1536
	ds_read_b32 v136, v7 offset:2048
	ds_read_b32 v137, v7 offset:2560
	ds_read_b32 v138, v7 offset:3072
	ds_read_b32 v139, v7 offset:3584
	ds_read_b32 v140, v7 offset:4096
	ds_read_b32 v141, v7 offset:4608
	ds_read_b32 v142, v7 offset:5120
	ds_read_b32 v143, v7 offset:5632
	ds_read_b32 v144, v7 offset:6144
	ds_read_b32 v145, v7 offset:6656
	ds_read_b32 v146, v7 offset:7168
	ds_read_b32 v147, v7 offset:7680
	s_waitcnt lgkmcnt(0)
	v_max_f32_e32 v132, v132, v132
	v_max_f32_e32 v133, v133, v133
	v_max_f32_e32 v134, v134, v134
	v_max_f32_e32 v135, v135, v135
	v_max_f32_e32 v136, v136, v136
	v_max_f32_e32 v137, v137, v137
	v_max_f32_e32 v138, v138, v138
	v_max_f32_e32 v139, v139, v139
	v_max_f32_e32 v140, v140, v140
	v_max_f32_e32 v141, v141, v141
	v_max_f32_e32 v142, v142, v142
	v_max_f32_e32 v143, v143, v143
	v_max_f32_e32 v144, v144, v144
	v_max_f32_e32 v145, v145, v145
	v_max_f32_e32 v146, v146, v146
	v_max_f32_e32 v147, v147, v147
	v_med3_f32 v132, v132, s20, v13
	v_med3_f32 v133, v133, s20, v13
	v_med3_f32 v134, v134, s20, v13
	v_med3_f32 v135, v135, s20, v13
	v_med3_f32 v136, v136, s20, v13
	v_med3_f32 v137, v137, s20, v13
	v_med3_f32 v138, v138, s20, v13
	v_med3_f32 v139, v139, s20, v13
	v_med3_f32 v140, v140, s20, v13
	v_med3_f32 v141, v141, s20, v13
	v_med3_f32 v142, v142, s20, v13
	v_med3_f32 v143, v143, s20, v13
	v_med3_f32 v144, v144, s20, v13
	v_med3_f32 v145, v145, s20, v13
	v_med3_f32 v146, v146, s20, v13
	v_med3_f32 v147, v147, s20, v13
	v_mov_b32_e32 v148, 0
	v_mov_b32_e32 v149, 0
	v_mov_b32_e32 v150, 0
	v_mov_b32_e32 v151, 0
	v_cvt_pk_fp8_f32 v148, v132, v133
	v_cvt_pk_fp8_f32 v149, v136, v137
	v_cvt_pk_fp8_f32 v150, v140, v141
	v_cvt_pk_fp8_f32 v151, v144, v145
	v_cvt_pk_fp8_f32 v148, v134, v135 op_sel:[0,0,1]
	v_cvt_pk_fp8_f32 v149, v138, v139 op_sel:[0,0,1]
	v_cvt_pk_fp8_f32 v150, v142, v143 op_sel:[0,0,1]
	v_cvt_pk_fp8_f32 v151, v146, v147 op_sel:[0,0,1]
	s_nop 0
	global_store_dwordx4 v11, v[148:151], s[14:15]
	ds_read_b32 v132, v9
	ds_read_b32 v133, v9 offset:512
	ds_read_b32 v134, v9 offset:1024
	ds_read_b32 v135, v9 offset:1536
	ds_read_b32 v136, v9 offset:2048
	ds_read_b32 v137, v9 offset:2560
	ds_read_b32 v138, v9 offset:3072
	ds_read_b32 v139, v9 offset:3584
	ds_read_b32 v140, v9 offset:4096
	ds_read_b32 v141, v9 offset:4608
	ds_read_b32 v142, v9 offset:5120
	ds_read_b32 v143, v9 offset:5632
	ds_read_b32 v144, v9 offset:6144
	ds_read_b32 v145, v9 offset:6656
	ds_read_b32 v146, v9 offset:7168
	ds_read_b32 v147, v9 offset:7680
	s_waitcnt lgkmcnt(0)
	v_max_f32_e32 v132, v132, v132
	v_max_f32_e32 v133, v133, v133
	v_max_f32_e32 v134, v134, v134
	v_max_f32_e32 v135, v135, v135
	v_max_f32_e32 v136, v136, v136
	v_max_f32_e32 v137, v137, v137
	v_max_f32_e32 v138, v138, v138
	v_max_f32_e32 v139, v139, v139
	v_max_f32_e32 v140, v140, v140
	v_max_f32_e32 v141, v141, v141
	v_max_f32_e32 v142, v142, v142
	v_max_f32_e32 v143, v143, v143
	v_max_f32_e32 v144, v144, v144
	v_max_f32_e32 v145, v145, v145
	v_max_f32_e32 v146, v146, v146
	v_max_f32_e32 v147, v147, v147
	v_med3_f32 v132, v132, s20, v13
	v_med3_f32 v133, v133, s20, v13
	v_med3_f32 v134, v134, s20, v13
	v_med3_f32 v135, v135, s20, v13
	v_med3_f32 v136, v136, s20, v13
	v_med3_f32 v137, v137, s20, v13
	v_med3_f32 v138, v138, s20, v13
	v_med3_f32 v139, v139, s20, v13
	v_med3_f32 v140, v140, s20, v13
	v_med3_f32 v141, v141, s20, v13
	v_med3_f32 v142, v142, s20, v13
	v_med3_f32 v143, v143, s20, v13
	v_med3_f32 v144, v144, s20, v13
	v_med3_f32 v145, v145, s20, v13
	v_med3_f32 v146, v146, s20, v13
	v_med3_f32 v147, v147, s20, v13
	v_mov_b32_e32 v148, 0
	v_mov_b32_e32 v149, 0
	v_mov_b32_e32 v150, 0
	v_mov_b32_e32 v151, 0
	v_cvt_pk_fp8_f32 v148, v132, v133
	v_cvt_pk_fp8_f32 v149, v136, v137
	v_cvt_pk_fp8_f32 v150, v140, v141
	v_cvt_pk_fp8_f32 v151, v144, v145
	v_cvt_pk_fp8_f32 v148, v134, v135 op_sel:[0,0,1]
	v_cvt_pk_fp8_f32 v149, v138, v139 op_sel:[0,0,1]
	v_cvt_pk_fp8_f32 v150, v142, v143 op_sel:[0,0,1]
	v_cvt_pk_fp8_f32 v151, v146, v147 op_sel:[0,0,1]
	s_nop 0
	global_store_dwordx4 v12, v[148:151], s[14:15]
	s_waitcnt vmcnt(22)
	v_mul_f32_e32 v36, 0x43000000, v36
	v_mul_f32_e32 v37, 0x43000000, v37
	v_mul_f32_e32 v38, 0x43000000, v38
	v_mul_f32_e32 v39, 0x43000000, v39
	ds_write_b128 v4, v[36:39]
	v_mul_f32_e32 v40, 0x43000000, v40
	v_mul_f32_e32 v41, 0x43000000, v41
	v_mul_f32_e32 v42, 0x43000000, v42
	v_mul_f32_e32 v43, 0x43000000, v43
	ds_write_b128 v4, v[40:43] offset:1024
	v_mul_f32_e32 v44, 0x43000000, v44
	v_mul_f32_e32 v45, 0x43000000, v45
	v_mul_f32_e32 v46, 0x43000000, v46
	v_mul_f32_e32 v47, 0x43000000, v47
	ds_write_b128 v4, v[44:47] offset:2048
	v_mul_f32_e32 v48, 0x43000000, v48
	v_mul_f32_e32 v49, 0x43000000, v49
	v_mul_f32_e32 v50, 0x43000000, v50
	v_mul_f32_e32 v51, 0x43000000, v51
	ds_write_b128 v4, v[48:51] offset:3072
	v_mul_f32_e32 v52, 0x43000000, v52
	v_mul_f32_e32 v53, 0x43000000, v53
	v_mul_f32_e32 v54, 0x43000000, v54
	v_mul_f32_e32 v55, 0x43000000, v55
	ds_write_b128 v4, v[52:55] offset:4096
	v_mul_f32_e32 v56, 0x43000000, v56
	v_mul_f32_e32 v57, 0x43000000, v57
	v_mul_f32_e32 v58, 0x43000000, v58
	v_mul_f32_e32 v59, 0x43000000, v59
	ds_write_b128 v4, v[56:59] offset:5120
	v_mul_f32_e32 v60, 0x43000000, v60
	v_mul_f32_e32 v61, 0x43000000, v61
	v_mul_f32_e32 v62, 0x43000000, v62
	v_mul_f32_e32 v63, 0x43000000, v63
	ds_write_b128 v4, v[60:63] offset:6144
	v_mul_f32_e32 v64, 0x43000000, v64
	v_mul_f32_e32 v65, 0x43000000, v65
	v_mul_f32_e32 v66, 0x43000000, v66
	v_mul_f32_e32 v67, 0x43000000, v67
	ds_write_b128 v4, v[64:67] offset:7168
	s_waitcnt lgkmcnt(0)
	s_barrier
; #define GAS __attribute__((address_space(1)))
; #define LAS __attribute__((address_space(3)))
; #define LDS_WAIT() asm volatile("s_waitcnt lgkmcnt(0)" ::: "memory")
; __device__ __forceinline__ unsigned pk4_fp8(float a, float b, float c, float d) {
;     a = fminf(fmaxf(a, -448.f), 448.f); b = fminf(fmaxf(b, -448.f), 448.f); c = fminf(fmaxf(c, -448.f), 448.f); d = fminf(fmaxf(d, -448.f), 448.f);
;     int w = __builtin_amdgcn_cvt_pk_fp8_f32(a, b, 0, false); w = __builtin_amdgcn_cvt_pk_fp8_f32(c, d, w, true); return (unsigned)w; }
;     const int pr = item >> 1, kb = 2 * (pr / nblk) + (item & 1), nb = pr % nblk, k0 = 64 * kb, n0 = 32 * nb;
;     const int nr = n0 + (lane & 31); const int sc = MAP == 1 ? src_col_in(nr) : nr;
;     float v[32];
; #pragma unroll
;     for (int i = 0; i < 32; ++i) v[i] = sc >= 0 ? W[(size_t)(k0 + 2 * i + (lane >> 5)) * Nsrc + sc] : 0.f;
; #pragma unroll
;     for (int i = 0; i < 32; ++i) { const int k = k0 + 2 * i + (lane >> 5); float x = v[i] * wscale; if (KS) x *= (k < ksplit ? ksA[k] : ksB[k - ksplit]); scr[(2 * i + (lane >> 5)) * 33 + (lane & 31)] = x; }
;     LDS_WAIT(); asm volatile("" ::: "memory");
;     const int c = lane & 7;
; #pragma unroll
;     for (int j = 0; j < 4; ++j) { const int n = (lane >> 3) + 8 * j; const LAS float* s = scr + (8 * c) * 33 + n;
;         const unsigned long long o = (unsigned long long)pg8::pk4_fp8(s[0 * 33], s[1 * 33], s[2 * 33], s[3 * 33]) | ((unsigned long long)pg8::pk4_fp8(s[4 * 33], s[5 * 33], s[6 * 33], s[7 * 33]) << 32);
;         *(GAS unsigned long long*)(WT + (size_t)(n0 + n) * K + k0 + 8 * c) = o; }
;     LDS_WAIT(); asm volatile("" ::: "memory");
	s_add_i32 s17, s16, 3168
	s_min_u32 s17, s17, 0xfff
	s_lshr_b32 s18, s17, 5
	s_add_i32 s18, s18, 0
	s_and_b32 s19, s17, 31
	s_lshl_b32 s18, s18, 21
	s_lshl_b32 s19, s19, 9
	s_add_u32 s18, s18, s19
	s_add_u32 s12, s2, s18
	s_addc_u32 s13, s3, 0
	global_load_dwordx4 v[36:39], v10, s[12:13]
	s_add_u32 s12, s12, 0x8000
	s_addc_u32 s13, s13, 0
	global_load_dwordx4 v[40:43], v10, s[12:13]
	s_add_u32 s12, s12, 0x8000
	s_addc_u32 s13, s13, 0
	global_load_dwordx4 v[44:47], v10, s[12:13]
	s_add_u32 s12, s12, 0x8000
	s_addc_u32 s13, s13, 0
	global_load_dwordx4 v[48:51], v10, s[12:13]
	s_add_u32 s12, s12, 0x8000
	s_addc_u32 s13, s13, 0
	global_load_dwordx4 v[52:55], v10, s[12:13]
	s_add_u32 s12, s12, 0x8000
	s_addc_u32 s13, s13, 0
	global_load_dwordx4 v[56:59], v10, s[12:13]
	s_add_u32 s12, s12, 0x8000
	s_addc_u32 s13, s13, 0
	global_load_dwordx4 v[60:63], v10, s[12:13]
	s_add_u32 s12, s12, 0x8000
	s_addc_u32 s13, s13, 0
	global_load_dwordx4 v[64:67], v10, s[12:13]
	s_add_i32 s17, s16, 2880
	s_min_u32 s17, s17, 0xfff
	s_lshr_b32 s18, s17, 5
	s_add_i32 s18, s18, 0
	s_and_b32 s19, s17, 31
	s_lshl_b32 s19, s19, 21
	s_lshl_b32 s18, s18, 7
	s_add_u32 s18, s18, s19
	s_add_u32 s14, s4, s18
	s_addc_u32 s15, s5, 0
	ds_read_b32 v132, v6
	ds_read_b32 v133, v6 offset:512
	ds_read_b32 v134, v6 offset:1024
	ds_read_b32 v135, v6 offset:1536
	ds_read_b32 v136, v6 offset:2048
	ds_read_b32 v137, v6 offset:2560
	ds_read_b32 v138, v6 offset:3072
	ds_read_b32 v139, v6 offset:3584
	ds_read_b32 v140, v6 offset:4096
	ds_read_b32 v141, v6 offset:4608
	ds_read_b32 v142, v6 offset:5120
	ds_read_b32 v143, v6 offset:5632
	ds_read_b32 v144, v6 offset:6144
	ds_read_b32 v145, v6 offset:6656
	ds_read_b32 v146, v6 offset:7168
	ds_read_b32 v147, v6 offset:7680
	s_waitcnt lgkmcnt(0)
	v_max_f32_e32 v132, v132, v132
	v_max_f32_e32 v133, v133, v133
	v_max_f32_e32 v134, v134, v134
	v_max_f32_e32 v135, v135, v135
	v_max_f32_e32 v136, v136, v136
	v_max_f32_e32 v137, v137, v137
	v_max_f32_e32 v138, v138, v138
	v_max_f32_e32 v139, v139, v139
	v_max_f32_e32 v140, v140, v140
	v_max_f32_e32 v141, v141, v141
	v_max_f32_e32 v142, v142, v142
	v_max_f32_e32 v143, v143, v143
	v_max_f32_e32 v144, v144, v144
	v_max_f32_e32 v145, v145, v145
	v_max_f32_e32 v146, v146, v146
	v_max_f32_e32 v147, v147, v147
	v_med3_f32 v132, v132, s20, v13
	v_med3_f32 v133, v133, s20, v13
	v_med3_f32 v134, v134, s20, v13
	v_med3_f32 v135, v135, s20, v13
	v_med3_f32 v136, v136, s20, v13
	v_med3_f32 v137, v137, s20, v13
	v_med3_f32 v138, v138, s20, v13
	v_med3_f32 v139, v139, s20, v13
	v_med3_f32 v140, v140, s20, v13
	v_med3_f32 v141, v141, s20, v13
	v_med3_f32 v142, v142, s20, v13
	v_med3_f32 v143, v143, s20, v13
	v_med3_f32 v144, v144, s20, v13
	v_med3_f32 v145, v145, s20, v13
	v_med3_f32 v146, v146, s20, v13
	v_med3_f32 v147, v147, s20, v13
	v_mov_b32_e32 v148, 0
	v_mov_b32_e32 v149, 0
	v_mov_b32_e32 v150, 0
	v_mov_b32_e32 v151, 0
	v_cvt_pk_fp8_f32 v148, v132, v133
	v_cvt_pk_fp8_f32 v149, v136, v137
	v_cvt_pk_fp8_f32 v150, v140, v141
	v_cvt_pk_fp8_f32 v151, v144, v145
	v_cvt_pk_fp8_f32 v148, v134, v135 op_sel:[0,0,1]
	v_cvt_pk_fp8_f32 v149, v138, v139 op_sel:[0,0,1]
	v_cvt_pk_fp8_f32 v150, v142, v143 op_sel:[0,0,1]
	v_cvt_pk_fp8_f32 v151, v146, v147 op_sel:[0,0,1]
	s_nop 0
	global_store_dwordx4 v11, v[148:151], s[14:15]
	ds_read_b32 v132, v8
	ds_read_b32 v133, v8 offset:512
	ds_read_b32 v134, v8 offset:1024
	ds_read_b32 v135, v8 offset:1536
	ds_read_b32 v136, v8 offset:2048
	ds_read_b32 v137, v8 offset:2560
	ds_read_b32 v138, v8 offset:3072
	ds_read_b32 v139, v8 offset:3584
	ds_read_b32 v140, v8 offset:4096
	ds_read_b32 v141, v8 offset:4608
	ds_read_b32 v142, v8 offset:5120
	ds_read_b32 v143, v8 offset:5632
	ds_read_b32 v144, v8 offset:6144
	ds_read_b32 v145, v8 offset:6656
	ds_read_b32 v146, v8 offset:7168
	ds_read_b32 v147, v8 offset:7680
	s_waitcnt lgkmcnt(0)
	v_max_f32_e32 v132, v132, v132
	v_max_f32_e32 v133, v133, v133
	v_max_f32_e32 v134, v134, v134
	v_max_f32_e32 v135, v135, v135
	v_max_f32_e32 v136, v136, v136
	v_max_f32_e32 v137, v137, v137
	v_max_f32_e32 v138, v138, v138
	v_max_f32_e32 v139, v139, v139
	v_max_f32_e32 v140, v140, v140
	v_max_f32_e32 v141, v141, v141
	v_max_f32_e32 v142, v142, v142
	v_max_f32_e32 v143, v143, v143
	v_max_f32_e32 v144, v144, v144
	v_max_f32_e32 v145, v145, v145
	v_max_f32_e32 v146, v146, v146
	v_max_f32_e32 v147, v147, v147
	v_med3_f32 v132, v132, s20, v13
	v_med3_f32 v133, v133, s20, v13
	v_med3_f32 v134, v134, s20, v13
	v_med3_f32 v135, v135, s20, v13
	v_med3_f32 v136, v136, s20, v13
	v_med3_f32 v137, v137, s20, v13
	v_med3_f32 v138, v138, s20, v13
	v_med3_f32 v139, v139, s20, v13
	v_med3_f32 v140, v140, s20, v13
	v_med3_f32 v141, v141, s20, v13
	v_med3_f32 v142, v142, s20, v13
	v_med3_f32 v143, v143, s20, v13
	v_med3_f32 v144, v144, s20, v13
	v_med3_f32 v145, v145, s20, v13
	v_med3_f32 v146, v146, s20, v13
	v_med3_f32 v147, v147, s20, v13
	v_mov_b32_e32 v148, 0
	v_mov_b32_e32 v149, 0
	v_mov_b32_e32 v150, 0
	v_mov_b32_e32 v151, 0
	v_cvt_pk_fp8_f32 v148, v132, v133
	v_cvt_pk_fp8_f32 v149, v136, v137
	v_cvt_pk_fp8_f32 v150, v140, v141
	v_cvt_pk_fp8_f32 v151, v144, v145
	v_cvt_pk_fp8_f32 v148, v134, v135 op_sel:[0,0,1]
	v_cvt_pk_fp8_f32 v149, v138, v139 op_sel:[0,0,1]
	v_cvt_pk_fp8_f32 v150, v142, v143 op_sel:[0,0,1]
	v_cvt_pk_fp8_f32 v151, v146, v147 op_sel:[0,0,1]
	s_nop 0
	global_store_dwordx4 v12, v[148:151], s[14:15]
	s_waitcnt vmcnt(22)
	v_mul_f32_e32 v68, 0x43000000, v68
	v_mul_f32_e32 v69, 0x43000000, v69
	v_mul_f32_e32 v70, 0x43000000, v70
	v_mul_f32_e32 v71, 0x43000000, v71
	ds_write_b128 v5, v[68:71]
	v_mul_f32_e32 v72, 0x43000000, v72
	v_mul_f32_e32 v73, 0x43000000, v73
	v_mul_f32_e32 v74, 0x43000000, v74
	v_mul_f32_e32 v75, 0x43000000, v75
	ds_write_b128 v5, v[72:75] offset:1024
	v_mul_f32_e32 v76, 0x43000000, v76
	v_mul_f32_e32 v77, 0x43000000, v77
	v_mul_f32_e32 v78, 0x43000000, v78
	v_mul_f32_e32 v79, 0x43000000, v79
	ds_write_b128 v5, v[76:79] offset:2048
	v_mul_f32_e32 v80, 0x43000000, v80
	v_mul_f32_e32 v81, 0x43000000, v81
	v_mul_f32_e32 v82, 0x43000000, v82
	v_mul_f32_e32 v83, 0x43000000, v83
	ds_write_b128 v5, v[80:83] offset:3072
	v_mul_f32_e32 v84, 0x43000000, v84
	v_mul_f32_e32 v85, 0x43000000, v85
	v_mul_f32_e32 v86, 0x43000000, v86
	v_mul_f32_e32 v87, 0x43000000, v87
	ds_write_b128 v5, v[84:87] offset:4096
	v_mul_f32_e32 v88, 0x43000000, v88
	v_mul_f32_e32 v89, 0x43000000, v89
	v_mul_f32_e32 v90, 0x43000000, v90
	v_mul_f32_e32 v91, 0x43000000, v91
	ds_write_b128 v5, v[88:91] offset:5120
	v_mul_f32_e32 v92, 0x43000000, v92
	v_mul_f32_e32 v93, 0x43000000, v93
	v_mul_f32_e32 v94, 0x43000000, v94
	v_mul_f32_e32 v95, 0x43000000, v95
	ds_write_b128 v5, v[92:95] offset:6144
	v_mul_f32_e32 v96, 0x43000000, v96
	v_mul_f32_e32 v97, 0x43000000, v97
	v_mul_f32_e32 v98, 0x43000000, v98
	v_mul_f32_e32 v99, 0x43000000, v99
	ds_write_b128 v5, v[96:99] offset:7168
	s_waitcnt lgkmcnt(0)
	s_barrier
; #define GAS __attribute__((address_space(1)))
; #define LAS __attribute__((address_space(3)))
; #define LDS_WAIT() asm volatile("s_waitcnt lgkmcnt(0)" ::: "memory")
; __device__ __forceinline__ unsigned pk4_fp8(float a, float b, float c, float d) {
;     a = fminf(fmaxf(a, -448.f), 448.f); b = fminf(fmaxf(b, -448.f), 448.f); c = fminf(fmaxf(c, -448.f), 448.f); d = fminf(fmaxf(d, -448.f), 448.f);
;     int w = __builtin_amdgcn_cvt_pk_fp8_f32(a, b, 0, false); w = __builtin_amdgcn_cvt_pk_fp8_f32(c, d, w, true); return (unsigned)w; }
;     const int pr = item >> 1, kb = 2 * (pr / nblk) + (item & 1), nb = pr % nblk, k0 = 64 * kb, n0 = 32 * nb;
;     const int nr = n0 + (lane & 31); const int sc = MAP == 1 ? src_col_in(nr) : nr;
;     float v[32];
; #pragma unroll
;     for (int i = 0; i < 32; ++i) v[i] = sc >= 0 ? W[(size_t)(k0 + 2 * i + (lane >> 5)) * Nsrc + sc] : 0.f;
; #pragma unroll
;     for (int i = 0; i < 32; ++i) { const int k = k0 + 2 * i + (lane >> 5); float x = v[i] * wscale; if (KS) x *= (k < ksplit ? ksA[k] : ksB[k - ksplit]); scr[(2 * i + (lane >> 5)) * 33 + (lane & 31)] = x; }
;     LDS_WAIT(); asm volatile("" ::: "memory");
;     const int c = lane & 7;
; #pragma unroll
;     for (int j = 0; j < 4; ++j) { const int n = (lane >> 3) + 8 * j; const LAS float* s = scr + (8 * c) * 33 + n;
;         const unsigned long long o = (unsigned long long)pg8::pk4_fp8(s[0 * 33], s[1 * 33], s[2 * 33], s[3 * 33]) | ((unsigned long long)pg8::pk4_fp8(s[4 * 33], s[5 * 33], s[6 * 33], s[7 * 33]) << 32);
;         *(GAS unsigned long long*)(WT + (size_t)(n0 + n) * K + k0 + 8 * c) = o; }
;     LDS_WAIT(); asm volatile("" ::: "memory");
	s_add_i32 s17, s16, 3264
	s_min_u32 s17, s17, 0xfff
	s_lshr_b32 s18, s17, 5
	s_add_i32 s18, s18, 0
	s_and_b32 s19, s17, 31
	s_lshl_b32 s18, s18, 21
	s_lshl_b32 s19, s19, 9
	s_add_u32 s18, s18, s19
	s_add_u32 s12, s2, s18
	s_addc_u32 s13, s3, 0
	global_load_dwordx4 v[68:71], v10, s[12:13]
	s_add_u32 s12, s12, 0x8000
	s_addc_u32 s13, s13, 0
	global_load_dwordx4 v[72:75], v10, s[12:13]
	s_add_u32 s12, s12, 0x8000
	s_addc_u32 s13, s13, 0
	global_load_dwordx4 v[76:79], v10, s[12:13]
	s_add_u32 s12, s12, 0x8000
	s_addc_u32 s13, s13, 0
	global_load_dwordx4 v[80:83], v10, s[12:13]
	s_add_u32 s12, s12, 0x8000
	s_addc_u32 s13, s13, 0
	global_load_dwordx4 v[84:87], v10, s[12:13]
	s_add_u32 s12, s12, 0x8000
	s_addc_u32 s13, s13, 0
	global_load_dwordx4 v[88:91], v10, s[12:13]
	s_add_u32 s12, s12, 0x8000
	s_addc_u32 s13, s13, 0
	global_load_dwordx4 v[92:95], v10, s[12:13]
	s_add_u32 s12, s12, 0x8000
	s_addc_u32 s13, s13, 0
	global_load_dwordx4 v[96:99], v10, s[12:13]
	s_add_i32 s17, s16, 2976
	s_min_u32 s17, s17, 0xfff
	s_lshr_b32 s18, s17, 5
	s_add_i32 s18, s18, 0
	s_and_b32 s19, s17, 31
	s_lshl_b32 s19, s19, 21
	s_lshl_b32 s18, s18, 7
	s_add_u32 s18, s18, s19
	s_add_u32 s14, s4, s18
	s_addc_u32 s15, s5, 0
	ds_read_b32 v132, v7
	ds_read_b32 v133, v7 offset:512
	ds_read_b32 v134, v7 offset:1024
	ds_read_b32 v135, v7 offset:1536
	ds_read_b32 v136, v7 offset:2048
	ds_read_b32 v137, v7 offset:2560
	ds_read_b32 v138, v7 offset:3072
	ds_read_b32 v139, v7 offset:3584
	ds_read_b32 v140, v7 offset:4096
	ds_read_b32 v141, v7 offset:4608
	ds_read_b32 v142, v7 offset:5120
	ds_read_b32 v143, v7 offset:5632
	ds_read_b32 v144, v7 offset:6144
	ds_read_b32 v145, v7 offset:6656
	ds_read_b32 v146, v7 offset:7168
	ds_read_b32 v147, v7 offset:7680
	s_waitcnt lgkmcnt(0)
	v_max_f32_e32 v132, v132, v132
	v_max_f32_e32 v133, v133, v133
	v_max_f32_e32 v134, v134, v134
	v_max_f32_e32 v135, v135, v135
	v_max_f32_e32 v136, v136, v136
	v_max_f32_e32 v137, v137, v137
	v_max_f32_e32 v138, v138, v138
	v_max_f32_e32 v139, v139, v139
	v_max_f32_e32 v140, v140, v140
	v_max_f32_e32 v141, v141, v141
	v_max_f32_e32 v142, v142, v142
	v_max_f32_e32 v143, v143, v143
	v_max_f32_e32 v144, v144, v144
	v_max_f32_e32 v145, v145, v145
	v_max_f32_e32 v146, v146, v146
	v_max_f32_e32 v147, v147, v147
	v_med3_f32 v132, v132, s20, v13
	v_med3_f32 v133, v133, s20, v13
	v_med3_f32 v134, v134, s20, v13
	v_med3_f32 v135, v135, s20, v13
	v_med3_f32 v136, v136, s20, v13
	v_med3_f32 v137, v137, s20, v13
	v_med3_f32 v138, v138, s20, v13
	v_med3_f32 v139, v139, s20, v13
	v_med3_f32 v140, v140, s20, v13
	v_med3_f32 v141, v141, s20, v13
	v_med3_f32 v142, v142, s20, v13
	v_med3_f32 v143, v143, s20, v13
	v_med3_f32 v144, v144, s20, v13
	v_med3_f32 v145, v145, s20, v13
	v_med3_f32 v146, v146, s20, v13
	v_med3_f32 v147, v147, s20, v13
	v_mov_b32_e32 v148, 0
	v_mov_b32_e32 v149, 0
	v_mov_b32_e32 v150, 0
	v_mov_b32_e32 v151, 0
	v_cvt_pk_fp8_f32 v148, v132, v133
	v_cvt_pk_fp8_f32 v149, v136, v137
	v_cvt_pk_fp8_f32 v150, v140, v141
	v_cvt_pk_fp8_f32 v151, v144, v145
	v_cvt_pk_fp8_f32 v148, v134, v135 op_sel:[0,0,1]
	v_cvt_pk_fp8_f32 v149, v138, v139 op_sel:[0,0,1]
	v_cvt_pk_fp8_f32 v150, v142, v143 op_sel:[0,0,1]
	v_cvt_pk_fp8_f32 v151, v146, v147 op_sel:[0,0,1]
	s_nop 0
	global_store_dwordx4 v11, v[148:151], s[14:15]
	ds_read_b32 v132, v9
	ds_read_b32 v133, v9 offset:512
	ds_read_b32 v134, v9 offset:1024
	ds_read_b32 v135, v9 offset:1536
	ds_read_b32 v136, v9 offset:2048
	ds_read_b32 v137, v9 offset:2560
	ds_read_b32 v138, v9 offset:3072
	ds_read_b32 v139, v9 offset:3584
	ds_read_b32 v140, v9 offset:4096
	ds_read_b32 v141, v9 offset:4608
	ds_read_b32 v142, v9 offset:5120
	ds_read_b32 v143, v9 offset:5632
	ds_read_b32 v144, v9 offset:6144
	ds_read_b32 v145, v9 offset:6656
	ds_read_b32 v146, v9 offset:7168
	ds_read_b32 v147, v9 offset:7680
	s_waitcnt lgkmcnt(0)
	v_max_f32_e32 v132, v132, v132
	v_max_f32_e32 v133, v133, v133
	v_max_f32_e32 v134, v134, v134
	v_max_f32_e32 v135, v135, v135
	v_max_f32_e32 v136, v136, v136
	v_max_f32_e32 v137, v137, v137
	v_max_f32_e32 v138, v138, v138
	v_max_f32_e32 v139, v139, v139
	v_max_f32_e32 v140, v140, v140
	v_max_f32_e32 v141, v141, v141
	v_max_f32_e32 v142, v142, v142
	v_max_f32_e32 v143, v143, v143
	v_max_f32_e32 v144, v144, v144
	v_max_f32_e32 v145, v145, v145
	v_max_f32_e32 v146, v146, v146
	v_max_f32_e32 v147, v147, v147
	v_med3_f32 v132, v132, s20, v13
	v_med3_f32 v133, v133, s20, v13
	v_med3_f32 v134, v134, s20, v13
	v_med3_f32 v135, v135, s20, v13
	v_med3_f32 v136, v136, s20, v13
	v_med3_f32 v137, v137, s20, v13
	v_med3_f32 v138, v138, s20, v13
	v_med3_f32 v139, v139, s20, v13
	v_med3_f32 v140, v140, s20, v13
	v_med3_f32 v141, v141, s20, v13
	v_med3_f32 v142, v142, s20, v13
	v_med3_f32 v143, v143, s20, v13
	v_med3_f32 v144, v144, s20, v13
	v_med3_f32 v145, v145, s20, v13
	v_med3_f32 v146, v146, s20, v13
	v_med3_f32 v147, v147, s20, v13
	v_mov_b32_e32 v148, 0
	v_mov_b32_e32 v149, 0
	v_mov_b32_e32 v150, 0
	v_mov_b32_e32 v151, 0
	v_cvt_pk_fp8_f32 v148, v132, v133
	v_cvt_pk_fp8_f32 v149, v136, v137
	v_cvt_pk_fp8_f32 v150, v140, v141
	v_cvt_pk_fp8_f32 v151, v144, v145
	v_cvt_pk_fp8_f32 v148, v134, v135 op_sel:[0,0,1]
	v_cvt_pk_fp8_f32 v149, v138, v139 op_sel:[0,0,1]
	v_cvt_pk_fp8_f32 v150, v142, v143 op_sel:[0,0,1]
	v_cvt_pk_fp8_f32 v151, v146, v147 op_sel:[0,0,1]
	s_nop 0
	global_store_dwordx4 v12, v[148:151], s[14:15]
	s_waitcnt vmcnt(22)
	v_mul_f32_e32 v100, 0x43000000, v100
	v_mul_f32_e32 v101, 0x43000000, v101
	v_mul_f32_e32 v102, 0x43000000, v102
	v_mul_f32_e32 v103, 0x43000000, v103
	ds_write_b128 v4, v[100:103]
	v_mul_f32_e32 v104, 0x43000000, v104
	v_mul_f32_e32 v105, 0x43000000, v105
	v_mul_f32_e32 v106, 0x43000000, v106
	v_mul_f32_e32 v107, 0x43000000, v107
	ds_write_b128 v4, v[104:107] offset:1024
	v_mul_f32_e32 v108, 0x43000000, v108
	v_mul_f32_e32 v109, 0x43000000, v109
	v_mul_f32_e32 v110, 0x43000000, v110
	v_mul_f32_e32 v111, 0x43000000, v111
	ds_write_b128 v4, v[108:111] offset:2048
	v_mul_f32_e32 v112, 0x43000000, v112
	v_mul_f32_e32 v113, 0x43000000, v113
	v_mul_f32_e32 v114, 0x43000000, v114
	v_mul_f32_e32 v115, 0x43000000, v115
	ds_write_b128 v4, v[112:115] offset:3072
	v_mul_f32_e32 v116, 0x43000000, v116
	v_mul_f32_e32 v117, 0x43000000, v117
	v_mul_f32_e32 v118, 0x43000000, v118
	v_mul_f32_e32 v119, 0x43000000, v119
	ds_write_b128 v4, v[116:119] offset:4096
	v_mul_f32_e32 v120, 0x43000000, v120
	v_mul_f32_e32 v121, 0x43000000, v121
	v_mul_f32_e32 v122, 0x43000000, v122
	v_mul_f32_e32 v123, 0x43000000, v123
	ds_write_b128 v4, v[120:123] offset:5120
	v_mul_f32_e32 v124, 0x43000000, v124
	v_mul_f32_e32 v125, 0x43000000, v125
	v_mul_f32_e32 v126, 0x43000000, v126
	v_mul_f32_e32 v127, 0x43000000, v127
	ds_write_b128 v4, v[124:127] offset:6144
	v_mul_f32_e32 v128, 0x43000000, v128
	v_mul_f32_e32 v129, 0x43000000, v129
	v_mul_f32_e32 v130, 0x43000000, v130
	v_mul_f32_e32 v131, 0x43000000, v131
	ds_write_b128 v4, v[128:131] offset:7168
	s_waitcnt lgkmcnt(0)
	s_barrier
; #define GAS __attribute__((address_space(1)))
; #define LAS __attribute__((address_space(3)))
; #define LDS_WAIT() asm volatile("s_waitcnt lgkmcnt(0)" ::: "memory")
; __device__ __forceinline__ unsigned pk4_fp8(float a, float b, float c, float d) {
;     a = fminf(fmaxf(a, -448.f), 448.f); b = fminf(fmaxf(b, -448.f), 448.f); c = fminf(fmaxf(c, -448.f), 448.f); d = fminf(fmaxf(d, -448.f), 448.f);
;     int w = __builtin_amdgcn_cvt_pk_fp8_f32(a, b, 0, false); w = __builtin_amdgcn_cvt_pk_fp8_f32(c, d, w, true); return (unsigned)w; }
;     const int pr = item >> 1, kb = 2 * (pr / nblk) + (item & 1), nb = pr % nblk, k0 = 64 * kb, n0 = 32 * nb;
;     const int nr = n0 + (lane & 31); const int sc = MAP == 1 ? src_col_in(nr) : nr;
;     float v[32];
; #pragma unroll
;     for (int i = 0; i < 32; ++i) v[i] = sc >= 0 ? W[(size_t)(k0 + 2 * i + (lane >> 5)) * Nsrc + sc] : 0.f;
; #pragma unroll
;     for (int i = 0; i < 32; ++i) { const int k = k0 + 2 * i + (lane >> 5); float x = v[i] * wscale; if (KS) x *= (k < ksplit ? ksA[k] : ksB[k - ksplit]); scr[(2 * i + (lane >> 5)) * 33 + (lane & 31)] = x; }
;     LDS_WAIT(); asm volatile("" ::: "memory");
;     const int c = lane & 7;
; #pragma unroll
;     for (int j = 0; j < 4; ++j) { const int n = (lane >> 3) + 8 * j; const LAS float* s = scr + (8 * c) * 33 + n;
;         const unsigned long long o = (unsigned long long)pg8::pk4_fp8(s[0 * 33], s[1 * 33], s[2 * 33], s[3 * 33]) | ((unsigned long long)pg8::pk4_fp8(s[4 * 33], s[5 * 33], s[6 * 33], s[7 * 33]) << 32);
;         *(GAS unsigned long long*)(WT + (size_t)(n0 + n) * K + k0 + 8 * c) = o; }
;     LDS_WAIT(); asm volatile("" ::: "memory");
	s_add_i32 s17, s16, 3360
	s_min_u32 s17, s17, 0xfff
	s_lshr_b32 s18, s17, 5
	s_add_i32 s18, s18, 0
	s_and_b32 s19, s17, 31
	s_lshl_b32 s18, s18, 21
	s_lshl_b32 s19, s19, 9
	s_add_u32 s18, s18, s19
	s_add_u32 s12, s2, s18
	s_addc_u32 s13, s3, 0
	global_load_dwordx4 v[100:103], v10, s[12:13]
	s_add_u32 s12, s12, 0x8000
	s_addc_u32 s13, s13, 0
	global_load_dwordx4 v[104:107], v10, s[12:13]
	s_add_u32 s12, s12, 0x8000
	s_addc_u32 s13, s13, 0
	global_load_dwordx4 v[108:111], v10, s[12:13]
	s_add_u32 s12, s12, 0x8000
	s_addc_u32 s13, s13, 0
	global_load_dwordx4 v[112:115], v10, s[12:13]
	s_add_u32 s12, s12, 0x8000
	s_addc_u32 s13, s13, 0
	global_load_dwordx4 v[116:119], v10, s[12:13]
	s_add_u32 s12, s12, 0x8000
	s_addc_u32 s13, s13, 0
	global_load_dwordx4 v[120:123], v10, s[12:13]
	s_add_u32 s12, s12, 0x8000
	s_addc_u32 s13, s13, 0
	global_load_dwordx4 v[124:127], v10, s[12:13]
	s_add_u32 s12, s12, 0x8000
	s_addc_u32 s13, s13, 0
	global_load_dwordx4 v[128:131], v10, s[12:13]
	s_add_i32 s17, s16, 3072
	s_min_u32 s17, s17, 0xfff
	s_lshr_b32 s18, s17, 5
	s_add_i32 s18, s18, 0
	s_and_b32 s19, s17, 31
	s_lshl_b32 s19, s19, 21
	s_lshl_b32 s18, s18, 7
	s_add_u32 s18, s18, s19
	s_add_u32 s14, s4, s18
	s_addc_u32 s15, s5, 0
	ds_read_b32 v132, v6
	ds_read_b32 v133, v6 offset:512
	ds_read_b32 v134, v6 offset:1024
	ds_read_b32 v135, v6 offset:1536
	ds_read_b32 v136, v6 offset:2048
	ds_read_b32 v137, v6 offset:2560
	ds_read_b32 v138, v6 offset:3072
	ds_read_b32 v139, v6 offset:3584
	ds_read_b32 v140, v6 offset:4096
	ds_read_b32 v141, v6 offset:4608
	ds_read_b32 v142, v6 offset:5120
	ds_read_b32 v143, v6 offset:5632
	ds_read_b32 v144, v6 offset:6144
	ds_read_b32 v145, v6 offset:6656
	ds_read_b32 v146, v6 offset:7168
	ds_read_b32 v147, v6 offset:7680
	s_waitcnt lgkmcnt(0)
	v_max_f32_e32 v132, v132, v132
	v_max_f32_e32 v133, v133, v133
	v_max_f32_e32 v134, v134, v134
	v_max_f32_e32 v135, v135, v135
	v_max_f32_e32 v136, v136, v136
	v_max_f32_e32 v137, v137, v137
	v_max_f32_e32 v138, v138, v138
	v_max_f32_e32 v139, v139, v139
	v_max_f32_e32 v140, v140, v140
	v_max_f32_e32 v141, v141, v141
	v_max_f32_e32 v142, v142, v142
	v_max_f32_e32 v143, v143, v143
	v_max_f32_e32 v144, v144, v144
	v_max_f32_e32 v145, v145, v145
	v_max_f32_e32 v146, v146, v146
	v_max_f32_e32 v147, v147, v147
	v_med3_f32 v132, v132, s20, v13
	v_med3_f32 v133, v133, s20, v13
	v_med3_f32 v134, v134, s20, v13
	v_med3_f32 v135, v135, s20, v13
	v_med3_f32 v136, v136, s20, v13
	v_med3_f32 v137, v137, s20, v13
	v_med3_f32 v138, v138, s20, v13
	v_med3_f32 v139, v139, s20, v13
	v_med3_f32 v140, v140, s20, v13
	v_med3_f32 v141, v141, s20, v13
	v_med3_f32 v142, v142, s20, v13
	v_med3_f32 v143, v143, s20, v13
	v_med3_f32 v144, v144, s20, v13
	v_med3_f32 v145, v145, s20, v13
	v_med3_f32 v146, v146, s20, v13
	v_med3_f32 v147, v147, s20, v13
	v_mov_b32_e32 v148, 0
	v_mov_b32_e32 v149, 0
	v_mov_b32_e32 v150, 0
	v_mov_b32_e32 v151, 0
	v_cvt_pk_fp8_f32 v148, v132, v133
	v_cvt_pk_fp8_f32 v149, v136, v137
	v_cvt_pk_fp8_f32 v150, v140, v141
	v_cvt_pk_fp8_f32 v151, v144, v145
	v_cvt_pk_fp8_f32 v148, v134, v135 op_sel:[0,0,1]
	v_cvt_pk_fp8_f32 v149, v138, v139 op_sel:[0,0,1]
	v_cvt_pk_fp8_f32 v150, v142, v143 op_sel:[0,0,1]
	v_cvt_pk_fp8_f32 v151, v146, v147 op_sel:[0,0,1]
	s_nop 0
	global_store_dwordx4 v11, v[148:151], s[14:15]
	ds_read_b32 v132, v8
	ds_read_b32 v133, v8 offset:512
	ds_read_b32 v134, v8 offset:1024
	ds_read_b32 v135, v8 offset:1536
	ds_read_b32 v136, v8 offset:2048
	ds_read_b32 v137, v8 offset:2560
	ds_read_b32 v138, v8 offset:3072
	ds_read_b32 v139, v8 offset:3584
	ds_read_b32 v140, v8 offset:4096
	ds_read_b32 v141, v8 offset:4608
	ds_read_b32 v142, v8 offset:5120
	ds_read_b32 v143, v8 offset:5632
	ds_read_b32 v144, v8 offset:6144
	ds_read_b32 v145, v8 offset:6656
	ds_read_b32 v146, v8 offset:7168
	ds_read_b32 v147, v8 offset:7680
	s_waitcnt lgkmcnt(0)
	v_max_f32_e32 v132, v132, v132
	v_max_f32_e32 v133, v133, v133
	v_max_f32_e32 v134, v134, v134
	v_max_f32_e32 v135, v135, v135
	v_max_f32_e32 v136, v136, v136
	v_max_f32_e32 v137, v137, v137
	v_max_f32_e32 v138, v138, v138
	v_max_f32_e32 v139, v139, v139
	v_max_f32_e32 v140, v140, v140
	v_max_f32_e32 v141, v141, v141
	v_max_f32_e32 v142, v142, v142
	v_max_f32_e32 v143, v143, v143
	v_max_f32_e32 v144, v144, v144
	v_max_f32_e32 v145, v145, v145
	v_max_f32_e32 v146, v146, v146
	v_max_f32_e32 v147, v147, v147
	v_med3_f32 v132, v132, s20, v13
	v_med3_f32 v133, v133, s20, v13
	v_med3_f32 v134, v134, s20, v13
	v_med3_f32 v135, v135, s20, v13
	v_med3_f32 v136, v136, s20, v13
	v_med3_f32 v137, v137, s20, v13
	v_med3_f32 v138, v138, s20, v13
	v_med3_f32 v139, v139, s20, v13
	v_med3_f32 v140, v140, s20, v13
	v_med3_f32 v141, v141, s20, v13
	v_med3_f32 v142, v142, s20, v13
	v_med3_f32 v143, v143, s20, v13
	v_med3_f32 v144, v144, s20, v13
	v_med3_f32 v145, v145, s20, v13
	v_med3_f32 v146, v146, s20, v13
	v_med3_f32 v147, v147, s20, v13
	v_mov_b32_e32 v148, 0
	v_mov_b32_e32 v149, 0
	v_mov_b32_e32 v150, 0
	v_mov_b32_e32 v151, 0
	v_cvt_pk_fp8_f32 v148, v132, v133
	v_cvt_pk_fp8_f32 v149, v136, v137
	v_cvt_pk_fp8_f32 v150, v140, v141
	v_cvt_pk_fp8_f32 v151, v144, v145
	v_cvt_pk_fp8_f32 v148, v134, v135 op_sel:[0,0,1]
	v_cvt_pk_fp8_f32 v149, v138, v139 op_sel:[0,0,1]
	v_cvt_pk_fp8_f32 v150, v142, v143 op_sel:[0,0,1]
	v_cvt_pk_fp8_f32 v151, v146, v147 op_sel:[0,0,1]
	s_nop 0
	global_store_dwordx4 v12, v[148:151], s[14:15]
	s_waitcnt vmcnt(22)
	v_mul_f32_e32 v36, 0x43000000, v36
	v_mul_f32_e32 v37, 0x43000000, v37
	v_mul_f32_e32 v38, 0x43000000, v38
	v_mul_f32_e32 v39, 0x43000000, v39
	ds_write_b128 v5, v[36:39]
	v_mul_f32_e32 v40, 0x43000000, v40
	v_mul_f32_e32 v41, 0x43000000, v41
	v_mul_f32_e32 v42, 0x43000000, v42
	v_mul_f32_e32 v43, 0x43000000, v43
	ds_write_b128 v5, v[40:43] offset:1024
	v_mul_f32_e32 v44, 0x43000000, v44
	v_mul_f32_e32 v45, 0x43000000, v45
	v_mul_f32_e32 v46, 0x43000000, v46
	v_mul_f32_e32 v47, 0x43000000, v47
	ds_write_b128 v5, v[44:47] offset:2048
	v_mul_f32_e32 v48, 0x43000000, v48
	v_mul_f32_e32 v49, 0x43000000, v49
	v_mul_f32_e32 v50, 0x43000000, v50
	v_mul_f32_e32 v51, 0x43000000, v51
	ds_write_b128 v5, v[48:51] offset:3072
	v_mul_f32_e32 v52, 0x43000000, v52
	v_mul_f32_e32 v53, 0x43000000, v53
	v_mul_f32_e32 v54, 0x43000000, v54
	v_mul_f32_e32 v55, 0x43000000, v55
	ds_write_b128 v5, v[52:55] offset:4096
	v_mul_f32_e32 v56, 0x43000000, v56
	v_mul_f32_e32 v57, 0x43000000, v57
	v_mul_f32_e32 v58, 0x43000000, v58
	v_mul_f32_e32 v59, 0x43000000, v59
	ds_write_b128 v5, v[56:59] offset:5120
	v_mul_f32_e32 v60, 0x43000000, v60
	v_mul_f32_e32 v61, 0x43000000, v61
	v_mul_f32_e32 v62, 0x43000000, v62
	v_mul_f32_e32 v63, 0x43000000, v63
	ds_write_b128 v5, v[60:63] offset:6144
	v_mul_f32_e32 v64, 0x43000000, v64
	v_mul_f32_e32 v65, 0x43000000, v65
	v_mul_f32_e32 v66, 0x43000000, v66
	v_mul_f32_e32 v67, 0x43000000, v67
	ds_write_b128 v5, v[64:67] offset:7168
	s_waitcnt lgkmcnt(0)
	s_barrier
; #define GAS __attribute__((address_space(1)))
; #define LAS __attribute__((address_space(3)))
; #define LDS_WAIT() asm volatile("s_waitcnt lgkmcnt(0)" ::: "memory")
; __device__ __forceinline__ unsigned pk4_fp8(float a, float b, float c, float d) {
;     a = fminf(fmaxf(a, -448.f), 448.f); b = fminf(fmaxf(b, -448.f), 448.f); c = fminf(fmaxf(c, -448.f), 448.f); d = fminf(fmaxf(d, -448.f), 448.f);
;     int w = __builtin_amdgcn_cvt_pk_fp8_f32(a, b, 0, false); w = __builtin_amdgcn_cvt_pk_fp8_f32(c, d, w, true); return (unsigned)w; }
;     const int pr = item >> 1, kb = 2 * (pr / nblk) + (item & 1), nb = pr % nblk, k0 = 64 * kb, n0 = 32 * nb;
;     const int nr = n0 + (lane & 31); const int sc = MAP == 1 ? src_col_in(nr) : nr;
;     float v[32];
; #pragma unroll
;     for (int i = 0; i < 32; ++i) v[i] = sc >= 0 ? W[(size_t)(k0 + 2 * i + (lane >> 5)) * Nsrc + sc] : 0.f;
; #pragma unroll
;     for (int i = 0; i < 32; ++i) { const int k = k0 + 2 * i + (lane >> 5); float x = v[i] * wscale; if (KS) x *= (k < ksplit ? ksA[k] : ksB[k - ksplit]); scr[(2 * i + (lane >> 5)) * 33 + (lane & 31)] = x; }
;     LDS_WAIT(); asm volatile("" ::: "memory");
;     const int c = lane & 7;
; #pragma unroll
;     for (int j = 0; j < 4; ++j) { const int n = (lane >> 3) + 8 * j; const LAS float* s = scr + (8 * c) * 33 + n;
;         const unsigned long long o = (unsigned long long)pg8::pk4_fp8(s[0 * 33], s[1 * 33], s[2 * 33], s[3 * 33]) | ((unsigned long long)pg8::pk4_fp8(s[4 * 33], s[5 * 33], s[6 * 33], s[7 * 33]) << 32);
;         *(GAS unsigned long long*)(WT + (size_t)(n0 + n) * K + k0 + 8 * c) = o; }
;     LDS_WAIT(); asm volatile("" ::: "memory");
	s_add_i32 s17, s16, 3456
	s_min_u32 s17, s17, 0xfff
	s_lshr_b32 s18, s17, 5
	s_add_i32 s18, s18, 0
	s_and_b32 s19, s17, 31
	s_lshl_b32 s18, s18, 21
	s_lshl_b32 s19, s19, 9
	s_add_u32 s18, s18, s19
	s_add_u32 s12, s2, s18
	s_addc_u32 s13, s3, 0
	global_load_dwordx4 v[36:39], v10, s[12:13]
	s_add_u32 s12, s12, 0x8000
	s_addc_u32 s13, s13, 0
	global_load_dwordx4 v[40:43], v10, s[12:13]
	s_add_u32 s12, s12, 0x8000
	s_addc_u32 s13, s13, 0
	global_load_dwordx4 v[44:47], v10, s[12:13]
	s_add_u32 s12, s12, 0x8000
	s_addc_u32 s13, s13, 0
	global_load_dwordx4 v[48:51], v10, s[12:13]
	s_add_u32 s12, s12, 0x8000
	s_addc_u32 s13, s13, 0
	global_load_dwordx4 v[52:55], v10, s[12:13]
	s_add_u32 s12, s12, 0x8000
	s_addc_u32 s13, s13, 0
	global_load_dwordx4 v[56:59], v10, s[12:13]
	s_add_u32 s12, s12, 0x8000
	s_addc_u32 s13, s13, 0
	global_load_dwordx4 v[60:63], v10, s[12:13]
	s_add_u32 s12, s12, 0x8000
	s_addc_u32 s13, s13, 0
	global_load_dwordx4 v[64:67], v10, s[12:13]
	s_add_i32 s17, s16, 3168
	s_min_u32 s17, s17, 0xfff
	s_lshr_b32 s18, s17, 5
	s_add_i32 s18, s18, 0
	s_and_b32 s19, s17, 31
	s_lshl_b32 s19, s19, 21
	s_lshl_b32 s18, s18, 7
	s_add_u32 s18, s18, s19
	s_add_u32 s14, s4, s18
	s_addc_u32 s15, s5, 0
	ds_read_b32 v132, v7
	ds_read_b32 v133, v7 offset:512
	ds_read_b32 v134, v7 offset:1024
	ds_read_b32 v135, v7 offset:1536
	ds_read_b32 v136, v7 offset:2048
	ds_read_b32 v137, v7 offset:2560
	ds_read_b32 v138, v7 offset:3072
	ds_read_b32 v139, v7 offset:3584
	ds_read_b32 v140, v7 offset:4096
	ds_read_b32 v141, v7 offset:4608
	ds_read_b32 v142, v7 offset:5120
	ds_read_b32 v143, v7 offset:5632
	ds_read_b32 v144, v7 offset:6144
	ds_read_b32 v145, v7 offset:6656
	ds_read_b32 v146, v7 offset:7168
	ds_read_b32 v147, v7 offset:7680
	s_waitcnt lgkmcnt(0)
	v_max_f32_e32 v132, v132, v132
	v_max_f32_e32 v133, v133, v133
	v_max_f32_e32 v134, v134, v134
	v_max_f32_e32 v135, v135, v135
	v_max_f32_e32 v136, v136, v136
	v_max_f32_e32 v137, v137, v137
	v_max_f32_e32 v138, v138, v138
	v_max_f32_e32 v139, v139, v139
	v_max_f32_e32 v140, v140, v140
	v_max_f32_e32 v141, v141, v141
	v_max_f32_e32 v142, v142, v142
	v_max_f32_e32 v143, v143, v143
	v_max_f32_e32 v144, v144, v144
	v_max_f32_e32 v145, v145, v145
	v_max_f32_e32 v146, v146, v146
	v_max_f32_e32 v147, v147, v147
	v_med3_f32 v132, v132, s20, v13
	v_med3_f32 v133, v133, s20, v13
	v_med3_f32 v134, v134, s20, v13
	v_med3_f32 v135, v135, s20, v13
	v_med3_f32 v136, v136, s20, v13
	v_med3_f32 v137, v137, s20, v13
	v_med3_f32 v138, v138, s20, v13
	v_med3_f32 v139, v139, s20, v13
	v_med3_f32 v140, v140, s20, v13
	v_med3_f32 v141, v141, s20, v13
	v_med3_f32 v142, v142, s20, v13
	v_med3_f32 v143, v143, s20, v13
	v_med3_f32 v144, v144, s20, v13
	v_med3_f32 v145, v145, s20, v13
	v_med3_f32 v146, v146, s20, v13
	v_med3_f32 v147, v147, s20, v13
	v_mov_b32_e32 v148, 0
	v_mov_b32_e32 v149, 0
	v_mov_b32_e32 v150, 0
	v_mov_b32_e32 v151, 0
	v_cvt_pk_fp8_f32 v148, v132, v133
	v_cvt_pk_fp8_f32 v149, v136, v137
	v_cvt_pk_fp8_f32 v150, v140, v141
	v_cvt_pk_fp8_f32 v151, v144, v145
	v_cvt_pk_fp8_f32 v148, v134, v135 op_sel:[0,0,1]
	v_cvt_pk_fp8_f32 v149, v138, v139 op_sel:[0,0,1]
	v_cvt_pk_fp8_f32 v150, v142, v143 op_sel:[0,0,1]
	v_cvt_pk_fp8_f32 v151, v146, v147 op_sel:[0,0,1]
	s_nop 0
	global_store_dwordx4 v11, v[148:151], s[14:15]
	ds_read_b32 v132, v9
	ds_read_b32 v133, v9 offset:512
	ds_read_b32 v134, v9 offset:1024
	ds_read_b32 v135, v9 offset:1536
	ds_read_b32 v136, v9 offset:2048
	ds_read_b32 v137, v9 offset:2560
	ds_read_b32 v138, v9 offset:3072
	ds_read_b32 v139, v9 offset:3584
	ds_read_b32 v140, v9 offset:4096
	ds_read_b32 v141, v9 offset:4608
	ds_read_b32 v142, v9 offset:5120
	ds_read_b32 v143, v9 offset:5632
	ds_read_b32 v144, v9 offset:6144
	ds_read_b32 v145, v9 offset:6656
	ds_read_b32 v146, v9 offset:7168
	ds_read_b32 v147, v9 offset:7680
	s_waitcnt lgkmcnt(0)
	v_max_f32_e32 v132, v132, v132
	v_max_f32_e32 v133, v133, v133
	v_max_f32_e32 v134, v134, v134
	v_max_f32_e32 v135, v135, v135
	v_max_f32_e32 v136, v136, v136
	v_max_f32_e32 v137, v137, v137
	v_max_f32_e32 v138, v138, v138
	v_max_f32_e32 v139, v139, v139
	v_max_f32_e32 v140, v140, v140
	v_max_f32_e32 v141, v141, v141
	v_max_f32_e32 v142, v142, v142
	v_max_f32_e32 v143, v143, v143
	v_max_f32_e32 v144, v144, v144
	v_max_f32_e32 v145, v145, v145
	v_max_f32_e32 v146, v146, v146
	v_max_f32_e32 v147, v147, v147
	v_med3_f32 v132, v132, s20, v13
	v_med3_f32 v133, v133, s20, v13
	v_med3_f32 v134, v134, s20, v13
	v_med3_f32 v135, v135, s20, v13
	v_med3_f32 v136, v136, s20, v13
	v_med3_f32 v137, v137, s20, v13
	v_med3_f32 v138, v138, s20, v13
	v_med3_f32 v139, v139, s20, v13
	v_med3_f32 v140, v140, s20, v13
	v_med3_f32 v141, v141, s20, v13
	v_med3_f32 v142, v142, s20, v13
	v_med3_f32 v143, v143, s20, v13
	v_med3_f32 v144, v144, s20, v13
	v_med3_f32 v145, v145, s20, v13
	v_med3_f32 v146, v146, s20, v13
	v_med3_f32 v147, v147, s20, v13
	v_mov_b32_e32 v148, 0
	v_mov_b32_e32 v149, 0
	v_mov_b32_e32 v150, 0
	v_mov_b32_e32 v151, 0
	v_cvt_pk_fp8_f32 v148, v132, v133
	v_cvt_pk_fp8_f32 v149, v136, v137
	v_cvt_pk_fp8_f32 v150, v140, v141
	v_cvt_pk_fp8_f32 v151, v144, v145
	v_cvt_pk_fp8_f32 v148, v134, v135 op_sel:[0,0,1]
	v_cvt_pk_fp8_f32 v149, v138, v139 op_sel:[0,0,1]
	v_cvt_pk_fp8_f32 v150, v142, v143 op_sel:[0,0,1]
	v_cvt_pk_fp8_f32 v151, v146, v147 op_sel:[0,0,1]
	s_nop 0
	global_store_dwordx4 v12, v[148:151], s[14:15]
	s_waitcnt vmcnt(22)
	v_mul_f32_e32 v68, 0x43000000, v68
	v_mul_f32_e32 v69, 0x43000000, v69
	v_mul_f32_e32 v70, 0x43000000, v70
	v_mul_f32_e32 v71, 0x43000000, v71
	ds_write_b128 v4, v[68:71]
	v_mul_f32_e32 v72, 0x43000000, v72
	v_mul_f32_e32 v73, 0x43000000, v73
	v_mul_f32_e32 v74, 0x43000000, v74
	v_mul_f32_e32 v75, 0x43000000, v75
	ds_write_b128 v4, v[72:75] offset:1024
	v_mul_f32_e32 v76, 0x43000000, v76
	v_mul_f32_e32 v77, 0x43000000, v77
	v_mul_f32_e32 v78, 0x43000000, v78
	v_mul_f32_e32 v79, 0x43000000, v79
	ds_write_b128 v4, v[76:79] offset:2048
	v_mul_f32_e32 v80, 0x43000000, v80
	v_mul_f32_e32 v81, 0x43000000, v81
	v_mul_f32_e32 v82, 0x43000000, v82
	v_mul_f32_e32 v83, 0x43000000, v83
	ds_write_b128 v4, v[80:83] offset:3072
	v_mul_f32_e32 v84, 0x43000000, v84
	v_mul_f32_e32 v85, 0x43000000, v85
	v_mul_f32_e32 v86, 0x43000000, v86
	v_mul_f32_e32 v87, 0x43000000, v87
	ds_write_b128 v4, v[84:87] offset:4096
	v_mul_f32_e32 v88, 0x43000000, v88
	v_mul_f32_e32 v89, 0x43000000, v89
	v_mul_f32_e32 v90, 0x43000000, v90
	v_mul_f32_e32 v91, 0x43000000, v91
	ds_write_b128 v4, v[88:91] offset:5120
	v_mul_f32_e32 v92, 0x43000000, v92
	v_mul_f32_e32 v93, 0x43000000, v93
	v_mul_f32_e32 v94, 0x43000000, v94
	v_mul_f32_e32 v95, 0x43000000, v95
	ds_write_b128 v4, v[92:95] offset:6144
	v_mul_f32_e32 v96, 0x43000000, v96
	v_mul_f32_e32 v97, 0x43000000, v97
	v_mul_f32_e32 v98, 0x43000000, v98
	v_mul_f32_e32 v99, 0x43000000, v99
	ds_write_b128 v4, v[96:99] offset:7168
	s_waitcnt lgkmcnt(0)
	s_barrier
; #define GAS __attribute__((address_space(1)))
; #define LAS __attribute__((address_space(3)))
; #define LDS_WAIT() asm volatile("s_waitcnt lgkmcnt(0)" ::: "memory")
; __device__ __forceinline__ unsigned pk4_fp8(float a, float b, float c, float d) {
;     a = fminf(fmaxf(a, -448.f), 448.f); b = fminf(fmaxf(b, -448.f), 448.f); c = fminf(fmaxf(c, -448.f), 448.f); d = fminf(fmaxf(d, -448.f), 448.f);
;     int w = __builtin_amdgcn_cvt_pk_fp8_f32(a, b, 0, false); w = __builtin_amdgcn_cvt_pk_fp8_f32(c, d, w, true); return (unsigned)w; }
;     const int pr = item >> 1, kb = 2 * (pr / nblk) + (item & 1), nb = pr % nblk, k0 = 64 * kb, n0 = 32 * nb;
;     const int nr = n0 + (lane & 31); const int sc = MAP == 1 ? src_col_in(nr) : nr;
;     float v[32];
; #pragma unroll
;     for (int i = 0; i < 32; ++i) v[i] = sc >= 0 ? W[(size_t)(k0 + 2 * i + (lane >> 5)) * Nsrc + sc] : 0.f;
; #pragma unroll
;     for (int i = 0; i < 32; ++i) { const int k = k0 + 2 * i + (lane >> 5); float x = v[i] * wscale; if (KS) x *= (k < ksplit ? ksA[k] : ksB[k - ksplit]); scr[(2 * i + (lane >> 5)) * 33 + (lane & 31)] = x; }
;     LDS_WAIT(); asm volatile("" ::: "memory");
;     const int c = lane & 7;
; #pragma unroll
;     for (int j = 0; j < 4; ++j) { const int n = (lane >> 3) + 8 * j; const LAS float* s = scr + (8 * c) * 33 + n;
;         const unsigned long long o = (unsigned long long)pg8::pk4_fp8(s[0 * 33], s[1 * 33], s[2 * 33], s[3 * 33]) | ((unsigned long long)pg8::pk4_fp8(s[4 * 33], s[5 * 33], s[6 * 33], s[7 * 33]) << 32);
;         *(GAS unsigned long long*)(WT + (size_t)(n0 + n) * K + k0 + 8 * c) = o; }
;     LDS_WAIT(); asm volatile("" ::: "memory");
	s_add_i32 s17, s16, 3552
	s_min_u32 s17, s17, 0xfff
	s_lshr_b32 s18, s17, 5
	s_add_i32 s18, s18, 0
	s_and_b32 s19, s17, 31
	s_lshl_b32 s18, s18, 21
	s_lshl_b32 s19, s19, 9
	s_add_u32 s18, s18, s19
	s_add_u32 s12, s2, s18
	s_addc_u32 s13, s3, 0
	global_load_dwordx4 v[68:71], v10, s[12:13]
	s_add_u32 s12, s12, 0x8000
	s_addc_u32 s13, s13, 0
	global_load_dwordx4 v[72:75], v10, s[12:13]
	s_add_u32 s12, s12, 0x8000
	s_addc_u32 s13, s13, 0
	global_load_dwordx4 v[76:79], v10, s[12:13]
	s_add_u32 s12, s12, 0x8000
	s_addc_u32 s13, s13, 0
	global_load_dwordx4 v[80:83], v10, s[12:13]
	s_add_u32 s12, s12, 0x8000
	s_addc_u32 s13, s13, 0
	global_load_dwordx4 v[84:87], v10, s[12:13]
	s_add_u32 s12, s12, 0x8000
	s_addc_u32 s13, s13, 0
	global_load_dwordx4 v[88:91], v10, s[12:13]
	s_add_u32 s12, s12, 0x8000
	s_addc_u32 s13, s13, 0
	global_load_dwordx4 v[92:95], v10, s[12:13]
	s_add_u32 s12, s12, 0x8000
	s_addc_u32 s13, s13, 0
	global_load_dwordx4 v[96:99], v10, s[12:13]
	s_add_i32 s17, s16, 3264
	s_min_u32 s17, s17, 0xfff
	s_lshr_b32 s18, s17, 5
	s_add_i32 s18, s18, 0
	s_and_b32 s19, s17, 31
	s_lshl_b32 s19, s19, 21
	s_lshl_b32 s18, s18, 7
	s_add_u32 s18, s18, s19
	s_add_u32 s14, s4, s18
	s_addc_u32 s15, s5, 0
	ds_read_b32 v132, v6
	ds_read_b32 v133, v6 offset:512
	ds_read_b32 v134, v6 offset:1024
	ds_read_b32 v135, v6 offset:1536
	ds_read_b32 v136, v6 offset:2048
	ds_read_b32 v137, v6 offset:2560
	ds_read_b32 v138, v6 offset:3072
	ds_read_b32 v139, v6 offset:3584
	ds_read_b32 v140, v6 offset:4096
	ds_read_b32 v141, v6 offset:4608
	ds_read_b32 v142, v6 offset:5120
	ds_read_b32 v143, v6 offset:5632
	ds_read_b32 v144, v6 offset:6144
	ds_read_b32 v145, v6 offset:6656
	ds_read_b32 v146, v6 offset:7168
	ds_read_b32 v147, v6 offset:7680
	s_waitcnt lgkmcnt(0)
	v_max_f32_e32 v132, v132, v132
	v_max_f32_e32 v133, v133, v133
	v_max_f32_e32 v134, v134, v134
	v_max_f32_e32 v135, v135, v135
	v_max_f32_e32 v136, v136, v136
	v_max_f32_e32 v137, v137, v137
	v_max_f32_e32 v138, v138, v138
	v_max_f32_e32 v139, v139, v139
	v_max_f32_e32 v140, v140, v140
	v_max_f32_e32 v141, v141, v141
	v_max_f32_e32 v142, v142, v142
	v_max_f32_e32 v143, v143, v143
	v_max_f32_e32 v144, v144, v144
	v_max_f32_e32 v145, v145, v145
	v_max_f32_e32 v146, v146, v146
	v_max_f32_e32 v147, v147, v147
	v_med3_f32 v132, v132, s20, v13
	v_med3_f32 v133, v133, s20, v13
	v_med3_f32 v134, v134, s20, v13
	v_med3_f32 v135, v135, s20, v13
	v_med3_f32 v136, v136, s20, v13
	v_med3_f32 v137, v137, s20, v13
	v_med3_f32 v138, v138, s20, v13
	v_med3_f32 v139, v139, s20, v13
	v_med3_f32 v140, v140, s20, v13
	v_med3_f32 v141, v141, s20, v13
	v_med3_f32 v142, v142, s20, v13
	v_med3_f32 v143, v143, s20, v13
	v_med3_f32 v144, v144, s20, v13
	v_med3_f32 v145, v145, s20, v13
	v_med3_f32 v146, v146, s20, v13
	v_med3_f32 v147, v147, s20, v13
	v_mov_b32_e32 v148, 0
	v_mov_b32_e32 v149, 0
	v_mov_b32_e32 v150, 0
	v_mov_b32_e32 v151, 0
	v_cvt_pk_fp8_f32 v148, v132, v133
	v_cvt_pk_fp8_f32 v149, v136, v137
	v_cvt_pk_fp8_f32 v150, v140, v141
	v_cvt_pk_fp8_f32 v151, v144, v145
	v_cvt_pk_fp8_f32 v148, v134, v135 op_sel:[0,0,1]
	v_cvt_pk_fp8_f32 v149, v138, v139 op_sel:[0,0,1]
	v_cvt_pk_fp8_f32 v150, v142, v143 op_sel:[0,0,1]
	v_cvt_pk_fp8_f32 v151, v146, v147 op_sel:[0,0,1]
	s_nop 0
	global_store_dwordx4 v11, v[148:151], s[14:15]
	ds_read_b32 v132, v8
	ds_read_b32 v133, v8 offset:512
	ds_read_b32 v134, v8 offset:1024
	ds_read_b32 v135, v8 offset:1536
	ds_read_b32 v136, v8 offset:2048
	ds_read_b32 v137, v8 offset:2560
	ds_read_b32 v138, v8 offset:3072
	ds_read_b32 v139, v8 offset:3584
	ds_read_b32 v140, v8 offset:4096
	ds_read_b32 v141, v8 offset:4608
	ds_read_b32 v142, v8 offset:5120
	ds_read_b32 v143, v8 offset:5632
	ds_read_b32 v144, v8 offset:6144
	ds_read_b32 v145, v8 offset:6656
	ds_read_b32 v146, v8 offset:7168
	ds_read_b32 v147, v8 offset:7680
	s_waitcnt lgkmcnt(0)
	v_max_f32_e32 v132, v132, v132
	v_max_f32_e32 v133, v133, v133
	v_max_f32_e32 v134, v134, v134
	v_max_f32_e32 v135, v135, v135
	v_max_f32_e32 v136, v136, v136
	v_max_f32_e32 v137, v137, v137
	v_max_f32_e32 v138, v138, v138
	v_max_f32_e32 v139, v139, v139
	v_max_f32_e32 v140, v140, v140
	v_max_f32_e32 v141, v141, v141
	v_max_f32_e32 v142, v142, v142
	v_max_f32_e32 v143, v143, v143
	v_max_f32_e32 v144, v144, v144
	v_max_f32_e32 v145, v145, v145
	v_max_f32_e32 v146, v146, v146
	v_max_f32_e32 v147, v147, v147
	v_med3_f32 v132, v132, s20, v13
	v_med3_f32 v133, v133, s20, v13
	v_med3_f32 v134, v134, s20, v13
	v_med3_f32 v135, v135, s20, v13
	v_med3_f32 v136, v136, s20, v13
	v_med3_f32 v137, v137, s20, v13
	v_med3_f32 v138, v138, s20, v13
	v_med3_f32 v139, v139, s20, v13
	v_med3_f32 v140, v140, s20, v13
	v_med3_f32 v141, v141, s20, v13
	v_med3_f32 v142, v142, s20, v13
	v_med3_f32 v143, v143, s20, v13
	v_med3_f32 v144, v144, s20, v13
	v_med3_f32 v145, v145, s20, v13
	v_med3_f32 v146, v146, s20, v13
	v_med3_f32 v147, v147, s20, v13
	v_mov_b32_e32 v148, 0
	v_mov_b32_e32 v149, 0
	v_mov_b32_e32 v150, 0
	v_mov_b32_e32 v151, 0
	v_cvt_pk_fp8_f32 v148, v132, v133
	v_cvt_pk_fp8_f32 v149, v136, v137
	v_cvt_pk_fp8_f32 v150, v140, v141
	v_cvt_pk_fp8_f32 v151, v144, v145
	v_cvt_pk_fp8_f32 v148, v134, v135 op_sel:[0,0,1]
	v_cvt_pk_fp8_f32 v149, v138, v139 op_sel:[0,0,1]
	v_cvt_pk_fp8_f32 v150, v142, v143 op_sel:[0,0,1]
	v_cvt_pk_fp8_f32 v151, v146, v147 op_sel:[0,0,1]
	s_nop 0
	global_store_dwordx4 v12, v[148:151], s[14:15]
	s_waitcnt vmcnt(22)
	v_mul_f32_e32 v100, 0x43000000, v100
	v_mul_f32_e32 v101, 0x43000000, v101
	v_mul_f32_e32 v102, 0x43000000, v102
	v_mul_f32_e32 v103, 0x43000000, v103
	ds_write_b128 v5, v[100:103]
	v_mul_f32_e32 v104, 0x43000000, v104
	v_mul_f32_e32 v105, 0x43000000, v105
	v_mul_f32_e32 v106, 0x43000000, v106
	v_mul_f32_e32 v107, 0x43000000, v107
	ds_write_b128 v5, v[104:107] offset:1024
	v_mul_f32_e32 v108, 0x43000000, v108
	v_mul_f32_e32 v109, 0x43000000, v109
	v_mul_f32_e32 v110, 0x43000000, v110
	v_mul_f32_e32 v111, 0x43000000, v111
	ds_write_b128 v5, v[108:111] offset:2048
	v_mul_f32_e32 v112, 0x43000000, v112
	v_mul_f32_e32 v113, 0x43000000, v113
	v_mul_f32_e32 v114, 0x43000000, v114
	v_mul_f32_e32 v115, 0x43000000, v115
	ds_write_b128 v5, v[112:115] offset:3072
	v_mul_f32_e32 v116, 0x43000000, v116
	v_mul_f32_e32 v117, 0x43000000, v117
	v_mul_f32_e32 v118, 0x43000000, v118
	v_mul_f32_e32 v119, 0x43000000, v119
	ds_write_b128 v5, v[116:119] offset:4096
	v_mul_f32_e32 v120, 0x43000000, v120
	v_mul_f32_e32 v121, 0x43000000, v121
	v_mul_f32_e32 v122, 0x43000000, v122
	v_mul_f32_e32 v123, 0x43000000, v123
	ds_write_b128 v5, v[120:123] offset:5120
	v_mul_f32_e32 v124, 0x43000000, v124
	v_mul_f32_e32 v125, 0x43000000, v125
	v_mul_f32_e32 v126, 0x43000000, v126
	v_mul_f32_e32 v127, 0x43000000, v127
	ds_write_b128 v5, v[124:127] offset:6144
	v_mul_f32_e32 v128, 0x43000000, v128
	v_mul_f32_e32 v129, 0x43000000, v129
	v_mul_f32_e32 v130, 0x43000000, v130
	v_mul_f32_e32 v131, 0x43000000, v131
	ds_write_b128 v5, v[128:131] offset:7168
	s_waitcnt lgkmcnt(0)
	s_barrier
; #define GAS __attribute__((address_space(1)))
; #define LAS __attribute__((address_space(3)))
; #define LDS_WAIT() asm volatile("s_waitcnt lgkmcnt(0)" ::: "memory")
; __device__ __forceinline__ unsigned pk4_fp8(float a, float b, float c, float d) {
;     a = fminf(fmaxf(a, -448.f), 448.f); b = fminf(fmaxf(b, -448.f), 448.f); c = fminf(fmaxf(c, -448.f), 448.f); d = fminf(fmaxf(d, -448.f), 448.f);
;     int w = __builtin_amdgcn_cvt_pk_fp8_f32(a, b, 0, false); w = __builtin_amdgcn_cvt_pk_fp8_f32(c, d, w, true); return (unsigned)w; }
;     const int pr = item >> 1, kb = 2 * (pr / nblk) + (item & 1), nb = pr % nblk, k0 = 64 * kb, n0 = 32 * nb;
;     const int nr = n0 + (lane & 31); const int sc = MAP == 1 ? src_col_in(nr) : nr;
;     float v[32];
; #pragma unroll
;     for (int i = 0; i < 32; ++i) v[i] = sc >= 0 ? W[(size_t)(k0 + 2 * i + (lane >> 5)) * Nsrc + sc] : 0.f;
; #pragma unroll
;     for (int i = 0; i < 32; ++i) { const int k = k0 + 2 * i + (lane >> 5); float x = v[i] * wscale; if (KS) x *= (k < ksplit ? ksA[k] : ksB[k - ksplit]); scr[(2 * i + (lane >> 5)) * 33 + (lane & 31)] = x; }
;     LDS_WAIT(); asm volatile("" ::: "memory");
;     const int c = lane & 7;
; #pragma unroll
;     for (int j = 0; j < 4; ++j) { const int n = (lane >> 3) + 8 * j; const LAS float* s = scr + (8 * c) * 33 + n;
;         const unsigned long long o = (unsigned long long)pg8::pk4_fp8(s[0 * 33], s[1 * 33], s[2 * 33], s[3 * 33]) | ((unsigned long long)pg8::pk4_fp8(s[4 * 33], s[5 * 33], s[6 * 33], s[7 * 33]) << 32);
;         *(GAS unsigned long long*)(WT + (size_t)(n0 + n) * K + k0 + 8 * c) = o; }
;     LDS_WAIT(); asm volatile("" ::: "memory");
	s_add_i32 s17, s16, 3648
	s_min_u32 s17, s17, 0xfff
	s_lshr_b32 s18, s17, 5
	s_add_i32 s18, s18, 0
	s_and_b32 s19, s17, 31
	s_lshl_b32 s18, s18, 21
	s_lshl_b32 s19, s19, 9
	s_add_u32 s18, s18, s19
	s_add_u32 s12, s2, s18
	s_addc_u32 s13, s3, 0
	global_load_dwordx4 v[100:103], v10, s[12:13]
	s_add_u32 s12, s12, 0x8000
	s_addc_u32 s13, s13, 0
	global_load_dwordx4 v[104:107], v10, s[12:13]
	s_add_u32 s12, s12, 0x8000
	s_addc_u32 s13, s13, 0
	global_load_dwordx4 v[108:111], v10, s[12:13]
	s_add_u32 s12, s12, 0x8000
	s_addc_u32 s13, s13, 0
	global_load_dwordx4 v[112:115], v10, s[12:13]
	s_add_u32 s12, s12, 0x8000
	s_addc_u32 s13, s13, 0
	global_load_dwordx4 v[116:119], v10, s[12:13]
	s_add_u32 s12, s12, 0x8000
	s_addc_u32 s13, s13, 0
	global_load_dwordx4 v[120:123], v10, s[12:13]
	s_add_u32 s12, s12, 0x8000
	s_addc_u32 s13, s13, 0
	global_load_dwordx4 v[124:127], v10, s[12:13]
	s_add_u32 s12, s12, 0x8000
	s_addc_u32 s13, s13, 0
	global_load_dwordx4 v[128:131], v10, s[12:13]
	s_add_i32 s17, s16, 3360
	s_min_u32 s17, s17, 0xfff
	s_lshr_b32 s18, s17, 5
	s_add_i32 s18, s18, 0
	s_and_b32 s19, s17, 31
	s_lshl_b32 s19, s19, 21
	s_lshl_b32 s18, s18, 7
	s_add_u32 s18, s18, s19
	s_add_u32 s14, s4, s18
	s_addc_u32 s15, s5, 0
	ds_read_b32 v132, v7
	ds_read_b32 v133, v7 offset:512
	ds_read_b32 v134, v7 offset:1024
	ds_read_b32 v135, v7 offset:1536
	ds_read_b32 v136, v7 offset:2048
	ds_read_b32 v137, v7 offset:2560
	ds_read_b32 v138, v7 offset:3072
	ds_read_b32 v139, v7 offset:3584
	ds_read_b32 v140, v7 offset:4096
	ds_read_b32 v141, v7 offset:4608
	ds_read_b32 v142, v7 offset:5120
	ds_read_b32 v143, v7 offset:5632
	ds_read_b32 v144, v7 offset:6144
	ds_read_b32 v145, v7 offset:6656
	ds_read_b32 v146, v7 offset:7168
	ds_read_b32 v147, v7 offset:7680
	s_waitcnt lgkmcnt(0)
	v_max_f32_e32 v132, v132, v132
	v_max_f32_e32 v133, v133, v133
	v_max_f32_e32 v134, v134, v134
	v_max_f32_e32 v135, v135, v135
	v_max_f32_e32 v136, v136, v136
	v_max_f32_e32 v137, v137, v137
	v_max_f32_e32 v138, v138, v138
	v_max_f32_e32 v139, v139, v139
	v_max_f32_e32 v140, v140, v140
	v_max_f32_e32 v141, v141, v141
	v_max_f32_e32 v142, v142, v142
	v_max_f32_e32 v143, v143, v143
	v_max_f32_e32 v144, v144, v144
	v_max_f32_e32 v145, v145, v145
	v_max_f32_e32 v146, v146, v146
	v_max_f32_e32 v147, v147, v147
	v_med3_f32 v132, v132, s20, v13
	v_med3_f32 v133, v133, s20, v13
	v_med3_f32 v134, v134, s20, v13
	v_med3_f32 v135, v135, s20, v13
	v_med3_f32 v136, v136, s20, v13
	v_med3_f32 v137, v137, s20, v13
	v_med3_f32 v138, v138, s20, v13
	v_med3_f32 v139, v139, s20, v13
	v_med3_f32 v140, v140, s20, v13
	v_med3_f32 v141, v141, s20, v13
	v_med3_f32 v142, v142, s20, v13
	v_med3_f32 v143, v143, s20, v13
	v_med3_f32 v144, v144, s20, v13
	v_med3_f32 v145, v145, s20, v13
	v_med3_f32 v146, v146, s20, v13
	v_med3_f32 v147, v147, s20, v13
	v_mov_b32_e32 v148, 0
	v_mov_b32_e32 v149, 0
	v_mov_b32_e32 v150, 0
	v_mov_b32_e32 v151, 0
	v_cvt_pk_fp8_f32 v148, v132, v133
	v_cvt_pk_fp8_f32 v149, v136, v137
	v_cvt_pk_fp8_f32 v150, v140, v141
	v_cvt_pk_fp8_f32 v151, v144, v145
	v_cvt_pk_fp8_f32 v148, v134, v135 op_sel:[0,0,1]
	v_cvt_pk_fp8_f32 v149, v138, v139 op_sel:[0,0,1]
	v_cvt_pk_fp8_f32 v150, v142, v143 op_sel:[0,0,1]
	v_cvt_pk_fp8_f32 v151, v146, v147 op_sel:[0,0,1]
	s_nop 0
	global_store_dwordx4 v11, v[148:151], s[14:15]
	ds_read_b32 v132, v9
	ds_read_b32 v133, v9 offset:512
	ds_read_b32 v134, v9 offset:1024
	ds_read_b32 v135, v9 offset:1536
	ds_read_b32 v136, v9 offset:2048
	ds_read_b32 v137, v9 offset:2560
	ds_read_b32 v138, v9 offset:3072
	ds_read_b32 v139, v9 offset:3584
	ds_read_b32 v140, v9 offset:4096
	ds_read_b32 v141, v9 offset:4608
	ds_read_b32 v142, v9 offset:5120
	ds_read_b32 v143, v9 offset:5632
	ds_read_b32 v144, v9 offset:6144
	ds_read_b32 v145, v9 offset:6656
	ds_read_b32 v146, v9 offset:7168
	ds_read_b32 v147, v9 offset:7680
	s_waitcnt lgkmcnt(0)
	v_max_f32_e32 v132, v132, v132
	v_max_f32_e32 v133, v133, v133
	v_max_f32_e32 v134, v134, v134
	v_max_f32_e32 v135, v135, v135
	v_max_f32_e32 v136, v136, v136
	v_max_f32_e32 v137, v137, v137
	v_max_f32_e32 v138, v138, v138
	v_max_f32_e32 v139, v139, v139
	v_max_f32_e32 v140, v140, v140
	v_max_f32_e32 v141, v141, v141
	v_max_f32_e32 v142, v142, v142
	v_max_f32_e32 v143, v143, v143
	v_max_f32_e32 v144, v144, v144
	v_max_f32_e32 v145, v145, v145
	v_max_f32_e32 v146, v146, v146
	v_max_f32_e32 v147, v147, v147
	v_med3_f32 v132, v132, s20, v13
	v_med3_f32 v133, v133, s20, v13
	v_med3_f32 v134, v134, s20, v13
	v_med3_f32 v135, v135, s20, v13
	v_med3_f32 v136, v136, s20, v13
	v_med3_f32 v137, v137, s20, v13
	v_med3_f32 v138, v138, s20, v13
	v_med3_f32 v139, v139, s20, v13
	v_med3_f32 v140, v140, s20, v13
	v_med3_f32 v141, v141, s20, v13
	v_med3_f32 v142, v142, s20, v13
	v_med3_f32 v143, v143, s20, v13
	v_med3_f32 v144, v144, s20, v13
	v_med3_f32 v145, v145, s20, v13
	v_med3_f32 v146, v146, s20, v13
	v_med3_f32 v147, v147, s20, v13
	v_mov_b32_e32 v148, 0
	v_mov_b32_e32 v149, 0
	v_mov_b32_e32 v150, 0
	v_mov_b32_e32 v151, 0
	v_cvt_pk_fp8_f32 v148, v132, v133
	v_cvt_pk_fp8_f32 v149, v136, v137
	v_cvt_pk_fp8_f32 v150, v140, v141
	v_cvt_pk_fp8_f32 v151, v144, v145
	v_cvt_pk_fp8_f32 v148, v134, v135 op_sel:[0,0,1]
	v_cvt_pk_fp8_f32 v149, v138, v139 op_sel:[0,0,1]
	v_cvt_pk_fp8_f32 v150, v142, v143 op_sel:[0,0,1]
	v_cvt_pk_fp8_f32 v151, v146, v147 op_sel:[0,0,1]
	s_nop 0
	global_store_dwordx4 v12, v[148:151], s[14:15]
	s_waitcnt vmcnt(22)
	v_mul_f32_e32 v36, 0x43000000, v36
	v_mul_f32_e32 v37, 0x43000000, v37
	v_mul_f32_e32 v38, 0x43000000, v38
	v_mul_f32_e32 v39, 0x43000000, v39
	ds_write_b128 v4, v[36:39]
	v_mul_f32_e32 v40, 0x43000000, v40
	v_mul_f32_e32 v41, 0x43000000, v41
	v_mul_f32_e32 v42, 0x43000000, v42
	v_mul_f32_e32 v43, 0x43000000, v43
	ds_write_b128 v4, v[40:43] offset:1024
	v_mul_f32_e32 v44, 0x43000000, v44
	v_mul_f32_e32 v45, 0x43000000, v45
	v_mul_f32_e32 v46, 0x43000000, v46
	v_mul_f32_e32 v47, 0x43000000, v47
	ds_write_b128 v4, v[44:47] offset:2048
	v_mul_f32_e32 v48, 0x43000000, v48
	v_mul_f32_e32 v49, 0x43000000, v49
	v_mul_f32_e32 v50, 0x43000000, v50
	v_mul_f32_e32 v51, 0x43000000, v51
	ds_write_b128 v4, v[48:51] offset:3072
	v_mul_f32_e32 v52, 0x43000000, v52
	v_mul_f32_e32 v53, 0x43000000, v53
	v_mul_f32_e32 v54, 0x43000000, v54
	v_mul_f32_e32 v55, 0x43000000, v55
	ds_write_b128 v4, v[52:55] offset:4096
	v_mul_f32_e32 v56, 0x43000000, v56
	v_mul_f32_e32 v57, 0x43000000, v57
	v_mul_f32_e32 v58, 0x43000000, v58
	v_mul_f32_e32 v59, 0x43000000, v59
	ds_write_b128 v4, v[56:59] offset:5120
	v_mul_f32_e32 v60, 0x43000000, v60
	v_mul_f32_e32 v61, 0x43000000, v61
	v_mul_f32_e32 v62, 0x43000000, v62
	v_mul_f32_e32 v63, 0x43000000, v63
	ds_write_b128 v4, v[60:63] offset:6144
	v_mul_f32_e32 v64, 0x43000000, v64
	v_mul_f32_e32 v65, 0x43000000, v65
	v_mul_f32_e32 v66, 0x43000000, v66
	v_mul_f32_e32 v67, 0x43000000, v67
	ds_write_b128 v4, v[64:67] offset:7168
	s_waitcnt lgkmcnt(0)
	s_barrier
; #define GAS __attribute__((address_space(1)))
; #define LAS __attribute__((address_space(3)))
; #define LDS_WAIT() asm volatile("s_waitcnt lgkmcnt(0)" ::: "memory")
; __device__ __forceinline__ unsigned pk4_fp8(float a, float b, float c, float d) {
;     a = fminf(fmaxf(a, -448.f), 448.f); b = fminf(fmaxf(b, -448.f), 448.f); c = fminf(fmaxf(c, -448.f), 448.f); d = fminf(fmaxf(d, -448.f), 448.f);
;     int w = __builtin_amdgcn_cvt_pk_fp8_f32(a, b, 0, false); w = __builtin_amdgcn_cvt_pk_fp8_f32(c, d, w, true); return (unsigned)w; }
;     const int pr = item >> 1, kb = 2 * (pr / nblk) + (item & 1), nb = pr % nblk, k0 = 64 * kb, n0 = 32 * nb;
;     const int nr = n0 + (lane & 31); const int sc = MAP == 1 ? src_col_in(nr) : nr;
;     float v[32];
; #pragma unroll
;     for (int i = 0; i < 32; ++i) v[i] = sc >= 0 ? W[(size_t)(k0 + 2 * i + (lane >> 5)) * Nsrc + sc] : 0.f;
; #pragma unroll
;     for (int i = 0; i < 32; ++i) { const int k = k0 + 2 * i + (lane >> 5); float x = v[i] * wscale; if (KS) x *= (k < ksplit ? ksA[k] : ksB[k - ksplit]); scr[(2 * i + (lane >> 5)) * 33 + (lane & 31)] = x; }
;     LDS_WAIT(); asm volatile("" ::: "memory");
;     const int c = lane & 7;
; #pragma unroll
;     for (int j = 0; j < 4; ++j) { const int n = (lane >> 3) + 8 * j; const LAS float* s = scr + (8 * c) * 33 + n;
;         const unsigned long long o = (unsigned long long)pg8::pk4_fp8(s[0 * 33], s[1 * 33], s[2 * 33], s[3 * 33]) | ((unsigned long long)pg8::pk4_fp8(s[4 * 33], s[5 * 33], s[6 * 33], s[7 * 33]) << 32);
;         *(GAS unsigned long long*)(WT + (size_t)(n0 + n) * K + k0 + 8 * c) = o; }
;     LDS_WAIT(); asm volatile("" ::: "memory");
	s_add_i32 s17, s16, 3744
	s_min_u32 s17, s17, 0xfff
	s_lshr_b32 s18, s17, 5
	s_add_i32 s18, s18, 0
	s_and_b32 s19, s17, 31
	s_lshl_b32 s18, s18, 21
	s_lshl_b32 s19, s19, 9
	s_add_u32 s18, s18, s19
	s_add_u32 s12, s2, s18
	s_addc_u32 s13, s3, 0
	global_load_dwordx4 v[36:39], v10, s[12:13]
	s_add_u32 s12, s12, 0x8000
	s_addc_u32 s13, s13, 0
	global_load_dwordx4 v[40:43], v10, s[12:13]
	s_add_u32 s12, s12, 0x8000
	s_addc_u32 s13, s13, 0
	global_load_dwordx4 v[44:47], v10, s[12:13]
	s_add_u32 s12, s12, 0x8000
	s_addc_u32 s13, s13, 0
	global_load_dwordx4 v[48:51], v10, s[12:13]
	s_add_u32 s12, s12, 0x8000
	s_addc_u32 s13, s13, 0
	global_load_dwordx4 v[52:55], v10, s[12:13]
	s_add_u32 s12, s12, 0x8000
	s_addc_u32 s13, s13, 0
	global_load_dwordx4 v[56:59], v10, s[12:13]
	s_add_u32 s12, s12, 0x8000
	s_addc_u32 s13, s13, 0
	global_load_dwordx4 v[60:63], v10, s[12:13]
	s_add_u32 s12, s12, 0x8000
	s_addc_u32 s13, s13, 0
	global_load_dwordx4 v[64:67], v10, s[12:13]
	s_add_i32 s17, s16, 3456
	s_min_u32 s17, s17, 0xfff
	s_lshr_b32 s18, s17, 5
	s_add_i32 s18, s18, 0
	s_and_b32 s19, s17, 31
	s_lshl_b32 s19, s19, 21
	s_lshl_b32 s18, s18, 7
	s_add_u32 s18, s18, s19
	s_add_u32 s14, s4, s18
	s_addc_u32 s15, s5, 0
	ds_read_b32 v132, v6
	ds_read_b32 v133, v6 offset:512
	ds_read_b32 v134, v6 offset:1024
	ds_read_b32 v135, v6 offset:1536
	ds_read_b32 v136, v6 offset:2048
	ds_read_b32 v137, v6 offset:2560
	ds_read_b32 v138, v6 offset:3072
	ds_read_b32 v139, v6 offset:3584
	ds_read_b32 v140, v6 offset:4096
	ds_read_b32 v141, v6 offset:4608
	ds_read_b32 v142, v6 offset:5120
	ds_read_b32 v143, v6 offset:5632
	ds_read_b32 v144, v6 offset:6144
	ds_read_b32 v145, v6 offset:6656
	ds_read_b32 v146, v6 offset:7168
	ds_read_b32 v147, v6 offset:7680
	s_waitcnt lgkmcnt(0)
	v_max_f32_e32 v132, v132, v132
	v_max_f32_e32 v133, v133, v133
	v_max_f32_e32 v134, v134, v134
	v_max_f32_e32 v135, v135, v135
	v_max_f32_e32 v136, v136, v136
	v_max_f32_e32 v137, v137, v137
	v_max_f32_e32 v138, v138, v138
	v_max_f32_e32 v139, v139, v139
	v_max_f32_e32 v140, v140, v140
	v_max_f32_e32 v141, v141, v141
	v_max_f32_e32 v142, v142, v142
	v_max_f32_e32 v143, v143, v143
	v_max_f32_e32 v144, v144, v144
	v_max_f32_e32 v145, v145, v145
	v_max_f32_e32 v146, v146, v146
	v_max_f32_e32 v147, v147, v147
	v_med3_f32 v132, v132, s20, v13
	v_med3_f32 v133, v133, s20, v13
	v_med3_f32 v134, v134, s20, v13
	v_med3_f32 v135, v135, s20, v13
	v_med3_f32 v136, v136, s20, v13
	v_med3_f32 v137, v137, s20, v13
	v_med3_f32 v138, v138, s20, v13
	v_med3_f32 v139, v139, s20, v13
	v_med3_f32 v140, v140, s20, v13
	v_med3_f32 v141, v141, s20, v13
	v_med3_f32 v142, v142, s20, v13
	v_med3_f32 v143, v143, s20, v13
	v_med3_f32 v144, v144, s20, v13
	v_med3_f32 v145, v145, s20, v13
	v_med3_f32 v146, v146, s20, v13
	v_med3_f32 v147, v147, s20, v13
	v_mov_b32_e32 v148, 0
	v_mov_b32_e32 v149, 0
	v_mov_b32_e32 v150, 0
	v_mov_b32_e32 v151, 0
	v_cvt_pk_fp8_f32 v148, v132, v133
	v_cvt_pk_fp8_f32 v149, v136, v137
	v_cvt_pk_fp8_f32 v150, v140, v141
	v_cvt_pk_fp8_f32 v151, v144, v145
	v_cvt_pk_fp8_f32 v148, v134, v135 op_sel:[0,0,1]
	v_cvt_pk_fp8_f32 v149, v138, v139 op_sel:[0,0,1]
	v_cvt_pk_fp8_f32 v150, v142, v143 op_sel:[0,0,1]
	v_cvt_pk_fp8_f32 v151, v146, v147 op_sel:[0,0,1]
	s_nop 0
	global_store_dwordx4 v11, v[148:151], s[14:15]
	ds_read_b32 v132, v8
	ds_read_b32 v133, v8 offset:512
	ds_read_b32 v134, v8 offset:1024
	ds_read_b32 v135, v8 offset:1536
	ds_read_b32 v136, v8 offset:2048
	ds_read_b32 v137, v8 offset:2560
	ds_read_b32 v138, v8 offset:3072
	ds_read_b32 v139, v8 offset:3584
	ds_read_b32 v140, v8 offset:4096
	ds_read_b32 v141, v8 offset:4608
	ds_read_b32 v142, v8 offset:5120
	ds_read_b32 v143, v8 offset:5632
	ds_read_b32 v144, v8 offset:6144
	ds_read_b32 v145, v8 offset:6656
	ds_read_b32 v146, v8 offset:7168
	ds_read_b32 v147, v8 offset:7680
	s_waitcnt lgkmcnt(0)
	v_max_f32_e32 v132, v132, v132
	v_max_f32_e32 v133, v133, v133
	v_max_f32_e32 v134, v134, v134
	v_max_f32_e32 v135, v135, v135
	v_max_f32_e32 v136, v136, v136
	v_max_f32_e32 v137, v137, v137
	v_max_f32_e32 v138, v138, v138
	v_max_f32_e32 v139, v139, v139
	v_max_f32_e32 v140, v140, v140
	v_max_f32_e32 v141, v141, v141
	v_max_f32_e32 v142, v142, v142
	v_max_f32_e32 v143, v143, v143
	v_max_f32_e32 v144, v144, v144
	v_max_f32_e32 v145, v145, v145
	v_max_f32_e32 v146, v146, v146
	v_max_f32_e32 v147, v147, v147
	v_med3_f32 v132, v132, s20, v13
	v_med3_f32 v133, v133, s20, v13
	v_med3_f32 v134, v134, s20, v13
	v_med3_f32 v135, v135, s20, v13
	v_med3_f32 v136, v136, s20, v13
	v_med3_f32 v137, v137, s20, v13
	v_med3_f32 v138, v138, s20, v13
	v_med3_f32 v139, v139, s20, v13
	v_med3_f32 v140, v140, s20, v13
	v_med3_f32 v141, v141, s20, v13
	v_med3_f32 v142, v142, s20, v13
	v_med3_f32 v143, v143, s20, v13
	v_med3_f32 v144, v144, s20, v13
	v_med3_f32 v145, v145, s20, v13
	v_med3_f32 v146, v146, s20, v13
	v_med3_f32 v147, v147, s20, v13
	v_mov_b32_e32 v148, 0
	v_mov_b32_e32 v149, 0
	v_mov_b32_e32 v150, 0
	v_mov_b32_e32 v151, 0
	v_cvt_pk_fp8_f32 v148, v132, v133
	v_cvt_pk_fp8_f32 v149, v136, v137
	v_cvt_pk_fp8_f32 v150, v140, v141
	v_cvt_pk_fp8_f32 v151, v144, v145
	v_cvt_pk_fp8_f32 v148, v134, v135 op_sel:[0,0,1]
	v_cvt_pk_fp8_f32 v149, v138, v139 op_sel:[0,0,1]
	v_cvt_pk_fp8_f32 v150, v142, v143 op_sel:[0,0,1]
	v_cvt_pk_fp8_f32 v151, v146, v147 op_sel:[0,0,1]
	s_nop 0
	global_store_dwordx4 v12, v[148:151], s[14:15]
	s_waitcnt vmcnt(22)
	v_mul_f32_e32 v68, 0x43000000, v68
	v_mul_f32_e32 v69, 0x43000000, v69
	v_mul_f32_e32 v70, 0x43000000, v70
	v_mul_f32_e32 v71, 0x43000000, v71
	ds_write_b128 v5, v[68:71]
	v_mul_f32_e32 v72, 0x43000000, v72
	v_mul_f32_e32 v73, 0x43000000, v73
	v_mul_f32_e32 v74, 0x43000000, v74
	v_mul_f32_e32 v75, 0x43000000, v75
	ds_write_b128 v5, v[72:75] offset:1024
	v_mul_f32_e32 v76, 0x43000000, v76
	v_mul_f32_e32 v77, 0x43000000, v77
	v_mul_f32_e32 v78, 0x43000000, v78
	v_mul_f32_e32 v79, 0x43000000, v79
	ds_write_b128 v5, v[76:79] offset:2048
	v_mul_f32_e32 v80, 0x43000000, v80
	v_mul_f32_e32 v81, 0x43000000, v81
	v_mul_f32_e32 v82, 0x43000000, v82
	v_mul_f32_e32 v83, 0x43000000, v83
	ds_write_b128 v5, v[80:83] offset:3072
	v_mul_f32_e32 v84, 0x43000000, v84
	v_mul_f32_e32 v85, 0x43000000, v85
	v_mul_f32_e32 v86, 0x43000000, v86
	v_mul_f32_e32 v87, 0x43000000, v87
	ds_write_b128 v5, v[84:87] offset:4096
	v_mul_f32_e32 v88, 0x43000000, v88
	v_mul_f32_e32 v89, 0x43000000, v89
	v_mul_f32_e32 v90, 0x43000000, v90
	v_mul_f32_e32 v91, 0x43000000, v91
	ds_write_b128 v5, v[88:91] offset:5120
	v_mul_f32_e32 v92, 0x43000000, v92
	v_mul_f32_e32 v93, 0x43000000, v93
	v_mul_f32_e32 v94, 0x43000000, v94
	v_mul_f32_e32 v95, 0x43000000, v95
	ds_write_b128 v5, v[92:95] offset:6144
	v_mul_f32_e32 v96, 0x43000000, v96
	v_mul_f32_e32 v97, 0x43000000, v97
	v_mul_f32_e32 v98, 0x43000000, v98
	v_mul_f32_e32 v99, 0x43000000, v99
	ds_write_b128 v5, v[96:99] offset:7168
	s_waitcnt lgkmcnt(0)
	s_barrier
; #define GAS __attribute__((address_space(1)))
; #define LAS __attribute__((address_space(3)))
; #define LDS_WAIT() asm volatile("s_waitcnt lgkmcnt(0)" ::: "memory")
; __device__ __forceinline__ unsigned pk4_fp8(float a, float b, float c, float d) {
;     a = fminf(fmaxf(a, -448.f), 448.f); b = fminf(fmaxf(b, -448.f), 448.f); c = fminf(fmaxf(c, -448.f), 448.f); d = fminf(fmaxf(d, -448.f), 448.f);
;     int w = __builtin_amdgcn_cvt_pk_fp8_f32(a, b, 0, false); w = __builtin_amdgcn_cvt_pk_fp8_f32(c, d, w, true); return (unsigned)w; }
;     const int pr = item >> 1, kb = 2 * (pr / nblk) + (item & 1), nb = pr % nblk, k0 = 64 * kb, n0 = 32 * nb;
;     const int nr = n0 + (lane & 31); const int sc = MAP == 1 ? src_col_in(nr) : nr;
;     float v[32];
; #pragma unroll
;     for (int i = 0; i < 32; ++i) v[i] = sc >= 0 ? W[(size_t)(k0 + 2 * i + (lane >> 5)) * Nsrc + sc] : 0.f;
; #pragma unroll
;     for (int i = 0; i < 32; ++i) { const int k = k0 + 2 * i + (lane >> 5); float x = v[i] * wscale; if (KS) x *= (k < ksplit ? ksA[k] : ksB[k - ksplit]); scr[(2 * i + (lane >> 5)) * 33 + (lane & 31)] = x; }
;     LDS_WAIT(); asm volatile("" ::: "memory");
;     const int c = lane & 7;
; #pragma unroll
;     for (int j = 0; j < 4; ++j) { const int n = (lane >> 3) + 8 * j; const LAS float* s = scr + (8 * c) * 33 + n;
;         const unsigned long long o = (unsigned long long)pg8::pk4_fp8(s[0 * 33], s[1 * 33], s[2 * 33], s[3 * 33]) | ((unsigned long long)pg8::pk4_fp8(s[4 * 33], s[5 * 33], s[6 * 33], s[7 * 33]) << 32);
;         *(GAS unsigned long long*)(WT + (size_t)(n0 + n) * K + k0 + 8 * c) = o; }
;     LDS_WAIT(); asm volatile("" ::: "memory");
	s_add_i32 s17, s16, 3840
	s_min_u32 s17, s17, 0xfff
	s_lshr_b32 s18, s17, 5
	s_add_i32 s18, s18, 0
	s_and_b32 s19, s17, 31
	s_lshl_b32 s18, s18, 21
	s_lshl_b32 s19, s19, 9
	s_add_u32 s18, s18, s19
	s_add_u32 s12, s2, s18
	s_addc_u32 s13, s3, 0
	global_load_dwordx4 v[68:71], v10, s[12:13]
	s_add_u32 s12, s12, 0x8000
	s_addc_u32 s13, s13, 0
	global_load_dwordx4 v[72:75], v10, s[12:13]
	s_add_u32 s12, s12, 0x8000
	s_addc_u32 s13, s13, 0
	global_load_dwordx4 v[76:79], v10, s[12:13]
	s_add_u32 s12, s12, 0x8000
	s_addc_u32 s13, s13, 0
	global_load_dwordx4 v[80:83], v10, s[12:13]
	s_add_u32 s12, s12, 0x8000
	s_addc_u32 s13, s13, 0
	global_load_dwordx4 v[84:87], v10, s[12:13]
	s_add_u32 s12, s12, 0x8000
	s_addc_u32 s13, s13, 0
	global_load_dwordx4 v[88:91], v10, s[12:13]
	s_add_u32 s12, s12, 0x8000
	s_addc_u32 s13, s13, 0
	global_load_dwordx4 v[92:95], v10, s[12:13]
	s_add_u32 s12, s12, 0x8000
	s_addc_u32 s13, s13, 0
	global_load_dwordx4 v[96:99], v10, s[12:13]
	s_add_i32 s17, s16, 3552
	s_min_u32 s17, s17, 0xfff
	s_lshr_b32 s18, s17, 5
	s_add_i32 s18, s18, 0
	s_and_b32 s19, s17, 31
	s_lshl_b32 s19, s19, 21
	s_lshl_b32 s18, s18, 7
	s_add_u32 s18, s18, s19
	s_add_u32 s14, s4, s18
	s_addc_u32 s15, s5, 0
	ds_read_b32 v132, v7
	ds_read_b32 v133, v7 offset:512
	ds_read_b32 v134, v7 offset:1024
	ds_read_b32 v135, v7 offset:1536
	ds_read_b32 v136, v7 offset:2048
	ds_read_b32 v137, v7 offset:2560
	ds_read_b32 v138, v7 offset:3072
	ds_read_b32 v139, v7 offset:3584
	ds_read_b32 v140, v7 offset:4096
	ds_read_b32 v141, v7 offset:4608
	ds_read_b32 v142, v7 offset:5120
	ds_read_b32 v143, v7 offset:5632
	ds_read_b32 v144, v7 offset:6144
	ds_read_b32 v145, v7 offset:6656
	ds_read_b32 v146, v7 offset:7168
	ds_read_b32 v147, v7 offset:7680
	s_waitcnt lgkmcnt(0)
	v_max_f32_e32 v132, v132, v132
	v_max_f32_e32 v133, v133, v133
	v_max_f32_e32 v134, v134, v134
	v_max_f32_e32 v135, v135, v135
	v_max_f32_e32 v136, v136, v136
	v_max_f32_e32 v137, v137, v137
	v_max_f32_e32 v138, v138, v138
	v_max_f32_e32 v139, v139, v139
	v_max_f32_e32 v140, v140, v140
	v_max_f32_e32 v141, v141, v141
	v_max_f32_e32 v142, v142, v142
	v_max_f32_e32 v143, v143, v143
	v_max_f32_e32 v144, v144, v144
	v_max_f32_e32 v145, v145, v145
	v_max_f32_e32 v146, v146, v146
	v_max_f32_e32 v147, v147, v147
	v_med3_f32 v132, v132, s20, v13
	v_med3_f32 v133, v133, s20, v13
	v_med3_f32 v134, v134, s20, v13
	v_med3_f32 v135, v135, s20, v13
	v_med3_f32 v136, v136, s20, v13
	v_med3_f32 v137, v137, s20, v13
	v_med3_f32 v138, v138, s20, v13
	v_med3_f32 v139, v139, s20, v13
	v_med3_f32 v140, v140, s20, v13
	v_med3_f32 v141, v141, s20, v13
	v_med3_f32 v142, v142, s20, v13
	v_med3_f32 v143, v143, s20, v13
	v_med3_f32 v144, v144, s20, v13
	v_med3_f32 v145, v145, s20, v13
	v_med3_f32 v146, v146, s20, v13
	v_med3_f32 v147, v147, s20, v13
	v_mov_b32_e32 v148, 0
	v_mov_b32_e32 v149, 0
	v_mov_b32_e32 v150, 0
	v_mov_b32_e32 v151, 0
	v_cvt_pk_fp8_f32 v148, v132, v133
	v_cvt_pk_fp8_f32 v149, v136, v137
	v_cvt_pk_fp8_f32 v150, v140, v141
	v_cvt_pk_fp8_f32 v151, v144, v145
	v_cvt_pk_fp8_f32 v148, v134, v135 op_sel:[0,0,1]
	v_cvt_pk_fp8_f32 v149, v138, v139 op_sel:[0,0,1]
	v_cvt_pk_fp8_f32 v150, v142, v143 op_sel:[0,0,1]
	v_cvt_pk_fp8_f32 v151, v146, v147 op_sel:[0,0,1]
	s_nop 0
	global_store_dwordx4 v11, v[148:151], s[14:15]
	ds_read_b32 v132, v9
	ds_read_b32 v133, v9 offset:512
	ds_read_b32 v134, v9 offset:1024
	ds_read_b32 v135, v9 offset:1536
	ds_read_b32 v136, v9 offset:2048
	ds_read_b32 v137, v9 offset:2560
	ds_read_b32 v138, v9 offset:3072
	ds_read_b32 v139, v9 offset:3584
	ds_read_b32 v140, v9 offset:4096
	ds_read_b32 v141, v9 offset:4608
	ds_read_b32 v142, v9 offset:5120
	ds_read_b32 v143, v9 offset:5632
	ds_read_b32 v144, v9 offset:6144
	ds_read_b32 v145, v9 offset:6656
	ds_read_b32 v146, v9 offset:7168
	ds_read_b32 v147, v9 offset:7680
	s_waitcnt lgkmcnt(0)
	v_max_f32_e32 v132, v132, v132
	v_max_f32_e32 v133, v133, v133
	v_max_f32_e32 v134, v134, v134
	v_max_f32_e32 v135, v135, v135
	v_max_f32_e32 v136, v136, v136
	v_max_f32_e32 v137, v137, v137
	v_max_f32_e32 v138, v138, v138
	v_max_f32_e32 v139, v139, v139
	v_max_f32_e32 v140, v140, v140
	v_max_f32_e32 v141, v141, v141
	v_max_f32_e32 v142, v142, v142
	v_max_f32_e32 v143, v143, v143
	v_max_f32_e32 v144, v144, v144
	v_max_f32_e32 v145, v145, v145
	v_max_f32_e32 v146, v146, v146
	v_max_f32_e32 v147, v147, v147
	v_med3_f32 v132, v132, s20, v13
	v_med3_f32 v133, v133, s20, v13
	v_med3_f32 v134, v134, s20, v13
	v_med3_f32 v135, v135, s20, v13
	v_med3_f32 v136, v136, s20, v13
	v_med3_f32 v137, v137, s20, v13
	v_med3_f32 v138, v138, s20, v13
	v_med3_f32 v139, v139, s20, v13
	v_med3_f32 v140, v140, s20, v13
	v_med3_f32 v141, v141, s20, v13
	v_med3_f32 v142, v142, s20, v13
	v_med3_f32 v143, v143, s20, v13
	v_med3_f32 v144, v144, s20, v13
	v_med3_f32 v145, v145, s20, v13
	v_med3_f32 v146, v146, s20, v13
	v_med3_f32 v147, v147, s20, v13
	v_mov_b32_e32 v148, 0
	v_mov_b32_e32 v149, 0
	v_mov_b32_e32 v150, 0
	v_mov_b32_e32 v151, 0
	v_cvt_pk_fp8_f32 v148, v132, v133
	v_cvt_pk_fp8_f32 v149, v136, v137
	v_cvt_pk_fp8_f32 v150, v140, v141
	v_cvt_pk_fp8_f32 v151, v144, v145
	v_cvt_pk_fp8_f32 v148, v134, v135 op_sel:[0,0,1]
	v_cvt_pk_fp8_f32 v149, v138, v139 op_sel:[0,0,1]
	v_cvt_pk_fp8_f32 v150, v142, v143 op_sel:[0,0,1]
	v_cvt_pk_fp8_f32 v151, v146, v147 op_sel:[0,0,1]
	s_nop 0
	global_store_dwordx4 v12, v[148:151], s[14:15]
	s_waitcnt vmcnt(22)
	v_mul_f32_e32 v100, 0x43000000, v100
	v_mul_f32_e32 v101, 0x43000000, v101
	v_mul_f32_e32 v102, 0x43000000, v102
	v_mul_f32_e32 v103, 0x43000000, v103
	ds_write_b128 v4, v[100:103]
	v_mul_f32_e32 v104, 0x43000000, v104
	v_mul_f32_e32 v105, 0x43000000, v105
	v_mul_f32_e32 v106, 0x43000000, v106
	v_mul_f32_e32 v107, 0x43000000, v107
	ds_write_b128 v4, v[104:107] offset:1024
	v_mul_f32_e32 v108, 0x43000000, v108
	v_mul_f32_e32 v109, 0x43000000, v109
	v_mul_f32_e32 v110, 0x43000000, v110
	v_mul_f32_e32 v111, 0x43000000, v111
	ds_write_b128 v4, v[108:111] offset:2048
	v_mul_f32_e32 v112, 0x43000000, v112
	v_mul_f32_e32 v113, 0x43000000, v113
	v_mul_f32_e32 v114, 0x43000000, v114
	v_mul_f32_e32 v115, 0x43000000, v115
	ds_write_b128 v4, v[112:115] offset:3072
	v_mul_f32_e32 v116, 0x43000000, v116
	v_mul_f32_e32 v117, 0x43000000, v117
	v_mul_f32_e32 v118, 0x43000000, v118
	v_mul_f32_e32 v119, 0x43000000, v119
	ds_write_b128 v4, v[116:119] offset:4096
	v_mul_f32_e32 v120, 0x43000000, v120
	v_mul_f32_e32 v121, 0x43000000, v121
	v_mul_f32_e32 v122, 0x43000000, v122
	v_mul_f32_e32 v123, 0x43000000, v123
	ds_write_b128 v4, v[120:123] offset:5120
	v_mul_f32_e32 v124, 0x43000000, v124
	v_mul_f32_e32 v125, 0x43000000, v125
	v_mul_f32_e32 v126, 0x43000000, v126
	v_mul_f32_e32 v127, 0x43000000, v127
	ds_write_b128 v4, v[124:127] offset:6144
	v_mul_f32_e32 v128, 0x43000000, v128
	v_mul_f32_e32 v129, 0x43000000, v129
	v_mul_f32_e32 v130, 0x43000000, v130
	v_mul_f32_e32 v131, 0x43000000, v131
	ds_write_b128 v4, v[128:131] offset:7168
	s_waitcnt lgkmcnt(0)
	s_barrier
; #define GAS __attribute__((address_space(1)))
; #define LAS __attribute__((address_space(3)))
; #define LDS_WAIT() asm volatile("s_waitcnt lgkmcnt(0)" ::: "memory")
; __device__ __forceinline__ unsigned pk4_fp8(float a, float b, float c, float d) {
;     a = fminf(fmaxf(a, -448.f), 448.f); b = fminf(fmaxf(b, -448.f), 448.f); c = fminf(fmaxf(c, -448.f), 448.f); d = fminf(fmaxf(d, -448.f), 448.f);
;     int w = __builtin_amdgcn_cvt_pk_fp8_f32(a, b, 0, false); w = __builtin_amdgcn_cvt_pk_fp8_f32(c, d, w, true); return (unsigned)w; }
;     const int pr = item >> 1, kb = 2 * (pr / nblk) + (item & 1), nb = pr % nblk, k0 = 64 * kb, n0 = 32 * nb;
;     const int nr = n0 + (lane & 31); const int sc = MAP == 1 ? src_col_in(nr) : nr;
;     float v[32];
; #pragma unroll
;     for (int i = 0; i < 32; ++i) v[i] = sc >= 0 ? W[(size_t)(k0 + 2 * i + (lane >> 5)) * Nsrc + sc] : 0.f;
; #pragma unroll
;     for (int i = 0; i < 32; ++i) { const int k = k0 + 2 * i + (lane >> 5); float x = v[i] * wscale; if (KS) x *= (k < ksplit ? ksA[k] : ksB[k - ksplit]); scr[(2 * i + (lane >> 5)) * 33 + (lane & 31)] = x; }
;     LDS_WAIT(); asm volatile("" ::: "memory");
;     const int c = lane & 7;
; #pragma unroll
;     for (int j = 0; j < 4; ++j) { const int n = (lane >> 3) + 8 * j; const LAS float* s = scr + (8 * c) * 33 + n;
;         const unsigned long long o = (unsigned long long)pg8::pk4_fp8(s[0 * 33], s[1 * 33], s[2 * 33], s[3 * 33]) | ((unsigned long long)pg8::pk4_fp8(s[4 * 33], s[5 * 33], s[6 * 33], s[7 * 33]) << 32);
;         *(GAS unsigned long long*)(WT + (size_t)(n0 + n) * K + k0 + 8 * c) = o; }
;     LDS_WAIT(); asm volatile("" ::: "memory");
	s_add_i32 s17, s16, 3936
	s_min_u32 s17, s17, 0xfff
	s_lshr_b32 s18, s17, 5
	s_add_i32 s18, s18, 0
	s_and_b32 s19, s17, 31
	s_lshl_b32 s18, s18, 21
	s_lshl_b32 s19, s19, 9
	s_add_u32 s18, s18, s19
	s_add_u32 s12, s2, s18
	s_addc_u32 s13, s3, 0
	global_load_dwordx4 v[100:103], v10, s[12:13]
	s_add_u32 s12, s12, 0x8000
	s_addc_u32 s13, s13, 0
	global_load_dwordx4 v[104:107], v10, s[12:13]
	s_add_u32 s12, s12, 0x8000
	s_addc_u32 s13, s13, 0
	global_load_dwordx4 v[108:111], v10, s[12:13]
	s_add_u32 s12, s12, 0x8000
	s_addc_u32 s13, s13, 0
	global_load_dwordx4 v[112:115], v10, s[12:13]
	s_add_u32 s12, s12, 0x8000
	s_addc_u32 s13, s13, 0
	global_load_dwordx4 v[116:119], v10, s[12:13]
	s_add_u32 s12, s12, 0x8000
	s_addc_u32 s13, s13, 0
	global_load_dwordx4 v[120:123], v10, s[12:13]
	s_add_u32 s12, s12, 0x8000
	s_addc_u32 s13, s13, 0
	global_load_dwordx4 v[124:127], v10, s[12:13]
	s_add_u32 s12, s12, 0x8000
	s_addc_u32 s13, s13, 0
	global_load_dwordx4 v[128:131], v10, s[12:13]
	s_add_i32 s17, s16, 3648
	s_min_u32 s17, s17, 0xfff
	s_lshr_b32 s18, s17, 5
	s_add_i32 s18, s18, 0
	s_and_b32 s19, s17, 31
	s_lshl_b32 s19, s19, 21
	s_lshl_b32 s18, s18, 7
	s_add_u32 s18, s18, s19
	s_add_u32 s14, s4, s18
	s_addc_u32 s15, s5, 0
	ds_read_b32 v132, v6
	ds_read_b32 v133, v6 offset:512
	ds_read_b32 v134, v6 offset:1024
	ds_read_b32 v135, v6 offset:1536
	ds_read_b32 v136, v6 offset:2048
	ds_read_b32 v137, v6 offset:2560
	ds_read_b32 v138, v6 offset:3072
	ds_read_b32 v139, v6 offset:3584
	ds_read_b32 v140, v6 offset:4096
	ds_read_b32 v141, v6 offset:4608
	ds_read_b32 v142, v6 offset:5120
	ds_read_b32 v143, v6 offset:5632
	ds_read_b32 v144, v6 offset:6144
	ds_read_b32 v145, v6 offset:6656
	ds_read_b32 v146, v6 offset:7168
	ds_read_b32 v147, v6 offset:7680
	s_waitcnt lgkmcnt(0)
	v_max_f32_e32 v132, v132, v132
	v_max_f32_e32 v133, v133, v133
	v_max_f32_e32 v134, v134, v134
	v_max_f32_e32 v135, v135, v135
	v_max_f32_e32 v136, v136, v136
	v_max_f32_e32 v137, v137, v137
	v_max_f32_e32 v138, v138, v138
	v_max_f32_e32 v139, v139, v139
	v_max_f32_e32 v140, v140, v140
	v_max_f32_e32 v141, v141, v141
	v_max_f32_e32 v142, v142, v142
	v_max_f32_e32 v143, v143, v143
	v_max_f32_e32 v144, v144, v144
	v_max_f32_e32 v145, v145, v145
	v_max_f32_e32 v146, v146, v146
	v_max_f32_e32 v147, v147, v147
	v_med3_f32 v132, v132, s20, v13
	v_med3_f32 v133, v133, s20, v13
	v_med3_f32 v134, v134, s20, v13
	v_med3_f32 v135, v135, s20, v13
	v_med3_f32 v136, v136, s20, v13
	v_med3_f32 v137, v137, s20, v13
	v_med3_f32 v138, v138, s20, v13
	v_med3_f32 v139, v139, s20, v13
	v_med3_f32 v140, v140, s20, v13
	v_med3_f32 v141, v141, s20, v13
	v_med3_f32 v142, v142, s20, v13
	v_med3_f32 v143, v143, s20, v13
	v_med3_f32 v144, v144, s20, v13
	v_med3_f32 v145, v145, s20, v13
	v_med3_f32 v146, v146, s20, v13
	v_med3_f32 v147, v147, s20, v13
	v_mov_b32_e32 v148, 0
	v_mov_b32_e32 v149, 0
	v_mov_b32_e32 v150, 0
	v_mov_b32_e32 v151, 0
	v_cvt_pk_fp8_f32 v148, v132, v133
	v_cvt_pk_fp8_f32 v149, v136, v137
	v_cvt_pk_fp8_f32 v150, v140, v141
	v_cvt_pk_fp8_f32 v151, v144, v145
	v_cvt_pk_fp8_f32 v148, v134, v135 op_sel:[0,0,1]
	v_cvt_pk_fp8_f32 v149, v138, v139 op_sel:[0,0,1]
	v_cvt_pk_fp8_f32 v150, v142, v143 op_sel:[0,0,1]
	v_cvt_pk_fp8_f32 v151, v146, v147 op_sel:[0,0,1]
	s_nop 0
	global_store_dwordx4 v11, v[148:151], s[14:15]
	ds_read_b32 v132, v8
	ds_read_b32 v133, v8 offset:512
	ds_read_b32 v134, v8 offset:1024
	ds_read_b32 v135, v8 offset:1536
	ds_read_b32 v136, v8 offset:2048
	ds_read_b32 v137, v8 offset:2560
	ds_read_b32 v138, v8 offset:3072
	ds_read_b32 v139, v8 offset:3584
	ds_read_b32 v140, v8 offset:4096
	ds_read_b32 v141, v8 offset:4608
	ds_read_b32 v142, v8 offset:5120
	ds_read_b32 v143, v8 offset:5632
	ds_read_b32 v144, v8 offset:6144
	ds_read_b32 v145, v8 offset:6656
	ds_read_b32 v146, v8 offset:7168
	ds_read_b32 v147, v8 offset:7680
	s_waitcnt lgkmcnt(0)
	v_max_f32_e32 v132, v132, v132
	v_max_f32_e32 v133, v133, v133
	v_max_f32_e32 v134, v134, v134
	v_max_f32_e32 v135, v135, v135
	v_max_f32_e32 v136, v136, v136
	v_max_f32_e32 v137, v137, v137
	v_max_f32_e32 v138, v138, v138
	v_max_f32_e32 v139, v139, v139
	v_max_f32_e32 v140, v140, v140
	v_max_f32_e32 v141, v141, v141
	v_max_f32_e32 v142, v142, v142
	v_max_f32_e32 v143, v143, v143
	v_max_f32_e32 v144, v144, v144
	v_max_f32_e32 v145, v145, v145
	v_max_f32_e32 v146, v146, v146
	v_max_f32_e32 v147, v147, v147
	v_med3_f32 v132, v132, s20, v13
	v_med3_f32 v133, v133, s20, v13
	v_med3_f32 v134, v134, s20, v13
	v_med3_f32 v135, v135, s20, v13
	v_med3_f32 v136, v136, s20, v13
	v_med3_f32 v137, v137, s20, v13
	v_med3_f32 v138, v138, s20, v13
	v_med3_f32 v139, v139, s20, v13
	v_med3_f32 v140, v140, s20, v13
	v_med3_f32 v141, v141, s20, v13
	v_med3_f32 v142, v142, s20, v13
	v_med3_f32 v143, v143, s20, v13
	v_med3_f32 v144, v144, s20, v13
	v_med3_f32 v145, v145, s20, v13
	v_med3_f32 v146, v146, s20, v13
	v_med3_f32 v147, v147, s20, v13
	v_mov_b32_e32 v148, 0
	v_mov_b32_e32 v149, 0
	v_mov_b32_e32 v150, 0
	v_mov_b32_e32 v151, 0
	v_cvt_pk_fp8_f32 v148, v132, v133
	v_cvt_pk_fp8_f32 v149, v136, v137
	v_cvt_pk_fp8_f32 v150, v140, v141
	v_cvt_pk_fp8_f32 v151, v144, v145
	v_cvt_pk_fp8_f32 v148, v134, v135 op_sel:[0,0,1]
	v_cvt_pk_fp8_f32 v149, v138, v139 op_sel:[0,0,1]
	v_cvt_pk_fp8_f32 v150, v142, v143 op_sel:[0,0,1]
	v_cvt_pk_fp8_f32 v151, v146, v147 op_sel:[0,0,1]
	s_nop 0
	global_store_dwordx4 v12, v[148:151], s[14:15]
	s_waitcnt vmcnt(22)
	v_mul_f32_e32 v36, 0x43000000, v36
	v_mul_f32_e32 v37, 0x43000000, v37
	v_mul_f32_e32 v38, 0x43000000, v38
	v_mul_f32_e32 v39, 0x43000000, v39
	ds_write_b128 v5, v[36:39]
	v_mul_f32_e32 v40, 0x43000000, v40
	v_mul_f32_e32 v41, 0x43000000, v41
	v_mul_f32_e32 v42, 0x43000000, v42
	v_mul_f32_e32 v43, 0x43000000, v43
	ds_write_b128 v5, v[40:43] offset:1024
	v_mul_f32_e32 v44, 0x43000000, v44
	v_mul_f32_e32 v45, 0x43000000, v45
	v_mul_f32_e32 v46, 0x43000000, v46
	v_mul_f32_e32 v47, 0x43000000, v47
	ds_write_b128 v5, v[44:47] offset:2048
	v_mul_f32_e32 v48, 0x43000000, v48
	v_mul_f32_e32 v49, 0x43000000, v49
	v_mul_f32_e32 v50, 0x43000000, v50
	v_mul_f32_e32 v51, 0x43000000, v51
	ds_write_b128 v5, v[48:51] offset:3072
	v_mul_f32_e32 v52, 0x43000000, v52
	v_mul_f32_e32 v53, 0x43000000, v53
	v_mul_f32_e32 v54, 0x43000000, v54
	v_mul_f32_e32 v55, 0x43000000, v55
	ds_write_b128 v5, v[52:55] offset:4096
	v_mul_f32_e32 v56, 0x43000000, v56
	v_mul_f32_e32 v57, 0x43000000, v57
	v_mul_f32_e32 v58, 0x43000000, v58
	v_mul_f32_e32 v59, 0x43000000, v59
	ds_write_b128 v5, v[56:59] offset:5120
	v_mul_f32_e32 v60, 0x43000000, v60
	v_mul_f32_e32 v61, 0x43000000, v61
	v_mul_f32_e32 v62, 0x43000000, v62
	v_mul_f32_e32 v63, 0x43000000, v63
	ds_write_b128 v5, v[60:63] offset:6144
	v_mul_f32_e32 v64, 0x43000000, v64
	v_mul_f32_e32 v65, 0x43000000, v65
	v_mul_f32_e32 v66, 0x43000000, v66
	v_mul_f32_e32 v67, 0x43000000, v67
	ds_write_b128 v5, v[64:67] offset:7168
	s_waitcnt lgkmcnt(0)
	s_barrier
; #define GAS __attribute__((address_space(1)))
; #define LAS __attribute__((address_space(3)))
; #define LDS_WAIT() asm volatile("s_waitcnt lgkmcnt(0)" ::: "memory")
; __device__ __forceinline__ unsigned pk4_fp8(float a, float b, float c, float d) {
;     a = fminf(fmaxf(a, -448.f), 448.f); b = fminf(fmaxf(b, -448.f), 448.f); c = fminf(fmaxf(c, -448.f), 448.f); d = fminf(fmaxf(d, -448.f), 448.f);
;     int w = __builtin_amdgcn_cvt_pk_fp8_f32(a, b, 0, false); w = __builtin_amdgcn_cvt_pk_fp8_f32(c, d, w, true); return (unsigned)w; }
;     const int pr = item >> 1, kb = 2 * (pr / nblk) + (item & 1), nb = pr % nblk, k0 = 64 * kb, n0 = 32 * nb;
;     const int nr = n0 + (lane & 31); const int sc = MAP == 1 ? src_col_in(nr) : nr;
;     float v[32];
; #pragma unroll
;     for (int i = 0; i < 32; ++i) v[i] = sc >= 0 ? W[(size_t)(k0 + 2 * i + (lane >> 5)) * Nsrc + sc] : 0.f;
; #pragma unroll
;     for (int i = 0; i < 32; ++i) { const int k = k0 + 2 * i + (lane >> 5); float x = v[i] * wscale; if (KS) x *= (k < ksplit ? ksA[k] : ksB[k - ksplit]); scr[(2 * i + (lane >> 5)) * 33 + (lane & 31)] = x; }
;     LDS_WAIT(); asm volatile("" ::: "memory");
;     const int c = lane & 7;
; #pragma unroll
;     for (int j = 0; j < 4; ++j) { const int n = (lane >> 3) + 8 * j; const LAS float* s = scr + (8 * c) * 33 + n;
;         const unsigned long long o = (unsigned long long)pg8::pk4_fp8(s[0 * 33], s[1 * 33], s[2 * 33], s[3 * 33]) | ((unsigned long long)pg8::pk4_fp8(s[4 * 33], s[5 * 33], s[6 * 33], s[7 * 33]) << 32);
;         *(GAS unsigned long long*)(WT + (size_t)(n0 + n) * K + k0 + 8 * c) = o; }
;     LDS_WAIT(); asm volatile("" ::: "memory");
	s_add_i32 s17, s16, 4032
	s_min_u32 s17, s17, 0xfff
	s_lshr_b32 s18, s17, 5
	s_add_i32 s18, s18, 0
	s_and_b32 s19, s17, 31
	s_lshl_b32 s18, s18, 21
	s_lshl_b32 s19, s19, 9
	s_add_u32 s18, s18, s19
	s_add_u32 s12, s2, s18
	s_addc_u32 s13, s3, 0
	global_load_dwordx4 v[36:39], v10, s[12:13]
	s_add_u32 s12, s12, 0x8000
	s_addc_u32 s13, s13, 0
	global_load_dwordx4 v[40:43], v10, s[12:13]
	s_add_u32 s12, s12, 0x8000
	s_addc_u32 s13, s13, 0
	global_load_dwordx4 v[44:47], v10, s[12:13]
	s_add_u32 s12, s12, 0x8000
	s_addc_u32 s13, s13, 0
	global_load_dwordx4 v[48:51], v10, s[12:13]
	s_add_u32 s12, s12, 0x8000
	s_addc_u32 s13, s13, 0
	global_load_dwordx4 v[52:55], v10, s[12:13]
	s_add_u32 s12, s12, 0x8000
	s_addc_u32 s13, s13, 0
	global_load_dwordx4 v[56:59], v10, s[12:13]
	s_add_u32 s12, s12, 0x8000
	s_addc_u32 s13, s13, 0
	global_load_dwordx4 v[60:63], v10, s[12:13]
	s_add_u32 s12, s12, 0x8000
	s_addc_u32 s13, s13, 0
	global_load_dwordx4 v[64:67], v10, s[12:13]
	s_add_i32 s17, s16, 3744
	s_min_u32 s17, s17, 0xfff
	s_lshr_b32 s18, s17, 5
	s_add_i32 s18, s18, 0
	s_and_b32 s19, s17, 31
	s_lshl_b32 s19, s19, 21
	s_lshl_b32 s18, s18, 7
	s_add_u32 s18, s18, s19
	s_add_u32 s14, s4, s18
	s_addc_u32 s15, s5, 0
	ds_read_b32 v132, v7
	ds_read_b32 v133, v7 offset:512
	ds_read_b32 v134, v7 offset:1024
	ds_read_b32 v135, v7 offset:1536
	ds_read_b32 v136, v7 offset:2048
	ds_read_b32 v137, v7 offset:2560
	ds_read_b32 v138, v7 offset:3072
	ds_read_b32 v139, v7 offset:3584
	ds_read_b32 v140, v7 offset:4096
	ds_read_b32 v141, v7 offset:4608
	ds_read_b32 v142, v7 offset:5120
	ds_read_b32 v143, v7 offset:5632
	ds_read_b32 v144, v7 offset:6144
	ds_read_b32 v145, v7 offset:6656
	ds_read_b32 v146, v7 offset:7168
	ds_read_b32 v147, v7 offset:7680
	s_waitcnt lgkmcnt(0)
	v_max_f32_e32 v132, v132, v132
	v_max_f32_e32 v133, v133, v133
	v_max_f32_e32 v134, v134, v134
	v_max_f32_e32 v135, v135, v135
	v_max_f32_e32 v136, v136, v136
	v_max_f32_e32 v137, v137, v137
	v_max_f32_e32 v138, v138, v138
	v_max_f32_e32 v139, v139, v139
	v_max_f32_e32 v140, v140, v140
	v_max_f32_e32 v141, v141, v141
	v_max_f32_e32 v142, v142, v142
	v_max_f32_e32 v143, v143, v143
	v_max_f32_e32 v144, v144, v144
	v_max_f32_e32 v145, v145, v145
	v_max_f32_e32 v146, v146, v146
	v_max_f32_e32 v147, v147, v147
	v_med3_f32 v132, v132, s20, v13
	v_med3_f32 v133, v133, s20, v13
	v_med3_f32 v134, v134, s20, v13
	v_med3_f32 v135, v135, s20, v13
	v_med3_f32 v136, v136, s20, v13
	v_med3_f32 v137, v137, s20, v13
	v_med3_f32 v138, v138, s20, v13
	v_med3_f32 v139, v139, s20, v13
	v_med3_f32 v140, v140, s20, v13
	v_med3_f32 v141, v141, s20, v13
	v_med3_f32 v142, v142, s20, v13
	v_med3_f32 v143, v143, s20, v13
	v_med3_f32 v144, v144, s20, v13
	v_med3_f32 v145, v145, s20, v13
	v_med3_f32 v146, v146, s20, v13
	v_med3_f32 v147, v147, s20, v13
	v_mov_b32_e32 v148, 0
	v_mov_b32_e32 v149, 0
	v_mov_b32_e32 v150, 0
	v_mov_b32_e32 v151, 0
	v_cvt_pk_fp8_f32 v148, v132, v133
	v_cvt_pk_fp8_f32 v149, v136, v137
	v_cvt_pk_fp8_f32 v150, v140, v141
	v_cvt_pk_fp8_f32 v151, v144, v145
	v_cvt_pk_fp8_f32 v148, v134, v135 op_sel:[0,0,1]
	v_cvt_pk_fp8_f32 v149, v138, v139 op_sel:[0,0,1]
	v_cvt_pk_fp8_f32 v150, v142, v143 op_sel:[0,0,1]
	v_cvt_pk_fp8_f32 v151, v146, v147 op_sel:[0,0,1]
	s_nop 0
	global_store_dwordx4 v11, v[148:151], s[14:15]
	ds_read_b32 v132, v9
	ds_read_b32 v133, v9 offset:512
	ds_read_b32 v134, v9 offset:1024
	ds_read_b32 v135, v9 offset:1536
	ds_read_b32 v136, v9 offset:2048
	ds_read_b32 v137, v9 offset:2560
	ds_read_b32 v138, v9 offset:3072
	ds_read_b32 v139, v9 offset:3584
	ds_read_b32 v140, v9 offset:4096
	ds_read_b32 v141, v9 offset:4608
	ds_read_b32 v142, v9 offset:5120
	ds_read_b32 v143, v9 offset:5632
	ds_read_b32 v144, v9 offset:6144
	ds_read_b32 v145, v9 offset:6656
	ds_read_b32 v146, v9 offset:7168
	ds_read_b32 v147, v9 offset:7680
	s_waitcnt lgkmcnt(0)
	v_max_f32_e32 v132, v132, v132
	v_max_f32_e32 v133, v133, v133
	v_max_f32_e32 v134, v134, v134
	v_max_f32_e32 v135, v135, v135
	v_max_f32_e32 v136, v136, v136
	v_max_f32_e32 v137, v137, v137
	v_max_f32_e32 v138, v138, v138
	v_max_f32_e32 v139, v139, v139
	v_max_f32_e32 v140, v140, v140
	v_max_f32_e32 v141, v141, v141
	v_max_f32_e32 v142, v142, v142
	v_max_f32_e32 v143, v143, v143
	v_max_f32_e32 v144, v144, v144
	v_max_f32_e32 v145, v145, v145
	v_max_f32_e32 v146, v146, v146
	v_max_f32_e32 v147, v147, v147
	v_med3_f32 v132, v132, s20, v13
	v_med3_f32 v133, v133, s20, v13
	v_med3_f32 v134, v134, s20, v13
	v_med3_f32 v135, v135, s20, v13
	v_med3_f32 v136, v136, s20, v13
	v_med3_f32 v137, v137, s20, v13
	v_med3_f32 v138, v138, s20, v13
	v_med3_f32 v139, v139, s20, v13
	v_med3_f32 v140, v140, s20, v13
	v_med3_f32 v141, v141, s20, v13
	v_med3_f32 v142, v142, s20, v13
	v_med3_f32 v143, v143, s20, v13
	v_med3_f32 v144, v144, s20, v13
	v_med3_f32 v145, v145, s20, v13
	v_med3_f32 v146, v146, s20, v13
	v_med3_f32 v147, v147, s20, v13
	v_mov_b32_e32 v148, 0
	v_mov_b32_e32 v149, 0
	v_mov_b32_e32 v150, 0
	v_mov_b32_e32 v151, 0
	v_cvt_pk_fp8_f32 v148, v132, v133
	v_cvt_pk_fp8_f32 v149, v136, v137
	v_cvt_pk_fp8_f32 v150, v140, v141
	v_cvt_pk_fp8_f32 v151, v144, v145
	v_cvt_pk_fp8_f32 v148, v134, v135 op_sel:[0,0,1]
	v_cvt_pk_fp8_f32 v149, v138, v139 op_sel:[0,0,1]
	v_cvt_pk_fp8_f32 v150, v142, v143 op_sel:[0,0,1]
	v_cvt_pk_fp8_f32 v151, v146, v147 op_sel:[0,0,1]
	s_nop 0
	global_store_dwordx4 v12, v[148:151], s[14:15]
	s_waitcnt vmcnt(22)
	v_mul_f32_e32 v68, 0x43000000, v68
	v_mul_f32_e32 v69, 0x43000000, v69
	v_mul_f32_e32 v70, 0x43000000, v70
	v_mul_f32_e32 v71, 0x43000000, v71
	ds_write_b128 v4, v[68:71]
	v_mul_f32_e32 v72, 0x43000000, v72
	v_mul_f32_e32 v73, 0x43000000, v73
	v_mul_f32_e32 v74, 0x43000000, v74
	v_mul_f32_e32 v75, 0x43000000, v75
	ds_write_b128 v4, v[72:75] offset:1024
	v_mul_f32_e32 v76, 0x43000000, v76
	v_mul_f32_e32 v77, 0x43000000, v77
	v_mul_f32_e32 v78, 0x43000000, v78
	v_mul_f32_e32 v79, 0x43000000, v79
	ds_write_b128 v4, v[76:79] offset:2048
	v_mul_f32_e32 v80, 0x43000000, v80
	v_mul_f32_e32 v81, 0x43000000, v81
	v_mul_f32_e32 v82, 0x43000000, v82
	v_mul_f32_e32 v83, 0x43000000, v83
	ds_write_b128 v4, v[80:83] offset:3072
	v_mul_f32_e32 v84, 0x43000000, v84
	v_mul_f32_e32 v85, 0x43000000, v85
	v_mul_f32_e32 v86, 0x43000000, v86
	v_mul_f32_e32 v87, 0x43000000, v87
	ds_write_b128 v4, v[84:87] offset:4096
	v_mul_f32_e32 v88, 0x43000000, v88
	v_mul_f32_e32 v89, 0x43000000, v89
	v_mul_f32_e32 v90, 0x43000000, v90
	v_mul_f32_e32 v91, 0x43000000, v91
	ds_write_b128 v4, v[88:91] offset:5120
	v_mul_f32_e32 v92, 0x43000000, v92
	v_mul_f32_e32 v93, 0x43000000, v93
	v_mul_f32_e32 v94, 0x43000000, v94
	v_mul_f32_e32 v95, 0x43000000, v95
	ds_write_b128 v4, v[92:95] offset:6144
	v_mul_f32_e32 v96, 0x43000000, v96
	v_mul_f32_e32 v97, 0x43000000, v97
	v_mul_f32_e32 v98, 0x43000000, v98
	v_mul_f32_e32 v99, 0x43000000, v99
	ds_write_b128 v4, v[96:99] offset:7168
	s_waitcnt lgkmcnt(0)
	s_barrier
; #define GAS __attribute__((address_space(1)))
; #define LAS __attribute__((address_space(3)))
; #define LDS_WAIT() asm volatile("s_waitcnt lgkmcnt(0)" ::: "memory")
; __device__ __forceinline__ unsigned pk4_fp8(float a, float b, float c, float d) {
;     a = fminf(fmaxf(a, -448.f), 448.f); b = fminf(fmaxf(b, -448.f), 448.f); c = fminf(fmaxf(c, -448.f), 448.f); d = fminf(fmaxf(d, -448.f), 448.f);
;     int w = __builtin_amdgcn_cvt_pk_fp8_f32(a, b, 0, false); w = __builtin_amdgcn_cvt_pk_fp8_f32(c, d, w, true); return (unsigned)w; }
;     const int pr = item >> 1, kb = 2 * (pr / nblk) + (item & 1), nb = pr % nblk, k0 = 64 * kb, n0 = 32 * nb;
;     const int nr = n0 + (lane & 31); const int sc = MAP == 1 ? src_col_in(nr) : nr;
;     float v[32];
; #pragma unroll
;     for (int i = 0; i < 32; ++i) v[i] = sc >= 0 ? W[(size_t)(k0 + 2 * i + (lane >> 5)) * Nsrc + sc] : 0.f;
; #pragma unroll
;     for (int i = 0; i < 32; ++i) { const int k = k0 + 2 * i + (lane >> 5); float x = v[i] * wscale; if (KS) x *= (k < ksplit ? ksA[k] : ksB[k - ksplit]); scr[(2 * i + (lane >> 5)) * 33 + (lane & 31)] = x; }
;     LDS_WAIT(); asm volatile("" ::: "memory");
;     const int c = lane & 7;
; #pragma unroll
;     for (int j = 0; j < 4; ++j) { const int n = (lane >> 3) + 8 * j; const LAS float* s = scr + (8 * c) * 33 + n;
;         const unsigned long long o = (unsigned long long)pg8::pk4_fp8(s[0 * 33], s[1 * 33], s[2 * 33], s[3 * 33]) | ((unsigned long long)pg8::pk4_fp8(s[4 * 33], s[5 * 33], s[6 * 33], s[7 * 33]) << 32);
;         *(GAS unsigned long long*)(WT + (size_t)(n0 + n) * K + k0 + 8 * c) = o; }
;     LDS_WAIT(); asm volatile("" ::: "memory");
	s_add_i32 s17, s16, 3840
	s_min_u32 s17, s17, 0xfff
	s_lshr_b32 s18, s17, 5
	s_add_i32 s18, s18, 0
	s_and_b32 s19, s17, 31
	s_lshl_b32 s19, s19, 21
	s_lshl_b32 s18, s18, 7
	s_add_u32 s18, s18, s19
	s_add_u32 s14, s4, s18
	s_addc_u32 s15, s5, 0
	ds_read_b32 v132, v6
	ds_read_b32 v133, v6 offset:512
	ds_read_b32 v134, v6 offset:1024
	ds_read_b32 v135, v6 offset:1536
	ds_read_b32 v136, v6 offset:2048
	ds_read_b32 v137, v6 offset:2560
	ds_read_b32 v138, v6 offset:3072
	ds_read_b32 v139, v6 offset:3584
	ds_read_b32 v140, v6 offset:4096
	ds_read_b32 v141, v6 offset:4608
	ds_read_b32 v142, v6 offset:5120
	ds_read_b32 v143, v6 offset:5632
	ds_read_b32 v144, v6 offset:6144
	ds_read_b32 v145, v6 offset:6656
	ds_read_b32 v146, v6 offset:7168
	ds_read_b32 v147, v6 offset:7680
	s_waitcnt lgkmcnt(0)
	v_max_f32_e32 v132, v132, v132
	v_max_f32_e32 v133, v133, v133
	v_max_f32_e32 v134, v134, v134
	v_max_f32_e32 v135, v135, v135
	v_max_f32_e32 v136, v136, v136
	v_max_f32_e32 v137, v137, v137
	v_max_f32_e32 v138, v138, v138
	v_max_f32_e32 v139, v139, v139
	v_max_f32_e32 v140, v140, v140
	v_max_f32_e32 v141, v141, v141
	v_max_f32_e32 v142, v142, v142
	v_max_f32_e32 v143, v143, v143
	v_max_f32_e32 v144, v144, v144
	v_max_f32_e32 v145, v145, v145
	v_max_f32_e32 v146, v146, v146
	v_max_f32_e32 v147, v147, v147
	v_med3_f32 v132, v132, s20, v13
	v_med3_f32 v133, v133, s20, v13
	v_med3_f32 v134, v134, s20, v13
	v_med3_f32 v135, v135, s20, v13
	v_med3_f32 v136, v136, s20, v13
	v_med3_f32 v137, v137, s20, v13
	v_med3_f32 v138, v138, s20, v13
	v_med3_f32 v139, v139, s20, v13
	v_med3_f32 v140, v140, s20, v13
	v_med3_f32 v141, v141, s20, v13
	v_med3_f32 v142, v142, s20, v13
	v_med3_f32 v143, v143, s20, v13
	v_med3_f32 v144, v144, s20, v13
	v_med3_f32 v145, v145, s20, v13
	v_med3_f32 v146, v146, s20, v13
	v_med3_f32 v147, v147, s20, v13
	v_mov_b32_e32 v148, 0
	v_mov_b32_e32 v149, 0
	v_mov_b32_e32 v150, 0
	v_mov_b32_e32 v151, 0
	v_cvt_pk_fp8_f32 v148, v132, v133
	v_cvt_pk_fp8_f32 v149, v136, v137
	v_cvt_pk_fp8_f32 v150, v140, v141
	v_cvt_pk_fp8_f32 v151, v144, v145
	v_cvt_pk_fp8_f32 v148, v134, v135 op_sel:[0,0,1]
	v_cvt_pk_fp8_f32 v149, v138, v139 op_sel:[0,0,1]
	v_cvt_pk_fp8_f32 v150, v142, v143 op_sel:[0,0,1]
	v_cvt_pk_fp8_f32 v151, v146, v147 op_sel:[0,0,1]
	s_nop 0
	global_store_dwordx4 v11, v[148:151], s[14:15]
	ds_read_b32 v132, v8
	ds_read_b32 v133, v8 offset:512
	ds_read_b32 v134, v8 offset:1024
	ds_read_b32 v135, v8 offset:1536
	ds_read_b32 v136, v8 offset:2048
	ds_read_b32 v137, v8 offset:2560
	ds_read_b32 v138, v8 offset:3072
	ds_read_b32 v139, v8 offset:3584
	ds_read_b32 v140, v8 offset:4096
	ds_read_b32 v141, v8 offset:4608
	ds_read_b32 v142, v8 offset:5120
	ds_read_b32 v143, v8 offset:5632
	ds_read_b32 v144, v8 offset:6144
	ds_read_b32 v145, v8 offset:6656
	ds_read_b32 v146, v8 offset:7168
	ds_read_b32 v147, v8 offset:7680
	s_waitcnt lgkmcnt(0)
	v_max_f32_e32 v132, v132, v132
	v_max_f32_e32 v133, v133, v133
	v_max_f32_e32 v134, v134, v134
	v_max_f32_e32 v135, v135, v135
	v_max_f32_e32 v136, v136, v136
	v_max_f32_e32 v137, v137, v137
	v_max_f32_e32 v138, v138, v138
	v_max_f32_e32 v139, v139, v139
	v_max_f32_e32 v140, v140, v140
	v_max_f32_e32 v141, v141, v141
	v_max_f32_e32 v142, v142, v142
	v_max_f32_e32 v143, v143, v143
	v_max_f32_e32 v144, v144, v144
	v_max_f32_e32 v145, v145, v145
	v_max_f32_e32 v146, v146, v146
	v_max_f32_e32 v147, v147, v147
	v_med3_f32 v132, v132, s20, v13
	v_med3_f32 v133, v133, s20, v13
	v_med3_f32 v134, v134, s20, v13
	v_med3_f32 v135, v135, s20, v13
	v_med3_f32 v136, v136, s20, v13
	v_med3_f32 v137, v137, s20, v13
	v_med3_f32 v138, v138, s20, v13
	v_med3_f32 v139, v139, s20, v13
	v_med3_f32 v140, v140, s20, v13
	v_med3_f32 v141, v141, s20, v13
	v_med3_f32 v142, v142, s20, v13
	v_med3_f32 v143, v143, s20, v13
	v_med3_f32 v144, v144, s20, v13
	v_med3_f32 v145, v145, s20, v13
	v_med3_f32 v146, v146, s20, v13
	v_med3_f32 v147, v147, s20, v13
	v_mov_b32_e32 v148, 0
	v_mov_b32_e32 v149, 0
	v_mov_b32_e32 v150, 0
	v_mov_b32_e32 v151, 0
	v_cvt_pk_fp8_f32 v148, v132, v133
	v_cvt_pk_fp8_f32 v149, v136, v137
	v_cvt_pk_fp8_f32 v150, v140, v141
	v_cvt_pk_fp8_f32 v151, v144, v145
	v_cvt_pk_fp8_f32 v148, v134, v135 op_sel:[0,0,1]
	v_cvt_pk_fp8_f32 v149, v138, v139 op_sel:[0,0,1]
	v_cvt_pk_fp8_f32 v150, v142, v143 op_sel:[0,0,1]
	v_cvt_pk_fp8_f32 v151, v146, v147 op_sel:[0,0,1]
	s_nop 0
	global_store_dwordx4 v12, v[148:151], s[14:15]
	s_waitcnt vmcnt(14)
	v_mul_f32_e32 v100, 0x43000000, v100
	v_mul_f32_e32 v101, 0x43000000, v101
	v_mul_f32_e32 v102, 0x43000000, v102
	v_mul_f32_e32 v103, 0x43000000, v103
	ds_write_b128 v5, v[100:103]
	v_mul_f32_e32 v104, 0x43000000, v104
	v_mul_f32_e32 v105, 0x43000000, v105
	v_mul_f32_e32 v106, 0x43000000, v106
	v_mul_f32_e32 v107, 0x43000000, v107
	ds_write_b128 v5, v[104:107] offset:1024
	v_mul_f32_e32 v108, 0x43000000, v108
	v_mul_f32_e32 v109, 0x43000000, v109
	v_mul_f32_e32 v110, 0x43000000, v110
	v_mul_f32_e32 v111, 0x43000000, v111
	ds_write_b128 v5, v[108:111] offset:2048
	v_mul_f32_e32 v112, 0x43000000, v112
	v_mul_f32_e32 v113, 0x43000000, v113
	v_mul_f32_e32 v114, 0x43000000, v114
	v_mul_f32_e32 v115, 0x43000000, v115
	ds_write_b128 v5, v[112:115] offset:3072
	v_mul_f32_e32 v116, 0x43000000, v116
	v_mul_f32_e32 v117, 0x43000000, v117
	v_mul_f32_e32 v118, 0x43000000, v118
	v_mul_f32_e32 v119, 0x43000000, v119
	ds_write_b128 v5, v[116:119] offset:4096
	v_mul_f32_e32 v120, 0x43000000, v120
	v_mul_f32_e32 v121, 0x43000000, v121
	v_mul_f32_e32 v122, 0x43000000, v122
	v_mul_f32_e32 v123, 0x43000000, v123
	ds_write_b128 v5, v[120:123] offset:5120
	v_mul_f32_e32 v124, 0x43000000, v124
	v_mul_f32_e32 v125, 0x43000000, v125
	v_mul_f32_e32 v126, 0x43000000, v126
	v_mul_f32_e32 v127, 0x43000000, v127
	ds_write_b128 v5, v[124:127] offset:6144
	v_mul_f32_e32 v128, 0x43000000, v128
	v_mul_f32_e32 v129, 0x43000000, v129
	v_mul_f32_e32 v130, 0x43000000, v130
	v_mul_f32_e32 v131, 0x43000000, v131
	ds_write_b128 v5, v[128:131] offset:7168
	s_waitcnt lgkmcnt(0)
	s_barrier
; #define GAS __attribute__((address_space(1)))
; #define LAS __attribute__((address_space(3)))
; #define LDS_WAIT() asm volatile("s_waitcnt lgkmcnt(0)" ::: "memory")
; __device__ __forceinline__ unsigned pk4_fp8(float a, float b, float c, float d) {
;     a = fminf(fmaxf(a, -448.f), 448.f); b = fminf(fmaxf(b, -448.f), 448.f); c = fminf(fmaxf(c, -448.f), 448.f); d = fminf(fmaxf(d, -448.f), 448.f);
;     int w = __builtin_amdgcn_cvt_pk_fp8_f32(a, b, 0, false); w = __builtin_amdgcn_cvt_pk_fp8_f32(c, d, w, true); return (unsigned)w; }
;     const int pr = item >> 1, kb = 2 * (pr / nblk) + (item & 1), nb = pr % nblk, k0 = 64 * kb, n0 = 32 * nb;
;     const int nr = n0 + (lane & 31); const int sc = MAP == 1 ? src_col_in(nr) : nr;
;     float v[32];
; #pragma unroll
;     for (int i = 0; i < 32; ++i) v[i] = sc >= 0 ? W[(size_t)(k0 + 2 * i + (lane >> 5)) * Nsrc + sc] : 0.f;
; #pragma unroll
;     for (int i = 0; i < 32; ++i) { const int k = k0 + 2 * i + (lane >> 5); float x = v[i] * wscale; if (KS) x *= (k < ksplit ? ksA[k] : ksB[k - ksplit]); scr[(2 * i + (lane >> 5)) * 33 + (lane & 31)] = x; }
;     LDS_WAIT(); asm volatile("" ::: "memory");
;     const int c = lane & 7;
; #pragma unroll
;     for (int j = 0; j < 4; ++j) { const int n = (lane >> 3) + 8 * j; const LAS float* s = scr + (8 * c) * 33 + n;
;         const unsigned long long o = (unsigned long long)pg8::pk4_fp8(s[0 * 33], s[1 * 33], s[2 * 33], s[3 * 33]) | ((unsigned long long)pg8::pk4_fp8(s[4 * 33], s[5 * 33], s[6 * 33], s[7 * 33]) << 32);
;         *(GAS unsigned long long*)(WT + (size_t)(n0 + n) * K + k0 + 8 * c) = o; }
;     LDS_WAIT(); asm volatile("" ::: "memory");
	s_add_i32 s17, s16, 3936
	s_min_u32 s17, s17, 0xfff
	s_lshr_b32 s18, s17, 5
	s_add_i32 s18, s18, 0
	s_and_b32 s19, s17, 31
	s_lshl_b32 s19, s19, 21
	s_lshl_b32 s18, s18, 7
	s_add_u32 s18, s18, s19
	s_add_u32 s14, s4, s18
	s_addc_u32 s15, s5, 0
	ds_read_b32 v132, v7
	ds_read_b32 v133, v7 offset:512
	ds_read_b32 v134, v7 offset:1024
	ds_read_b32 v135, v7 offset:1536
	ds_read_b32 v136, v7 offset:2048
	ds_read_b32 v137, v7 offset:2560
	ds_read_b32 v138, v7 offset:3072
	ds_read_b32 v139, v7 offset:3584
	ds_read_b32 v140, v7 offset:4096
	ds_read_b32 v141, v7 offset:4608
	ds_read_b32 v142, v7 offset:5120
	ds_read_b32 v143, v7 offset:5632
	ds_read_b32 v144, v7 offset:6144
	ds_read_b32 v145, v7 offset:6656
	ds_read_b32 v146, v7 offset:7168
	ds_read_b32 v147, v7 offset:7680
	s_waitcnt lgkmcnt(0)
	v_max_f32_e32 v132, v132, v132
	v_max_f32_e32 v133, v133, v133
	v_max_f32_e32 v134, v134, v134
	v_max_f32_e32 v135, v135, v135
	v_max_f32_e32 v136, v136, v136
	v_max_f32_e32 v137, v137, v137
	v_max_f32_e32 v138, v138, v138
	v_max_f32_e32 v139, v139, v139
	v_max_f32_e32 v140, v140, v140
	v_max_f32_e32 v141, v141, v141
	v_max_f32_e32 v142, v142, v142
	v_max_f32_e32 v143, v143, v143
	v_max_f32_e32 v144, v144, v144
	v_max_f32_e32 v145, v145, v145
	v_max_f32_e32 v146, v146, v146
	v_max_f32_e32 v147, v147, v147
	v_med3_f32 v132, v132, s20, v13
	v_med3_f32 v133, v133, s20, v13
	v_med3_f32 v134, v134, s20, v13
	v_med3_f32 v135, v135, s20, v13
	v_med3_f32 v136, v136, s20, v13
	v_med3_f32 v137, v137, s20, v13
	v_med3_f32 v138, v138, s20, v13
	v_med3_f32 v139, v139, s20, v13
	v_med3_f32 v140, v140, s20, v13
	v_med3_f32 v141, v141, s20, v13
	v_med3_f32 v142, v142, s20, v13
	v_med3_f32 v143, v143, s20, v13
	v_med3_f32 v144, v144, s20, v13
	v_med3_f32 v145, v145, s20, v13
	v_med3_f32 v146, v146, s20, v13
	v_med3_f32 v147, v147, s20, v13
	v_mov_b32_e32 v148, 0
	v_mov_b32_e32 v149, 0
	v_mov_b32_e32 v150, 0
	v_mov_b32_e32 v151, 0
	v_cvt_pk_fp8_f32 v148, v132, v133
	v_cvt_pk_fp8_f32 v149, v136, v137
	v_cvt_pk_fp8_f32 v150, v140, v141
	v_cvt_pk_fp8_f32 v151, v144, v145
	v_cvt_pk_fp8_f32 v148, v134, v135 op_sel:[0,0,1]
	v_cvt_pk_fp8_f32 v149, v138, v139 op_sel:[0,0,1]
	v_cvt_pk_fp8_f32 v150, v142, v143 op_sel:[0,0,1]
	v_cvt_pk_fp8_f32 v151, v146, v147 op_sel:[0,0,1]
	s_nop 0
	global_store_dwordx4 v11, v[148:151], s[14:15]
	ds_read_b32 v132, v9
	ds_read_b32 v133, v9 offset:512
	ds_read_b32 v134, v9 offset:1024
	ds_read_b32 v135, v9 offset:1536
	ds_read_b32 v136, v9 offset:2048
	ds_read_b32 v137, v9 offset:2560
	ds_read_b32 v138, v9 offset:3072
	ds_read_b32 v139, v9 offset:3584
	ds_read_b32 v140, v9 offset:4096
	ds_read_b32 v141, v9 offset:4608
	ds_read_b32 v142, v9 offset:5120
	ds_read_b32 v143, v9 offset:5632
	ds_read_b32 v144, v9 offset:6144
	ds_read_b32 v145, v9 offset:6656
	ds_read_b32 v146, v9 offset:7168
	ds_read_b32 v147, v9 offset:7680
	s_waitcnt lgkmcnt(0)
	v_max_f32_e32 v132, v132, v132
	v_max_f32_e32 v133, v133, v133
	v_max_f32_e32 v134, v134, v134
	v_max_f32_e32 v135, v135, v135
	v_max_f32_e32 v136, v136, v136
	v_max_f32_e32 v137, v137, v137
	v_max_f32_e32 v138, v138, v138
	v_max_f32_e32 v139, v139, v139
	v_max_f32_e32 v140, v140, v140
	v_max_f32_e32 v141, v141, v141
	v_max_f32_e32 v142, v142, v142
	v_max_f32_e32 v143, v143, v143
	v_max_f32_e32 v144, v144, v144
	v_max_f32_e32 v145, v145, v145
	v_max_f32_e32 v146, v146, v146
	v_max_f32_e32 v147, v147, v147
	v_med3_f32 v132, v132, s20, v13
	v_med3_f32 v133, v133, s20, v13
	v_med3_f32 v134, v134, s20, v13
	v_med3_f32 v135, v135, s20, v13
	v_med3_f32 v136, v136, s20, v13
	v_med3_f32 v137, v137, s20, v13
	v_med3_f32 v138, v138, s20, v13
	v_med3_f32 v139, v139, s20, v13
	v_med3_f32 v140, v140, s20, v13
	v_med3_f32 v141, v141, s20, v13
	v_med3_f32 v142, v142, s20, v13
	v_med3_f32 v143, v143, s20, v13
	v_med3_f32 v144, v144, s20, v13
	v_med3_f32 v145, v145, s20, v13
	v_med3_f32 v146, v146, s20, v13
	v_med3_f32 v147, v147, s20, v13
	v_mov_b32_e32 v148, 0
	v_mov_b32_e32 v149, 0
	v_mov_b32_e32 v150, 0
	v_mov_b32_e32 v151, 0
	v_cvt_pk_fp8_f32 v148, v132, v133
	v_cvt_pk_fp8_f32 v149, v136, v137
	v_cvt_pk_fp8_f32 v150, v140, v141
	v_cvt_pk_fp8_f32 v151, v144, v145
	v_cvt_pk_fp8_f32 v148, v134, v135 op_sel:[0,0,1]
	v_cvt_pk_fp8_f32 v149, v138, v139 op_sel:[0,0,1]
	v_cvt_pk_fp8_f32 v150, v142, v143 op_sel:[0,0,1]
	v_cvt_pk_fp8_f32 v151, v146, v147 op_sel:[0,0,1]
	s_nop 0
	global_store_dwordx4 v12, v[148:151], s[14:15]
	s_waitcnt vmcnt(6)
	v_mul_f32_e32 v36, 0x43000000, v36
	v_mul_f32_e32 v37, 0x43000000, v37
	v_mul_f32_e32 v38, 0x43000000, v38
	v_mul_f32_e32 v39, 0x43000000, v39
	ds_write_b128 v4, v[36:39]
	v_mul_f32_e32 v40, 0x43000000, v40
	v_mul_f32_e32 v41, 0x43000000, v41
	v_mul_f32_e32 v42, 0x43000000, v42
	v_mul_f32_e32 v43, 0x43000000, v43
	ds_write_b128 v4, v[40:43] offset:1024
	v_mul_f32_e32 v44, 0x43000000, v44
	v_mul_f32_e32 v45, 0x43000000, v45
	v_mul_f32_e32 v46, 0x43000000, v46
	v_mul_f32_e32 v47, 0x43000000, v47
	ds_write_b128 v4, v[44:47] offset:2048
	v_mul_f32_e32 v48, 0x43000000, v48
	v_mul_f32_e32 v49, 0x43000000, v49
	v_mul_f32_e32 v50, 0x43000000, v50
	v_mul_f32_e32 v51, 0x43000000, v51
	ds_write_b128 v4, v[48:51] offset:3072
	v_mul_f32_e32 v52, 0x43000000, v52
	v_mul_f32_e32 v53, 0x43000000, v53
	v_mul_f32_e32 v54, 0x43000000, v54
	v_mul_f32_e32 v55, 0x43000000, v55
	ds_write_b128 v4, v[52:55] offset:4096
	v_mul_f32_e32 v56, 0x43000000, v56
	v_mul_f32_e32 v57, 0x43000000, v57
	v_mul_f32_e32 v58, 0x43000000, v58
	v_mul_f32_e32 v59, 0x43000000, v59
	ds_write_b128 v4, v[56:59] offset:5120
	v_mul_f32_e32 v60, 0x43000000, v60
	v_mul_f32_e32 v61, 0x43000000, v61
	v_mul_f32_e32 v62, 0x43000000, v62
	v_mul_f32_e32 v63, 0x43000000, v63
	ds_write_b128 v4, v[60:63] offset:6144
	v_mul_f32_e32 v64, 0x43000000, v64
	v_mul_f32_e32 v65, 0x43000000, v65
	v_mul_f32_e32 v66, 0x43000000, v66
	v_mul_f32_e32 v67, 0x43000000, v67
	ds_write_b128 v4, v[64:67] offset:7168
	s_waitcnt lgkmcnt(0)
	s_barrier
; #define GAS __attribute__((address_space(1)))
; #define LAS __attribute__((address_space(3)))
; #define LDS_WAIT() asm volatile("s_waitcnt lgkmcnt(0)" ::: "memory")
; __device__ __forceinline__ unsigned pk4_fp8(float a, float b, float c, float d) {
;     a = fminf(fmaxf(a, -448.f), 448.f); b = fminf(fmaxf(b, -448.f), 448.f); c = fminf(fmaxf(c, -448.f), 448.f); d = fminf(fmaxf(d, -448.f), 448.f);
;     int w = __builtin_amdgcn_cvt_pk_fp8_f32(a, b, 0, false); w = __builtin_amdgcn_cvt_pk_fp8_f32(c, d, w, true); return (unsigned)w; }
;     const int pr = item >> 1, kb = 2 * (pr / nblk) + (item & 1), nb = pr % nblk, k0 = 64 * kb, n0 = 32 * nb;
;     const int nr = n0 + (lane & 31); const int sc = MAP == 1 ? src_col_in(nr) : nr;
;     float v[32];
; #pragma unroll
;     for (int i = 0; i < 32; ++i) v[i] = sc >= 0 ? W[(size_t)(k0 + 2 * i + (lane >> 5)) * Nsrc + sc] : 0.f;
; #pragma unroll
;     for (int i = 0; i < 32; ++i) { const int k = k0 + 2 * i + (lane >> 5); float x = v[i] * wscale; if (KS) x *= (k < ksplit ? ksA[k] : ksB[k - ksplit]); scr[(2 * i + (lane >> 5)) * 33 + (lane & 31)] = x; }
;     LDS_WAIT(); asm volatile("" ::: "memory");
;     const int c = lane & 7;
; #pragma unroll
;     for (int j = 0; j < 4; ++j) { const int n = (lane >> 3) + 8 * j; const LAS float* s = scr + (8 * c) * 33 + n;
;         const unsigned long long o = (unsigned long long)pg8::pk4_fp8(s[0 * 33], s[1 * 33], s[2 * 33], s[3 * 33]) | ((unsigned long long)pg8::pk4_fp8(s[4 * 33], s[5 * 33], s[6 * 33], s[7 * 33]) << 32);
;         *(GAS unsigned long long*)(WT + (size_t)(n0 + n) * K + k0 + 8 * c) = o; }
;     LDS_WAIT(); asm volatile("" ::: "memory");
	s_add_i32 s17, s16, 4032
	s_min_u32 s17, s17, 0xfff
	s_lshr_b32 s18, s17, 5
	s_add_i32 s18, s18, 0
	s_and_b32 s19, s17, 31
	s_lshl_b32 s19, s19, 21
	s_lshl_b32 s18, s18, 7
	s_add_u32 s18, s18, s19
	s_add_u32 s14, s4, s18
	s_addc_u32 s15, s5, 0
	ds_read_b32 v132, v6
	ds_read_b32 v133, v6 offset:512
	ds_read_b32 v134, v6 offset:1024
	ds_read_b32 v135, v6 offset:1536
	ds_read_b32 v136, v6 offset:2048
	ds_read_b32 v137, v6 offset:2560
	ds_read_b32 v138, v6 offset:3072
	ds_read_b32 v139, v6 offset:3584
	ds_read_b32 v140, v6 offset:4096
	ds_read_b32 v141, v6 offset:4608
	ds_read_b32 v142, v6 offset:5120
	ds_read_b32 v143, v6 offset:5632
	ds_read_b32 v144, v6 offset:6144
	ds_read_b32 v145, v6 offset:6656
	ds_read_b32 v146, v6 offset:7168
	ds_read_b32 v147, v6 offset:7680
	s_waitcnt lgkmcnt(0)
	v_max_f32_e32 v132, v132, v132
	v_max_f32_e32 v133, v133, v133
	v_max_f32_e32 v134, v134, v134
	v_max_f32_e32 v135, v135, v135
	v_max_f32_e32 v136, v136, v136
	v_max_f32_e32 v137, v137, v137
	v_max_f32_e32 v138, v138, v138
	v_max_f32_e32 v139, v139, v139
	v_max_f32_e32 v140, v140, v140
	v_max_f32_e32 v141, v141, v141
	v_max_f32_e32 v142, v142, v142
	v_max_f32_e32 v143, v143, v143
	v_max_f32_e32 v144, v144, v144
	v_max_f32_e32 v145, v145, v145
	v_max_f32_e32 v146, v146, v146
	v_max_f32_e32 v147, v147, v147
	v_med3_f32 v132, v132, s20, v13
	v_med3_f32 v133, v133, s20, v13
	v_med3_f32 v134, v134, s20, v13
	v_med3_f32 v135, v135, s20, v13
	v_med3_f32 v136, v136, s20, v13
	v_med3_f32 v137, v137, s20, v13
	v_med3_f32 v138, v138, s20, v13
	v_med3_f32 v139, v139, s20, v13
	v_med3_f32 v140, v140, s20, v13
	v_med3_f32 v141, v141, s20, v13
	v_med3_f32 v142, v142, s20, v13
	v_med3_f32 v143, v143, s20, v13
	v_med3_f32 v144, v144, s20, v13
	v_med3_f32 v145, v145, s20, v13
	v_med3_f32 v146, v146, s20, v13
	v_med3_f32 v147, v147, s20, v13
	v_mov_b32_e32 v148, 0
	v_mov_b32_e32 v149, 0
	v_mov_b32_e32 v150, 0
	v_mov_b32_e32 v151, 0
	v_cvt_pk_fp8_f32 v148, v132, v133
	v_cvt_pk_fp8_f32 v149, v136, v137
	v_cvt_pk_fp8_f32 v150, v140, v141
	v_cvt_pk_fp8_f32 v151, v144, v145
	v_cvt_pk_fp8_f32 v148, v134, v135 op_sel:[0,0,1]
	v_cvt_pk_fp8_f32 v149, v138, v139 op_sel:[0,0,1]
	v_cvt_pk_fp8_f32 v150, v142, v143 op_sel:[0,0,1]
	v_cvt_pk_fp8_f32 v151, v146, v147 op_sel:[0,0,1]
	s_nop 0
	global_store_dwordx4 v11, v[148:151], s[14:15]
	ds_read_b32 v132, v8
	ds_read_b32 v133, v8 offset:512
	ds_read_b32 v134, v8 offset:1024
	ds_read_b32 v135, v8 offset:1536
	ds_read_b32 v136, v8 offset:2048
	ds_read_b32 v137, v8 offset:2560
	ds_read_b32 v138, v8 offset:3072
	ds_read_b32 v139, v8 offset:3584
	ds_read_b32 v140, v8 offset:4096
	ds_read_b32 v141, v8 offset:4608
	ds_read_b32 v142, v8 offset:5120
	ds_read_b32 v143, v8 offset:5632
	ds_read_b32 v144, v8 offset:6144
	ds_read_b32 v145, v8 offset:6656
	ds_read_b32 v146, v8 offset:7168
	ds_read_b32 v147, v8 offset:7680
	s_waitcnt lgkmcnt(0)
	v_max_f32_e32 v132, v132, v132
	v_max_f32_e32 v133, v133, v133
	v_max_f32_e32 v134, v134, v134
	v_max_f32_e32 v135, v135, v135
	v_max_f32_e32 v136, v136, v136
	v_max_f32_e32 v137, v137, v137
	v_max_f32_e32 v138, v138, v138
	v_max_f32_e32 v139, v139, v139
	v_max_f32_e32 v140, v140, v140
	v_max_f32_e32 v141, v141, v141
	v_max_f32_e32 v142, v142, v142
	v_max_f32_e32 v143, v143, v143
	v_max_f32_e32 v144, v144, v144
	v_max_f32_e32 v145, v145, v145
	v_max_f32_e32 v146, v146, v146
	v_max_f32_e32 v147, v147, v147
	v_med3_f32 v132, v132, s20, v13
	v_med3_f32 v133, v133, s20, v13
	v_med3_f32 v134, v134, s20, v13
	v_med3_f32 v135, v135, s20, v13
	v_med3_f32 v136, v136, s20, v13
	v_med3_f32 v137, v137, s20, v13
	v_med3_f32 v138, v138, s20, v13
	v_med3_f32 v139, v139, s20, v13
	v_med3_f32 v140, v140, s20, v13
	v_med3_f32 v141, v141, s20, v13
	v_med3_f32 v142, v142, s20, v13
	v_med3_f32 v143, v143, s20, v13
	v_med3_f32 v144, v144, s20, v13
	v_med3_f32 v145, v145, s20, v13
	v_med3_f32 v146, v146, s20, v13
	v_med3_f32 v147, v147, s20, v13
	v_mov_b32_e32 v148, 0
	v_mov_b32_e32 v149, 0
	v_mov_b32_e32 v150, 0
	v_mov_b32_e32 v151, 0
	v_cvt_pk_fp8_f32 v148, v132, v133
	v_cvt_pk_fp8_f32 v149, v136, v137
	v_cvt_pk_fp8_f32 v150, v140, v141
	v_cvt_pk_fp8_f32 v151, v144, v145
	v_cvt_pk_fp8_f32 v148, v134, v135 op_sel:[0,0,1]
	v_cvt_pk_fp8_f32 v149, v138, v139 op_sel:[0,0,1]
	v_cvt_pk_fp8_f32 v150, v142, v143 op_sel:[0,0,1]
	v_cvt_pk_fp8_f32 v151, v146, v147 op_sel:[0,0,1]
	s_nop 0
	global_store_dwordx4 v12, v[148:151], s[14:15]
	s_waitcnt vmcnt(0) lgkmcnt(0)
	s_barrier
